# PEER u block scales stored as chunk-pair dwords: the P12 dot-product loop (unrolled by two chunks) gathers scales on even chunks only and keeps them in VGPRs; odd-chunk scale loads replaced by one hot
# speedup vs baseline: 1.0319x; 1.0086x over previous
; __device__ __forceinline__ unsigned f2bf(float f) { unsigned u = __builtin_bit_cast(unsigned, f); return (u + 0x7fffu + ((u >> 16) & 1u)) >> 16; }
; __device__ __forceinline__ void quant_rows4(const float* src, const float* cscale, unsigned char* dst, bf16* bscale, int nrows, int gw, int ngw, int lane) {
;     ...
;             const unsigned sb = f2bf(m * (1.0f / 7.0f)); const float s = __uint_as_float(sb << 16); const float inv = s > 0.f ? 1.0f / s : 0.f;
;             const int q0 = min(max((int)rintf(v.x * inv), -7), 7), q1 = min(max((int)rintf(v.y * inv), -7), 7), q2 = min(max((int)rintf(v.z * inv), -7), 7), q3 = min(max((int)rintf(v.w * inv), -7), 7);
;             const unsigned P = (unsigned)(q0 + 8) | ((unsigned)(q1 + 8) << 8) | ((unsigned)(q2 + 8) << 16) | ((unsigned)(q3 + 8) << 24);
;             const unsigned Q = (unsigned)__builtin_amdgcn_update_dpp(0, (int)P, 0xB1, 0xF, 0xF, false);
;             if ((lane & 1) == 0) d4[(size_t)j * (16384 * 32)] = P | (Q << 4);
;             if ((lane & 7) == 0) bscale[((size_t)j * 16384 + r) * 8 + (lane >> 3)] = (bf16)sb;
.LBB0_166:
	s_or_b64 exec, exec, s[6:7]
	v_lshl_add_u64 v[160:161], v[154:155], 1, s[68:69]
	s_and_saveexec_b64 s[6:7], s[4:5]
	s_cbranch_execz .LBB0_168
	v_add_co_u32_e32 v164, vcc, 0xf400000, v160
	s_nop 1
	v_addc_co_u32_e32 v165, vcc, 0, v161, vcc
	global_store_short_d16_hi v[164:165], v163, off

; __device__ __forceinline__ unsigned f2bf(float f) { unsigned u = __builtin_bit_cast(unsigned, f); return (u + 0x7fffu + ((u >> 16) & 1u)) >> 16; }
; __device__ __forceinline__ void quant_rows4(const float* src, const float* cscale, unsigned char* dst, bf16* bscale, int nrows, int gw, int ngw, int lane) {
;     ...
;             const unsigned sb = f2bf(m * (1.0f / 7.0f)); const float s = __uint_as_float(sb << 16); const float inv = s > 0.f ? 1.0f / s : 0.f;
;             const int q0 = min(max((int)rintf(v.x * inv), -7), 7), q1 = min(max((int)rintf(v.y * inv), -7), 7), q2 = min(max((int)rintf(v.z * inv), -7), 7), q3 = min(max((int)rintf(v.w * inv), -7), 7);
;             const unsigned P = (unsigned)(q0 + 8) | ((unsigned)(q1 + 8) << 8) | ((unsigned)(q2 + 8) << 16) | ((unsigned)(q3 + 8) << 24);
;             const unsigned Q = (unsigned)__builtin_amdgcn_update_dpp(0, (int)P, 0xB1, 0xF, 0xF, false);
;             if ((lane & 1) == 0) d4[(size_t)j * (16384 * 32)] = P | (Q << 4);
;             if ((lane & 7) == 0) bscale[((size_t)j * 16384 + r) * 8 + (lane >> 3)] = (bf16)sb;
.LBB0_170:
	s_or_b64 exec, exec, s[6:7]
	s_and_saveexec_b64 s[6:7], s[4:5]
	s_cbranch_execz .LBB0_172
	v_add_co_u32_e32 v116, vcc, 0xf400002, v160
	s_nop 1
	v_addc_co_u32_e32 v117, vcc, 0, v161, vcc
	global_store_short_d16_hi v[116:117], v114, off

; __device__ __forceinline__ unsigned f2bf(float f) { unsigned u = __builtin_bit_cast(unsigned, f); return (u + 0x7fffu + ((u >> 16) & 1u)) >> 16; }
; __device__ __forceinline__ void quant_rows4(const float* src, const float* cscale, unsigned char* dst, bf16* bscale, int nrows, int gw, int ngw, int lane) {
;     ...
;             const unsigned sb = f2bf(m * (1.0f / 7.0f)); const float s = __uint_as_float(sb << 16); const float inv = s > 0.f ? 1.0f / s : 0.f;
;             const int q0 = min(max((int)rintf(v.x * inv), -7), 7), q1 = min(max((int)rintf(v.y * inv), -7), 7), q2 = min(max((int)rintf(v.z * inv), -7), 7), q3 = min(max((int)rintf(v.w * inv), -7), 7);
;             const unsigned P = (unsigned)(q0 + 8) | ((unsigned)(q1 + 8) << 8) | ((unsigned)(q2 + 8) << 16) | ((unsigned)(q3 + 8) << 24);
;             const unsigned Q = (unsigned)__builtin_amdgcn_update_dpp(0, (int)P, 0xB1, 0xF, 0xF, false);
;             if ((lane & 1) == 0) d4[(size_t)j * (16384 * 32)] = P | (Q << 4);
;             if ((lane & 7) == 0) bscale[((size_t)j * 16384 + r) * 8 + (lane >> 3)] = (bf16)sb;
.LBB0_178:
	s_or_b64 exec, exec, s[6:7]
	s_and_saveexec_b64 s[6:7], s[4:5]
	s_cbranch_execz .LBB0_180
	v_add_co_u32_e32 v100, vcc, 0xf480002, v160
	s_nop 1
	v_addc_co_u32_e32 v101, vcc, 0, v161, vcc
	global_store_short_d16_hi v[100:101], v98, off

; __device__ __forceinline__ unsigned f2bf(float f) { unsigned u = __builtin_bit_cast(unsigned, f); return (u + 0x7fffu + ((u >> 16) & 1u)) >> 16; }
; __device__ __forceinline__ void quant_rows4(const float* src, const float* cscale, unsigned char* dst, bf16* bscale, int nrows, int gw, int ngw, int lane) {
;     ...
;             const unsigned sb = f2bf(m * (1.0f / 7.0f)); const float s = __uint_as_float(sb << 16); const float inv = s > 0.f ? 1.0f / s : 0.f;
;             const int q0 = min(max((int)rintf(v.x * inv), -7), 7), q1 = min(max((int)rintf(v.y * inv), -7), 7), q2 = min(max((int)rintf(v.z * inv), -7), 7), q3 = min(max((int)rintf(v.w * inv), -7), 7);
;             const unsigned P = (unsigned)(q0 + 8) | ((unsigned)(q1 + 8) << 8) | ((unsigned)(q2 + 8) << 16) | ((unsigned)(q3 + 8) << 24);
;             const unsigned Q = (unsigned)__builtin_amdgcn_update_dpp(0, (int)P, 0xB1, 0xF, 0xF, false);
;             if ((lane & 1) == 0) d4[(size_t)j * (16384 * 32)] = P | (Q << 4);
;             if ((lane & 7) == 0) bscale[((size_t)j * 16384 + r) * 8 + (lane >> 3)] = (bf16)sb;
.LBB0_186:
	s_or_b64 exec, exec, s[6:7]
	s_and_saveexec_b64 s[6:7], s[4:5]
	s_cbranch_execz .LBB0_188
	v_add_co_u32_e32 v84, vcc, 0xf500002, v160
	s_nop 1
	v_addc_co_u32_e32 v85, vcc, 0, v161, vcc
	global_store_short_d16_hi v[84:85], v82, off

; __device__ __forceinline__ unsigned f2bf(float f) { unsigned u = __builtin_bit_cast(unsigned, f); return (u + 0x7fffu + ((u >> 16) & 1u)) >> 16; }
; __device__ __forceinline__ void quant_rows4(const float* src, const float* cscale, unsigned char* dst, bf16* bscale, int nrows, int gw, int ngw, int lane) {
;     ...
;             const unsigned sb = f2bf(m * (1.0f / 7.0f)); const float s = __uint_as_float(sb << 16); const float inv = s > 0.f ? 1.0f / s : 0.f;
;             const int q0 = min(max((int)rintf(v.x * inv), -7), 7), q1 = min(max((int)rintf(v.y * inv), -7), 7), q2 = min(max((int)rintf(v.z * inv), -7), 7), q3 = min(max((int)rintf(v.w * inv), -7), 7);
;             const unsigned P = (unsigned)(q0 + 8) | ((unsigned)(q1 + 8) << 8) | ((unsigned)(q2 + 8) << 16) | ((unsigned)(q3 + 8) << 24);
;             const unsigned Q = (unsigned)__builtin_amdgcn_update_dpp(0, (int)P, 0xB1, 0xF, 0xF, false);
;             if ((lane & 1) == 0) d4[(size_t)j * (16384 * 32)] = P | (Q << 4);
;             if ((lane & 7) == 0) bscale[((size_t)j * 16384 + r) * 8 + (lane >> 3)] = (bf16)sb;
.LBB0_194:
	s_or_b64 exec, exec, s[6:7]
	s_and_saveexec_b64 s[6:7], s[4:5]
	s_cbranch_execz .LBB0_196
	v_add_co_u32_e32 v68, vcc, 0xf580002, v160
	s_nop 1
	v_addc_co_u32_e32 v69, vcc, 0, v161, vcc
	global_store_short_d16_hi v[68:69], v66, off

; __device__ __forceinline__ unsigned f2bf(float f) { unsigned u = __builtin_bit_cast(unsigned, f); return (u + 0x7fffu + ((u >> 16) & 1u)) >> 16; }
; __device__ __forceinline__ void quant_rows4(const float* src, const float* cscale, unsigned char* dst, bf16* bscale, int nrows, int gw, int ngw, int lane) {
;     ...
;             const unsigned sb = f2bf(m * (1.0f / 7.0f)); const float s = __uint_as_float(sb << 16); const float inv = s > 0.f ? 1.0f / s : 0.f;
;             const int q0 = min(max((int)rintf(v.x * inv), -7), 7), q1 = min(max((int)rintf(v.y * inv), -7), 7), q2 = min(max((int)rintf(v.z * inv), -7), 7), q3 = min(max((int)rintf(v.w * inv), -7), 7);
;             const unsigned P = (unsigned)(q0 + 8) | ((unsigned)(q1 + 8) << 8) | ((unsigned)(q2 + 8) << 16) | ((unsigned)(q3 + 8) << 24);
;             const unsigned Q = (unsigned)__builtin_amdgcn_update_dpp(0, (int)P, 0xB1, 0xF, 0xF, false);
;             if ((lane & 1) == 0) d4[(size_t)j * (16384 * 32)] = P | (Q << 4);
;             if ((lane & 7) == 0) bscale[((size_t)j * 16384 + r) * 8 + (lane >> 3)] = (bf16)sb;
.LBB0_202:
	s_or_b64 exec, exec, s[6:7]
	s_and_saveexec_b64 s[6:7], s[4:5]
	s_cbranch_execz .LBB0_204
	v_add_co_u32_e32 v52, vcc, 0xf600002, v160
	s_nop 1
	v_addc_co_u32_e32 v53, vcc, 0, v161, vcc
	global_store_short_d16_hi v[52:53], v50, off

; __device__ __forceinline__ unsigned f2bf(float f) { unsigned u = __builtin_bit_cast(unsigned, f); return (u + 0x7fffu + ((u >> 16) & 1u)) >> 16; }
; __device__ __forceinline__ void quant_rows4(const float* src, const float* cscale, unsigned char* dst, bf16* bscale, int nrows, int gw, int ngw, int lane) {
;     ...
;             const unsigned sb = f2bf(m * (1.0f / 7.0f)); const float s = __uint_as_float(sb << 16); const float inv = s > 0.f ? 1.0f / s : 0.f;
;             const int q0 = min(max((int)rintf(v.x * inv), -7), 7), q1 = min(max((int)rintf(v.y * inv), -7), 7), q2 = min(max((int)rintf(v.z * inv), -7), 7), q3 = min(max((int)rintf(v.w * inv), -7), 7);
;             const unsigned P = (unsigned)(q0 + 8) | ((unsigned)(q1 + 8) << 8) | ((unsigned)(q2 + 8) << 16) | ((unsigned)(q3 + 8) << 24);
;             const unsigned Q = (unsigned)__builtin_amdgcn_update_dpp(0, (int)P, 0xB1, 0xF, 0xF, false);
;             if ((lane & 1) == 0) d4[(size_t)j * (16384 * 32)] = P | (Q << 4);
;             if ((lane & 7) == 0) bscale[((size_t)j * 16384 + r) * 8 + (lane >> 3)] = (bf16)sb;
.LBB0_210:
	s_or_b64 exec, exec, s[6:7]
	s_and_saveexec_b64 s[6:7], s[4:5]
	s_cbranch_execz .LBB0_212
	v_add_co_u32_e32 v36, vcc, 0xf680002, v160
	s_nop 1
	v_addc_co_u32_e32 v37, vcc, 0, v161, vcc
	global_store_short_d16_hi v[36:37], v34, off

; __device__ __forceinline__ unsigned f2bf(float f) { unsigned u = __builtin_bit_cast(unsigned, f); return (u + 0x7fffu + ((u >> 16) & 1u)) >> 16; }
; __device__ __forceinline__ void quant_rows4(const float* src, const float* cscale, unsigned char* dst, bf16* bscale, int nrows, int gw, int ngw, int lane) {
;     ...
;             const unsigned sb = f2bf(m * (1.0f / 7.0f)); const float s = __uint_as_float(sb << 16); const float inv = s > 0.f ? 1.0f / s : 0.f;
;             const int q0 = min(max((int)rintf(v.x * inv), -7), 7), q1 = min(max((int)rintf(v.y * inv), -7), 7), q2 = min(max((int)rintf(v.z * inv), -7), 7), q3 = min(max((int)rintf(v.w * inv), -7), 7);
;             const unsigned P = (unsigned)(q0 + 8) | ((unsigned)(q1 + 8) << 8) | ((unsigned)(q2 + 8) << 16) | ((unsigned)(q3 + 8) << 24);
;             const unsigned Q = (unsigned)__builtin_amdgcn_update_dpp(0, (int)P, 0xB1, 0xF, 0xF, false);
;             if ((lane & 1) == 0) d4[(size_t)j * (16384 * 32)] = P | (Q << 4);
;             if ((lane & 7) == 0) bscale[((size_t)j * 16384 + r) * 8 + (lane >> 3)] = (bf16)sb;
.LBB0_218:
	s_or_b64 exec, exec, s[6:7]
	s_and_saveexec_b64 s[6:7], s[4:5]
	s_cbranch_execz .LBB0_220
	v_add_co_u32_e32 v20, vcc, 0xf700002, v160
	s_nop 1
	v_addc_co_u32_e32 v21, vcc, 0, v161, vcc
	global_store_short_d16_hi v[20:21], v18, off

; __device__ __forceinline__ unsigned f2bf(float f) { unsigned u = __builtin_bit_cast(unsigned, f); return (u + 0x7fffu + ((u >> 16) & 1u)) >> 16; }
; __device__ __forceinline__ void quant_rows4(const float* src, const float* cscale, unsigned char* dst, bf16* bscale, int nrows, int gw, int ngw, int lane) {
;     ...
;             const unsigned sb = f2bf(m * (1.0f / 7.0f)); const float s = __uint_as_float(sb << 16); const float inv = s > 0.f ? 1.0f / s : 0.f;
;             const int q0 = min(max((int)rintf(v.x * inv), -7), 7), q1 = min(max((int)rintf(v.y * inv), -7), 7), q2 = min(max((int)rintf(v.z * inv), -7), 7), q3 = min(max((int)rintf(v.w * inv), -7), 7);
;             const unsigned P = (unsigned)(q0 + 8) | ((unsigned)(q1 + 8) << 8) | ((unsigned)(q2 + 8) << 16) | ((unsigned)(q3 + 8) << 24);
;             const unsigned Q = (unsigned)__builtin_amdgcn_update_dpp(0, (int)P, 0xB1, 0xF, 0xF, false);
;             if ((lane & 1) == 0) d4[(size_t)j * (16384 * 32)] = P | (Q << 4);
;             if ((lane & 7) == 0) bscale[((size_t)j * 16384 + r) * 8 + (lane >> 3)] = (bf16)sb;
.LBB0_226:
	s_or_b64 exec, exec, s[6:7]
	s_and_saveexec_b64 s[6:7], s[4:5]
	s_cbranch_execz .LBB0_163
	v_add_co_u32_e32 v4, vcc, 0xf780002, v160
	s_nop 1
	v_addc_co_u32_e32 v5, vcc, 0, v161, vcc
	global_store_short_d16_hi v[4:5], v2, off
	s_branch .LBB0_163

; __device__ __forceinline__ unsigned f2bf(float f) { unsigned u = __builtin_bit_cast(unsigned, f); return (u + 0x7fffu + ((u >> 16) & 1u)) >> 16; }
; __device__ __forceinline__ void quant_rows4(const float* src, const float* cscale, unsigned char* dst, bf16* bscale, int nrows, int gw, int ngw, int lane) {
;     ...
;             const unsigned sb = f2bf(m * (1.0f / 7.0f)); const float s = __uint_as_float(sb << 16); const float inv = s > 0.f ? 1.0f / s : 0.f;
;             const int q0 = min(max((int)rintf(v.x * inv), -7), 7), q1 = min(max((int)rintf(v.y * inv), -7), 7), q2 = min(max((int)rintf(v.z * inv), -7), 7), q3 = min(max((int)rintf(v.w * inv), -7), 7);
;             const unsigned P = (unsigned)(q0 + 8) | ((unsigned)(q1 + 8) << 8) | ((unsigned)(q2 + 8) << 16) | ((unsigned)(q3 + 8) << 24);
;             const unsigned Q = (unsigned)__builtin_amdgcn_update_dpp(0, (int)P, 0xB1, 0xF, 0xF, false);
;             if ((lane & 1) == 0) d4[(size_t)j * (16384 * 32)] = P | (Q << 4);
;             if ((lane & 7) == 0) bscale[((size_t)j * 16384 + r) * 8 + (lane >> 3)] = (bf16)sb;
.LBB0_815:
	s_or_b64 exec, exec, s[6:7]
	v_lshl_add_u64 v[160:161], v[152:153], 1, s[68:69]
	s_and_saveexec_b64 s[6:7], s[4:5]
	s_cbranch_execz .LBB0_817
	v_add_co_u32_e32 v164, vcc, 0xf400000, v160
	s_nop 1
	v_addc_co_u32_e32 v165, vcc, 0, v161, vcc
	global_store_short_d16_hi v[164:165], v163, off

; __device__ __forceinline__ unsigned f2bf(float f) { unsigned u = __builtin_bit_cast(unsigned, f); return (u + 0x7fffu + ((u >> 16) & 1u)) >> 16; }
; __device__ __forceinline__ void quant_rows4(const float* src, const float* cscale, unsigned char* dst, bf16* bscale, int nrows, int gw, int ngw, int lane) {
;     ...
;             const unsigned sb = f2bf(m * (1.0f / 7.0f)); const float s = __uint_as_float(sb << 16); const float inv = s > 0.f ? 1.0f / s : 0.f;
;             const int q0 = min(max((int)rintf(v.x * inv), -7), 7), q1 = min(max((int)rintf(v.y * inv), -7), 7), q2 = min(max((int)rintf(v.z * inv), -7), 7), q3 = min(max((int)rintf(v.w * inv), -7), 7);
;             const unsigned P = (unsigned)(q0 + 8) | ((unsigned)(q1 + 8) << 8) | ((unsigned)(q2 + 8) << 16) | ((unsigned)(q3 + 8) << 24);
;             const unsigned Q = (unsigned)__builtin_amdgcn_update_dpp(0, (int)P, 0xB1, 0xF, 0xF, false);
;             if ((lane & 1) == 0) d4[(size_t)j * (16384 * 32)] = P | (Q << 4);
;             if ((lane & 7) == 0) bscale[((size_t)j * 16384 + r) * 8 + (lane >> 3)] = (bf16)sb;
.LBB0_2101:
	s_or_b64 exec, exec, s[6:7]
	v_lshl_add_u64 v[160:161], v[152:153], 1, s[68:69]
	s_and_saveexec_b64 s[6:7], s[4:5]
	s_cbranch_execz .LBB0_2103
	v_add_co_u32_e32 v166, vcc, 0xf400000, v160
	s_nop 1
	v_addc_co_u32_e32 v167, vcc, 0, v161, vcc
	global_store_short_d16_hi v[166:167], v165, off

; __device__ __forceinline__ void p12_peer(Frame& F) {
;     const bf16* HN = (const bf16*)(F.ws + WS_HN);
;     const unsigned char* U4 = F.ws + WS_U8; const unsigned short* USS = (const unsigned short*)(F.ws + WS_USC); const unsigned char* V8 = F.ws + WS_V8; const float* VSC = (const float*)(F.ws + WS_VSC);
;     const int* PIDX = (const int*)(F.ws + WS_PIDX); const float* PGT = (const float*)(F.ws + WS_PG); const float* PSQ = (const float*)(F.ws + WS_PSQ);
;     const float* lnf = F.in[22];
;     LAS unsigned char* XQ = F.lds + F.wave * 17408;
;     LAS unsigned short* EL = (LAS unsigned short*)(XQ + 16384);
;     LAS float* WL = (LAS float*)XQ;
;     const int g8 = F.lane >> 3, k8 = F.lane & 7;
;     float sx[4];
; #pragma unroll
;     for (int i = 0; i < 4; ++i) {
;         const int t = F.gw + i * F.NGW; v4u xp[8]; float mxa = 0.f;
; #pragma unroll
;         for (int j = 0; j < 8; ++j) { xp[j] = ((const v4u*)(HN + (size_t)t * D_))[F.lane + 64 * j];
;             mxa = fmaxf(fmaxf(fmaxf(mxa, fmaxf(fabsf(bflo(xp[j].x)), fabsf(bfhi(xp[j].x)))), fmaxf(fabsf(bflo(xp[j].y)), fabsf(bfhi(xp[j].y)))), fmaxf(fmaxf(fabsf(bflo(xp[j].z)), fabsf(bfhi(xp[j].z))), fmaxf(fabsf(bflo(xp[j].w)), fabsf(bfhi(xp[j].w))))); }
;         mxa = wave_max(mxa); const float inv = mxa > 0.f ? 127.0f / mxa : 0.f;
;         const float rsn = 1.0f / sqrtf(wave_sum(PSQ[(size_t)t * 64 + F.lane]) * (1.f / D_) + 1e-6f);
;         sx[i] = mxa * rsn * (1.0f / 127.0f);
; #pragma unroll
;         for (int j = 0; j < 8; ++j) {
;             const int q0 = (int)rintf(bflo(xp[j].x) * inv), q1 = (int)rintf(bfhi(xp[j].x) * inv), q2 = (int)rintf(bflo(xp[j].y) * inv), q3 = (int)rintf(bfhi(xp[j].y) * inv);
;             const int q4 = (int)rintf(bflo(xp[j].z) * inv), q5 = (int)rintf(bfhi(xp[j].z) * inv), q6 = (int)rintf(bflo(xp[j].w) * inv), q7 = (int)rintf(bfhi(xp[j].w) * inv);
;             *(LAS v2u*)(XQ + i * 4096 + 8 * (F.lane + 64 * j)) = (v2u){(unsigned)((q0 & 0xff) | ((q1 & 0xff) << 8) | ((q2 & 0xff) << 16) | (q3 << 24)), (unsigned)((q4 & 0xff) | ((q5 & 0xff) << 8) | ((q6 & 0xff) << 16) | (q7 << 24))}; }
;         EL[i * 128 + F.lane] = (unsigned short)PIDX[(size_t)t * 128 + F.lane]; EL[i * 128 + 64 + F.lane] = (unsigned short)PIDX[(size_t)t * 128 + 64 + F.lane];
;         asm volatile("" ::: "memory");
;     }
;     LDS_WAIT(); asm volatile("" ::: "memory");
;     float psum[4][16];
.LBB0_3270:
	s_cmp_gt_i32 s84, 12
	s_cselect_b64 s[0:1], -1, 0
	s_cmp_lt_i32 s85, 13
	s_cselect_b64 s[2:3], -1, 0
	s_or_b64 s[0:1], s[0:1], s[2:3]
	s_and_b64 vcc, exec, s[0:1]
	s_cbranch_vccnz .LBB0_3413
	s_add_u32 s6, s68, 0x23400000
	s_addc_u32 s7, s69, 0
	s_add_u32 s0, s68, 0x7000000
	s_addc_u32 s1, s69, 0
	s_waitcnt lgkmcnt(0)
	s_add_u32 s18, s68, 0xe00000
	s_addc_u32 s19, s69, 0
	s_add_u32 s22, s68, 0x800000
	s_addc_u32 s23, s69, 0
	s_mul_i32 s2, s66, 0x4400
	s_ashr_i32 s95, s94, 31
	s_add_i32 s20, s2, 0
	s_lshl_b64 s[2:3], s[94:95], 13
	v_mbcnt_lo_u32_b32 v92, -1, 0
	v_mbcnt_hi_u32_b32 v92, -1, v92
	s_add_u32 s2, s6, s2
	v_ashrrev_i32_e32 v93, 31, v92
	s_addc_u32 s3, s7, s3
	s_waitcnt vmcnt(7)
	v_lshlrev_b64 v[18:19], 4, v[92:93]
	v_lshl_add_u64 v[0:1], s[2:3], 0, v[18:19]
	global_load_dwordx4 v[12:15], v[0:1], off
	global_load_dwordx4 v[26:29], v[0:1], off offset:1024
	global_load_dwordx4 v[60:63], v[0:1], off offset:2048
	global_load_dwordx4 v[64:67], v[0:1], off offset:3072
	s_movk_i32 s28, 0x1000
	s_waitcnt vmcnt(4)
	v_add_co_u32_e32 v46, vcc, s28, v0
	s_lshl_b64 s[2:3], s[94:95], 8
	s_nop 0
	v_addc_co_u32_e32 v47, vcc, 0, v1, vcc
	global_load_dwordx4 v[0:3], v[46:47], off
	global_load_dwordx4 v[4:7], v[46:47], off offset:1024
	global_load_dwordx4 v[8:11], v[46:47], off offset:2048
	s_add_u32 s4, s22, s2
	s_addc_u32 s5, s23, s3
	s_lshl_b64 s[2:3], s[94:95], 9
	v_lshlrev_b64 v[16:17], 2, v[92:93]
	s_add_u32 s8, s18, s2
	v_lshl_add_u64 v[20:21], s[4:5], 0, v[16:17]
	s_addc_u32 s9, s19, s3
	v_lshl_add_u64 v[22:23], s[8:9], 0, v[16:17]
	s_mov_b32 s29, 0x42fe0000
	s_mov_b32 s21, 0x40c0c00
	v_lshl_add_u32 v25, v92, 3, s20
	s_add_i32 s4, s34, s94
	s_ashr_i32 s5, s4, 31
	s_lshl_b64 s[8:9], s[4:5], 13
	s_add_u32 s8, s6, s8
	v_lshl_add_u32 v24, v92, 1, s20
	s_addc_u32 s9, s7, s9
	v_ashrrev_i32_e32 v94, 3, v92
	v_lshl_add_u32 v93, v94, 1, s20
	v_and_b32_e32 v164, 7, v92
	v_lshlrev_b32_e32 v95, 1, v164
	v_lshlrev_b32_e32 v165, 4, v164
	v_mov_b32_e32 v109, 0
	s_mov_b32 s43, 0x5040100
	v_lshl_add_u32 v166, v164, 5, s20
	s_mov_b32 s44, 0
	v_mov_b32_e32 v108, 0
	v_mov_b32_e32 v110, 0
	v_mov_b32_e32 v111, v109
	v_mov_b32_e32 v112, 0
	v_mov_b32_e32 v113, v109
	v_mov_b32_e32 v114, 0
	v_mov_b32_e32 v115, v109
	v_mov_b32_e32 v116, 0
	v_mov_b32_e32 v117, v109
	v_mov_b32_e32 v118, 0
	v_mov_b32_e32 v119, v109
	v_mov_b32_e32 v120, 0
	v_mov_b32_e32 v121, v109
	v_mov_b32_e32 v122, 0
	v_mov_b32_e32 v123, v109
	v_mov_b32_e32 v124, 0
	v_mov_b32_e32 v125, v109
	v_mov_b32_e32 v126, 0
	v_mov_b32_e32 v127, v109
	v_mov_b32_e32 v128, 0
	v_mov_b32_e32 v129, v109
	v_mov_b32_e32 v130, 0
	v_mov_b32_e32 v131, v109
	v_mov_b32_e32 v132, 0
	v_mov_b32_e32 v133, v109
	v_mov_b32_e32 v134, 0
	v_mov_b32_e32 v135, v109
	v_mov_b32_e32 v136, 0
	v_mov_b32_e32 v137, v109
	v_mov_b32_e32 v138, 0
	v_mov_b32_e32 v139, v109
	v_mov_b32_e32 v140, 0
	v_mov_b32_e32 v141, v109
	v_mov_b32_e32 v142, 0
	v_mov_b32_e32 v143, v109
	v_mov_b32_e32 v144, 0
	v_mov_b32_e32 v145, v109
	v_mov_b32_e32 v146, 0
	v_mov_b32_e32 v147, v109
	v_mov_b32_e32 v148, 0
	v_mov_b32_e32 v149, v109
	v_mov_b32_e32 v150, 0
	v_mov_b32_e32 v151, v109
	s_waitcnt vmcnt(6)
	v_lshlrev_b32_e32 v58, 16, v12
	v_and_b32_e32 v57, 0xffff0000, v12
	v_lshlrev_b32_e32 v56, 16, v13
	v_and_b32_e32 v55, 0xffff0000, v13
	v_lshlrev_b32_e32 v52, 16, v15
	v_and_b32_e32 v51, 0xffff0000, v15
	v_lshlrev_b32_e32 v54, 16, v14
	v_and_b32_e32 v53, 0xffff0000, v14
	s_waitcnt vmcnt(5)
	v_lshlrev_b32_e32 v48, 16, v26
	v_and_b32_e32 v45, 0xffff0000, v26
	v_lshlrev_b32_e32 v38, 16, v29
	v_and_b32_e32 v37, 0xffff0000, v29
	v_max_f32_e64 v12, |v57|, |v57|
	v_max_f32_e64 v13, |v58|, |v58|
	v_max_f32_e64 v14, |v55|, |v55|
	v_max_f32_e64 v15, |v56|, |v56|
	v_max_f32_e64 v32, |v51|, |v51|
	v_max_f32_e64 v35, |v52|, |v52|
	v_lshlrev_b32_e32 v43, 16, v27
	v_and_b32_e32 v41, 0xffff0000, v27
	v_max_f32_e64 v36, |v45|, |v45|
	v_max_f32_e64 v42, |v48|, |v48|
	v_max_f32_e64 v50, |v37|, |v37|
	v_max_f32_e64 v59, |v38|, |v38|
	v_max_f32_e32 v12, v13, v12
	v_max_f32_e32 v13, v15, v14
	v_max_f32_e32 v14, v35, v32
	v_lshlrev_b32_e32 v40, 16, v28
	v_and_b32_e32 v39, 0xffff0000, v28
	s_waitcnt vmcnt(4)
	v_lshlrev_b32_e32 v34, 16, v60
	v_and_b32_e32 v33, 0xffff0000, v60
	v_lshlrev_b32_e32 v31, 16, v61
	v_and_b32_e32 v30, 0xffff0000, v61
	v_max_f32_e64 v44, |v41|, |v41|
	v_max_f32_e64 v49, |v43|, |v43|
	v_max_f32_e32 v15, v42, v36
	v_max_f32_e32 v35, v59, v50
	v_max3_f32 v12, v12, 0, v13
	v_max3_f32 v13, |v54|, |v53|, v14
	v_lshlrev_b32_e32 v29, 16, v62
	v_and_b32_e32 v28, 0xffff0000, v62
	v_lshlrev_b32_e32 v27, 16, v63
	v_and_b32_e32 v26, 0xffff0000, v63
	v_max_f32_e64 v60, |v33|, |v33|
	v_max_f32_e64 v61, |v34|, |v34|
	v_max_f32_e64 v62, |v30|, |v30|
	v_max_f32_e64 v63, |v31|, |v31|
	v_max_f32_e32 v32, v49, v44
	v_max3_f32 v14, |v40|, |v39|, v35
	v_max3_f32 v12, v12, v13, v15
	v_max_f32_e32 v36, v61, v60
	v_max_f32_e32 v42, v63, v62
	v_max3_f32 v12, v12, v32, v14
	v_max_f32_e64 v68, |v26|, |v26|
	v_max3_f32 v32, v12, v36, v42
	v_max_f32_e64 v12, |v27|, |v27|
	v_max_f32_e32 v12, v12, v68
	v_max3_f32 v42, |v29|, |v28|, v12
	global_load_dwordx4 v[12:15], v[46:47], off offset:3072
	s_waitcnt vmcnt(4)
	v_lshlrev_b32_e32 v36, 16, v64
	v_and_b32_e32 v35, 0xffff0000, v64
	v_max_f32_e64 v44, |v35|, |v35|
	v_max_f32_e64 v46, |v36|, |v36|
	v_max_f32_e32 v44, v46, v44
	v_lshlrev_b32_e32 v50, 16, v65
	v_and_b32_e32 v47, 0xffff0000, v65
	v_max3_f32 v32, v32, v42, v44
	v_max_f32_e64 v42, |v47|, |v47|
	v_max_f32_e64 v44, |v50|, |v50|
	v_max_f32_e32 v59, v44, v42
	v_lshlrev_b32_e32 v44, 16, v67
	v_and_b32_e32 v42, 0xffff0000, v67
	v_max_f32_e64 v60, |v42|, |v42|
	v_max_f32_e64 v61, |v44|, |v44|
	v_lshlrev_b32_e32 v49, 16, v66
	v_and_b32_e32 v46, 0xffff0000, v66
	v_max_f32_e32 v60, v61, v60
	v_max3_f32 v60, |v49|, |v46|, v60
	v_max3_f32 v59, v32, v59, v60
	global_load_dword v32, v[20:21], off
	global_load_dword v60, v[22:23], off
	global_load_dword v61, v[22:23], off offset:256
	s_waitcnt vmcnt(6)
; #define LAS __attribute__((address_space(3)))
; __device__ __forceinline__ float bflo(unsigned w) { return __uint_as_float(w << 16); }
; __device__ __forceinline__ float bfhi(unsigned w) { return __uint_as_float(w & 0xffff0000u); }
; __device__ __forceinline__ float wave_sum(float v) { v = dpp_add16(v); return (rdlane(v, 0) + rdlane(v, 16)) + (rdlane(v, 32) + rdlane(v, 48)); }
; __device__ __forceinline__ float wave_max(float v) { v = dpp_max16(v); return fmaxf(fmaxf(rdlane(v, 0), rdlane(v, 16)), fmaxf(rdlane(v, 32), rdlane(v, 48))); }
; __device__ __forceinline__ void p12_peer(Frame& F) {
;     ...
;         const int t = F.gw + i * F.NGW; v4u xp[8]; float mxa = 0.f;
; #pragma unroll
;         for (int j = 0; j < 8; ++j) { xp[j] = ((const v4u*)(HN + (size_t)t * D_))[F.lane + 64 * j];
;             mxa = fmaxf(fmaxf(fmaxf(mxa, fmaxf(fabsf(bflo(xp[j].x)), fabsf(bfhi(xp[j].x)))), fmaxf(fabsf(bflo(xp[j].y)), fabsf(bfhi(xp[j].y)))), fmaxf(fmaxf(fabsf(bflo(xp[j].z)), fabsf(bfhi(xp[j].z))), fmaxf(fabsf(bflo(xp[j].w)), fabsf(bfhi(xp[j].w))))); }
;         mxa = wave_max(mxa); const float inv = mxa > 0.f ? 127.0f / mxa : 0.f;
;         const float rsn = 1.0f / sqrtf(wave_sum(PSQ[(size_t)t * 64 + F.lane]) * (1.f / D_) + 1e-6f);
;         sx[i] = mxa * rsn * (1.0f / 127.0f);
; #pragma unroll
;         for (int j = 0; j < 8; ++j) {
;             const int q0 = (int)rintf(bflo(xp[j].x) * inv), q1 = (int)rintf(bfhi(xp[j].x) * inv), q2 = (int)rintf(bflo(xp[j].y) * inv), q3 = (int)rintf(bfhi(xp[j].y) * inv);
;             const int q4 = (int)rintf(bflo(xp[j].z) * inv), q5 = (int)rintf(bfhi(xp[j].z) * inv), q6 = (int)rintf(bflo(xp[j].w) * inv), q7 = (int)rintf(bfhi(xp[j].w) * inv);
;             *(LAS v2u*)(XQ + i * 4096 + 8 * (F.lane + 64 * j)) = (v2u){(unsigned)((q0 & 0xff) | ((q1 & 0xff) << 8) | ((q2 & 0xff) << 16) | (q3 << 24)), (unsigned)((q4 & 0xff) | ((q5 & 0xff) << 8) | ((q6 & 0xff) << 16) | (q7 << 24))}; }
	v_lshlrev_b32_e32 v20, 16, v0
	v_and_b32_e32 v21, 0xffff0000, v0
	v_max_f32_e64 v0, |v21|, |v21|
	v_max_f32_e64 v22, |v20|, |v20|
	v_max_f32_e32 v0, v22, v0
	v_lshlrev_b32_e32 v22, 16, v1
	v_and_b32_e32 v23, 0xffff0000, v1
	v_max_f32_e64 v1, |v23|, |v23|
	v_max_f32_e64 v62, |v22|, |v22|
	v_max_f32_e32 v1, v62, v1
	v_lshlrev_b32_e32 v63, 16, v3
	v_and_b32_e32 v64, 0xffff0000, v3
	v_max3_f32 v0, v59, v0, v1
	v_lshlrev_b32_e32 v59, 16, v2
	v_and_b32_e32 v62, 0xffff0000, v2
	v_max_f32_e64 v1, |v64|, |v64|
	v_max_f32_e64 v2, |v63|, |v63|
	s_waitcnt vmcnt(5)
	v_lshlrev_b32_e32 v65, 16, v4
	v_and_b32_e32 v66, 0xffff0000, v4
	v_max_f32_e32 v1, v2, v1
	v_max_f32_e64 v2, |v66|, |v66|
	v_max_f32_e64 v3, |v65|, |v65|
	v_max3_f32 v1, |v59|, |v62|, v1
	v_max_f32_e32 v2, v3, v2
	v_lshlrev_b32_e32 v67, 16, v5
	v_and_b32_e32 v68, 0xffff0000, v5
	v_max3_f32 v0, v0, v1, v2
	v_max_f32_e64 v1, |v68|, |v68|
	v_max_f32_e64 v2, |v67|, |v67|
	v_lshlrev_b32_e32 v70, 16, v7
	v_and_b32_e32 v7, 0xffff0000, v7
	v_max_f32_e32 v1, v2, v1
	v_max_f32_e64 v2, |v7|, |v7|
	v_max_f32_e64 v3, |v70|, |v70|
	v_lshlrev_b32_e32 v69, 16, v6
	v_and_b32_e32 v6, 0xffff0000, v6
	v_max_f32_e32 v2, v3, v2
	v_max3_f32 v2, |v69|, |v6|, v2
	s_waitcnt vmcnt(4)
	v_lshlrev_b32_e32 v71, 16, v8
	v_and_b32_e32 v8, 0xffff0000, v8
	v_max3_f32 v0, v0, v1, v2
	v_max_f32_e64 v1, |v8|, |v8|
	v_max_f32_e64 v2, |v71|, |v71|
	v_lshlrev_b32_e32 v72, 16, v9
	v_and_b32_e32 v9, 0xffff0000, v9
	v_max_f32_e32 v1, v2, v1
	v_max_f32_e64 v2, |v9|, |v9|
	v_max_f32_e64 v3, |v72|, |v72|
	v_max_f32_e32 v2, v3, v2
	v_lshlrev_b32_e32 v74, 16, v11
	v_and_b32_e32 v11, 0xffff0000, v11
	v_max3_f32 v0, v0, v1, v2
	v_max_f32_e64 v1, |v11|, |v11|
	v_max_f32_e64 v2, |v74|, |v74|
	v_lshlrev_b32_e32 v73, 16, v10
	v_and_b32_e32 v10, 0xffff0000, v10
	v_max_f32_e32 v1, v2, v1
	v_max3_f32 v1, |v73|, |v10|, v1
	s_waitcnt vmcnt(3)
	v_lshlrev_b32_e32 v75, 16, v12
	v_and_b32_e32 v12, 0xffff0000, v12
	v_max_f32_e64 v2, |v12|, |v12|
	v_max_f32_e64 v3, |v75|, |v75|
	v_max_f32_e32 v2, v3, v2
	v_lshlrev_b32_e32 v76, 16, v13
	v_and_b32_e32 v13, 0xffff0000, v13
	v_max3_f32 v0, v0, v1, v2
	v_max_f32_e64 v1, |v13|, |v13|
	v_max_f32_e64 v2, |v76|, |v76|
	v_lshlrev_b32_e32 v78, 16, v15
	v_and_b32_e32 v15, 0xffff0000, v15
	v_max_f32_e32 v1, v2, v1
	v_max_f32_e64 v2, |v15|, |v15|
	v_max_f32_e64 v3, |v78|, |v78|
	v_lshlrev_b32_e32 v77, 16, v14
	v_and_b32_e32 v14, 0xffff0000, v14
	v_max_f32_e32 v2, v3, v2
	v_max3_f32 v2, |v77|, |v14|, v2
	v_max3_f32 v0, v0, v1, v2
	v_mov_b32_e32 v1, 0
	s_waitcnt vmcnt(2)
	v_add_f32_dpp v32, v32, v32 quad_perm:[1,0,3,2] row_mask:0xf bank_mask:0xf bound_ctrl:1
	v_mov_b32_e32 v152, 0
	v_mov_b32_dpp v1, v0 quad_perm:[1,0,3,2] row_mask:0xf bank_mask:0xf
	v_max_f32_e32 v1, v1, v1
	v_max_f32_e32 v0, v0, v1
	v_mov_b32_e32 v1, 0
	v_add_f32_dpp v32, v32, v32 quad_perm:[2,3,0,1] row_mask:0xf bank_mask:0xf bound_ctrl:1
	v_mov_b32_e32 v153, v109
	v_mov_b32_dpp v1, v0 quad_perm:[2,3,0,1] row_mask:0xf bank_mask:0xf
	v_max_f32_e32 v1, v1, v1
	v_max_f32_e32 v0, v0, v1
	v_mov_b32_e32 v1, 0
	v_add_f32_dpp v32, v32, v32 row_half_mirror row_mask:0xf bank_mask:0xf bound_ctrl:1
	v_mov_b32_e32 v154, 0
	v_mov_b32_dpp v1, v0 row_half_mirror row_mask:0xf bank_mask:0xf
	v_max_f32_e32 v1, v1, v1
	v_max_f32_e32 v0, v0, v1
	v_mov_b32_e32 v1, 0
	v_add_f32_dpp v32, v32, v32 row_mirror row_mask:0xf bank_mask:0xf bound_ctrl:1
	v_mov_b32_e32 v155, v109
	v_mov_b32_dpp v1, v0 row_mirror row_mask:0xf bank_mask:0xf
	v_max_f32_e32 v1, v1, v1
	v_max_f32_e32 v0, v0, v1
	v_readlane_b32 s39, v32, 0
	v_readlane_b32 s12, v0, 32
	v_readlane_b32 s13, v0, 48
	v_readlane_b32 s10, v0, 0
	v_readlane_b32 s11, v0, 16
	v_max_f32_e64 v0, s13, s13
	v_max_f32_e64 v1, s12, s12
	v_max_f32_e32 v0, v1, v0
	v_mov_b32_e32 v1, s11
	v_max3_f32 v163, s10, v1, v0
	v_div_scale_f32 v2, s[10:11], v163, v163, s29
	v_rcp_f32_e32 v3, v2
	v_lshl_add_u64 v[0:1], s[8:9], 0, v[18:19]
	s_lshl_b64 s[8:9], s[4:5], 8
	s_add_u32 s8, s22, s8
	v_fma_f32 v4, -v2, v3, 1.0
	v_fmac_f32_e32 v3, v4, v3
	v_div_scale_f32 v4, vcc, s29, v163, s29
	v_mul_f32_e32 v5, v4, v3
	v_fma_f32 v79, -v2, v5, v4
	v_fmac_f32_e32 v5, v79, v3
	v_fma_f32 v2, -v2, v5, v4
	v_div_fmas_f32 v2, v2, v3, v5
	v_div_fixup_f32 v2, v2, v163, s29
	v_cmp_lt_f32_e32 vcc, 0, v163
	s_addc_u32 s9, s23, s9
	s_lshl_b64 s[16:17], s[4:5], 9
	v_cndmask_b32_e32 v79, 0, v2, vcc
	v_mul_f32_e32 v3, v79, v57
	v_mul_f32_e32 v2, v79, v58
	v_rndne_f32_e32 v3, v3
	v_mul_f32_e32 v4, v79, v56
	v_mul_f32_e32 v5, v79, v55
	v_rndne_f32_e32 v2, v2
	v_cvt_i32_f32_e32 v3, v3
	v_rndne_f32_e32 v4, v4
	v_rndne_f32_e32 v5, v5
	v_mul_f32_e32 v53, v79, v53
	v_cvt_i32_f32_e32 v2, v2
	v_cvt_i32_f32_sdwa v4, v4 dst_sel:WORD_1 dst_unused:UNUSED_PAD src0_sel:DWORD
	v_cvt_i32_f32_e32 v5, v5
	v_mul_f32_e32 v54, v79, v54
	v_rndne_f32_e32 v53, v53
	v_mul_f32_e32 v52, v79, v52
	v_mul_f32_e32 v51, v79, v51
	v_rndne_f32_e32 v54, v54
	v_cvt_i32_f32_e32 v53, v53
	v_rndne_f32_e32 v52, v52
	v_rndne_f32_e32 v51, v51
	v_cvt_i32_f32_e32 v54, v54
	v_cvt_i32_f32_sdwa v52, v52 dst_sel:WORD_1 dst_unused:UNUSED_PAD src0_sel:DWORD
	v_cvt_i32_f32_e32 v51, v51
	v_lshlrev_b32_e32 v3, 8, v3
	v_and_b32_e32 v3, 0xff00, v3
	v_and_b32_e32 v4, 0xff0000, v4
	v_perm_b32 v2, v5, v2, s21
	v_or3_b32 v2, v2, v3, v4
	v_lshlrev_b32_e32 v3, 8, v53
	v_and_b32_e32 v3, 0xff00, v3
	v_and_b32_e32 v4, 0xff0000, v52
	v_perm_b32 v5, v51, v54, s21
	v_or3_b32 v3, v5, v3, v4
	v_mul_f32_e32 v5, v79, v45
	v_mul_f32_e32 v4, v79, v48
	v_rndne_f32_e32 v5, v5
	v_mul_f32_e32 v43, v79, v43
	v_mul_f32_e32 v41, v79, v41
	v_rndne_f32_e32 v4, v4
	v_cvt_i32_f32_e32 v5, v5
	v_rndne_f32_e32 v43, v43
	v_rndne_f32_e32 v41, v41
; #define LAS __attribute__((address_space(3)))
; __device__ __forceinline__ float bflo(unsigned w) { return __uint_as_float(w << 16); }
; __device__ __forceinline__ float bfhi(unsigned w) { return __uint_as_float(w & 0xffff0000u); }
; __device__ __forceinline__ void p12_peer(Frame& F) {
;     ...
;         for (int j = 0; j < 8; ++j) {
;             const int q0 = (int)rintf(bflo(xp[j].x) * inv), q1 = (int)rintf(bfhi(xp[j].x) * inv), q2 = (int)rintf(bflo(xp[j].y) * inv), q3 = (int)rintf(bfhi(xp[j].y) * inv);
;             const int q4 = (int)rintf(bflo(xp[j].z) * inv), q5 = (int)rintf(bfhi(xp[j].z) * inv), q6 = (int)rintf(bflo(xp[j].w) * inv), q7 = (int)rintf(bfhi(xp[j].w) * inv);
;             *(LAS v2u*)(XQ + i * 4096 + 8 * (F.lane + 64 * j)) = (v2u){(unsigned)((q0 & 0xff) | ((q1 & 0xff) << 8) | ((q2 & 0xff) << 16) | (q3 << 24)), (unsigned)((q4 & 0xff) | ((q5 & 0xff) << 8) | ((q6 & 0xff) << 16) | (q7 << 24))}; }
	v_mul_f32_e32 v39, v79, v39
	v_cvt_i32_f32_e32 v4, v4
	v_cvt_i32_f32_sdwa v43, v43 dst_sel:WORD_1 dst_unused:UNUSED_PAD src0_sel:DWORD
	v_cvt_i32_f32_e32 v41, v41
	v_mul_f32_e32 v40, v79, v40
	v_rndne_f32_e32 v39, v39
	v_mul_f32_e32 v38, v79, v38
	v_mul_f32_e32 v37, v79, v37
	v_rndne_f32_e32 v40, v40
	v_cvt_i32_f32_e32 v39, v39
	v_rndne_f32_e32 v38, v38
	v_rndne_f32_e32 v37, v37
	v_cvt_i32_f32_e32 v40, v40
	v_cvt_i32_f32_sdwa v38, v38 dst_sel:WORD_1 dst_unused:UNUSED_PAD src0_sel:DWORD
	v_cvt_i32_f32_e32 v37, v37
	v_lshlrev_b32_e32 v5, 8, v5
	v_and_b32_e32 v5, 0xff00, v5
	v_and_b32_e32 v43, 0xff0000, v43
	v_perm_b32 v4, v41, v4, s21
	v_or3_b32 v4, v4, v5, v43
	v_lshlrev_b32_e32 v5, 8, v39
	v_and_b32_e32 v5, 0xff00, v5
	v_and_b32_e32 v38, 0xff0000, v38
	v_perm_b32 v37, v37, v40, s21
	v_or3_b32 v5, v37, v5, v38
	ds_write2st64_b64 v25, v[2:3], v[4:5] offset1:1
	v_mul_f32_e32 v3, v79, v33
	v_mul_f32_e32 v2, v79, v34
	v_rndne_f32_e32 v3, v3
	v_mul_f32_e32 v4, v79, v31
	v_mul_f32_e32 v5, v79, v30
	v_rndne_f32_e32 v2, v2
	v_cvt_i32_f32_e32 v3, v3
	v_rndne_f32_e32 v4, v4
	v_rndne_f32_e32 v5, v5
	v_mul_f32_e32 v28, v79, v28
	v_cvt_i32_f32_e32 v2, v2
	v_cvt_i32_f32_sdwa v4, v4 dst_sel:WORD_1 dst_unused:UNUSED_PAD src0_sel:DWORD
	v_cvt_i32_f32_e32 v5, v5
	v_mul_f32_e32 v29, v79, v29
	v_rndne_f32_e32 v28, v28
	v_mul_f32_e32 v27, v79, v27
	v_mul_f32_e32 v26, v79, v26
	v_rndne_f32_e32 v29, v29
	v_cvt_i32_f32_e32 v28, v28
	v_rndne_f32_e32 v27, v27
	v_rndne_f32_e32 v26, v26
	v_cvt_i32_f32_e32 v29, v29
	v_cvt_i32_f32_sdwa v27, v27 dst_sel:WORD_1 dst_unused:UNUSED_PAD src0_sel:DWORD
	v_cvt_i32_f32_e32 v26, v26
	v_lshlrev_b32_e32 v3, 8, v3
	v_and_b32_e32 v3, 0xff00, v3
	v_and_b32_e32 v4, 0xff0000, v4
	v_perm_b32 v2, v5, v2, s21
	v_or3_b32 v2, v2, v3, v4
	v_lshlrev_b32_e32 v3, 8, v28
	v_and_b32_e32 v3, 0xff00, v3
	v_and_b32_e32 v4, 0xff0000, v27
	v_perm_b32 v5, v26, v29, s21
	v_or3_b32 v3, v5, v3, v4
	v_mul_f32_e32 v5, v79, v35
	v_mul_f32_e32 v4, v79, v36
	v_rndne_f32_e32 v5, v5
	v_mul_f32_e32 v26, v79, v50
	v_mul_f32_e32 v27, v79, v47
	v_rndne_f32_e32 v4, v4
	v_cvt_i32_f32_e32 v5, v5
	v_rndne_f32_e32 v26, v26
	v_rndne_f32_e32 v27, v27
	v_mul_f32_e32 v29, v79, v46
	v_cvt_i32_f32_e32 v4, v4
	v_cvt_i32_f32_sdwa v26, v26 dst_sel:WORD_1 dst_unused:UNUSED_PAD src0_sel:DWORD
	v_cvt_i32_f32_e32 v27, v27
	v_mul_f32_e32 v28, v79, v49
	v_rndne_f32_e32 v29, v29
	v_mul_f32_e32 v30, v79, v44
	v_mul_f32_e32 v31, v79, v42
	v_rndne_f32_e32 v28, v28
	v_cvt_i32_f32_e32 v29, v29
	v_rndne_f32_e32 v30, v30
	v_rndne_f32_e32 v31, v31
	v_cvt_i32_f32_e32 v28, v28
	v_cvt_i32_f32_sdwa v30, v30 dst_sel:WORD_1 dst_unused:UNUSED_PAD src0_sel:DWORD
	v_cvt_i32_f32_e32 v31, v31
	v_lshlrev_b32_e32 v5, 8, v5
	v_and_b32_e32 v5, 0xff00, v5
	v_and_b32_e32 v26, 0xff0000, v26
	v_perm_b32 v4, v27, v4, s21
	v_or3_b32 v4, v4, v5, v26
	v_lshlrev_b32_e32 v5, 8, v29
	v_and_b32_e32 v5, 0xff00, v5
	v_and_b32_e32 v26, 0xff0000, v30
	v_perm_b32 v27, v31, v28, s21
	v_or3_b32 v5, v27, v5, v26
	ds_write2st64_b64 v25, v[2:3], v[4:5] offset0:2 offset1:3
	v_mul_f32_e32 v3, v79, v21
	v_mul_f32_e32 v2, v79, v20
	v_rndne_f32_e32 v3, v3
	v_mul_f32_e32 v4, v79, v22
	v_mul_f32_e32 v5, v79, v23
	v_rndne_f32_e32 v2, v2
	v_cvt_i32_f32_e32 v3, v3
	v_rndne_f32_e32 v4, v4
	v_rndne_f32_e32 v5, v5
	v_mul_f32_e32 v21, v79, v62
	v_cvt_i32_f32_e32 v2, v2
	v_cvt_i32_f32_sdwa v4, v4 dst_sel:WORD_1 dst_unused:UNUSED_PAD src0_sel:DWORD
	v_cvt_i32_f32_e32 v5, v5
	v_mul_f32_e32 v20, v79, v59
	v_rndne_f32_e32 v21, v21
	v_mul_f32_e32 v22, v79, v63
	v_mul_f32_e32 v23, v79, v64
	v_rndne_f32_e32 v20, v20
	v_cvt_i32_f32_e32 v21, v21
	v_rndne_f32_e32 v22, v22
	v_rndne_f32_e32 v23, v23
	v_cvt_i32_f32_e32 v20, v20
	v_cvt_i32_f32_sdwa v22, v22 dst_sel:WORD_1 dst_unused:UNUSED_PAD src0_sel:DWORD
	v_cvt_i32_f32_e32 v23, v23
	v_lshlrev_b32_e32 v3, 8, v3
	v_and_b32_e32 v3, 0xff00, v3
	v_and_b32_e32 v4, 0xff0000, v4
	v_perm_b32 v2, v5, v2, s21
	v_or3_b32 v2, v2, v3, v4
	v_lshlrev_b32_e32 v3, 8, v21
	v_and_b32_e32 v3, 0xff00, v3
	v_and_b32_e32 v4, 0xff0000, v22
	v_perm_b32 v5, v23, v20, s21
	v_or3_b32 v3, v5, v3, v4
	v_mul_f32_e32 v5, v79, v66
	v_mul_f32_e32 v4, v79, v65
	v_rndne_f32_e32 v5, v5
	v_mul_f32_e32 v20, v79, v67
	v_mul_f32_e32 v21, v79, v68
	v_rndne_f32_e32 v4, v4
	v_cvt_i32_f32_e32 v5, v5
	v_rndne_f32_e32 v20, v20
	v_rndne_f32_e32 v21, v21
	v_mul_f32_e32 v6, v79, v6
	v_cvt_i32_f32_e32 v4, v4
	v_cvt_i32_f32_sdwa v20, v20 dst_sel:WORD_1 dst_unused:UNUSED_PAD src0_sel:DWORD
	v_cvt_i32_f32_e32 v21, v21
	v_mul_f32_e32 v22, v79, v69
	v_rndne_f32_e32 v6, v6
	v_mul_f32_e32 v23, v79, v70
	v_mul_f32_e32 v7, v79, v7
	v_rndne_f32_e32 v22, v22
	v_cvt_i32_f32_e32 v6, v6
	v_rndne_f32_e32 v23, v23
	v_rndne_f32_e32 v7, v7
	v_cvt_i32_f32_e32 v22, v22
	v_cvt_i32_f32_sdwa v23, v23 dst_sel:WORD_1 dst_unused:UNUSED_PAD src0_sel:DWORD
	v_cvt_i32_f32_e32 v7, v7
	v_lshlrev_b32_e32 v5, 8, v5
	v_and_b32_e32 v5, 0xff00, v5
	v_and_b32_e32 v20, 0xff0000, v20
	v_perm_b32 v4, v21, v4, s21
	v_or3_b32 v4, v4, v5, v20
	v_lshlrev_b32_e32 v5, 8, v6
	v_and_b32_e32 v5, 0xff00, v5
	v_and_b32_e32 v6, 0xff0000, v23
	v_perm_b32 v7, v7, v22, s21
	v_or3_b32 v5, v7, v5, v6
	ds_write2st64_b64 v25, v[2:3], v[4:5] offset0:4 offset1:5
	v_mul_f32_e32 v3, v79, v8
	v_mul_f32_e32 v2, v79, v71
	v_rndne_f32_e32 v3, v3
	v_mul_f32_e32 v4, v79, v72
	v_mul_f32_e32 v5, v79, v9
	v_rndne_f32_e32 v2, v2
	v_cvt_i32_f32_e32 v3, v3
	v_rndne_f32_e32 v4, v4
	v_rndne_f32_e32 v5, v5
	v_mul_f32_e32 v7, v79, v10
	v_cvt_i32_f32_e32 v2, v2
	v_cvt_i32_f32_sdwa v4, v4 dst_sel:WORD_1 dst_unused:UNUSED_PAD src0_sel:DWORD
	v_cvt_i32_f32_e32 v5, v5
	v_mul_f32_e32 v6, v79, v73
	v_rndne_f32_e32 v7, v7
; #define LAS __attribute__((address_space(3)))
; __device__ __forceinline__ float bflo(unsigned w) { return __uint_as_float(w << 16); }
; __device__ __forceinline__ float bfhi(unsigned w) { return __uint_as_float(w & 0xffff0000u); }
; __device__ __forceinline__ float wave_sum(float v) { v = dpp_add16(v); return (rdlane(v, 0) + rdlane(v, 16)) + (rdlane(v, 32) + rdlane(v, 48)); }
; __device__ __forceinline__ float wave_max(float v) { v = dpp_max16(v); return fmaxf(fmaxf(rdlane(v, 0), rdlane(v, 16)), fmaxf(rdlane(v, 32), rdlane(v, 48))); }
; __device__ __forceinline__ void p12_peer(Frame& F) {
;     ...
;         const int t = F.gw + i * F.NGW; v4u xp[8]; float mxa = 0.f;
; #pragma unroll
;         for (int j = 0; j < 8; ++j) { xp[j] = ((const v4u*)(HN + (size_t)t * D_))[F.lane + 64 * j];
;             mxa = fmaxf(fmaxf(fmaxf(mxa, fmaxf(fabsf(bflo(xp[j].x)), fabsf(bfhi(xp[j].x)))), fmaxf(fabsf(bflo(xp[j].y)), fabsf(bfhi(xp[j].y)))), fmaxf(fmaxf(fabsf(bflo(xp[j].z)), fabsf(bfhi(xp[j].z))), fmaxf(fabsf(bflo(xp[j].w)), fabsf(bfhi(xp[j].w))))); }
;         mxa = wave_max(mxa); const float inv = mxa > 0.f ? 127.0f / mxa : 0.f;
;         const float rsn = 1.0f / sqrtf(wave_sum(PSQ[(size_t)t * 64 + F.lane]) * (1.f / D_) + 1e-6f);
;         sx[i] = mxa * rsn * (1.0f / 127.0f);
; #pragma unroll
;         for (int j = 0; j < 8; ++j) {
;             const int q0 = (int)rintf(bflo(xp[j].x) * inv), q1 = (int)rintf(bfhi(xp[j].x) * inv), q2 = (int)rintf(bflo(xp[j].y) * inv), q3 = (int)rintf(bfhi(xp[j].y) * inv);
;             const int q4 = (int)rintf(bflo(xp[j].z) * inv), q5 = (int)rintf(bfhi(xp[j].z) * inv), q6 = (int)rintf(bflo(xp[j].w) * inv), q7 = (int)rintf(bfhi(xp[j].w) * inv);
;             *(LAS v2u*)(XQ + i * 4096 + 8 * (F.lane + 64 * j)) = (v2u){(unsigned)((q0 & 0xff) | ((q1 & 0xff) << 8) | ((q2 & 0xff) << 16) | (q3 << 24)), (unsigned)((q4 & 0xff) | ((q5 & 0xff) << 8) | ((q6 & 0xff) << 16) | (q7 << 24))}; }
;         EL[i * 128 + F.lane] = (unsigned short)PIDX[(size_t)t * 128 + F.lane]; EL[i * 128 + 64 + F.lane] = (unsigned short)PIDX[(size_t)t * 128 + 64 + F.lane];
;         asm volatile("" ::: "memory");
;     }
	v_mul_f32_e32 v8, v79, v74
	v_mul_f32_e32 v9, v79, v11
	v_rndne_f32_e32 v6, v6
	v_cvt_i32_f32_e32 v7, v7
	v_rndne_f32_e32 v8, v8
	v_rndne_f32_e32 v9, v9
	v_cvt_i32_f32_e32 v6, v6
	v_cvt_i32_f32_sdwa v8, v8 dst_sel:WORD_1 dst_unused:UNUSED_PAD src0_sel:DWORD
	v_cvt_i32_f32_e32 v9, v9
	v_lshlrev_b32_e32 v3, 8, v3
	v_and_b32_e32 v3, 0xff00, v3
	v_and_b32_e32 v4, 0xff0000, v4
	v_perm_b32 v2, v5, v2, s21
	v_or3_b32 v2, v2, v3, v4
	v_lshlrev_b32_e32 v3, 8, v7
	v_and_b32_e32 v3, 0xff00, v3
	v_and_b32_e32 v4, 0xff0000, v8
	v_perm_b32 v5, v9, v6, s21
	v_or3_b32 v3, v5, v3, v4
	v_mul_f32_e32 v5, v79, v12
	v_mul_f32_e32 v4, v79, v75
	v_rndne_f32_e32 v5, v5
	v_mul_f32_e32 v6, v79, v76
	v_mul_f32_e32 v7, v79, v13
	v_rndne_f32_e32 v4, v4
	v_cvt_i32_f32_e32 v5, v5
	v_rndne_f32_e32 v6, v6
	v_rndne_f32_e32 v7, v7
	v_mul_f32_e32 v9, v79, v14
	v_cvt_i32_f32_e32 v4, v4
	v_cvt_i32_f32_sdwa v6, v6 dst_sel:WORD_1 dst_unused:UNUSED_PAD src0_sel:DWORD
	v_cvt_i32_f32_e32 v7, v7
	v_mul_f32_e32 v8, v79, v77
	v_rndne_f32_e32 v9, v9
	v_mul_f32_e32 v10, v79, v78
	v_mul_f32_e32 v11, v79, v15
	v_rndne_f32_e32 v8, v8
	v_cvt_i32_f32_e32 v9, v9
	v_rndne_f32_e32 v10, v10
	v_rndne_f32_e32 v11, v11
	v_cvt_i32_f32_e32 v8, v8
	v_cvt_i32_f32_sdwa v10, v10 dst_sel:WORD_1 dst_unused:UNUSED_PAD src0_sel:DWORD
	v_cvt_i32_f32_e32 v11, v11
	v_lshlrev_b32_e32 v5, 8, v5
	v_and_b32_e32 v5, 0xff00, v5
	v_and_b32_e32 v6, 0xff0000, v6
	v_perm_b32 v4, v7, v4, s21
	v_or3_b32 v4, v4, v5, v6
	v_lshlrev_b32_e32 v5, 8, v9
	v_and_b32_e32 v5, 0xff00, v5
	v_and_b32_e32 v6, 0xff0000, v10
	v_perm_b32 v7, v11, v8, s21
	v_or3_b32 v5, v7, v5, v6
	ds_write2st64_b64 v25, v[2:3], v[4:5] offset0:6 offset1:7
	s_waitcnt vmcnt(1)
	ds_write_b16 v24, v60 offset:16384
	s_waitcnt vmcnt(0)
	ds_write_b16 v24, v61 offset:16512
	global_load_dwordx4 v[4:7], v[0:1], off
	global_load_dwordx4 v[8:11], v[0:1], off offset:1024
	global_load_dwordx4 v[12:15], v[0:1], off offset:2048
	global_load_dwordx4 v[60:63], v[0:1], off offset:3072
	v_add_co_u32_e32 v56, vcc, s28, v0
	v_lshl_add_u64 v[20:21], s[8:9], 0, v[16:17]
	s_nop 0
	v_addc_co_u32_e32 v57, vcc, 0, v1, vcc
	s_add_u32 s8, s18, s16
	s_addc_u32 s9, s19, s17
	v_lshl_add_u64 v[22:23], s[8:9], 0, v[16:17]
	s_add_i32 s8, s4, s34
	s_ashr_i32 s9, s8, 31
	s_lshl_b64 s[10:11], s[8:9], 13
	s_add_u32 s10, s6, s10
	s_addc_u32 s11, s7, s11
	v_readlane_b32 s41, v32, 16
	v_readlane_b32 s40, v32, 32
	v_readlane_b32 s42, v32, 48
	v_mov_b32_e32 v156, 0
	v_mov_b32_e32 v157, v109
	v_mov_b32_e32 v158, 0
	v_mov_b32_e32 v159, v109
	v_mov_b32_e32 v106, 0
	v_mov_b32_e32 v107, v109
	v_mov_b32_e32 v104, 0
	v_mov_b32_e32 v105, v109
	v_mov_b32_e32 v102, 0
	v_mov_b32_e32 v103, v109
	v_mov_b32_e32 v100, 0
	v_mov_b32_e32 v101, v109
	v_mov_b32_e32 v98, 0
	v_mov_b32_e32 v99, v109
	v_mov_b32_e32 v96, 0
	v_mov_b32_e32 v97, v109
	s_waitcnt vmcnt(3)
	v_lshlrev_b32_e32 v27, 16, v4
	v_and_b32_e32 v26, 0xffff0000, v4
	v_max_f32_e64 v2, |v26|, |v26|
	v_max_f32_e64 v3, |v27|, |v27|
	v_max_f32_e32 v4, v3, v2
	global_load_dwordx4 v[0:3], v[56:57], off
	v_lshlrev_b32_e32 v41, 16, v5
	v_and_b32_e32 v38, 0xffff0000, v5
	v_max_f32_e64 v5, |v38|, |v38|
	v_max_f32_e64 v28, |v41|, |v41|
	v_max_f32_e32 v5, v28, v5
	v_lshlrev_b32_e32 v36, 16, v7
	v_and_b32_e32 v34, 0xffff0000, v7
	v_max3_f32 v30, v4, 0, v5
	v_max_f32_e64 v4, |v34|, |v34|
	v_max_f32_e64 v5, |v36|, |v36|
	v_lshlrev_b32_e32 v42, 16, v6
	v_and_b32_e32 v39, 0xffff0000, v6
	v_max_f32_e32 v4, v5, v4
	v_max3_f32 v31, |v42|, |v39|, v4
	s_waitcnt vmcnt(3)
	v_lshlrev_b32_e32 v29, 16, v8
	v_and_b32_e32 v28, 0xffff0000, v8
	global_load_dwordx4 v[4:7], v[56:57], off offset:1024
	v_max_f32_e64 v8, |v28|, |v28|
	v_max_f32_e64 v33, |v29|, |v29|
	v_max_f32_e32 v8, v33, v8
	v_lshlrev_b32_e32 v48, 16, v9
	v_and_b32_e32 v45, 0xffff0000, v9
	v_lshlrev_b32_e32 v43, 16, v11
	v_and_b32_e32 v40, 0xffff0000, v11
	v_max3_f32 v8, v30, v31, v8
	v_max_f32_e64 v9, |v45|, |v45|
	v_max_f32_e64 v30, |v48|, |v48|
	v_lshlrev_b32_e32 v46, 16, v10
	v_and_b32_e32 v44, 0xffff0000, v10
	v_max_f32_e64 v10, |v40|, |v40|
	v_max_f32_e64 v11, |v43|, |v43|
	v_max_f32_e32 v9, v30, v9
	v_max_f32_e32 v10, v11, v10
	s_waitcnt vmcnt(3)
	v_lshlrev_b32_e32 v31, 16, v12
	v_and_b32_e32 v30, 0xffff0000, v12
	v_max3_f32 v10, |v46|, |v44|, v10
	v_max_f32_e64 v12, |v30|, |v30|
	v_max_f32_e64 v35, |v31|, |v31|
	v_lshlrev_b32_e32 v53, 16, v13
	v_and_b32_e32 v50, 0xffff0000, v13
	v_max3_f32 v33, v8, v9, v10
	global_load_dwordx4 v[8:11], v[56:57], off offset:2048
	v_max_f32_e32 v12, v35, v12
	v_max_f32_e64 v13, |v50|, |v50|
	v_max_f32_e64 v35, |v53|, |v53|
	v_max_f32_e32 v13, v35, v13
	v_lshlrev_b32_e32 v49, 16, v15
	v_and_b32_e32 v47, 0xffff0000, v15
	v_max3_f32 v33, v33, v12, v13
	v_max_f32_e64 v12, |v47|, |v47|
	v_max_f32_e64 v13, |v49|, |v49|
	v_lshlrev_b32_e32 v54, 16, v14
	v_and_b32_e32 v51, 0xffff0000, v14
	v_max_f32_e32 v12, v13, v12
	v_max3_f32 v52, |v54|, |v51|, v12
	global_load_dwordx4 v[12:15], v[56:57], off offset:3072
	s_waitcnt vmcnt(4)
	v_lshlrev_b32_e32 v37, 16, v60
	v_and_b32_e32 v35, 0xffff0000, v60
	v_max_f32_e64 v55, |v35|, |v35|
	v_max_f32_e64 v56, |v37|, |v37|
	v_max_f32_e32 v55, v56, v55
	v_lshlrev_b32_e32 v59, 16, v61
	v_and_b32_e32 v57, 0xffff0000, v61
	v_max3_f32 v33, v33, v52, v55
	v_max_f32_e64 v52, |v57|, |v57|
	v_max_f32_e64 v55, |v59|, |v59|
	v_max_f32_e32 v60, v55, v52
	v_lshlrev_b32_e32 v55, 16, v63
	v_and_b32_e32 v52, 0xffff0000, v63
	v_lshlrev_b32_e32 v58, 16, v62
	v_and_b32_e32 v56, 0xffff0000, v62
	v_max_f32_e64 v61, |v52|, |v52|
	v_max_f32_e64 v62, |v55|, |v55|
	v_max_f32_e32 v61, v62, v61
	v_max3_f32 v61, |v58|, |v56|, v61
	v_max3_f32 v60, v33, v60, v61
	global_load_dword v33, v[20:21], off
	global_load_dword v61, v[22:23], off
	global_load_dword v62, v[22:23], off offset:256
	s_waitcnt vmcnt(6)
; #define LAS __attribute__((address_space(3)))
; __device__ __forceinline__ float bflo(unsigned w) { return __uint_as_float(w << 16); }
; __device__ __forceinline__ float bfhi(unsigned w) { return __uint_as_float(w & 0xffff0000u); }
; __device__ __forceinline__ float wave_sum(float v) { v = dpp_add16(v); return (rdlane(v, 0) + rdlane(v, 16)) + (rdlane(v, 32) + rdlane(v, 48)); }
; __device__ __forceinline__ float wave_max(float v) { v = dpp_max16(v); return fmaxf(fmaxf(rdlane(v, 0), rdlane(v, 16)), fmaxf(rdlane(v, 32), rdlane(v, 48))); }
; __device__ __forceinline__ void p12_peer(Frame& F) {
;     ...
;         const int t = F.gw + i * F.NGW; v4u xp[8]; float mxa = 0.f;
; #pragma unroll
;         for (int j = 0; j < 8; ++j) { xp[j] = ((const v4u*)(HN + (size_t)t * D_))[F.lane + 64 * j];
;             mxa = fmaxf(fmaxf(fmaxf(mxa, fmaxf(fabsf(bflo(xp[j].x)), fabsf(bfhi(xp[j].x)))), fmaxf(fabsf(bflo(xp[j].y)), fabsf(bfhi(xp[j].y)))), fmaxf(fmaxf(fabsf(bflo(xp[j].z)), fabsf(bfhi(xp[j].z))), fmaxf(fabsf(bflo(xp[j].w)), fabsf(bfhi(xp[j].w))))); }
;         mxa = wave_max(mxa); const float inv = mxa > 0.f ? 127.0f / mxa : 0.f;
;         const float rsn = 1.0f / sqrtf(wave_sum(PSQ[(size_t)t * 64 + F.lane]) * (1.f / D_) + 1e-6f);
;         sx[i] = mxa * rsn * (1.0f / 127.0f);
; #pragma unroll
;         for (int j = 0; j < 8; ++j) {
;             const int q0 = (int)rintf(bflo(xp[j].x) * inv), q1 = (int)rintf(bfhi(xp[j].x) * inv), q2 = (int)rintf(bflo(xp[j].y) * inv), q3 = (int)rintf(bfhi(xp[j].y) * inv);
;             const int q4 = (int)rintf(bflo(xp[j].z) * inv), q5 = (int)rintf(bfhi(xp[j].z) * inv), q6 = (int)rintf(bflo(xp[j].w) * inv), q7 = (int)rintf(bfhi(xp[j].w) * inv);
;             *(LAS v2u*)(XQ + i * 4096 + 8 * (F.lane + 64 * j)) = (v2u){(unsigned)((q0 & 0xff) | ((q1 & 0xff) << 8) | ((q2 & 0xff) << 16) | (q3 << 24)), (unsigned)((q4 & 0xff) | ((q5 & 0xff) << 8) | ((q6 & 0xff) << 16) | (q7 << 24))}; }
	v_lshlrev_b32_e32 v20, 16, v0
	v_and_b32_e32 v21, 0xffff0000, v0
	v_max_f32_e64 v0, |v21|, |v21|
	v_max_f32_e64 v22, |v20|, |v20|
	v_max_f32_e32 v0, v22, v0
	v_lshlrev_b32_e32 v22, 16, v1
	v_and_b32_e32 v23, 0xffff0000, v1
	v_max_f32_e64 v1, |v23|, |v23|
	v_max_f32_e64 v63, |v22|, |v22|
	v_max_f32_e32 v1, v63, v1
	v_lshlrev_b32_e32 v64, 16, v3
	v_and_b32_e32 v65, 0xffff0000, v3
	v_max3_f32 v0, v60, v0, v1
	v_lshlrev_b32_e32 v60, 16, v2
	v_and_b32_e32 v63, 0xffff0000, v2
	v_max_f32_e64 v1, |v65|, |v65|
	v_max_f32_e64 v2, |v64|, |v64|
	s_waitcnt vmcnt(5)
	v_lshlrev_b32_e32 v66, 16, v4
	v_and_b32_e32 v67, 0xffff0000, v4
	v_max_f32_e32 v1, v2, v1
	v_max_f32_e64 v2, |v67|, |v67|
	v_max_f32_e64 v3, |v66|, |v66|
	v_max3_f32 v1, |v60|, |v63|, v1
	v_max_f32_e32 v2, v3, v2
	v_lshlrev_b32_e32 v68, 16, v5
	v_and_b32_e32 v69, 0xffff0000, v5
	v_max3_f32 v0, v0, v1, v2
	v_max_f32_e64 v1, |v69|, |v69|
	v_max_f32_e64 v2, |v68|, |v68|
	v_lshlrev_b32_e32 v71, 16, v7
	v_and_b32_e32 v7, 0xffff0000, v7
	v_max_f32_e32 v1, v2, v1
	v_max_f32_e64 v2, |v7|, |v7|
	v_max_f32_e64 v3, |v71|, |v71|
	v_lshlrev_b32_e32 v70, 16, v6
	v_and_b32_e32 v6, 0xffff0000, v6
	v_max_f32_e32 v2, v3, v2
	v_max3_f32 v2, |v70|, |v6|, v2
	v_max3_f32 v0, v0, v1, v2
	s_waitcnt vmcnt(4)
	v_lshlrev_b32_e32 v72, 16, v8
	v_and_b32_e32 v8, 0xffff0000, v8
	v_max_f32_e64 v1, |v8|, |v8|
	v_max_f32_e64 v2, |v72|, |v72|
	v_lshlrev_b32_e32 v73, 16, v9
	v_and_b32_e32 v9, 0xffff0000, v9
	v_max_f32_e32 v1, v2, v1
	v_max_f32_e64 v2, |v9|, |v9|
	v_max_f32_e64 v3, |v73|, |v73|
	v_max_f32_e32 v2, v3, v2
	v_lshlrev_b32_e32 v75, 16, v11
	v_and_b32_e32 v11, 0xffff0000, v11
	v_max3_f32 v0, v0, v1, v2
	v_max_f32_e64 v1, |v11|, |v11|
	v_max_f32_e64 v2, |v75|, |v75|
	s_waitcnt vmcnt(3)
	v_lshlrev_b32_e32 v76, 16, v12
	v_and_b32_e32 v12, 0xffff0000, v12
	v_lshlrev_b32_e32 v74, 16, v10
	v_and_b32_e32 v10, 0xffff0000, v10
	v_max_f32_e32 v1, v2, v1
	v_max_f32_e64 v2, |v12|, |v12|
	v_max_f32_e64 v3, |v76|, |v76|
	v_max3_f32 v1, |v74|, |v10|, v1
	v_max_f32_e32 v2, v3, v2
	v_lshlrev_b32_e32 v77, 16, v13
	v_and_b32_e32 v13, 0xffff0000, v13
	v_max3_f32 v0, v0, v1, v2
	v_max_f32_e64 v1, |v13|, |v13|
	v_max_f32_e64 v2, |v77|, |v77|
	v_lshlrev_b32_e32 v79, 16, v15
	v_and_b32_e32 v15, 0xffff0000, v15
	v_max_f32_e32 v1, v2, v1
	v_max_f32_e64 v2, |v15|, |v15|
	v_max_f32_e64 v3, |v79|, |v79|
	v_lshlrev_b32_e32 v78, 16, v14
	v_and_b32_e32 v14, 0xffff0000, v14
	v_max_f32_e32 v2, v3, v2
	v_max3_f32 v2, |v78|, |v14|, v2
	v_max3_f32 v0, v0, v1, v2
	v_mov_b32_e32 v1, 0
	s_waitcnt vmcnt(2)
	v_add_f32_dpp v32, v33, v33 quad_perm:[1,0,3,2] row_mask:0xf bank_mask:0xf bound_ctrl:1
	v_mov_b32_dpp v1, v0 quad_perm:[1,0,3,2] row_mask:0xf bank_mask:0xf
	v_max_f32_e32 v1, v1, v1
	v_max_f32_e32 v0, v0, v1
	v_mov_b32_e32 v1, 0
	v_add_f32_dpp v32, v32, v32 quad_perm:[2,3,0,1] row_mask:0xf bank_mask:0xf bound_ctrl:1
	s_nop 0
	v_mov_b32_dpp v1, v0 quad_perm:[2,3,0,1] row_mask:0xf bank_mask:0xf
	v_max_f32_e32 v1, v1, v1
	v_max_f32_e32 v0, v0, v1
	v_mov_b32_e32 v1, 0
	v_add_f32_dpp v32, v32, v32 row_half_mirror row_mask:0xf bank_mask:0xf bound_ctrl:1
	s_nop 0
	v_mov_b32_dpp v1, v0 row_half_mirror row_mask:0xf bank_mask:0xf
	v_max_f32_e32 v1, v1, v1
	v_max_f32_e32 v0, v0, v1
	v_mov_b32_e32 v1, 0
	v_add_f32_dpp v32, v32, v32 row_mirror row_mask:0xf bank_mask:0xf bound_ctrl:1
	s_nop 0
	v_mov_b32_dpp v1, v0 row_mirror row_mask:0xf bank_mask:0xf
	v_max_f32_e32 v1, v1, v1
	v_max_f32_e32 v0, v0, v1
	v_readlane_b32 s37, v32, 16
	v_readlane_b32 s14, v0, 32
	v_readlane_b32 s15, v0, 48
	v_readlane_b32 s12, v0, 0
	v_readlane_b32 s13, v0, 16
	v_max_f32_e64 v0, s15, s15
	v_max_f32_e64 v1, s14, s14
	v_max_f32_e32 v0, v1, v0
	v_mov_b32_e32 v1, s13
	v_max3_f32 v162, s12, v1, v0
	v_div_scale_f32 v2, s[12:13], v162, v162, s29
	v_rcp_f32_e32 v3, v2
	v_lshl_add_u64 v[0:1], s[10:11], 0, v[18:19]
	s_lshl_b64 s[10:11], s[8:9], 8
	s_add_u32 s10, s22, s10
	v_fma_f32 v4, -v2, v3, 1.0
	v_fmac_f32_e32 v3, v4, v3
	v_div_scale_f32 v4, vcc, s29, v162, s29
	v_mul_f32_e32 v5, v4, v3
	v_fma_f32 v80, -v2, v5, v4
	v_fmac_f32_e32 v5, v80, v3
	v_fma_f32 v2, -v2, v5, v4
	v_div_fmas_f32 v2, v2, v3, v5
	v_div_fixup_f32 v2, v2, v162, s29
	v_cmp_lt_f32_e32 vcc, 0, v162
	s_addc_u32 s11, s23, s11
	s_lshl_b64 s[14:15], s[8:9], 9
	v_cndmask_b32_e32 v80, 0, v2, vcc
	v_mul_f32_e32 v3, v80, v26
	v_mul_f32_e32 v2, v80, v27
	v_rndne_f32_e32 v3, v3
	v_mul_f32_e32 v4, v80, v41
	v_mul_f32_e32 v5, v80, v38
	v_rndne_f32_e32 v2, v2
	v_cvt_i32_f32_e32 v3, v3
	v_rndne_f32_e32 v4, v4
	v_rndne_f32_e32 v5, v5
	v_mul_f32_e32 v27, v80, v39
	v_cvt_i32_f32_e32 v2, v2
	v_cvt_i32_f32_sdwa v4, v4 dst_sel:WORD_1 dst_unused:UNUSED_PAD src0_sel:DWORD
	v_cvt_i32_f32_e32 v5, v5
	v_mul_f32_e32 v26, v80, v42
	v_rndne_f32_e32 v27, v27
	v_mul_f32_e32 v36, v80, v36
	v_mul_f32_e32 v34, v80, v34
	v_rndne_f32_e32 v26, v26
	v_cvt_i32_f32_e32 v27, v27
	v_rndne_f32_e32 v36, v36
	v_rndne_f32_e32 v34, v34
	v_cvt_i32_f32_e32 v26, v26
	v_cvt_i32_f32_sdwa v36, v36 dst_sel:WORD_1 dst_unused:UNUSED_PAD src0_sel:DWORD
	v_cvt_i32_f32_e32 v34, v34
	v_lshlrev_b32_e32 v3, 8, v3
	v_and_b32_e32 v3, 0xff00, v3
	v_and_b32_e32 v4, 0xff0000, v4
	v_perm_b32 v2, v5, v2, s21
	v_or3_b32 v2, v2, v3, v4
	v_lshlrev_b32_e32 v3, 8, v27
	v_and_b32_e32 v3, 0xff00, v3
	v_and_b32_e32 v4, 0xff0000, v36
	v_perm_b32 v5, v34, v26, s21
	v_or3_b32 v3, v5, v3, v4
	v_mul_f32_e32 v5, v80, v28
	v_mul_f32_e32 v4, v80, v29
	v_rndne_f32_e32 v5, v5
	v_mul_f32_e32 v26, v80, v48
	v_mul_f32_e32 v27, v80, v45
	v_rndne_f32_e32 v4, v4
	v_cvt_i32_f32_e32 v5, v5
	v_rndne_f32_e32 v26, v26
	v_rndne_f32_e32 v27, v27
	v_mul_f32_e32 v29, v80, v44
	v_cvt_i32_f32_e32 v4, v4
; #define LAS __attribute__((address_space(3)))
; __device__ __forceinline__ float bflo(unsigned w) { return __uint_as_float(w << 16); }
; __device__ __forceinline__ float bfhi(unsigned w) { return __uint_as_float(w & 0xffff0000u); }
; __device__ __forceinline__ void p12_peer(Frame& F) {
;     ...
;         for (int j = 0; j < 8; ++j) {
;             const int q0 = (int)rintf(bflo(xp[j].x) * inv), q1 = (int)rintf(bfhi(xp[j].x) * inv), q2 = (int)rintf(bflo(xp[j].y) * inv), q3 = (int)rintf(bfhi(xp[j].y) * inv);
;             const int q4 = (int)rintf(bflo(xp[j].z) * inv), q5 = (int)rintf(bfhi(xp[j].z) * inv), q6 = (int)rintf(bflo(xp[j].w) * inv), q7 = (int)rintf(bfhi(xp[j].w) * inv);
;             *(LAS v2u*)(XQ + i * 4096 + 8 * (F.lane + 64 * j)) = (v2u){(unsigned)((q0 & 0xff) | ((q1 & 0xff) << 8) | ((q2 & 0xff) << 16) | (q3 << 24)), (unsigned)((q4 & 0xff) | ((q5 & 0xff) << 8) | ((q6 & 0xff) << 16) | (q7 << 24))}; }
	v_cvt_i32_f32_sdwa v26, v26 dst_sel:WORD_1 dst_unused:UNUSED_PAD src0_sel:DWORD
	v_cvt_i32_f32_e32 v27, v27
	v_mul_f32_e32 v28, v80, v46
	v_rndne_f32_e32 v29, v29
	v_mul_f32_e32 v34, v80, v43
	v_mul_f32_e32 v36, v80, v40
	v_rndne_f32_e32 v28, v28
	v_cvt_i32_f32_e32 v29, v29
	v_rndne_f32_e32 v34, v34
	v_rndne_f32_e32 v36, v36
	v_cvt_i32_f32_e32 v28, v28
	v_cvt_i32_f32_sdwa v34, v34 dst_sel:WORD_1 dst_unused:UNUSED_PAD src0_sel:DWORD
	v_cvt_i32_f32_e32 v36, v36
	v_lshlrev_b32_e32 v5, 8, v5
	v_and_b32_e32 v5, 0xff00, v5
	v_and_b32_e32 v26, 0xff0000, v26
	v_perm_b32 v4, v27, v4, s21
	v_or3_b32 v4, v4, v5, v26
	v_lshlrev_b32_e32 v5, 8, v29
	v_and_b32_e32 v5, 0xff00, v5
	v_and_b32_e32 v26, 0xff0000, v34
	v_perm_b32 v27, v36, v28, s21
	v_or3_b32 v5, v27, v5, v26
	ds_write2st64_b64 v25, v[2:3], v[4:5] offset0:8 offset1:9
	v_mul_f32_e32 v3, v80, v30
	v_mul_f32_e32 v2, v80, v31
	v_rndne_f32_e32 v3, v3
	v_mul_f32_e32 v4, v80, v53
	v_mul_f32_e32 v5, v80, v50
	v_rndne_f32_e32 v2, v2
	v_cvt_i32_f32_e32 v3, v3
	v_rndne_f32_e32 v4, v4
	v_rndne_f32_e32 v5, v5
	v_mul_f32_e32 v27, v80, v51
	v_cvt_i32_f32_e32 v2, v2
	v_cvt_i32_f32_sdwa v4, v4 dst_sel:WORD_1 dst_unused:UNUSED_PAD src0_sel:DWORD
	v_cvt_i32_f32_e32 v5, v5
	v_mul_f32_e32 v26, v80, v54
	v_rndne_f32_e32 v27, v27
	v_mul_f32_e32 v28, v80, v49
	v_mul_f32_e32 v29, v80, v47
	v_rndne_f32_e32 v26, v26
	v_cvt_i32_f32_e32 v27, v27
	v_rndne_f32_e32 v28, v28
	v_rndne_f32_e32 v29, v29
	v_cvt_i32_f32_e32 v26, v26
	v_cvt_i32_f32_sdwa v28, v28 dst_sel:WORD_1 dst_unused:UNUSED_PAD src0_sel:DWORD
	v_cvt_i32_f32_e32 v29, v29
	v_lshlrev_b32_e32 v3, 8, v3
	v_and_b32_e32 v3, 0xff00, v3
	v_and_b32_e32 v4, 0xff0000, v4
	v_perm_b32 v2, v5, v2, s21
	v_or3_b32 v2, v2, v3, v4
	v_lshlrev_b32_e32 v3, 8, v27
	v_and_b32_e32 v3, 0xff00, v3
	v_and_b32_e32 v4, 0xff0000, v28
	v_perm_b32 v5, v29, v26, s21
	v_or3_b32 v3, v5, v3, v4
	v_mul_f32_e32 v5, v80, v35
	v_mul_f32_e32 v4, v80, v37
	v_rndne_f32_e32 v5, v5
	v_mul_f32_e32 v26, v80, v59
	v_mul_f32_e32 v27, v80, v57
	v_rndne_f32_e32 v4, v4
	v_cvt_i32_f32_e32 v5, v5
	v_rndne_f32_e32 v26, v26
	v_rndne_f32_e32 v27, v27
	v_mul_f32_e32 v29, v80, v56
	v_cvt_i32_f32_e32 v4, v4
	v_cvt_i32_f32_sdwa v26, v26 dst_sel:WORD_1 dst_unused:UNUSED_PAD src0_sel:DWORD
	v_cvt_i32_f32_e32 v27, v27
	v_mul_f32_e32 v28, v80, v58
	v_rndne_f32_e32 v29, v29
	v_mul_f32_e32 v30, v80, v55
	v_mul_f32_e32 v31, v80, v52
	v_rndne_f32_e32 v28, v28
	v_cvt_i32_f32_e32 v29, v29
	v_rndne_f32_e32 v30, v30
	v_rndne_f32_e32 v31, v31
	v_cvt_i32_f32_e32 v28, v28
	v_cvt_i32_f32_sdwa v30, v30 dst_sel:WORD_1 dst_unused:UNUSED_PAD src0_sel:DWORD
	v_cvt_i32_f32_e32 v31, v31
	v_lshlrev_b32_e32 v5, 8, v5
	v_and_b32_e32 v5, 0xff00, v5
	v_and_b32_e32 v26, 0xff0000, v26
	v_perm_b32 v4, v27, v4, s21
	v_or3_b32 v4, v4, v5, v26
	v_lshlrev_b32_e32 v5, 8, v29
	v_and_b32_e32 v5, 0xff00, v5
	v_and_b32_e32 v26, 0xff0000, v30
	v_perm_b32 v27, v31, v28, s21
	v_or3_b32 v5, v27, v5, v26
	ds_write2st64_b64 v25, v[2:3], v[4:5] offset0:10 offset1:11
	v_mul_f32_e32 v3, v80, v21
	v_mul_f32_e32 v2, v80, v20
	v_rndne_f32_e32 v3, v3
	v_mul_f32_e32 v4, v80, v22
	v_mul_f32_e32 v5, v80, v23
	v_rndne_f32_e32 v2, v2
	v_cvt_i32_f32_e32 v3, v3
	v_rndne_f32_e32 v4, v4
	v_rndne_f32_e32 v5, v5
	v_mul_f32_e32 v21, v80, v63
	v_cvt_i32_f32_e32 v2, v2
	v_cvt_i32_f32_sdwa v4, v4 dst_sel:WORD_1 dst_unused:UNUSED_PAD src0_sel:DWORD
	v_cvt_i32_f32_e32 v5, v5
	v_mul_f32_e32 v20, v80, v60
	v_rndne_f32_e32 v21, v21
	v_mul_f32_e32 v22, v80, v64
	v_mul_f32_e32 v23, v80, v65
	v_rndne_f32_e32 v20, v20
	v_cvt_i32_f32_e32 v21, v21
	v_rndne_f32_e32 v22, v22
	v_rndne_f32_e32 v23, v23
	v_cvt_i32_f32_e32 v20, v20
	v_cvt_i32_f32_sdwa v22, v22 dst_sel:WORD_1 dst_unused:UNUSED_PAD src0_sel:DWORD
	v_cvt_i32_f32_e32 v23, v23
	v_lshlrev_b32_e32 v3, 8, v3
	v_and_b32_e32 v3, 0xff00, v3
	v_and_b32_e32 v4, 0xff0000, v4
	v_perm_b32 v2, v5, v2, s21
	v_or3_b32 v2, v2, v3, v4
	v_lshlrev_b32_e32 v3, 8, v21
	v_and_b32_e32 v3, 0xff00, v3
	v_and_b32_e32 v4, 0xff0000, v22
	v_perm_b32 v5, v23, v20, s21
	v_or3_b32 v3, v5, v3, v4
	v_mul_f32_e32 v5, v80, v67
	v_mul_f32_e32 v4, v80, v66
	v_rndne_f32_e32 v5, v5
	v_mul_f32_e32 v20, v80, v68
	v_mul_f32_e32 v21, v80, v69
	v_rndne_f32_e32 v4, v4
	v_cvt_i32_f32_e32 v5, v5
	v_rndne_f32_e32 v20, v20
	v_rndne_f32_e32 v21, v21
	v_mul_f32_e32 v6, v80, v6
	v_cvt_i32_f32_e32 v4, v4
	v_cvt_i32_f32_sdwa v20, v20 dst_sel:WORD_1 dst_unused:UNUSED_PAD src0_sel:DWORD
	v_cvt_i32_f32_e32 v21, v21
	v_mul_f32_e32 v22, v80, v70
	v_rndne_f32_e32 v6, v6
	v_mul_f32_e32 v23, v80, v71
	v_mul_f32_e32 v7, v80, v7
	v_rndne_f32_e32 v22, v22
	v_cvt_i32_f32_e32 v6, v6
	v_rndne_f32_e32 v23, v23
	v_rndne_f32_e32 v7, v7
	v_cvt_i32_f32_e32 v22, v22
	v_cvt_i32_f32_sdwa v23, v23 dst_sel:WORD_1 dst_unused:UNUSED_PAD src0_sel:DWORD
	v_cvt_i32_f32_e32 v7, v7
	v_lshlrev_b32_e32 v5, 8, v5
	v_and_b32_e32 v5, 0xff00, v5
	v_and_b32_e32 v20, 0xff0000, v20
	v_perm_b32 v4, v21, v4, s21
	v_or3_b32 v4, v4, v5, v20
	v_lshlrev_b32_e32 v5, 8, v6
	v_and_b32_e32 v5, 0xff00, v5
	v_and_b32_e32 v6, 0xff0000, v23
	v_perm_b32 v7, v7, v22, s21
	v_or3_b32 v5, v7, v5, v6
	ds_write2st64_b64 v25, v[2:3], v[4:5] offset0:12 offset1:13
	v_mul_f32_e32 v3, v80, v8
	v_mul_f32_e32 v2, v80, v72
	v_rndne_f32_e32 v3, v3
	v_mul_f32_e32 v4, v80, v73
	v_mul_f32_e32 v5, v80, v9
	v_rndne_f32_e32 v2, v2
	v_cvt_i32_f32_e32 v3, v3
	v_rndne_f32_e32 v4, v4
	v_rndne_f32_e32 v5, v5
	v_mul_f32_e32 v7, v80, v10
	v_cvt_i32_f32_e32 v2, v2
	v_cvt_i32_f32_sdwa v4, v4 dst_sel:WORD_1 dst_unused:UNUSED_PAD src0_sel:DWORD
	v_cvt_i32_f32_e32 v5, v5
	v_mul_f32_e32 v6, v80, v74
	v_rndne_f32_e32 v7, v7
	v_mul_f32_e32 v8, v80, v75
	v_mul_f32_e32 v9, v80, v11
; #define LAS __attribute__((address_space(3)))
; __device__ __forceinline__ float bflo(unsigned w) { return __uint_as_float(w << 16); }
; __device__ __forceinline__ float bfhi(unsigned w) { return __uint_as_float(w & 0xffff0000u); }
; __device__ __forceinline__ float wave_sum(float v) { v = dpp_add16(v); return (rdlane(v, 0) + rdlane(v, 16)) + (rdlane(v, 32) + rdlane(v, 48)); }
; __device__ __forceinline__ float wave_max(float v) { v = dpp_max16(v); return fmaxf(fmaxf(rdlane(v, 0), rdlane(v, 16)), fmaxf(rdlane(v, 32), rdlane(v, 48))); }
; __device__ __forceinline__ void p12_peer(Frame& F) {
;     ...
;         const int t = F.gw + i * F.NGW; v4u xp[8]; float mxa = 0.f;
; #pragma unroll
;         for (int j = 0; j < 8; ++j) { xp[j] = ((const v4u*)(HN + (size_t)t * D_))[F.lane + 64 * j];
;             mxa = fmaxf(fmaxf(fmaxf(mxa, fmaxf(fabsf(bflo(xp[j].x)), fabsf(bfhi(xp[j].x)))), fmaxf(fabsf(bflo(xp[j].y)), fabsf(bfhi(xp[j].y)))), fmaxf(fmaxf(fabsf(bflo(xp[j].z)), fabsf(bfhi(xp[j].z))), fmaxf(fabsf(bflo(xp[j].w)), fabsf(bfhi(xp[j].w))))); }
;         mxa = wave_max(mxa); const float inv = mxa > 0.f ? 127.0f / mxa : 0.f;
;         const float rsn = 1.0f / sqrtf(wave_sum(PSQ[(size_t)t * 64 + F.lane]) * (1.f / D_) + 1e-6f);
;         sx[i] = mxa * rsn * (1.0f / 127.0f);
; #pragma unroll
;         for (int j = 0; j < 8; ++j) {
;             const int q0 = (int)rintf(bflo(xp[j].x) * inv), q1 = (int)rintf(bfhi(xp[j].x) * inv), q2 = (int)rintf(bflo(xp[j].y) * inv), q3 = (int)rintf(bfhi(xp[j].y) * inv);
;             const int q4 = (int)rintf(bflo(xp[j].z) * inv), q5 = (int)rintf(bfhi(xp[j].z) * inv), q6 = (int)rintf(bflo(xp[j].w) * inv), q7 = (int)rintf(bfhi(xp[j].w) * inv);
;             *(LAS v2u*)(XQ + i * 4096 + 8 * (F.lane + 64 * j)) = (v2u){(unsigned)((q0 & 0xff) | ((q1 & 0xff) << 8) | ((q2 & 0xff) << 16) | (q3 << 24)), (unsigned)((q4 & 0xff) | ((q5 & 0xff) << 8) | ((q6 & 0xff) << 16) | (q7 << 24))}; }
;         EL[i * 128 + F.lane] = (unsigned short)PIDX[(size_t)t * 128 + F.lane]; EL[i * 128 + 64 + F.lane] = (unsigned short)PIDX[(size_t)t * 128 + 64 + F.lane];
;         asm volatile("" ::: "memory");
;     }
	v_rndne_f32_e32 v6, v6
	v_cvt_i32_f32_e32 v7, v7
	v_rndne_f32_e32 v8, v8
	v_rndne_f32_e32 v9, v9
	v_cvt_i32_f32_e32 v6, v6
	v_cvt_i32_f32_sdwa v8, v8 dst_sel:WORD_1 dst_unused:UNUSED_PAD src0_sel:DWORD
	v_cvt_i32_f32_e32 v9, v9
	v_lshlrev_b32_e32 v3, 8, v3
	v_and_b32_e32 v3, 0xff00, v3
	v_and_b32_e32 v4, 0xff0000, v4
	v_perm_b32 v2, v5, v2, s21
	v_or3_b32 v2, v2, v3, v4
	v_lshlrev_b32_e32 v3, 8, v7
	v_and_b32_e32 v3, 0xff00, v3
	v_and_b32_e32 v4, 0xff0000, v8
	v_perm_b32 v5, v9, v6, s21
	v_or3_b32 v3, v5, v3, v4
	v_mul_f32_e32 v5, v80, v12
	v_mul_f32_e32 v4, v80, v76
	v_rndne_f32_e32 v5, v5
	v_mul_f32_e32 v6, v80, v77
	v_mul_f32_e32 v7, v80, v13
	v_rndne_f32_e32 v4, v4
	v_cvt_i32_f32_e32 v5, v5
	v_rndne_f32_e32 v6, v6
	v_rndne_f32_e32 v7, v7
	v_mul_f32_e32 v9, v80, v14
	v_cvt_i32_f32_e32 v4, v4
	v_cvt_i32_f32_sdwa v6, v6 dst_sel:WORD_1 dst_unused:UNUSED_PAD src0_sel:DWORD
	v_cvt_i32_f32_e32 v7, v7
	v_mul_f32_e32 v8, v80, v78
	v_rndne_f32_e32 v9, v9
	v_mul_f32_e32 v10, v80, v79
	v_mul_f32_e32 v11, v80, v15
	v_rndne_f32_e32 v8, v8
	v_cvt_i32_f32_e32 v9, v9
	v_rndne_f32_e32 v10, v10
	v_rndne_f32_e32 v11, v11
	v_cvt_i32_f32_e32 v8, v8
	v_cvt_i32_f32_sdwa v10, v10 dst_sel:WORD_1 dst_unused:UNUSED_PAD src0_sel:DWORD
	v_cvt_i32_f32_e32 v11, v11
	v_lshlrev_b32_e32 v5, 8, v5
	v_and_b32_e32 v5, 0xff00, v5
	v_and_b32_e32 v6, 0xff0000, v6
	v_perm_b32 v4, v7, v4, s21
	v_or3_b32 v4, v4, v5, v6
	v_lshlrev_b32_e32 v5, 8, v9
	v_and_b32_e32 v5, 0xff00, v5
	v_and_b32_e32 v6, 0xff0000, v10
	v_perm_b32 v7, v11, v8, s21
	v_or3_b32 v5, v7, v5, v6
	ds_write2st64_b64 v25, v[2:3], v[4:5] offset0:14 offset1:15
	s_waitcnt vmcnt(1)
	ds_write_b16 v24, v61 offset:16640
	s_waitcnt vmcnt(0)
	ds_write_b16 v24, v62 offset:16768
	global_load_dwordx4 v[4:7], v[0:1], off
	global_load_dwordx4 v[8:11], v[0:1], off offset:1024
	global_load_dwordx4 v[12:15], v[0:1], off offset:2048
	global_load_dwordx4 v[60:63], v[0:1], off offset:3072
	v_add_co_u32_e32 v56, vcc, s28, v0
	v_lshl_add_u64 v[20:21], s[10:11], 0, v[16:17]
	s_nop 0
	v_addc_co_u32_e32 v57, vcc, 0, v1, vcc
	s_add_u32 s10, s18, s14
	s_addc_u32 s11, s19, s15
	v_lshl_add_u64 v[22:23], s[10:11], 0, v[16:17]
	s_add_i32 s10, s8, s34
	s_ashr_i32 s11, s10, 31
	s_lshl_b64 s[12:13], s[10:11], 13
	s_add_u32 s12, s6, s12
	s_addc_u32 s13, s7, s13
	v_readlane_b32 s36, v32, 32
	v_readlane_b32 s38, v32, 48
	s_waitcnt vmcnt(3)
	v_lshlrev_b32_e32 v27, 16, v4
	v_and_b32_e32 v26, 0xffff0000, v4
	v_max_f32_e64 v2, |v26|, |v26|
	v_max_f32_e64 v3, |v27|, |v27|
	v_max_f32_e32 v4, v3, v2
	global_load_dwordx4 v[0:3], v[56:57], off
	v_lshlrev_b32_e32 v42, 16, v5
	v_and_b32_e32 v39, 0xffff0000, v5
	v_max_f32_e64 v5, |v39|, |v39|
	v_max_f32_e64 v28, |v42|, |v42|
	v_max_f32_e32 v5, v28, v5
	v_lshlrev_b32_e32 v37, 16, v7
	v_and_b32_e32 v35, 0xffff0000, v7
	v_max3_f32 v30, v4, 0, v5
	v_max_f32_e64 v4, |v35|, |v35|
	v_max_f32_e64 v5, |v37|, |v37|
	v_lshlrev_b32_e32 v43, 16, v6
	v_and_b32_e32 v40, 0xffff0000, v6
	v_max_f32_e32 v4, v5, v4
	v_max3_f32 v31, |v43|, |v40|, v4
	s_waitcnt vmcnt(3)
	v_lshlrev_b32_e32 v29, 16, v8
	v_and_b32_e32 v28, 0xffff0000, v8
	global_load_dwordx4 v[4:7], v[56:57], off offset:1024
	v_max_f32_e64 v8, |v28|, |v28|
	v_max_f32_e64 v34, |v29|, |v29|
	v_max_f32_e32 v8, v34, v8
	v_lshlrev_b32_e32 v49, 16, v9
	v_and_b32_e32 v46, 0xffff0000, v9
	v_lshlrev_b32_e32 v44, 16, v11
	v_and_b32_e32 v41, 0xffff0000, v11
	v_max3_f32 v8, v30, v31, v8
	v_max_f32_e64 v9, |v46|, |v46|
	v_max_f32_e64 v30, |v49|, |v49|
	v_lshlrev_b32_e32 v47, 16, v10
	v_and_b32_e32 v45, 0xffff0000, v10
	v_max_f32_e64 v10, |v41|, |v41|
	v_max_f32_e64 v11, |v44|, |v44|
	v_max_f32_e32 v9, v30, v9
	v_max_f32_e32 v10, v11, v10
	s_waitcnt vmcnt(3)
	v_lshlrev_b32_e32 v31, 16, v12
	v_and_b32_e32 v30, 0xffff0000, v12
	v_max3_f32 v10, |v47|, |v45|, v10
	v_max_f32_e64 v12, |v30|, |v30|
	v_max_f32_e64 v36, |v31|, |v31|
	v_lshlrev_b32_e32 v54, 16, v13
	v_and_b32_e32 v51, 0xffff0000, v13
	v_max3_f32 v34, v8, v9, v10
	global_load_dwordx4 v[8:11], v[56:57], off offset:2048
	v_max_f32_e32 v12, v36, v12
	v_max_f32_e64 v13, |v51|, |v51|
	v_max_f32_e64 v36, |v54|, |v54|
	v_max_f32_e32 v13, v36, v13
	v_lshlrev_b32_e32 v50, 16, v15
	v_and_b32_e32 v48, 0xffff0000, v15
	v_max3_f32 v34, v34, v12, v13
	v_max_f32_e64 v12, |v48|, |v48|
	v_max_f32_e64 v13, |v50|, |v50|
	v_lshlrev_b32_e32 v55, 16, v14
	v_and_b32_e32 v52, 0xffff0000, v14
	v_max_f32_e32 v12, v13, v12
	v_max3_f32 v53, |v55|, |v52|, v12
	global_load_dwordx4 v[12:15], v[56:57], off offset:3072
	s_waitcnt vmcnt(4)
	v_lshlrev_b32_e32 v38, 16, v60
	v_and_b32_e32 v36, 0xffff0000, v60
	v_max_f32_e64 v56, |v36|, |v36|
	v_max_f32_e64 v57, |v38|, |v38|
	v_max_f32_e32 v56, v57, v56
	v_lshlrev_b32_e32 v60, 16, v61
	v_and_b32_e32 v58, 0xffff0000, v61
	v_max3_f32 v34, v34, v53, v56
	v_max_f32_e64 v53, |v58|, |v58|
	v_max_f32_e64 v56, |v60|, |v60|
	v_max_f32_e32 v61, v56, v53
	v_lshlrev_b32_e32 v56, 16, v63
	v_and_b32_e32 v53, 0xffff0000, v63
	v_lshlrev_b32_e32 v59, 16, v62
	v_and_b32_e32 v57, 0xffff0000, v62
	v_max_f32_e64 v62, |v53|, |v53|
	v_max_f32_e64 v63, |v56|, |v56|
	v_max_f32_e32 v62, v63, v62
	v_max3_f32 v62, |v59|, |v57|, v62
	v_max3_f32 v61, v34, v61, v62
	global_load_dword v34, v[20:21], off
	global_load_dword v62, v[22:23], off
	global_load_dword v63, v[22:23], off offset:256
	s_waitcnt vmcnt(6)
	v_lshlrev_b32_e32 v20, 16, v0
	v_and_b32_e32 v21, 0xffff0000, v0
	v_max_f32_e64 v0, |v21|, |v21|
	v_max_f32_e64 v22, |v20|, |v20|
	v_max_f32_e32 v0, v22, v0
	v_lshlrev_b32_e32 v22, 16, v1
	v_and_b32_e32 v23, 0xffff0000, v1
	v_max_f32_e64 v1, |v23|, |v23|
	v_max_f32_e64 v64, |v22|, |v22|
	v_max_f32_e32 v1, v64, v1
	v_lshlrev_b32_e32 v65, 16, v3
	v_and_b32_e32 v66, 0xffff0000, v3
	v_max3_f32 v0, v61, v0, v1
	v_lshlrev_b32_e32 v61, 16, v2
	v_and_b32_e32 v64, 0xffff0000, v2
	v_max_f32_e64 v1, |v66|, |v66|
	v_max_f32_e64 v2, |v65|, |v65|
	s_waitcnt vmcnt(5)
; #define LAS __attribute__((address_space(3)))
; __device__ __forceinline__ float bflo(unsigned w) { return __uint_as_float(w << 16); }
; __device__ __forceinline__ float bfhi(unsigned w) { return __uint_as_float(w & 0xffff0000u); }
; __device__ __forceinline__ float wave_sum(float v) { v = dpp_add16(v); return (rdlane(v, 0) + rdlane(v, 16)) + (rdlane(v, 32) + rdlane(v, 48)); }
; __device__ __forceinline__ float wave_max(float v) { v = dpp_max16(v); return fmaxf(fmaxf(rdlane(v, 0), rdlane(v, 16)), fmaxf(rdlane(v, 32), rdlane(v, 48))); }
; __device__ __forceinline__ void p12_peer(Frame& F) {
;     ...
;         const int t = F.gw + i * F.NGW; v4u xp[8]; float mxa = 0.f;
; #pragma unroll
;         for (int j = 0; j < 8; ++j) { xp[j] = ((const v4u*)(HN + (size_t)t * D_))[F.lane + 64 * j];
;             mxa = fmaxf(fmaxf(fmaxf(mxa, fmaxf(fabsf(bflo(xp[j].x)), fabsf(bfhi(xp[j].x)))), fmaxf(fabsf(bflo(xp[j].y)), fabsf(bfhi(xp[j].y)))), fmaxf(fmaxf(fabsf(bflo(xp[j].z)), fabsf(bfhi(xp[j].z))), fmaxf(fabsf(bflo(xp[j].w)), fabsf(bfhi(xp[j].w))))); }
;         mxa = wave_max(mxa); const float inv = mxa > 0.f ? 127.0f / mxa : 0.f;
;         const float rsn = 1.0f / sqrtf(wave_sum(PSQ[(size_t)t * 64 + F.lane]) * (1.f / D_) + 1e-6f);
;         sx[i] = mxa * rsn * (1.0f / 127.0f);
; #pragma unroll
;         for (int j = 0; j < 8; ++j) {
;             const int q0 = (int)rintf(bflo(xp[j].x) * inv), q1 = (int)rintf(bfhi(xp[j].x) * inv), q2 = (int)rintf(bflo(xp[j].y) * inv), q3 = (int)rintf(bfhi(xp[j].y) * inv);
;             const int q4 = (int)rintf(bflo(xp[j].z) * inv), q5 = (int)rintf(bfhi(xp[j].z) * inv), q6 = (int)rintf(bflo(xp[j].w) * inv), q7 = (int)rintf(bfhi(xp[j].w) * inv);
;             *(LAS v2u*)(XQ + i * 4096 + 8 * (F.lane + 64 * j)) = (v2u){(unsigned)((q0 & 0xff) | ((q1 & 0xff) << 8) | ((q2 & 0xff) << 16) | (q3 << 24)), (unsigned)((q4 & 0xff) | ((q5 & 0xff) << 8) | ((q6 & 0xff) << 16) | (q7 << 24))}; }
	v_lshlrev_b32_e32 v67, 16, v4
	v_and_b32_e32 v68, 0xffff0000, v4
	v_max_f32_e32 v1, v2, v1
	v_max_f32_e64 v2, |v68|, |v68|
	v_max_f32_e64 v3, |v67|, |v67|
	v_max3_f32 v1, |v61|, |v64|, v1
	v_max_f32_e32 v2, v3, v2
	v_lshlrev_b32_e32 v69, 16, v5
	v_and_b32_e32 v70, 0xffff0000, v5
	v_max3_f32 v0, v0, v1, v2
	v_max_f32_e64 v1, |v70|, |v70|
	v_max_f32_e64 v2, |v69|, |v69|
	v_lshlrev_b32_e32 v72, 16, v7
	v_and_b32_e32 v7, 0xffff0000, v7
	v_max_f32_e32 v1, v2, v1
	v_max_f32_e64 v2, |v7|, |v7|
	v_max_f32_e64 v3, |v72|, |v72|
	v_lshlrev_b32_e32 v71, 16, v6
	v_and_b32_e32 v6, 0xffff0000, v6
	v_max_f32_e32 v2, v3, v2
	v_max3_f32 v2, |v71|, |v6|, v2
	v_max3_f32 v0, v0, v1, v2
	s_waitcnt vmcnt(4)
	v_lshlrev_b32_e32 v73, 16, v8
	v_and_b32_e32 v8, 0xffff0000, v8
	v_max_f32_e64 v1, |v8|, |v8|
	v_max_f32_e64 v2, |v73|, |v73|
	v_lshlrev_b32_e32 v74, 16, v9
	v_and_b32_e32 v9, 0xffff0000, v9
	v_max_f32_e32 v1, v2, v1
	v_max_f32_e64 v2, |v9|, |v9|
	v_max_f32_e64 v3, |v74|, |v74|
	v_max_f32_e32 v2, v3, v2
	v_lshlrev_b32_e32 v76, 16, v11
	v_and_b32_e32 v11, 0xffff0000, v11
	v_max3_f32 v0, v0, v1, v2
	v_max_f32_e64 v1, |v11|, |v11|
	v_max_f32_e64 v2, |v76|, |v76|
	s_waitcnt vmcnt(3)
	v_lshlrev_b32_e32 v77, 16, v12
	v_and_b32_e32 v12, 0xffff0000, v12
	v_lshlrev_b32_e32 v75, 16, v10
	v_and_b32_e32 v10, 0xffff0000, v10
	v_max_f32_e32 v1, v2, v1
	v_max_f32_e64 v2, |v12|, |v12|
	v_max_f32_e64 v3, |v77|, |v77|
	v_max3_f32 v1, |v75|, |v10|, v1
	v_max_f32_e32 v2, v3, v2
	v_lshlrev_b32_e32 v78, 16, v13
	v_and_b32_e32 v13, 0xffff0000, v13
	v_max3_f32 v0, v0, v1, v2
	v_max_f32_e64 v1, |v13|, |v13|
	v_max_f32_e64 v2, |v78|, |v78|
	v_lshlrev_b32_e32 v80, 16, v15
	v_and_b32_e32 v15, 0xffff0000, v15
	v_max_f32_e32 v1, v2, v1
	v_max_f32_e64 v2, |v15|, |v15|
	v_max_f32_e64 v3, |v80|, |v80|
	v_lshlrev_b32_e32 v79, 16, v14
	v_and_b32_e32 v14, 0xffff0000, v14
	v_max_f32_e32 v2, v3, v2
	v_max3_f32 v2, |v79|, |v14|, v2
	v_max3_f32 v0, v0, v1, v2
	v_mov_b32_e32 v1, 0
	s_nop 1
	v_mov_b32_dpp v1, v0 quad_perm:[1,0,3,2] row_mask:0xf bank_mask:0xf
	v_max_f32_e32 v1, v1, v1
	v_max_f32_e32 v0, v0, v1
	v_mov_b32_e32 v1, 0
	s_nop 1
	v_mov_b32_dpp v1, v0 quad_perm:[2,3,0,1] row_mask:0xf bank_mask:0xf
	v_max_f32_e32 v1, v1, v1
	v_max_f32_e32 v0, v0, v1
	v_mov_b32_e32 v1, 0
	s_nop 1
	v_mov_b32_dpp v1, v0 row_half_mirror row_mask:0xf bank_mask:0xf
	v_max_f32_e32 v1, v1, v1
	v_max_f32_e32 v0, v0, v1
	v_mov_b32_e32 v1, 0
	s_nop 1
	v_mov_b32_dpp v1, v0 row_mirror row_mask:0xf bank_mask:0xf
	v_max_f32_e32 v1, v1, v1
	v_max_f32_e32 v0, v0, v1
	s_nop 0
	v_readlane_b32 s33, v0, 32
	v_readlane_b32 s35, v0, 48
	v_readlane_b32 s30, v0, 0
	v_readlane_b32 s31, v0, 16
	v_max_f32_e64 v0, s35, s35
	v_max_f32_e64 v1, s33, s33
	v_max_f32_e32 v0, v1, v0
	v_mov_b32_e32 v1, s31
	v_max3_f32 v161, s30, v1, v0
	v_div_scale_f32 v2, s[30:31], v161, v161, s29
	v_rcp_f32_e32 v3, v2
	v_lshl_add_u64 v[0:1], s[12:13], 0, v[18:19]
	s_lshl_b64 s[12:13], s[10:11], 8
	s_add_u32 s12, s22, s12
	v_fma_f32 v4, -v2, v3, 1.0
	v_fmac_f32_e32 v3, v4, v3
	v_div_scale_f32 v4, vcc, s29, v161, s29
	v_mul_f32_e32 v5, v4, v3
	v_fma_f32 v18, -v2, v5, v4
	v_fmac_f32_e32 v5, v18, v3
	v_fma_f32 v2, -v2, v5, v4
	v_div_fmas_f32 v2, v2, v3, v5
	v_div_fixup_f32 v2, v2, v161, s29
	v_cmp_lt_f32_e32 vcc, 0, v161
	s_addc_u32 s13, s23, s13
	v_readlane_b32 s35, v32, 0
	v_cndmask_b32_e32 v18, 0, v2, vcc
	v_mul_f32_e32 v3, v18, v26
	v_mul_f32_e32 v2, v18, v27
	v_rndne_f32_e32 v3, v3
	v_mul_f32_e32 v4, v18, v42
	v_mul_f32_e32 v5, v18, v39
	v_rndne_f32_e32 v2, v2
	v_cvt_i32_f32_e32 v3, v3
	v_rndne_f32_e32 v4, v4
	v_rndne_f32_e32 v5, v5
	v_mul_f32_e32 v26, v18, v40
	v_cvt_i32_f32_e32 v2, v2
	v_cvt_i32_f32_sdwa v4, v4 dst_sel:WORD_1 dst_unused:UNUSED_PAD src0_sel:DWORD
	v_cvt_i32_f32_e32 v5, v5
	v_mul_f32_e32 v19, v18, v43
	v_rndne_f32_e32 v26, v26
	v_mul_f32_e32 v27, v18, v37
	v_mul_f32_e32 v35, v18, v35
	v_rndne_f32_e32 v19, v19
	v_cvt_i32_f32_e32 v26, v26
	v_rndne_f32_e32 v27, v27
	v_rndne_f32_e32 v35, v35
	v_cvt_i32_f32_e32 v19, v19
	v_cvt_i32_f32_sdwa v27, v27 dst_sel:WORD_1 dst_unused:UNUSED_PAD src0_sel:DWORD
	v_cvt_i32_f32_e32 v35, v35
	v_lshlrev_b32_e32 v3, 8, v3
	v_and_b32_e32 v3, 0xff00, v3
	v_and_b32_e32 v4, 0xff0000, v4
	v_perm_b32 v2, v5, v2, s21
	v_or3_b32 v2, v2, v3, v4
	v_lshlrev_b32_e32 v3, 8, v26
	v_and_b32_e32 v3, 0xff00, v3
	v_and_b32_e32 v4, 0xff0000, v27
	v_perm_b32 v5, v35, v19, s21
	v_or3_b32 v3, v5, v3, v4
	v_mul_f32_e32 v5, v18, v28
	v_mul_f32_e32 v4, v18, v29
	v_rndne_f32_e32 v5, v5
	v_mul_f32_e32 v19, v18, v49
	v_mul_f32_e32 v26, v18, v46
	v_rndne_f32_e32 v4, v4
	v_cvt_i32_f32_e32 v5, v5
	v_rndne_f32_e32 v19, v19
	v_rndne_f32_e32 v26, v26
	v_mul_f32_e32 v28, v18, v45
	v_cvt_i32_f32_e32 v4, v4
	v_cvt_i32_f32_sdwa v19, v19 dst_sel:WORD_1 dst_unused:UNUSED_PAD src0_sel:DWORD
	v_cvt_i32_f32_e32 v26, v26
	v_mul_f32_e32 v27, v18, v47
	v_rndne_f32_e32 v28, v28
	v_mul_f32_e32 v29, v18, v44
	v_mul_f32_e32 v35, v18, v41
	v_rndne_f32_e32 v27, v27
	v_cvt_i32_f32_e32 v28, v28
	v_rndne_f32_e32 v29, v29
	v_rndne_f32_e32 v35, v35
	v_cvt_i32_f32_e32 v27, v27
	v_cvt_i32_f32_sdwa v29, v29 dst_sel:WORD_1 dst_unused:UNUSED_PAD src0_sel:DWORD
	v_cvt_i32_f32_e32 v35, v35
	v_lshlrev_b32_e32 v5, 8, v5
	v_and_b32_e32 v5, 0xff00, v5
	v_and_b32_e32 v19, 0xff0000, v19
	v_perm_b32 v4, v26, v4, s21
	v_or3_b32 v4, v4, v5, v19
	v_lshlrev_b32_e32 v5, 8, v28
	v_and_b32_e32 v5, 0xff00, v5
	v_and_b32_e32 v19, 0xff0000, v29
	v_perm_b32 v26, v35, v27, s21
	v_or3_b32 v5, v26, v5, v19
	ds_write2st64_b64 v25, v[2:3], v[4:5] offset0:16 offset1:17
	v_mul_f32_e32 v3, v18, v30
	v_mul_f32_e32 v2, v18, v31
	v_rndne_f32_e32 v3, v3
	v_mul_f32_e32 v4, v18, v54
	v_mul_f32_e32 v5, v18, v51
; #define LAS __attribute__((address_space(3)))
; __device__ __forceinline__ float bflo(unsigned w) { return __uint_as_float(w << 16); }
; __device__ __forceinline__ float bfhi(unsigned w) { return __uint_as_float(w & 0xffff0000u); }
; __device__ __forceinline__ void p12_peer(Frame& F) {
;     ...
;         for (int j = 0; j < 8; ++j) {
;             const int q0 = (int)rintf(bflo(xp[j].x) * inv), q1 = (int)rintf(bfhi(xp[j].x) * inv), q2 = (int)rintf(bflo(xp[j].y) * inv), q3 = (int)rintf(bfhi(xp[j].y) * inv);
;             const int q4 = (int)rintf(bflo(xp[j].z) * inv), q5 = (int)rintf(bfhi(xp[j].z) * inv), q6 = (int)rintf(bflo(xp[j].w) * inv), q7 = (int)rintf(bfhi(xp[j].w) * inv);
;             *(LAS v2u*)(XQ + i * 4096 + 8 * (F.lane + 64 * j)) = (v2u){(unsigned)((q0 & 0xff) | ((q1 & 0xff) << 8) | ((q2 & 0xff) << 16) | (q3 << 24)), (unsigned)((q4 & 0xff) | ((q5 & 0xff) << 8) | ((q6 & 0xff) << 16) | (q7 << 24))}; }
	v_rndne_f32_e32 v2, v2
	v_cvt_i32_f32_e32 v3, v3
	v_rndne_f32_e32 v4, v4
	v_rndne_f32_e32 v5, v5
	v_mul_f32_e32 v26, v18, v52
	v_cvt_i32_f32_e32 v2, v2
	v_cvt_i32_f32_sdwa v4, v4 dst_sel:WORD_1 dst_unused:UNUSED_PAD src0_sel:DWORD
	v_cvt_i32_f32_e32 v5, v5
	v_mul_f32_e32 v19, v18, v55
	v_rndne_f32_e32 v26, v26
	v_mul_f32_e32 v27, v18, v50
	v_mul_f32_e32 v28, v18, v48
	v_rndne_f32_e32 v19, v19
	v_cvt_i32_f32_e32 v26, v26
	v_rndne_f32_e32 v27, v27
	v_rndne_f32_e32 v28, v28
	v_cvt_i32_f32_e32 v19, v19
	v_cvt_i32_f32_sdwa v27, v27 dst_sel:WORD_1 dst_unused:UNUSED_PAD src0_sel:DWORD
	v_cvt_i32_f32_e32 v28, v28
	v_lshlrev_b32_e32 v3, 8, v3
	v_and_b32_e32 v3, 0xff00, v3
	v_and_b32_e32 v4, 0xff0000, v4
	v_perm_b32 v2, v5, v2, s21
	v_or3_b32 v2, v2, v3, v4
	v_lshlrev_b32_e32 v3, 8, v26
	v_and_b32_e32 v3, 0xff00, v3
	v_and_b32_e32 v4, 0xff0000, v27
	v_perm_b32 v5, v28, v19, s21
	v_or3_b32 v3, v5, v3, v4
	v_mul_f32_e32 v5, v18, v36
	v_mul_f32_e32 v4, v18, v38
	v_rndne_f32_e32 v5, v5
	v_mul_f32_e32 v19, v18, v60
	v_mul_f32_e32 v26, v18, v58
	v_rndne_f32_e32 v4, v4
	v_cvt_i32_f32_e32 v5, v5
	v_rndne_f32_e32 v19, v19
	v_rndne_f32_e32 v26, v26
	v_mul_f32_e32 v28, v18, v57
	v_cvt_i32_f32_e32 v4, v4
	v_cvt_i32_f32_sdwa v19, v19 dst_sel:WORD_1 dst_unused:UNUSED_PAD src0_sel:DWORD
	v_cvt_i32_f32_e32 v26, v26
	v_mul_f32_e32 v27, v18, v59
	v_rndne_f32_e32 v28, v28
	v_mul_f32_e32 v29, v18, v56
	v_mul_f32_e32 v30, v18, v53
	v_rndne_f32_e32 v27, v27
	v_cvt_i32_f32_e32 v28, v28
	v_rndne_f32_e32 v29, v29
	v_rndne_f32_e32 v30, v30
	v_cvt_i32_f32_e32 v27, v27
	v_cvt_i32_f32_sdwa v29, v29 dst_sel:WORD_1 dst_unused:UNUSED_PAD src0_sel:DWORD
	v_cvt_i32_f32_e32 v30, v30
	v_lshlrev_b32_e32 v5, 8, v5
	v_and_b32_e32 v5, 0xff00, v5
	v_and_b32_e32 v19, 0xff0000, v19
	v_perm_b32 v4, v26, v4, s21
	v_or3_b32 v4, v4, v5, v19
	v_lshlrev_b32_e32 v5, 8, v28
	v_and_b32_e32 v5, 0xff00, v5
	v_and_b32_e32 v19, 0xff0000, v29
	v_perm_b32 v26, v30, v27, s21
	v_or3_b32 v5, v26, v5, v19
	ds_write2st64_b64 v25, v[2:3], v[4:5] offset0:18 offset1:19
	v_mul_f32_e32 v3, v18, v21
	v_mul_f32_e32 v2, v18, v20
	v_rndne_f32_e32 v3, v3
	v_mul_f32_e32 v4, v18, v22
	v_mul_f32_e32 v5, v18, v23
	v_rndne_f32_e32 v2, v2
	v_cvt_i32_f32_e32 v3, v3
	v_rndne_f32_e32 v4, v4
	v_rndne_f32_e32 v5, v5
	v_mul_f32_e32 v20, v18, v64
	v_cvt_i32_f32_e32 v2, v2
	v_cvt_i32_f32_sdwa v4, v4 dst_sel:WORD_1 dst_unused:UNUSED_PAD src0_sel:DWORD
	v_cvt_i32_f32_e32 v5, v5
	v_mul_f32_e32 v19, v18, v61
	v_rndne_f32_e32 v20, v20
	v_mul_f32_e32 v21, v18, v65
	v_mul_f32_e32 v22, v18, v66
	v_rndne_f32_e32 v19, v19
	v_cvt_i32_f32_e32 v20, v20
	v_rndne_f32_e32 v21, v21
	v_rndne_f32_e32 v22, v22
	v_cvt_i32_f32_e32 v19, v19
	v_cvt_i32_f32_sdwa v21, v21 dst_sel:WORD_1 dst_unused:UNUSED_PAD src0_sel:DWORD
	v_cvt_i32_f32_e32 v22, v22
	v_lshlrev_b32_e32 v3, 8, v3
	v_and_b32_e32 v3, 0xff00, v3
	v_and_b32_e32 v4, 0xff0000, v4
	v_perm_b32 v2, v5, v2, s21
	v_or3_b32 v2, v2, v3, v4
	v_lshlrev_b32_e32 v3, 8, v20
	v_and_b32_e32 v3, 0xff00, v3
	v_and_b32_e32 v4, 0xff0000, v21
	v_perm_b32 v5, v22, v19, s21
	v_or3_b32 v3, v5, v3, v4
	v_mul_f32_e32 v5, v18, v68
	v_mul_f32_e32 v4, v18, v67
	v_rndne_f32_e32 v5, v5
	v_mul_f32_e32 v19, v18, v69
	v_mul_f32_e32 v20, v18, v70
	v_rndne_f32_e32 v4, v4
	v_cvt_i32_f32_e32 v5, v5
	v_rndne_f32_e32 v19, v19
	v_rndne_f32_e32 v20, v20
	v_mul_f32_e32 v6, v18, v6
	v_cvt_i32_f32_e32 v4, v4
	v_cvt_i32_f32_sdwa v19, v19 dst_sel:WORD_1 dst_unused:UNUSED_PAD src0_sel:DWORD
	v_cvt_i32_f32_e32 v20, v20
	v_mul_f32_e32 v21, v18, v71
	v_rndne_f32_e32 v6, v6
	v_mul_f32_e32 v22, v18, v72
	v_mul_f32_e32 v7, v18, v7
	v_rndne_f32_e32 v21, v21
	v_cvt_i32_f32_e32 v6, v6
	v_rndne_f32_e32 v22, v22
	v_rndne_f32_e32 v7, v7
	v_cvt_i32_f32_e32 v21, v21
	v_cvt_i32_f32_sdwa v22, v22 dst_sel:WORD_1 dst_unused:UNUSED_PAD src0_sel:DWORD
	v_cvt_i32_f32_e32 v7, v7
	v_lshlrev_b32_e32 v5, 8, v5
	v_and_b32_e32 v5, 0xff00, v5
	v_and_b32_e32 v19, 0xff0000, v19
	v_perm_b32 v4, v20, v4, s21
	v_or3_b32 v4, v4, v5, v19
	v_lshlrev_b32_e32 v5, 8, v6
	v_and_b32_e32 v5, 0xff00, v5
	v_and_b32_e32 v6, 0xff0000, v22
	v_perm_b32 v7, v7, v21, s21
	v_or3_b32 v5, v7, v5, v6
	ds_write2st64_b64 v25, v[2:3], v[4:5] offset0:20 offset1:21
	v_mul_f32_e32 v3, v18, v8
	v_mul_f32_e32 v2, v18, v73
	v_rndne_f32_e32 v3, v3
	v_mul_f32_e32 v4, v18, v74
	v_mul_f32_e32 v5, v18, v9
	v_rndne_f32_e32 v2, v2
	v_cvt_i32_f32_e32 v3, v3
	v_rndne_f32_e32 v4, v4
	v_rndne_f32_e32 v5, v5
	v_mul_f32_e32 v7, v18, v10
	v_cvt_i32_f32_e32 v2, v2
	v_cvt_i32_f32_sdwa v4, v4 dst_sel:WORD_1 dst_unused:UNUSED_PAD src0_sel:DWORD
	v_cvt_i32_f32_e32 v5, v5
	v_mul_f32_e32 v6, v18, v75
	v_rndne_f32_e32 v7, v7
	v_mul_f32_e32 v8, v18, v76
	v_mul_f32_e32 v9, v18, v11
	v_rndne_f32_e32 v6, v6
	v_cvt_i32_f32_e32 v7, v7
	v_rndne_f32_e32 v8, v8
	v_rndne_f32_e32 v9, v9
	v_cvt_i32_f32_e32 v6, v6
	v_cvt_i32_f32_sdwa v8, v8 dst_sel:WORD_1 dst_unused:UNUSED_PAD src0_sel:DWORD
	v_cvt_i32_f32_e32 v9, v9
	v_lshlrev_b32_e32 v3, 8, v3
	v_and_b32_e32 v3, 0xff00, v3
	v_and_b32_e32 v4, 0xff0000, v4
	v_perm_b32 v2, v5, v2, s21
	v_or3_b32 v2, v2, v3, v4
	v_lshlrev_b32_e32 v3, 8, v7
	v_and_b32_e32 v3, 0xff00, v3
	v_and_b32_e32 v4, 0xff0000, v8
	v_perm_b32 v5, v9, v6, s21
	v_or3_b32 v3, v5, v3, v4
	v_mul_f32_e32 v5, v18, v12
	v_mul_f32_e32 v4, v18, v77
	v_rndne_f32_e32 v5, v5
	v_mul_f32_e32 v6, v18, v78
	v_mul_f32_e32 v7, v18, v13
	v_rndne_f32_e32 v4, v4
	v_cvt_i32_f32_e32 v5, v5
	v_rndne_f32_e32 v6, v6
	v_rndne_f32_e32 v7, v7
	v_mul_f32_e32 v9, v18, v14
	v_cvt_i32_f32_e32 v4, v4
	v_cvt_i32_f32_sdwa v6, v6 dst_sel:WORD_1 dst_unused:UNUSED_PAD src0_sel:DWORD
	v_cvt_i32_f32_e32 v7, v7
	v_mul_f32_e32 v8, v18, v79
	v_rndne_f32_e32 v9, v9
	v_mul_f32_e32 v10, v18, v80
	v_mul_f32_e32 v11, v18, v15
	v_rndne_f32_e32 v8, v8
	v_cvt_i32_f32_e32 v9, v9
	v_rndne_f32_e32 v10, v10
	v_rndne_f32_e32 v11, v11
	v_cvt_i32_f32_e32 v8, v8
	v_cvt_i32_f32_sdwa v10, v10 dst_sel:WORD_1 dst_unused:UNUSED_PAD src0_sel:DWORD
	v_cvt_i32_f32_e32 v11, v11
	v_lshlrev_b32_e32 v5, 8, v5
	v_and_b32_e32 v5, 0xff00, v5
	v_and_b32_e32 v6, 0xff0000, v6
	v_perm_b32 v4, v7, v4, s21
	v_or3_b32 v4, v4, v5, v6
	v_lshlrev_b32_e32 v5, 8, v9
	v_and_b32_e32 v5, 0xff00, v5
	v_and_b32_e32 v6, 0xff0000, v10
	v_perm_b32 v7, v11, v8, s21
	v_or3_b32 v5, v7, v5, v6
	ds_write2st64_b64 v25, v[2:3], v[4:5] offset0:22 offset1:23
	s_waitcnt vmcnt(1)
; __device__ __forceinline__ float bflo(unsigned w) { return __uint_as_float(w << 16); }
; __device__ __forceinline__ float bfhi(unsigned w) { return __uint_as_float(w & 0xffff0000u); }
; __device__ __forceinline__ float wave_sum(float v) { v = dpp_add16(v); return (rdlane(v, 0) + rdlane(v, 16)) + (rdlane(v, 32) + rdlane(v, 48)); }
; __device__ __forceinline__ float wave_max(float v) { v = dpp_max16(v); return fmaxf(fmaxf(rdlane(v, 0), rdlane(v, 16)), fmaxf(rdlane(v, 32), rdlane(v, 48))); }
; __device__ __forceinline__ void p12_peer(Frame& F) {
;     ...
;         const int t = F.gw + i * F.NGW; v4u xp[8]; float mxa = 0.f;
; #pragma unroll
;         for (int j = 0; j < 8; ++j) { xp[j] = ((const v4u*)(HN + (size_t)t * D_))[F.lane + 64 * j];
;             mxa = fmaxf(fmaxf(fmaxf(mxa, fmaxf(fabsf(bflo(xp[j].x)), fabsf(bfhi(xp[j].x)))), fmaxf(fabsf(bflo(xp[j].y)), fabsf(bfhi(xp[j].y)))), fmaxf(fmaxf(fabsf(bflo(xp[j].z)), fabsf(bfhi(xp[j].z))), fmaxf(fabsf(bflo(xp[j].w)), fabsf(bfhi(xp[j].w))))); }
;         mxa = wave_max(mxa); const float inv = mxa > 0.f ? 127.0f / mxa : 0.f;
;         const float rsn = 1.0f / sqrtf(wave_sum(PSQ[(size_t)t * 64 + F.lane]) * (1.f / D_) + 1e-6f);
;     ...
;         EL[i * 128 + F.lane] = (unsigned short)PIDX[(size_t)t * 128 + F.lane]; EL[i * 128 + 64 + F.lane] = (unsigned short)PIDX[(size_t)t * 128 + 64 + F.lane];
	ds_write_b16 v24, v62 offset:16896
	s_waitcnt vmcnt(0)
	ds_write_b16 v24, v63 offset:17024
	global_load_dwordx4 v[4:7], v[0:1], off
	global_load_dwordx4 v[8:11], v[0:1], off offset:1024
	global_load_dwordx4 v[12:15], v[0:1], off offset:2048
	global_load_dwordx4 v[58:61], v[0:1], off offset:3072
	v_add_co_u32_e32 v54, vcc, s28, v0
	v_lshl_add_u64 v[18:19], s[12:13], 0, v[16:17]
	s_nop 0
	v_addc_co_u32_e32 v55, vcc, 0, v1, vcc
	s_lshl_b64 s[12:13], s[10:11], 9
	s_add_u32 s18, s18, s12
	s_addc_u32 s19, s19, s13
	v_lshl_add_u64 v[16:17], s[18:19], 0, v[16:17]
	s_add_u32 s18, s68, 0xf400000
	v_add_f32_dpp v32, v34, v34 quad_perm:[1,0,3,2] row_mask:0xf bank_mask:0xf bound_ctrl:1
	s_waitcnt vmcnt(3)
	v_lshlrev_b32_e32 v21, 16, v4
	v_and_b32_e32 v20, 0xffff0000, v4
	v_max_f32_e64 v2, |v20|, |v20|
	v_max_f32_e64 v3, |v21|, |v21|
	v_max_f32_e32 v4, v3, v2
	global_load_dwordx4 v[0:3], v[54:55], off
	v_lshlrev_b32_e32 v39, 16, v5
	v_and_b32_e32 v36, 0xffff0000, v5
	v_max_f32_e64 v5, |v36|, |v36|
	v_max_f32_e64 v22, |v39|, |v39|
	v_max_f32_e32 v5, v22, v5
	v_lshlrev_b32_e32 v30, 16, v7
	v_and_b32_e32 v28, 0xffff0000, v7
	v_max3_f32 v26, v4, 0, v5
	v_max_f32_e64 v4, |v28|, |v28|
	v_max_f32_e64 v5, |v30|, |v30|
	v_lshlrev_b32_e32 v40, 16, v6
	v_and_b32_e32 v37, 0xffff0000, v6
	v_max_f32_e32 v4, v5, v4
	v_max3_f32 v27, |v40|, |v37|, v4
	s_waitcnt vmcnt(3)
	v_lshlrev_b32_e32 v23, 16, v8
	v_and_b32_e32 v22, 0xffff0000, v8
	global_load_dwordx4 v[4:7], v[54:55], off offset:1024
	v_max_f32_e64 v8, |v22|, |v22|
	v_max_f32_e64 v29, |v23|, |v23|
	v_max_f32_e32 v8, v29, v8
	v_lshlrev_b32_e32 v46, 16, v9
	v_and_b32_e32 v43, 0xffff0000, v9
	v_lshlrev_b32_e32 v41, 16, v11
	v_and_b32_e32 v38, 0xffff0000, v11
	v_max3_f32 v8, v26, v27, v8
	v_max_f32_e64 v9, |v43|, |v43|
	v_max_f32_e64 v26, |v46|, |v46|
	v_lshlrev_b32_e32 v44, 16, v10
	v_and_b32_e32 v42, 0xffff0000, v10
	v_max_f32_e64 v10, |v38|, |v38|
	v_max_f32_e64 v11, |v41|, |v41|
	v_max_f32_e32 v9, v26, v9
	v_max_f32_e32 v10, v11, v10
	s_waitcnt vmcnt(3)
	v_lshlrev_b32_e32 v27, 16, v12
	v_and_b32_e32 v26, 0xffff0000, v12
	v_max3_f32 v10, |v44|, |v42|, v10
	v_max_f32_e64 v12, |v26|, |v26|
	v_max_f32_e64 v31, |v27|, |v27|
	v_lshlrev_b32_e32 v51, 16, v13
	v_and_b32_e32 v48, 0xffff0000, v13
	v_max3_f32 v29, v8, v9, v10
	global_load_dwordx4 v[8:11], v[54:55], off offset:2048
	v_max_f32_e32 v12, v31, v12
	v_max_f32_e64 v13, |v48|, |v48|
	v_max_f32_e64 v31, |v51|, |v51|
	v_max_f32_e32 v13, v31, v13
	v_lshlrev_b32_e32 v47, 16, v15
	v_and_b32_e32 v45, 0xffff0000, v15
	v_max3_f32 v35, v29, v12, v13
	v_max_f32_e64 v12, |v45|, |v45|
	v_max_f32_e64 v13, |v47|, |v47|
	v_lshlrev_b32_e32 v52, 16, v14
	v_and_b32_e32 v49, 0xffff0000, v14
	v_max_f32_e32 v12, v13, v12
	v_max3_f32 v50, |v52|, |v49|, v12
	global_load_dwordx4 v[12:15], v[54:55], off offset:3072
	s_waitcnt vmcnt(4)
	v_lshlrev_b32_e32 v31, 16, v58
	v_and_b32_e32 v29, 0xffff0000, v58
	v_max_f32_e64 v53, |v29|, |v29|
	v_max_f32_e64 v54, |v31|, |v31|
	v_max_f32_e32 v53, v54, v53
	v_lshlrev_b32_e32 v57, 16, v59
	v_and_b32_e32 v55, 0xffff0000, v59
	v_max3_f32 v35, v35, v50, v53
	v_max_f32_e64 v50, |v55|, |v55|
	v_max_f32_e64 v53, |v57|, |v57|
	v_max_f32_e32 v58, v53, v50
	v_lshlrev_b32_e32 v53, 16, v61
	v_and_b32_e32 v50, 0xffff0000, v61
	v_lshlrev_b32_e32 v56, 16, v60
	v_and_b32_e32 v54, 0xffff0000, v60
	v_max_f32_e64 v59, |v50|, |v50|
	v_max_f32_e64 v60, |v53|, |v53|
	v_max_f32_e32 v59, v60, v59
	v_max3_f32 v59, |v56|, |v54|, v59
	v_max3_f32 v58, v35, v58, v59
	global_load_dword v35, v[18:19], off
	global_load_dword v59, v[16:17], off
	global_load_dword v60, v[16:17], off offset:256
	v_add_f32_dpp v32, v32, v32 quad_perm:[2,3,0,1] row_mask:0xf bank_mask:0xf bound_ctrl:1
	s_waitcnt vmcnt(6)
	v_lshlrev_b32_e32 v16, 16, v0
	v_and_b32_e32 v17, 0xffff0000, v0
	v_max_f32_e64 v0, |v17|, |v17|
	v_max_f32_e64 v18, |v16|, |v16|
	v_max_f32_e32 v0, v18, v0
	v_lshlrev_b32_e32 v18, 16, v1
	v_and_b32_e32 v19, 0xffff0000, v1
	v_max_f32_e64 v1, |v19|, |v19|
	v_max_f32_e64 v61, |v18|, |v18|
	v_max_f32_e32 v1, v61, v1
	v_lshlrev_b32_e32 v62, 16, v3
	v_and_b32_e32 v63, 0xffff0000, v3
	v_max3_f32 v0, v58, v0, v1
	v_lshlrev_b32_e32 v58, 16, v2
	v_and_b32_e32 v61, 0xffff0000, v2
	v_max_f32_e64 v1, |v63|, |v63|
	v_max_f32_e64 v2, |v62|, |v62|
	s_waitcnt vmcnt(5)
	v_lshlrev_b32_e32 v64, 16, v4
	v_and_b32_e32 v4, 0xffff0000, v4
	v_max_f32_e32 v1, v2, v1
	v_max_f32_e64 v2, |v4|, |v4|
	v_max_f32_e64 v3, |v64|, |v64|
	v_max3_f32 v1, |v58|, |v61|, v1
	v_max_f32_e32 v2, v3, v2
	v_lshlrev_b32_e32 v65, 16, v5
	v_and_b32_e32 v5, 0xffff0000, v5
	v_max3_f32 v0, v0, v1, v2
	v_max_f32_e64 v1, |v5|, |v5|
	v_max_f32_e64 v2, |v65|, |v65|
	v_lshlrev_b32_e32 v67, 16, v7
	v_and_b32_e32 v7, 0xffff0000, v7
	v_max_f32_e32 v1, v2, v1
	v_max_f32_e64 v2, |v7|, |v7|
	v_max_f32_e64 v3, |v67|, |v67|
	v_lshlrev_b32_e32 v66, 16, v6
	v_and_b32_e32 v6, 0xffff0000, v6
	v_max_f32_e32 v2, v3, v2
	v_max3_f32 v2, |v66|, |v6|, v2
	v_max3_f32 v0, v0, v1, v2
	v_add_f32_dpp v32, v32, v32 row_half_mirror row_mask:0xf bank_mask:0xf bound_ctrl:1
	s_waitcnt vmcnt(4)
	v_lshlrev_b32_e32 v68, 16, v8
	v_and_b32_e32 v8, 0xffff0000, v8
	v_max_f32_e64 v1, |v8|, |v8|
	v_max_f32_e64 v2, |v68|, |v68|
	v_lshlrev_b32_e32 v69, 16, v9
	v_and_b32_e32 v9, 0xffff0000, v9
	v_max_f32_e32 v1, v2, v1
	v_max_f32_e64 v2, |v9|, |v9|
	v_max_f32_e64 v3, |v69|, |v69|
	v_max_f32_e32 v2, v3, v2
	v_lshlrev_b32_e32 v71, 16, v11
	v_and_b32_e32 v11, 0xffff0000, v11
	v_max3_f32 v0, v0, v1, v2
	v_max_f32_e64 v1, |v11|, |v11|
	v_max_f32_e64 v2, |v71|, |v71|
	s_waitcnt vmcnt(3)
; #define LAS __attribute__((address_space(3)))
; __device__ __forceinline__ float bflo(unsigned w) { return __uint_as_float(w << 16); }
; __device__ __forceinline__ float bfhi(unsigned w) { return __uint_as_float(w & 0xffff0000u); }
; __device__ __forceinline__ float wave_sum(float v) { v = dpp_add16(v); return (rdlane(v, 0) + rdlane(v, 16)) + (rdlane(v, 32) + rdlane(v, 48)); }
; __device__ __forceinline__ float wave_max(float v) { v = dpp_max16(v); return fmaxf(fmaxf(rdlane(v, 0), rdlane(v, 16)), fmaxf(rdlane(v, 32), rdlane(v, 48))); }
; __device__ __forceinline__ void p12_peer(Frame& F) {
;     ...
;             mxa = fmaxf(fmaxf(fmaxf(mxa, fmaxf(fabsf(bflo(xp[j].x)), fabsf(bfhi(xp[j].x)))), fmaxf(fabsf(bflo(xp[j].y)), fabsf(bfhi(xp[j].y)))), fmaxf(fmaxf(fabsf(bflo(xp[j].z)), fabsf(bfhi(xp[j].z))), fmaxf(fabsf(bflo(xp[j].w)), fabsf(bfhi(xp[j].w))))); }
;         mxa = wave_max(mxa); const float inv = mxa > 0.f ? 127.0f / mxa : 0.f;
;         const float rsn = 1.0f / sqrtf(wave_sum(PSQ[(size_t)t * 64 + F.lane]) * (1.f / D_) + 1e-6f);
;         sx[i] = mxa * rsn * (1.0f / 127.0f);
; #pragma unroll
;         for (int j = 0; j < 8; ++j) {
;             const int q0 = (int)rintf(bflo(xp[j].x) * inv), q1 = (int)rintf(bfhi(xp[j].x) * inv), q2 = (int)rintf(bflo(xp[j].y) * inv), q3 = (int)rintf(bfhi(xp[j].y) * inv);
;             const int q4 = (int)rintf(bflo(xp[j].z) * inv), q5 = (int)rintf(bfhi(xp[j].z) * inv), q6 = (int)rintf(bflo(xp[j].w) * inv), q7 = (int)rintf(bfhi(xp[j].w) * inv);
;             *(LAS v2u*)(XQ + i * 4096 + 8 * (F.lane + 64 * j)) = (v2u){(unsigned)((q0 & 0xff) | ((q1 & 0xff) << 8) | ((q2 & 0xff) << 16) | (q3 << 24)), (unsigned)((q4 & 0xff) | ((q5 & 0xff) << 8) | ((q6 & 0xff) << 16) | (q7 << 24))}; }
	v_lshlrev_b32_e32 v72, 16, v12
	v_and_b32_e32 v12, 0xffff0000, v12
	v_lshlrev_b32_e32 v70, 16, v10
	v_and_b32_e32 v10, 0xffff0000, v10
	v_max_f32_e32 v1, v2, v1
	v_max_f32_e64 v2, |v12|, |v12|
	v_max_f32_e64 v3, |v72|, |v72|
	v_max3_f32 v1, |v70|, |v10|, v1
	v_max_f32_e32 v2, v3, v2
	v_lshlrev_b32_e32 v73, 16, v13
	v_and_b32_e32 v13, 0xffff0000, v13
	v_max3_f32 v0, v0, v1, v2
	v_max_f32_e64 v1, |v13|, |v13|
	v_max_f32_e64 v2, |v73|, |v73|
	v_lshlrev_b32_e32 v75, 16, v15
	v_and_b32_e32 v15, 0xffff0000, v15
	v_max_f32_e32 v1, v2, v1
	v_max_f32_e64 v2, |v15|, |v15|
	v_max_f32_e64 v3, |v75|, |v75|
	v_lshlrev_b32_e32 v74, 16, v14
	v_and_b32_e32 v14, 0xffff0000, v14
	v_max_f32_e32 v2, v3, v2
	v_max3_f32 v2, |v74|, |v14|, v2
	v_max3_f32 v0, v0, v1, v2
	v_mov_b32_e32 v1, 0
	v_add_f32_dpp v32, v32, v32 row_mirror row_mask:0xf bank_mask:0xf bound_ctrl:1
	s_nop 0
	v_mov_b32_dpp v1, v0 quad_perm:[1,0,3,2] row_mask:0xf bank_mask:0xf
	v_max_f32_e32 v1, v1, v1
	v_max_f32_e32 v0, v0, v1
	v_mov_b32_e32 v1, 0
	v_readlane_b32 s31, v32, 16
	v_readlane_b32 s30, v32, 32
	v_mov_b32_dpp v1, v0 quad_perm:[2,3,0,1] row_mask:0xf bank_mask:0xf
	v_max_f32_e32 v1, v1, v1
	v_max_f32_e32 v0, v0, v1
	v_mov_b32_e32 v1, 0
	v_readlane_b32 s33, v32, 48
	s_nop 0
	v_mov_b32_dpp v1, v0 row_half_mirror row_mask:0xf bank_mask:0xf
	v_max_f32_e32 v1, v1, v1
	v_max_f32_e32 v0, v0, v1
	v_mov_b32_e32 v1, 0
	s_nop 1
	v_mov_b32_dpp v1, v0 row_mirror row_mask:0xf bank_mask:0xf
	v_max_f32_e32 v1, v1, v1
	v_max_f32_e32 v0, v0, v1
	s_nop 0
	v_readlane_b32 s23, v0, 32
	v_readlane_b32 s28, v0, 48
	v_readlane_b32 s19, v0, 0
	v_readlane_b32 s22, v0, 16
	v_max_f32_e64 v0, s28, s28
	v_max_f32_e64 v1, s23, s23
	v_max_f32_e32 v0, v1, v0
	v_mov_b32_e32 v1, s22
	v_max3_f32 v160, s19, v1, v0
	v_div_scale_f32 v0, s[22:23], v160, v160, s29
	v_rcp_f32_e32 v1, v0
	s_addc_u32 s19, s69, 0
	v_fma_f32 v2, -v0, v1, 1.0
	v_fmac_f32_e32 v1, v2, v1
	v_div_scale_f32 v2, vcc, s29, v160, s29
	v_mul_f32_e32 v3, v2, v1
	v_fma_f32 v76, -v0, v3, v2
	v_fmac_f32_e32 v3, v76, v1
	v_fma_f32 v0, -v0, v3, v2
	v_div_fmas_f32 v0, v0, v1, v3
	v_div_fixup_f32 v0, v0, v160, s29
	v_cmp_lt_f32_e32 vcc, 0, v160
	v_readlane_b32 s29, v32, 0
	s_waitcnt vmcnt(2)
	v_add_f32_dpp v32, v35, v35 quad_perm:[1,0,3,2] row_mask:0xf bank_mask:0xf bound_ctrl:1
	v_cndmask_b32_e32 v76, 0, v0, vcc
	v_mul_f32_e32 v1, v76, v20
	v_mul_f32_e32 v0, v76, v21
	v_rndne_f32_e32 v1, v1
	v_mul_f32_e32 v2, v76, v39
	v_mul_f32_e32 v3, v76, v36
	v_rndne_f32_e32 v0, v0
	v_cvt_i32_f32_e32 v1, v1
	v_rndne_f32_e32 v2, v2
	v_rndne_f32_e32 v3, v3
	v_mul_f32_e32 v21, v76, v37
	v_cvt_i32_f32_e32 v0, v0
	v_cvt_i32_f32_sdwa v2, v2 dst_sel:WORD_1 dst_unused:UNUSED_PAD src0_sel:DWORD
	v_cvt_i32_f32_e32 v3, v3
	v_mul_f32_e32 v20, v76, v40
	v_rndne_f32_e32 v21, v21
	v_mul_f32_e32 v30, v76, v30
	v_mul_f32_e32 v28, v76, v28
	v_rndne_f32_e32 v20, v20
	v_cvt_i32_f32_e32 v21, v21
	v_rndne_f32_e32 v30, v30
	v_rndne_f32_e32 v28, v28
	v_cvt_i32_f32_e32 v20, v20
	v_cvt_i32_f32_sdwa v30, v30 dst_sel:WORD_1 dst_unused:UNUSED_PAD src0_sel:DWORD
	v_cvt_i32_f32_e32 v28, v28
	v_lshlrev_b32_e32 v1, 8, v1
	v_and_b32_e32 v1, 0xff00, v1
	v_and_b32_e32 v2, 0xff0000, v2
	v_perm_b32 v0, v3, v0, s21
	v_or3_b32 v0, v0, v1, v2
	v_lshlrev_b32_e32 v1, 8, v21
	v_and_b32_e32 v1, 0xff00, v1
	v_and_b32_e32 v2, 0xff0000, v30
	v_perm_b32 v3, v28, v20, s21
	v_or3_b32 v1, v3, v1, v2
	v_mul_f32_e32 v3, v76, v22
	v_mul_f32_e32 v2, v76, v23
	v_rndne_f32_e32 v3, v3
	v_mul_f32_e32 v20, v76, v46
	v_mul_f32_e32 v21, v76, v43
	v_rndne_f32_e32 v2, v2
	v_cvt_i32_f32_e32 v3, v3
	v_rndne_f32_e32 v20, v20
	v_rndne_f32_e32 v21, v21
	v_mul_f32_e32 v23, v76, v42
	v_cvt_i32_f32_e32 v2, v2
	v_cvt_i32_f32_sdwa v20, v20 dst_sel:WORD_1 dst_unused:UNUSED_PAD src0_sel:DWORD
	v_cvt_i32_f32_e32 v21, v21
	v_mul_f32_e32 v22, v76, v44
	v_rndne_f32_e32 v23, v23
	v_mul_f32_e32 v28, v76, v41
	v_mul_f32_e32 v30, v76, v38
	v_rndne_f32_e32 v22, v22
	v_cvt_i32_f32_e32 v23, v23
	v_rndne_f32_e32 v28, v28
	v_rndne_f32_e32 v30, v30
	v_cvt_i32_f32_e32 v22, v22
	v_cvt_i32_f32_sdwa v28, v28 dst_sel:WORD_1 dst_unused:UNUSED_PAD src0_sel:DWORD
	v_cvt_i32_f32_e32 v30, v30
	v_lshlrev_b32_e32 v3, 8, v3
	v_and_b32_e32 v3, 0xff00, v3
	v_and_b32_e32 v20, 0xff0000, v20
	v_perm_b32 v2, v21, v2, s21
	v_or3_b32 v2, v2, v3, v20
	v_lshlrev_b32_e32 v3, 8, v23
	v_and_b32_e32 v3, 0xff00, v3
	v_and_b32_e32 v20, 0xff0000, v28
	v_perm_b32 v21, v30, v22, s21
	v_or3_b32 v3, v21, v3, v20
	ds_write2st64_b64 v25, v[0:1], v[2:3] offset0:24 offset1:25
	v_mul_f32_e32 v1, v76, v26
	v_mul_f32_e32 v0, v76, v27
	v_rndne_f32_e32 v1, v1
	v_mul_f32_e32 v2, v76, v51
	v_mul_f32_e32 v3, v76, v48
	v_rndne_f32_e32 v0, v0
	v_cvt_i32_f32_e32 v1, v1
	v_rndne_f32_e32 v2, v2
	v_rndne_f32_e32 v3, v3
	v_mul_f32_e32 v21, v76, v49
	v_cvt_i32_f32_e32 v0, v0
	v_cvt_i32_f32_sdwa v2, v2 dst_sel:WORD_1 dst_unused:UNUSED_PAD src0_sel:DWORD
	v_cvt_i32_f32_e32 v3, v3
	v_mul_f32_e32 v20, v76, v52
	v_rndne_f32_e32 v21, v21
	v_mul_f32_e32 v22, v76, v47
	v_mul_f32_e32 v23, v76, v45
	v_rndne_f32_e32 v20, v20
	v_cvt_i32_f32_e32 v21, v21
	v_rndne_f32_e32 v22, v22
	v_rndne_f32_e32 v23, v23
	v_cvt_i32_f32_e32 v20, v20
	v_cvt_i32_f32_sdwa v22, v22 dst_sel:WORD_1 dst_unused:UNUSED_PAD src0_sel:DWORD
	v_cvt_i32_f32_e32 v23, v23
	v_lshlrev_b32_e32 v1, 8, v1
	v_and_b32_e32 v1, 0xff00, v1
	v_and_b32_e32 v2, 0xff0000, v2
	v_perm_b32 v0, v3, v0, s21
	v_or3_b32 v0, v0, v1, v2
	v_lshlrev_b32_e32 v1, 8, v21
	v_and_b32_e32 v1, 0xff00, v1
	v_and_b32_e32 v2, 0xff0000, v22
	v_perm_b32 v3, v23, v20, s21
	v_or3_b32 v1, v3, v1, v2
	v_mul_f32_e32 v3, v76, v29
	v_mul_f32_e32 v2, v76, v31
	v_rndne_f32_e32 v3, v3
	v_mul_f32_e32 v20, v76, v57
; #define LAS __attribute__((address_space(3)))
; __device__ __forceinline__ float bflo(unsigned w) { return __uint_as_float(w << 16); }
; __device__ __forceinline__ float bfhi(unsigned w) { return __uint_as_float(w & 0xffff0000u); }
; #define P12_ISSUE(c_, i_, h_, CW_, SC_) do { _Pragma("unroll") for (int bb = 0; bb < 8; ++bb) { const unsigned ro = (unsigned)(c_) * 16384u + (unsigned)EL[(i_) * 128 + ((h_) * 8 + bb) * 8 + g8]; \
;         CW_[bb] = *(const v4u*)(U4 + (size_t)(ro * 128u + 16u * (unsigned)k8)); SC_[bb] = USS[(size_t)(ro * 8u + (unsigned)k8)]; } } while (0)
; __device__ __forceinline__ void p12_peer(Frame& F) {
;     ...
;         for (int j = 0; j < 8; ++j) {
;             const int q0 = (int)rintf(bflo(xp[j].x) * inv), q1 = (int)rintf(bfhi(xp[j].x) * inv), q2 = (int)rintf(bflo(xp[j].y) * inv), q3 = (int)rintf(bfhi(xp[j].y) * inv);
;             const int q4 = (int)rintf(bflo(xp[j].z) * inv), q5 = (int)rintf(bfhi(xp[j].z) * inv), q6 = (int)rintf(bflo(xp[j].w) * inv), q7 = (int)rintf(bfhi(xp[j].w) * inv);
;             *(LAS v2u*)(XQ + i * 4096 + 8 * (F.lane + 64 * j)) = (v2u){(unsigned)((q0 & 0xff) | ((q1 & 0xff) << 8) | ((q2 & 0xff) << 16) | (q3 << 24)), (unsigned)((q4 & 0xff) | ((q5 & 0xff) << 8) | ((q6 & 0xff) << 16) | (q7 << 24))}; }
;         EL[i * 128 + F.lane] = (unsigned short)PIDX[(size_t)t * 128 + F.lane]; EL[i * 128 + 64 + F.lane] = (unsigned short)PIDX[(size_t)t * 128 + 64 + F.lane];
;     ...
;     { v4u cwA[8], cwB[8]; unsigned scA[8], scB[8]; v4u xa, xb; int xo;
;       P12_ISSUE(0, 0, 0, cwA, scA);
	v_mul_f32_e32 v21, v76, v55
	v_rndne_f32_e32 v2, v2
	v_cvt_i32_f32_e32 v3, v3
	v_rndne_f32_e32 v20, v20
	v_rndne_f32_e32 v21, v21
	v_mul_f32_e32 v23, v76, v54
	v_cvt_i32_f32_e32 v2, v2
	v_cvt_i32_f32_sdwa v20, v20 dst_sel:WORD_1 dst_unused:UNUSED_PAD src0_sel:DWORD
	v_cvt_i32_f32_e32 v21, v21
	v_mul_f32_e32 v22, v76, v56
	v_rndne_f32_e32 v23, v23
	v_mul_f32_e32 v26, v76, v53
	v_mul_f32_e32 v27, v76, v50
	v_rndne_f32_e32 v22, v22
	v_cvt_i32_f32_e32 v23, v23
	v_rndne_f32_e32 v26, v26
	v_rndne_f32_e32 v27, v27
	v_cvt_i32_f32_e32 v22, v22
	v_cvt_i32_f32_sdwa v26, v26 dst_sel:WORD_1 dst_unused:UNUSED_PAD src0_sel:DWORD
	v_cvt_i32_f32_e32 v27, v27
	v_lshlrev_b32_e32 v3, 8, v3
	v_and_b32_e32 v3, 0xff00, v3
	v_and_b32_e32 v20, 0xff0000, v20
	v_perm_b32 v2, v21, v2, s21
	v_or3_b32 v2, v2, v3, v20
	v_lshlrev_b32_e32 v3, 8, v23
	v_and_b32_e32 v3, 0xff00, v3
	v_and_b32_e32 v20, 0xff0000, v26
	v_perm_b32 v21, v27, v22, s21
	v_or3_b32 v3, v21, v3, v20
	ds_write2st64_b64 v25, v[0:1], v[2:3] offset0:26 offset1:27
	v_mul_f32_e32 v1, v76, v17
	v_mul_f32_e32 v0, v76, v16
	v_rndne_f32_e32 v1, v1
	v_mul_f32_e32 v2, v76, v18
	v_mul_f32_e32 v3, v76, v19
	v_rndne_f32_e32 v0, v0
	v_cvt_i32_f32_e32 v1, v1
	v_rndne_f32_e32 v2, v2
	v_rndne_f32_e32 v3, v3
	v_mul_f32_e32 v17, v76, v61
	v_cvt_i32_f32_e32 v0, v0
	v_cvt_i32_f32_sdwa v2, v2 dst_sel:WORD_1 dst_unused:UNUSED_PAD src0_sel:DWORD
	v_cvt_i32_f32_e32 v3, v3
	v_mul_f32_e32 v16, v76, v58
	v_rndne_f32_e32 v17, v17
	v_mul_f32_e32 v18, v76, v62
	v_mul_f32_e32 v19, v76, v63
	v_rndne_f32_e32 v16, v16
	v_cvt_i32_f32_e32 v17, v17
	v_rndne_f32_e32 v18, v18
	v_rndne_f32_e32 v19, v19
	v_cvt_i32_f32_e32 v16, v16
	v_cvt_i32_f32_sdwa v18, v18 dst_sel:WORD_1 dst_unused:UNUSED_PAD src0_sel:DWORD
	v_cvt_i32_f32_e32 v19, v19
	v_lshlrev_b32_e32 v1, 8, v1
	v_and_b32_e32 v1, 0xff00, v1
	v_and_b32_e32 v2, 0xff0000, v2
	v_perm_b32 v0, v3, v0, s21
	v_or3_b32 v0, v0, v1, v2
	v_lshlrev_b32_e32 v1, 8, v17
	v_and_b32_e32 v1, 0xff00, v1
	v_and_b32_e32 v2, 0xff0000, v18
	v_perm_b32 v3, v19, v16, s21
	v_or3_b32 v1, v3, v1, v2
	v_mul_f32_e32 v3, v76, v4
	v_mul_f32_e32 v2, v76, v64
	v_rndne_f32_e32 v3, v3
	v_mul_f32_e32 v4, v76, v65
	v_mul_f32_e32 v5, v76, v5
	v_rndne_f32_e32 v2, v2
	v_cvt_i32_f32_e32 v3, v3
	v_rndne_f32_e32 v4, v4
	v_rndne_f32_e32 v5, v5
	v_mul_f32_e32 v6, v76, v6
	v_cvt_i32_f32_e32 v2, v2
	v_cvt_i32_f32_sdwa v4, v4 dst_sel:WORD_1 dst_unused:UNUSED_PAD src0_sel:DWORD
	v_cvt_i32_f32_e32 v5, v5
	v_mul_f32_e32 v16, v76, v66
	v_rndne_f32_e32 v6, v6
	v_mul_f32_e32 v17, v76, v67
	v_mul_f32_e32 v7, v76, v7
	v_rndne_f32_e32 v16, v16
	v_cvt_i32_f32_e32 v6, v6
	v_rndne_f32_e32 v17, v17
	v_rndne_f32_e32 v7, v7
	v_cvt_i32_f32_e32 v16, v16
	v_cvt_i32_f32_sdwa v17, v17 dst_sel:WORD_1 dst_unused:UNUSED_PAD src0_sel:DWORD
	v_cvt_i32_f32_e32 v7, v7
	v_lshlrev_b32_e32 v3, 8, v3
	v_and_b32_e32 v3, 0xff00, v3
	v_and_b32_e32 v4, 0xff0000, v4
	v_perm_b32 v2, v5, v2, s21
	v_or3_b32 v2, v2, v3, v4
	v_lshlrev_b32_e32 v3, 8, v6
	v_and_b32_e32 v3, 0xff00, v3
	v_and_b32_e32 v4, 0xff0000, v17
	v_perm_b32 v5, v7, v16, s21
	v_or3_b32 v3, v5, v3, v4
	ds_write2st64_b64 v25, v[0:1], v[2:3] offset0:28 offset1:29
	v_mul_f32_e32 v1, v76, v8
	v_mul_f32_e32 v0, v76, v68
	v_rndne_f32_e32 v1, v1
	v_mul_f32_e32 v2, v76, v69
	v_mul_f32_e32 v3, v76, v9
	v_rndne_f32_e32 v0, v0
	v_cvt_i32_f32_e32 v1, v1
	v_rndne_f32_e32 v2, v2
	v_rndne_f32_e32 v3, v3
	v_mul_f32_e32 v5, v76, v10
	v_cvt_i32_f32_e32 v0, v0
	v_cvt_i32_f32_sdwa v2, v2 dst_sel:WORD_1 dst_unused:UNUSED_PAD src0_sel:DWORD
	v_cvt_i32_f32_e32 v3, v3
	v_mul_f32_e32 v4, v76, v70
	v_rndne_f32_e32 v5, v5
	v_mul_f32_e32 v6, v76, v71
	v_mul_f32_e32 v7, v76, v11
	v_rndne_f32_e32 v4, v4
	v_cvt_i32_f32_e32 v5, v5
	v_rndne_f32_e32 v6, v6
	v_rndne_f32_e32 v7, v7
	v_cvt_i32_f32_e32 v4, v4
	v_cvt_i32_f32_sdwa v6, v6 dst_sel:WORD_1 dst_unused:UNUSED_PAD src0_sel:DWORD
	v_cvt_i32_f32_e32 v7, v7
	v_lshlrev_b32_e32 v1, 8, v1
	v_and_b32_e32 v1, 0xff00, v1
	v_and_b32_e32 v2, 0xff0000, v2
	v_perm_b32 v0, v3, v0, s21
	v_or3_b32 v0, v0, v1, v2
	v_lshlrev_b32_e32 v1, 8, v5
	v_and_b32_e32 v1, 0xff00, v1
	v_and_b32_e32 v2, 0xff0000, v6
	v_perm_b32 v3, v7, v4, s21
	v_or3_b32 v1, v3, v1, v2
	v_mul_f32_e32 v3, v76, v12
	v_mul_f32_e32 v2, v76, v72
	v_rndne_f32_e32 v3, v3
	v_mul_f32_e32 v4, v76, v73
	v_mul_f32_e32 v5, v76, v13
	v_rndne_f32_e32 v2, v2
	v_cvt_i32_f32_e32 v3, v3
	v_rndne_f32_e32 v4, v4
	v_rndne_f32_e32 v5, v5
	v_mul_f32_e32 v7, v76, v14
	v_cvt_i32_f32_e32 v2, v2
	v_cvt_i32_f32_sdwa v4, v4 dst_sel:WORD_1 dst_unused:UNUSED_PAD src0_sel:DWORD
	v_cvt_i32_f32_e32 v5, v5
	v_mul_f32_e32 v6, v76, v74
	v_rndne_f32_e32 v7, v7
	v_mul_f32_e32 v8, v76, v75
	v_mul_f32_e32 v9, v76, v15
	v_rndne_f32_e32 v6, v6
	v_cvt_i32_f32_e32 v7, v7
	v_rndne_f32_e32 v8, v8
	v_rndne_f32_e32 v9, v9
	v_cvt_i32_f32_e32 v6, v6
	v_cvt_i32_f32_sdwa v8, v8 dst_sel:WORD_1 dst_unused:UNUSED_PAD src0_sel:DWORD
	v_cvt_i32_f32_e32 v9, v9
	v_lshlrev_b32_e32 v3, 8, v3
	v_and_b32_e32 v3, 0xff00, v3
	v_and_b32_e32 v4, 0xff0000, v4
	v_perm_b32 v2, v5, v2, s21
	v_or3_b32 v2, v2, v3, v4
	v_lshlrev_b32_e32 v3, 8, v7
	v_and_b32_e32 v3, 0xff00, v3
	v_and_b32_e32 v4, 0xff0000, v8
	v_perm_b32 v5, v9, v6, s21
	v_or3_b32 v3, v5, v3, v4
	ds_write2st64_b64 v25, v[0:1], v[2:3] offset0:30 offset1:31
	s_waitcnt vmcnt(1)
	ds_write_b16 v24, v59 offset:17152
	s_waitcnt vmcnt(0)
	ds_write_b16 v24, v60 offset:17280
	s_waitcnt lgkmcnt(0)
	v_lshlrev_b32_e32 v248, 1, v95
	s_mov_b32 s48, 0x7060302
	ds_read_u16 v0, v93 offset:16384
	ds_read_u16 v1, v93 offset:16400
	ds_read_u16 v2, v93 offset:16416
	ds_read_u16 v3, v93 offset:16432
	ds_read_u16 v4, v93 offset:16448
	ds_read_u16 v5, v93 offset:16464
	ds_read_u16 v6, v93 offset:16480
	ds_read_u16 v36, v93 offset:16496
	s_waitcnt lgkmcnt(7)
; #define P12_ISSUE(c_, i_, h_, CW_, SC_) do { _Pragma("unroll") for (int bb = 0; bb < 8; ++bb) { const unsigned ro = (unsigned)(c_) * 16384u + (unsigned)EL[(i_) * 128 + ((h_) * 8 + bb) * 8 + g8]; \
;         CW_[bb] = *(const v4u*)(U4 + (size_t)(ro * 128u + 16u * (unsigned)k8)); SC_[bb] = USS[(size_t)(ro * 8u + (unsigned)k8)]; } } while (0)
; #define P12_COMP(i_, h_, CW_, SC_) do { _Pragma("unroll") for (int bb = 0; bb < 8; ++bb) { int a0 = 0, a1 = 0; P12_U4(CW_[bb].x, xa.x, xa.y, a0); P12_U4(CW_[bb].y, xa.z, xa.w, a1); P12_U4(CW_[bb].z, xb.x, xb.y, a0); P12_U4(CW_[bb].w, xb.z, xb.w, a1); \
;         psum[(i_)][(h_) * 8 + bb] += __uint_as_float(SC_[bb] << 16) * (float)((a0 + a1) - xo); } } while (0)
; #define P12_BAR() asm volatile("" ::: "memory")
; __device__ __forceinline__ void p12_peer(Frame& F) {
;     ...
;     { v4u cwA[8], cwB[8]; unsigned scA[8], scB[8]; v4u xa, xb; int xo;
;       P12_ISSUE(0, 0, 0, cwA, scA);
; _Pragma("nounroll")
;       for (int c = 0; c < 16; ++c) { const int cn = c + 1 < 16 ? c + 1 : 15;
;           P12_XQ(c, 0); P12_ISSUE(c, 0, 1, cwB, scB); P12_BAR(); P12_COMP(0, 0, cwA, scA); P12_ISSUE(c, 1, 0, cwA, scA); P12_BAR(); P12_COMP(0, 1, cwB, scB);
	v_lshl_or_b32 v7, v0, 5, v248
	s_waitcnt lgkmcnt(5)
	v_lshl_or_b32 v8, v2, 5, v248
	s_waitcnt lgkmcnt(3)
	v_lshl_or_b32 v9, v4, 5, v248
	s_waitcnt lgkmcnt(1)
	v_lshl_or_b32 v10, v6, 5, v248
	global_load_dword v184, v7, s[18:19]
	global_load_dword v186, v8, s[18:19]
	global_load_dword v188, v9, s[18:19]
	global_load_dword v190, v10, s[18:19]
	s_waitcnt lgkmcnt(0)
	v_lshl_or_b32 v10, v36, 5, v248
	v_lshl_or_b32 v0, v0, 7, v165
	v_lshl_or_b32 v7, v1, 5, v248
	v_lshl_or_b32 v8, v3, 5, v248
	v_lshl_or_b32 v9, v5, 5, v248
	global_load_dword v191, v10, s[18:19]
	global_load_dword v189, v9, s[18:19]
	global_load_dword v187, v8, s[18:19]
	global_load_dword v185, v7, s[18:19]
	global_load_dwordx4 v[28:31], v0, s[0:1]
	v_lshl_or_b32 v0, v1, 7, v165
	global_load_dwordx4 v[24:27], v0, s[0:1]
	v_lshl_or_b32 v0, v2, 7, v165
	global_load_dwordx4 v[20:23], v0, s[0:1]
	v_lshl_or_b32 v0, v3, 7, v165
	global_load_dwordx4 v[16:19], v0, s[0:1]
	v_lshl_or_b32 v0, v4, 7, v165
	global_load_dwordx4 v[12:15], v0, s[0:1]
	v_lshl_or_b32 v0, v5, 7, v165
	global_load_dwordx4 v[8:11], v0, s[0:1]
	v_lshl_or_b32 v0, v6, 7, v165
	global_load_dwordx4 v[4:7], v0, s[0:1]
	v_lshl_or_b32 v0, v36, 7, v165
	global_load_dwordx4 v[0:3], v0, s[0:1]
	v_add_f32_dpp v32, v32, v32 quad_perm:[2,3,0,1] row_mask:0xf bank_mask:0xf bound_ctrl:1
	s_waitcnt vmcnt(11)
	v_perm_b32 v40, v190, v191, s43
	v_add_f32_dpp v32, v32, v32 row_half_mirror row_mask:0xf bank_mask:0xf bound_ctrl:1
	s_waitcnt vmcnt(10)
	v_perm_b32 v41, v188, v189, s43
	s_waitcnt vmcnt(9)
	v_perm_b32 v42, v186, v187, s43
	v_add_f32_dpp v32, v32, v32 row_mirror row_mask:0xf bank_mask:0xf bound_ctrl:1
	s_waitcnt vmcnt(8)
	v_perm_b32 v43, v184, v185, s43
	v_readlane_b32 s21, v32, 0
	v_readlane_b32 s23, v32, 16
	v_readlane_b32 s22, v32, 32
	v_readlane_b32 s28, v32, 48
.LBB0_3272:
	s_lshl_b32 s49, s44, 4
	s_sub_u32 s46, s18, s49
	s_subb_u32 s47, s19, 0
	ds_read_b128 v[36:39], v166
	ds_read_b128 v[32:35], v166 offset:16
	ds_read_u16 v44, v93 offset:16512
	ds_read_u16 v45, v93 offset:16528
	ds_read_u16 v46, v93 offset:16544
	ds_read_u16 v47, v93 offset:16560
	v_mov_b32_e32 v48, 0
	s_waitcnt lgkmcnt(3)
	v_add_u32_e32 v44, s44, v44
	v_lshl_or_b32 v49, v44, 7, v165
	global_load_dwordx4 v[88:91], v49, s[0:1]
	v_lshl_or_b32 v49, v44, 5, v248
	s_waitcnt lgkmcnt(2)
	v_add_u32_e32 v44, s44, v45
	v_lshl_or_b32 v45, v44, 7, v165
	v_lshl_or_b32 v50, v44, 5, v248
	s_waitcnt lgkmcnt(1)
	v_add_u32_e32 v44, s44, v46
	global_load_dwordx4 v[84:87], v45, s[0:1]
	v_lshl_or_b32 v45, v44, 7, v165
	v_lshl_or_b32 v51, v44, 5, v248
	s_waitcnt lgkmcnt(0)
	v_add_u32_e32 v44, s44, v47
	global_load_dwordx4 v[80:83], v45, s[0:1]
	v_lshl_or_b32 v45, v44, 7, v165
	v_lshl_or_b32 v56, v44, 5, v248
	ds_read_u16 v44, v93 offset:16576
	global_load_dwordx4 v[76:79], v45, s[0:1]
	v_dot4c_i32_i8_e32 v48, 0x1010101, v36
	v_dot4c_i32_i8_e32 v48, 0x1010101, v37
	v_dot4c_i32_i8_e32 v48, 0x1010101, v38
	s_waitcnt lgkmcnt(0)
	v_add_u32_e32 v44, s44, v44
	v_lshl_or_b32 v45, v44, 7, v165
	v_lshl_or_b32 v57, v44, 5, v248
	ds_read_u16 v44, v93 offset:16592
	global_load_dwordx4 v[68:71], v45, s[0:1]
	v_dot4c_i32_i8_e32 v48, 0x1010101, v39
	v_dot4c_i32_i8_e32 v48, 0x1010101, v32
	v_dot4c_i32_i8_e32 v48, 0x1010101, v33
	s_waitcnt lgkmcnt(0)
	v_add_u32_e32 v44, s44, v44
	v_lshl_or_b32 v45, v44, 7, v165
	v_lshl_or_b32 v58, v44, 5, v248
	ds_read_u16 v44, v93 offset:16608
	global_load_dwordx4 v[60:63], v45, s[0:1]
	v_dot4c_i32_i8_e32 v48, 0x1010101, v34
	v_dot4c_i32_i8_e32 v48, 0x1010101, v35
	s_add_i32 s45, s44, 0x4000
	s_waitcnt lgkmcnt(0)
	v_add_u32_e32 v44, s44, v44
	v_lshl_or_b32 v45, v44, 7, v165
	v_lshl_or_b32 v59, v44, 5, v248
	ds_read_u16 v44, v93 offset:16624
	global_load_dwordx4 v[52:55], v45, s[0:1]
	v_lshlrev_b32_e32 v171, 3, v48
	s_waitcnt vmcnt(14)
	v_and_b32_e32 v48, 0xf0f0f0f, v28
	v_lshrrev_b32_e32 v28, 4, v28
	s_waitcnt lgkmcnt(0)
	v_add_u32_e32 v64, s44, v44
	v_lshl_or_b32 v44, v64, 7, v165
	global_load_dwordx4 v[44:47], v44, s[0:1]
	v_lshl_or_b32 v64, v64, 5, v248
	global_load_dword v193, v50, s[46:47]
	global_load_dword v192, v49, s[46:47]
	global_load_dword v195, v56, s[46:47]
	global_load_dword v194, v51, s[46:47]
	global_load_dword v197, v58, s[46:47]
	global_load_dword v196, v57, s[46:47]
	global_load_dword v199, v64, s[46:47]
	global_load_dword v198, v59, s[46:47]
	v_mov_b32_e32 v49, 0
	v_dot4c_i32_i8_e32 v49, v48, v36
	v_and_b32_e32 v28, 0xf0f0f0f, v28
	v_dot4c_i32_i8_e32 v49, v28, v37
	v_and_b32_e32 v28, 0xf0f0f0f, v29
	v_mov_b32_e32 v48, 0
	v_dot4c_i32_i8_e32 v48, v28, v38
	v_lshrrev_b32_e32 v28, 4, v29
	v_and_b32_e32 v28, 0xf0f0f0f, v28
	v_dot4c_i32_i8_e32 v48, v28, v39
	v_and_b32_e32 v28, 0xf0f0f0f, v30
	v_dot4c_i32_i8_e32 v49, v28, v32
	v_lshrrev_b32_e32 v28, 4, v30
	v_and_b32_e32 v28, 0xf0f0f0f, v28
	v_dot4c_i32_i8_e32 v49, v28, v33
	v_and_b32_e32 v28, 0xf0f0f0f, v31
	v_dot4c_i32_i8_e32 v48, v28, v34
	v_lshrrev_b32_e32 v28, 4, v31
	v_and_b32_e32 v28, 0xf0f0f0f, v28
	v_dot4c_i32_i8_e32 v48, v28, v35
	s_waitcnt vmcnt(22)
	v_and_b32_e32 v28, 0xf0f0f0f, v24
	v_mov_b32_e32 v29, 0
	v_lshrrev_b32_e32 v24, 4, v24
	v_dot4c_i32_i8_e32 v29, v28, v36
	v_and_b32_e32 v24, 0xf0f0f0f, v24
	v_dot4c_i32_i8_e32 v29, v24, v37
	v_and_b32_e32 v24, 0xf0f0f0f, v25
	v_mov_b32_e32 v28, 0
	v_dot4c_i32_i8_e32 v28, v24, v38
	v_lshrrev_b32_e32 v24, 4, v25
	v_and_b32_e32 v24, 0xf0f0f0f, v24
	v_dot4c_i32_i8_e32 v28, v24, v39
	v_and_b32_e32 v24, 0xf0f0f0f, v26
	v_dot4c_i32_i8_e32 v29, v24, v32
	v_lshrrev_b32_e32 v24, 4, v26
	v_and_b32_e32 v24, 0xf0f0f0f, v24
	v_dot4c_i32_i8_e32 v29, v24, v33
	v_and_b32_e32 v24, 0xf0f0f0f, v27
	v_dot4c_i32_i8_e32 v28, v24, v34
	v_lshrrev_b32_e32 v24, 4, v27
	v_and_b32_e32 v24, 0xf0f0f0f, v24
	v_dot4c_i32_i8_e32 v28, v24, v35
	v_add_u32_e32 v26, v49, v48
	v_sub_u32_e32 v26, v26, v171
	v_and_b32_e32 v25, 0xffff0000, v43
	v_add_u32_e32 v27, v29, v28
	v_sub_u32_e32 v28, v27, v171
	v_cvt_f32_i32_e32 v27, v26
	v_cvt_f32_i32_e32 v26, v28
	v_lshlrev_b32_e32 v24, 16, v43
	s_cmp_eq_u32 s44, 0x3c000
	v_pk_fma_f32 v[158:159], v[24:25], v[26:27], v[158:159]
	s_waitcnt vmcnt(21)
	v_and_b32_e32 v24, 0xf0f0f0f, v20
	v_mov_b32_e32 v25, 0
	v_lshrrev_b32_e32 v20, 4, v20
	v_dot4c_i32_i8_e32 v25, v24, v36
	v_and_b32_e32 v20, 0xf0f0f0f, v20
	v_dot4c_i32_i8_e32 v25, v20, v37
	v_and_b32_e32 v20, 0xf0f0f0f, v21
	v_mov_b32_e32 v24, 0
	v_dot4c_i32_i8_e32 v24, v20, v38
	v_lshrrev_b32_e32 v20, 4, v21
	v_and_b32_e32 v20, 0xf0f0f0f, v20
	v_dot4c_i32_i8_e32 v24, v20, v39
	v_and_b32_e32 v20, 0xf0f0f0f, v22
	v_dot4c_i32_i8_e32 v25, v20, v32
	v_lshrrev_b32_e32 v20, 4, v22
	v_and_b32_e32 v20, 0xf0f0f0f, v20
	v_dot4c_i32_i8_e32 v25, v20, v33
	v_and_b32_e32 v20, 0xf0f0f0f, v23
	v_dot4c_i32_i8_e32 v24, v20, v34
	v_lshrrev_b32_e32 v20, 4, v23
	v_and_b32_e32 v20, 0xf0f0f0f, v20
	v_dot4c_i32_i8_e32 v24, v20, v35
	s_waitcnt vmcnt(20)
	v_and_b32_e32 v20, 0xf0f0f0f, v16
	v_mov_b32_e32 v21, 0
	v_lshrrev_b32_e32 v16, 4, v16
	v_dot4c_i32_i8_e32 v21, v20, v36
	v_and_b32_e32 v16, 0xf0f0f0f, v16
	v_dot4c_i32_i8_e32 v21, v16, v37
	v_and_b32_e32 v16, 0xf0f0f0f, v17
	v_mov_b32_e32 v20, 0
	v_dot4c_i32_i8_e32 v20, v16, v38
	v_lshrrev_b32_e32 v16, 4, v17
	v_and_b32_e32 v16, 0xf0f0f0f, v16
	v_dot4c_i32_i8_e32 v20, v16, v39
	v_and_b32_e32 v16, 0xf0f0f0f, v18
	v_dot4c_i32_i8_e32 v21, v16, v32
	v_lshrrev_b32_e32 v16, 4, v18
	v_and_b32_e32 v16, 0xf0f0f0f, v16
	v_dot4c_i32_i8_e32 v21, v16, v33
	v_and_b32_e32 v16, 0xf0f0f0f, v19
	v_dot4c_i32_i8_e32 v20, v16, v34
	v_lshrrev_b32_e32 v16, 4, v19
	v_and_b32_e32 v16, 0xf0f0f0f, v16
	v_dot4c_i32_i8_e32 v20, v16, v35
	v_add_u32_e32 v18, v25, v24
	v_sub_u32_e32 v18, v18, v171
	v_and_b32_e32 v17, 0xffff0000, v42
	v_add_u32_e32 v19, v21, v20
	v_sub_u32_e32 v20, v19, v171
	v_cvt_f32_i32_e32 v19, v18
	v_cvt_f32_i32_e32 v18, v20
	v_lshlrev_b32_e32 v16, 16, v42
	v_pk_fma_f32 v[156:157], v[16:17], v[18:19], v[156:157]
	s_waitcnt vmcnt(19)
	v_and_b32_e32 v16, 0xf0f0f0f, v12
	v_mov_b32_e32 v17, 0
	v_lshrrev_b32_e32 v12, 4, v12
	v_dot4c_i32_i8_e32 v17, v16, v36
	v_and_b32_e32 v12, 0xf0f0f0f, v12
	v_dot4c_i32_i8_e32 v17, v12, v37
	v_and_b32_e32 v12, 0xf0f0f0f, v13
	v_mov_b32_e32 v16, 0
	v_dot4c_i32_i8_e32 v16, v12, v38
	v_lshrrev_b32_e32 v12, 4, v13
	v_and_b32_e32 v12, 0xf0f0f0f, v12
	v_dot4c_i32_i8_e32 v16, v12, v39
	v_and_b32_e32 v12, 0xf0f0f0f, v14
	v_dot4c_i32_i8_e32 v17, v12, v32
	v_lshrrev_b32_e32 v12, 4, v14
	v_and_b32_e32 v12, 0xf0f0f0f, v12
	v_dot4c_i32_i8_e32 v17, v12, v33
	v_and_b32_e32 v12, 0xf0f0f0f, v15
	v_dot4c_i32_i8_e32 v16, v12, v34
	v_lshrrev_b32_e32 v12, 4, v15
	v_and_b32_e32 v12, 0xf0f0f0f, v12
	v_dot4c_i32_i8_e32 v16, v12, v35
	s_waitcnt vmcnt(18)
	v_and_b32_e32 v12, 0xf0f0f0f, v8
	v_mov_b32_e32 v13, 0
	v_lshrrev_b32_e32 v8, 4, v8
	v_dot4c_i32_i8_e32 v13, v12, v36
	v_and_b32_e32 v8, 0xf0f0f0f, v8
	v_dot4c_i32_i8_e32 v13, v8, v37
	v_and_b32_e32 v8, 0xf0f0f0f, v9
	v_mov_b32_e32 v12, 0
	v_dot4c_i32_i8_e32 v12, v8, v38
	v_lshrrev_b32_e32 v8, 4, v9
	v_and_b32_e32 v8, 0xf0f0f0f, v8
	v_dot4c_i32_i8_e32 v12, v8, v39
	v_and_b32_e32 v8, 0xf0f0f0f, v10
	v_dot4c_i32_i8_e32 v13, v8, v32
	v_lshrrev_b32_e32 v8, 4, v10
	v_and_b32_e32 v8, 0xf0f0f0f, v8
	v_dot4c_i32_i8_e32 v13, v8, v33
	v_and_b32_e32 v8, 0xf0f0f0f, v11
	v_dot4c_i32_i8_e32 v12, v8, v34
	v_lshrrev_b32_e32 v8, 4, v11
	v_and_b32_e32 v8, 0xf0f0f0f, v8
	v_dot4c_i32_i8_e32 v12, v8, v35
	v_add_u32_e32 v10, v17, v16
	v_sub_u32_e32 v10, v10, v171
	v_and_b32_e32 v9, 0xffff0000, v41
	v_add_u32_e32 v11, v13, v12
	v_sub_u32_e32 v12, v11, v171
	v_cvt_f32_i32_e32 v11, v10
	v_cvt_f32_i32_e32 v10, v12
	v_lshlrev_b32_e32 v8, 16, v41
	v_pk_fma_f32 v[154:155], v[8:9], v[10:11], v[154:155]
	s_waitcnt vmcnt(17)
	v_and_b32_e32 v8, 0xf0f0f0f, v4
	v_mov_b32_e32 v9, 0
	v_lshrrev_b32_e32 v4, 4, v4
	v_dot4c_i32_i8_e32 v9, v8, v36
	v_and_b32_e32 v4, 0xf0f0f0f, v4
	v_dot4c_i32_i8_e32 v9, v4, v37
	v_and_b32_e32 v4, 0xf0f0f0f, v5
	v_mov_b32_e32 v8, 0
	v_dot4c_i32_i8_e32 v8, v4, v38
	v_lshrrev_b32_e32 v4, 4, v5
	v_and_b32_e32 v4, 0xf0f0f0f, v4
	v_dot4c_i32_i8_e32 v8, v4, v39
	v_and_b32_e32 v4, 0xf0f0f0f, v6
	v_dot4c_i32_i8_e32 v9, v4, v32
	v_lshrrev_b32_e32 v4, 4, v6
	v_and_b32_e32 v4, 0xf0f0f0f, v4
	v_dot4c_i32_i8_e32 v9, v4, v33
	v_and_b32_e32 v4, 0xf0f0f0f, v7
	v_dot4c_i32_i8_e32 v8, v4, v34
	v_lshrrev_b32_e32 v4, 4, v7
	v_and_b32_e32 v4, 0xf0f0f0f, v4
	v_dot4c_i32_i8_e32 v8, v4, v35
	s_waitcnt vmcnt(16)
	v_and_b32_e32 v4, 0xf0f0f0f, v0
	v_mov_b32_e32 v5, 0
	v_lshrrev_b32_e32 v0, 4, v0
	v_dot4c_i32_i8_e32 v5, v4, v36
	v_and_b32_e32 v0, 0xf0f0f0f, v0
	v_dot4c_i32_i8_e32 v5, v0, v37
	v_and_b32_e32 v0, 0xf0f0f0f, v1
	v_mov_b32_e32 v4, 0
	v_dot4c_i32_i8_e32 v4, v0, v38
	v_lshrrev_b32_e32 v0, 4, v1
	v_and_b32_e32 v0, 0xf0f0f0f, v0
	v_dot4c_i32_i8_e32 v4, v0, v39
	v_and_b32_e32 v0, 0xf0f0f0f, v2
	v_dot4c_i32_i8_e32 v5, v0, v32
	v_lshrrev_b32_e32 v0, 4, v2
	v_and_b32_e32 v0, 0xf0f0f0f, v0
	v_dot4c_i32_i8_e32 v5, v0, v33
	v_and_b32_e32 v0, 0xf0f0f0f, v3
	v_dot4c_i32_i8_e32 v4, v0, v34
	v_lshrrev_b32_e32 v0, 4, v3
	v_and_b32_e32 v0, 0xf0f0f0f, v0
	v_dot4c_i32_i8_e32 v4, v0, v35
	v_add_u32_e32 v2, v9, v8
	v_sub_u32_e32 v2, v2, v171
	v_and_b32_e32 v1, 0xffff0000, v40
	v_add_u32_e32 v3, v5, v4
	v_sub_u32_e32 v4, v3, v171
	v_cvt_f32_i32_e32 v3, v2
	v_cvt_f32_i32_e32 v2, v4
	v_lshlrev_b32_e32 v0, 16, v40
	v_pk_fma_f32 v[152:153], v[0:1], v[2:3], v[152:153]
	ds_read_u16 v0, v93 offset:16640
	ds_read_u16 v1, v93 offset:16656
	ds_read_u16 v2, v93 offset:16672
	ds_read_u16 v3, v93 offset:16688
	s_waitcnt lgkmcnt(3)
	v_add_u32_e32 v0, s44, v0
	v_lshl_or_b32 v4, v0, 7, v165
	s_waitcnt lgkmcnt(2)
	v_add_u32_e32 v1, s44, v1
	global_load_dwordx4 v[72:75], v4, s[0:1]
	v_lshl_or_b32 v4, v1, 7, v165
	s_waitcnt lgkmcnt(1)
	v_add_u32_e32 v2, s44, v2
	global_load_dwordx4 v[64:67], v4, s[0:1]
	v_lshl_or_b32 v4, v2, 7, v165
	s_waitcnt lgkmcnt(0)
	v_add_u32_e32 v3, s44, v3
	global_load_dwordx4 v[56:59], v4, s[0:1]
	v_lshl_or_b32 v4, v3, 7, v165
	global_load_dwordx4 v[48:51], v4, s[0:1]
	ds_read_u16 v4, v93 offset:16704
	v_lshl_or_b32 v0, v0, 5, v248
	v_lshl_or_b32 v1, v1, 5, v248
	v_lshl_or_b32 v2, v2, 5, v248
	v_lshl_or_b32 v3, v3, 5, v248
	s_waitcnt lgkmcnt(0)
	v_add_u32_e32 v4, s44, v4
	v_lshl_or_b32 v5, v4, 7, v165
	global_load_dwordx4 v[40:43], v5, s[0:1]
	ds_read_u16 v5, v93 offset:16720
	v_lshl_or_b32 v4, v4, 5, v248
	s_waitcnt lgkmcnt(0)
	v_add_u32_e32 v5, s44, v5
	v_lshl_or_b32 v6, v5, 7, v165
	global_load_dwordx4 v[24:27], v6, s[0:1]
	ds_read_u16 v6, v93 offset:16736
	v_lshl_or_b32 v5, v5, 5, v248
	s_waitcnt lgkmcnt(0)
	v_add_u32_e32 v6, s44, v6
	v_lshl_or_b32 v7, v6, 7, v165
	global_load_dwordx4 v[12:15], v7, s[0:1]
	ds_read_u16 v7, v93 offset:16752
	v_lshl_or_b32 v6, v6, 5, v248
	s_waitcnt lgkmcnt(0)
	v_add_u32_e32 v7, s44, v7
	v_lshl_or_b32 v8, v7, 7, v165
	global_load_dwordx4 v[8:11], v8, s[0:1]
	v_lshl_or_b32 v7, v7, 5, v248
	global_load_dword v201, v1, s[46:47]
	global_load_dword v200, v0, s[46:47]
	global_load_dword v203, v3, s[46:47]
	global_load_dword v202, v2, s[46:47]
	global_load_dword v205, v5, s[46:47]
	global_load_dword v204, v4, s[46:47]
	global_load_dword v207, v7, s[46:47]
	global_load_dword v206, v6, s[46:47]
	s_waitcnt vmcnt(31)
	v_and_b32_e32 v0, 0xf0f0f0f, v88
	v_mov_b32_e32 v2, 0
	v_dot4c_i32_i8_e32 v2, v0, v36
	v_lshrrev_b32_e32 v0, 4, v88
	v_and_b32_e32 v0, 0xf0f0f0f, v0
	v_dot4c_i32_i8_e32 v2, v0, v37
	v_and_b32_e32 v0, 0xf0f0f0f, v89
	v_mov_b32_e32 v3, 0
	v_dot4c_i32_i8_e32 v3, v0, v38
	v_lshrrev_b32_e32 v0, 4, v89
	v_and_b32_e32 v0, 0xf0f0f0f, v0
	v_dot4c_i32_i8_e32 v3, v0, v39
	v_and_b32_e32 v0, 0xf0f0f0f, v90
	v_dot4c_i32_i8_e32 v2, v0, v32
	v_lshrrev_b32_e32 v0, 4, v90
	v_and_b32_e32 v0, 0xf0f0f0f, v0
	v_dot4c_i32_i8_e32 v2, v0, v33
	v_and_b32_e32 v0, 0xf0f0f0f, v91
	v_dot4c_i32_i8_e32 v3, v0, v34
	v_lshrrev_b32_e32 v0, 4, v91
	v_and_b32_e32 v0, 0xf0f0f0f, v0
	v_dot4c_i32_i8_e32 v3, v0, v35
	s_waitcnt vmcnt(30)
	v_and_b32_e32 v0, 0xf0f0f0f, v84
	v_mov_b32_e32 v4, 0
	v_dot4c_i32_i8_e32 v4, v0, v36
	v_lshrrev_b32_e32 v0, 4, v84
	v_and_b32_e32 v0, 0xf0f0f0f, v0
	v_dot4c_i32_i8_e32 v4, v0, v37
	v_and_b32_e32 v0, 0xf0f0f0f, v85
	v_mov_b32_e32 v5, 0
	v_dot4c_i32_i8_e32 v5, v0, v38
	v_lshrrev_b32_e32 v0, 4, v85
	v_and_b32_e32 v0, 0xf0f0f0f, v0
	v_dot4c_i32_i8_e32 v5, v0, v39
	v_and_b32_e32 v0, 0xf0f0f0f, v86
	v_dot4c_i32_i8_e32 v4, v0, v32
	v_lshrrev_b32_e32 v0, 4, v86
	v_and_b32_e32 v0, 0xf0f0f0f, v0
	v_dot4c_i32_i8_e32 v4, v0, v33
	v_and_b32_e32 v0, 0xf0f0f0f, v87
	v_dot4c_i32_i8_e32 v5, v0, v34
	v_lshrrev_b32_e32 v0, 4, v87
	v_and_b32_e32 v0, 0xf0f0f0f, v0
	v_dot4c_i32_i8_e32 v5, v0, v35
	v_add_u32_e32 v2, v2, v3
	v_sub_u32_e32 v2, v2, v171
	s_waitcnt vmcnt(22)
	v_lshlrev_b32_e32 v1, 16, v192
	v_sub_u32_e32 v3, v5, v171
	v_add_u32_e32 v4, v3, v4
	v_cvt_f32_i32_e32 v3, v2
	v_cvt_f32_i32_e32 v2, v4
	v_lshlrev_b32_e32 v0, 16, v193
	v_mov_b32_e32 v4, 0
	v_mov_b32_e32 v5, 0
	v_pk_fma_f32 v[150:151], v[0:1], v[2:3], v[150:151]
	v_and_b32_e32 v0, 0xf0f0f0f, v80
	v_mov_b32_e32 v2, 0
	v_dot4c_i32_i8_e32 v2, v0, v36
	v_lshrrev_b32_e32 v0, 4, v80
	v_and_b32_e32 v0, 0xf0f0f0f, v0
	v_dot4c_i32_i8_e32 v2, v0, v37
	v_and_b32_e32 v0, 0xf0f0f0f, v81
	v_mov_b32_e32 v3, 0
	v_dot4c_i32_i8_e32 v3, v0, v38
	v_lshrrev_b32_e32 v0, 4, v81
	v_and_b32_e32 v0, 0xf0f0f0f, v0
	v_dot4c_i32_i8_e32 v3, v0, v39
	v_and_b32_e32 v0, 0xf0f0f0f, v82
	v_dot4c_i32_i8_e32 v2, v0, v32
	v_lshrrev_b32_e32 v0, 4, v82
	v_and_b32_e32 v0, 0xf0f0f0f, v0
	v_dot4c_i32_i8_e32 v2, v0, v33
	v_and_b32_e32 v0, 0xf0f0f0f, v83
	v_dot4c_i32_i8_e32 v3, v0, v34
	v_lshrrev_b32_e32 v0, 4, v83
	v_and_b32_e32 v0, 0xf0f0f0f, v0
	v_dot4c_i32_i8_e32 v3, v0, v35
	v_and_b32_e32 v0, 0xf0f0f0f, v76
	v_dot4c_i32_i8_e32 v4, v0, v36
	v_lshrrev_b32_e32 v0, 4, v76
	v_and_b32_e32 v0, 0xf0f0f0f, v0
	v_dot4c_i32_i8_e32 v4, v0, v37
	v_and_b32_e32 v0, 0xf0f0f0f, v77
	v_dot4c_i32_i8_e32 v5, v0, v38
	v_lshrrev_b32_e32 v0, 4, v77
	v_and_b32_e32 v0, 0xf0f0f0f, v0
	v_dot4c_i32_i8_e32 v5, v0, v39
	v_and_b32_e32 v0, 0xf0f0f0f, v78
	v_dot4c_i32_i8_e32 v4, v0, v32
	v_lshrrev_b32_e32 v0, 4, v78
	v_and_b32_e32 v0, 0xf0f0f0f, v0
	v_dot4c_i32_i8_e32 v4, v0, v33
	v_and_b32_e32 v0, 0xf0f0f0f, v79
	v_dot4c_i32_i8_e32 v5, v0, v34
	v_lshrrev_b32_e32 v0, 4, v79
	v_and_b32_e32 v0, 0xf0f0f0f, v0
	v_dot4c_i32_i8_e32 v5, v0, v35
	v_sub_u32_e32 v3, v3, v171
	v_add_u32_e32 v2, v3, v2
	v_cvt_f32_i32_e32 v3, v2
	v_sub_u32_e32 v5, v5, v171
	v_add_u32_e32 v4, v5, v4
	v_cvt_f32_i32_e32 v2, v4
	s_waitcnt vmcnt(20)
	v_lshlrev_b32_e32 v1, 16, v194
	v_lshlrev_b32_e32 v0, 16, v195
	v_mov_b32_e32 v4, 0
	v_pk_fma_f32 v[148:149], v[0:1], v[2:3], v[148:149]
	v_and_b32_e32 v0, 0xf0f0f0f, v68
	v_mov_b32_e32 v2, 0
	v_dot4c_i32_i8_e32 v2, v0, v36
	v_lshrrev_b32_e32 v0, 4, v68
	v_and_b32_e32 v0, 0xf0f0f0f, v0
	v_dot4c_i32_i8_e32 v2, v0, v37
	v_and_b32_e32 v0, 0xf0f0f0f, v69
	v_mov_b32_e32 v3, 0
	v_dot4c_i32_i8_e32 v3, v0, v38
	v_lshrrev_b32_e32 v0, 4, v69
	v_and_b32_e32 v0, 0xf0f0f0f, v0
	v_dot4c_i32_i8_e32 v3, v0, v39
	v_and_b32_e32 v0, 0xf0f0f0f, v70
	v_dot4c_i32_i8_e32 v2, v0, v32
	v_lshrrev_b32_e32 v0, 4, v70
	v_and_b32_e32 v0, 0xf0f0f0f, v0
	v_dot4c_i32_i8_e32 v2, v0, v33
	v_and_b32_e32 v0, 0xf0f0f0f, v71
	v_dot4c_i32_i8_e32 v3, v0, v34
	v_lshrrev_b32_e32 v0, 4, v71
	v_and_b32_e32 v0, 0xf0f0f0f, v0
	v_dot4c_i32_i8_e32 v3, v0, v35
	v_and_b32_e32 v0, 0xf0f0f0f, v60
	v_dot4c_i32_i8_e32 v4, v0, v36
	v_lshrrev_b32_e32 v0, 4, v60
	v_and_b32_e32 v0, 0xf0f0f0f, v0
	v_dot4c_i32_i8_e32 v4, v0, v37
	v_and_b32_e32 v0, 0xf0f0f0f, v61
	v_mov_b32_e32 v5, 0
	v_dot4c_i32_i8_e32 v5, v0, v38
	v_lshrrev_b32_e32 v0, 4, v61
	v_and_b32_e32 v0, 0xf0f0f0f, v0
	v_dot4c_i32_i8_e32 v5, v0, v39
	v_and_b32_e32 v0, 0xf0f0f0f, v62
	v_dot4c_i32_i8_e32 v4, v0, v32
	v_lshrrev_b32_e32 v0, 4, v62
	v_and_b32_e32 v0, 0xf0f0f0f, v0
	v_dot4c_i32_i8_e32 v4, v0, v33
	v_and_b32_e32 v0, 0xf0f0f0f, v63
	v_dot4c_i32_i8_e32 v5, v0, v34
	v_lshrrev_b32_e32 v0, 4, v63
	v_and_b32_e32 v0, 0xf0f0f0f, v0
	v_dot4c_i32_i8_e32 v5, v0, v35
	v_sub_u32_e32 v3, v3, v171
	v_add_u32_e32 v2, v3, v2
	v_cvt_f32_i32_e32 v3, v2
	v_sub_u32_e32 v5, v5, v171
	v_add_u32_e32 v4, v5, v4
	v_cvt_f32_i32_e32 v2, v4
	s_waitcnt vmcnt(18)
	v_lshlrev_b32_e32 v1, 16, v196
	v_lshlrev_b32_e32 v0, 16, v197
	v_mov_b32_e32 v4, 0
	v_pk_fma_f32 v[146:147], v[0:1], v[2:3], v[146:147]
	v_and_b32_e32 v0, 0xf0f0f0f, v52
	v_mov_b32_e32 v2, 0
	v_dot4c_i32_i8_e32 v2, v0, v36
	v_lshrrev_b32_e32 v0, 4, v52
	v_and_b32_e32 v0, 0xf0f0f0f, v0
	v_dot4c_i32_i8_e32 v2, v0, v37
	v_and_b32_e32 v0, 0xf0f0f0f, v53
	v_mov_b32_e32 v3, 0
	v_dot4c_i32_i8_e32 v3, v0, v38
	v_lshrrev_b32_e32 v0, 4, v53
	v_and_b32_e32 v0, 0xf0f0f0f, v0
	v_dot4c_i32_i8_e32 v3, v0, v39
	v_and_b32_e32 v0, 0xf0f0f0f, v54
	v_dot4c_i32_i8_e32 v2, v0, v32
	v_lshrrev_b32_e32 v0, 4, v54
	v_and_b32_e32 v0, 0xf0f0f0f, v0
	v_dot4c_i32_i8_e32 v2, v0, v33
	v_and_b32_e32 v0, 0xf0f0f0f, v55
	v_dot4c_i32_i8_e32 v3, v0, v34
	v_lshrrev_b32_e32 v0, 4, v55
	v_and_b32_e32 v0, 0xf0f0f0f, v0
	v_dot4c_i32_i8_e32 v3, v0, v35
	v_and_b32_e32 v0, 0xf0f0f0f, v44
	v_dot4c_i32_i8_e32 v4, v0, v36
	v_lshrrev_b32_e32 v0, 4, v44
	v_and_b32_e32 v0, 0xf0f0f0f, v0
	v_dot4c_i32_i8_e32 v4, v0, v37
	v_and_b32_e32 v0, 0xf0f0f0f, v45
	v_mov_b32_e32 v5, 0
	v_dot4c_i32_i8_e32 v5, v0, v38
	v_lshrrev_b32_e32 v0, 4, v45
	v_and_b32_e32 v0, 0xf0f0f0f, v0
	v_dot4c_i32_i8_e32 v5, v0, v39
	v_and_b32_e32 v0, 0xf0f0f0f, v46
	v_dot4c_i32_i8_e32 v4, v0, v32
	v_lshrrev_b32_e32 v0, 4, v46
	v_and_b32_e32 v0, 0xf0f0f0f, v0
	v_dot4c_i32_i8_e32 v4, v0, v33
	v_and_b32_e32 v0, 0xf0f0f0f, v47
	v_dot4c_i32_i8_e32 v5, v0, v34
	v_lshrrev_b32_e32 v0, 4, v47
	v_and_b32_e32 v0, 0xf0f0f0f, v0
	v_dot4c_i32_i8_e32 v5, v0, v35
	v_sub_u32_e32 v3, v3, v171
	v_add_u32_e32 v2, v3, v2
	v_cvt_f32_i32_e32 v3, v2
	v_sub_u32_e32 v5, v5, v171
	v_add_u32_e32 v4, v5, v4
	v_cvt_f32_i32_e32 v2, v4
	s_waitcnt vmcnt(16)
	v_lshlrev_b32_e32 v1, 16, v198
	v_lshlrev_b32_e32 v0, 16, v199
	v_pk_fma_f32 v[144:145], v[0:1], v[2:3], v[144:145]
	ds_read_b128 v[4:7], v166 offset:4096
	ds_read_b128 v[0:3], v166 offset:4112
	ds_read_u16 v16, v93 offset:16768
	ds_read_u16 v17, v93 offset:16784
	ds_read_u16 v18, v93 offset:16800
	ds_read_u16 v19, v93 offset:16816
	v_mov_b32_e32 v44, 0
	s_waitcnt lgkmcnt(3)
	v_add_u32_e32 v16, s44, v16
	v_lshl_or_b32 v20, v16, 7, v165
	v_lshl_or_b32 v45, v16, 5, v248
	s_waitcnt lgkmcnt(2)
	v_add_u32_e32 v16, s44, v17
	v_lshl_or_b32 v17, v16, 7, v165
	v_lshl_or_b32 v46, v16, 5, v248
	s_waitcnt lgkmcnt(1)
	v_add_u32_e32 v16, s44, v18
	global_load_dwordx4 v[80:83], v20, s[0:1]
	global_load_dwordx4 v[68:71], v17, s[0:1]
	v_lshl_or_b32 v17, v16, 7, v165
	v_lshl_or_b32 v47, v16, 5, v248
	s_waitcnt lgkmcnt(0)
	v_add_u32_e32 v16, s44, v19
	global_load_dwordx4 v[52:55], v17, s[0:1]
	v_lshl_or_b32 v17, v16, 7, v165
	v_lshl_or_b32 v60, v16, 5, v248
	ds_read_u16 v16, v93 offset:16832
	global_load_dwordx4 v[36:39], v17, s[0:1]
	v_dot4c_i32_i8_e32 v44, 0x1010101, v4
	v_dot4c_i32_i8_e32 v44, 0x1010101, v5
	v_dot4c_i32_i8_e32 v44, 0x1010101, v6
	s_waitcnt lgkmcnt(0)
	v_add_u32_e32 v16, s44, v16
	v_lshl_or_b32 v17, v16, 7, v165
	v_lshl_or_b32 v61, v16, 5, v248
	ds_read_u16 v16, v93 offset:16848
	global_load_dwordx4 v[32:35], v17, s[0:1]
	v_dot4c_i32_i8_e32 v44, 0x1010101, v7
	v_dot4c_i32_i8_e32 v44, 0x1010101, v0
	v_dot4c_i32_i8_e32 v44, 0x1010101, v1
	s_waitcnt lgkmcnt(0)
	v_add_u32_e32 v16, s44, v16
	v_lshl_or_b32 v17, v16, 7, v165
	v_lshl_or_b32 v62, v16, 5, v248
	ds_read_u16 v16, v93 offset:16864
	global_load_dwordx4 v[28:31], v17, s[0:1]
	v_dot4c_i32_i8_e32 v44, 0x1010101, v2
	v_dot4c_i32_i8_e32 v44, 0x1010101, v3
	s_waitcnt lgkmcnt(0)
	v_add_u32_e32 v16, s44, v16
	v_lshl_or_b32 v17, v16, 7, v165
	v_lshl_or_b32 v63, v16, 5, v248
	ds_read_u16 v16, v93 offset:16880
	global_load_dwordx4 v[20:23], v17, s[0:1]
	v_lshlrev_b32_e32 v84, 3, v44
	s_waitcnt vmcnt(22)
	v_and_b32_e32 v44, 0xf0f0f0f, v72
	s_waitcnt lgkmcnt(0)
	v_add_u32_e32 v76, s44, v16
	v_lshl_or_b32 v16, v76, 7, v165
	global_load_dwordx4 v[16:19], v16, s[0:1]
	v_lshl_or_b32 v76, v76, 5, v248
	global_load_dword v209, v46, s[46:47]
	global_load_dword v208, v45, s[46:47]
	global_load_dword v211, v60, s[46:47]
	global_load_dword v210, v47, s[46:47]
	global_load_dword v213, v62, s[46:47]
	global_load_dword v212, v61, s[46:47]
	global_load_dword v215, v76, s[46:47]
	global_load_dword v214, v63, s[46:47]
	v_mov_b32_e32 v46, 0
	v_dot4c_i32_i8_e32 v46, v44, v4
	v_lshrrev_b32_e32 v44, 4, v72
	v_and_b32_e32 v44, 0xf0f0f0f, v44
	v_dot4c_i32_i8_e32 v46, v44, v5
	v_and_b32_e32 v44, 0xf0f0f0f, v73
	v_mov_b32_e32 v47, 0
	v_dot4c_i32_i8_e32 v47, v44, v6
	v_lshrrev_b32_e32 v44, 4, v73
	v_and_b32_e32 v44, 0xf0f0f0f, v44
	v_dot4c_i32_i8_e32 v47, v44, v7
	v_and_b32_e32 v44, 0xf0f0f0f, v74
	v_dot4c_i32_i8_e32 v46, v44, v0
	v_lshrrev_b32_e32 v44, 4, v74
	v_and_b32_e32 v44, 0xf0f0f0f, v44
	v_dot4c_i32_i8_e32 v46, v44, v1
	v_and_b32_e32 v44, 0xf0f0f0f, v75
	v_dot4c_i32_i8_e32 v47, v44, v2
	v_lshrrev_b32_e32 v44, 4, v75
	v_and_b32_e32 v44, 0xf0f0f0f, v44
	v_dot4c_i32_i8_e32 v47, v44, v3
	s_waitcnt vmcnt(30)
	v_and_b32_e32 v44, 0xf0f0f0f, v64
	v_mov_b32_e32 v60, 0
	v_dot4c_i32_i8_e32 v60, v44, v4
	v_lshrrev_b32_e32 v44, 4, v64
	v_and_b32_e32 v44, 0xf0f0f0f, v44
	v_dot4c_i32_i8_e32 v60, v44, v5
	v_and_b32_e32 v44, 0xf0f0f0f, v65
	v_mov_b32_e32 v61, 0
	v_dot4c_i32_i8_e32 v61, v44, v6
	v_lshrrev_b32_e32 v44, 4, v65
	v_and_b32_e32 v44, 0xf0f0f0f, v44
	v_dot4c_i32_i8_e32 v61, v44, v7
	v_and_b32_e32 v44, 0xf0f0f0f, v66
	v_dot4c_i32_i8_e32 v60, v44, v0
	v_lshrrev_b32_e32 v44, 4, v66
	v_and_b32_e32 v44, 0xf0f0f0f, v44
	v_dot4c_i32_i8_e32 v60, v44, v1
	v_and_b32_e32 v44, 0xf0f0f0f, v67
	v_dot4c_i32_i8_e32 v61, v44, v2
	v_lshrrev_b32_e32 v44, 4, v67
	v_and_b32_e32 v44, 0xf0f0f0f, v44
	v_dot4c_i32_i8_e32 v61, v44, v3
	v_add_u32_e32 v46, v46, v47
	v_sub_u32_e32 v46, v46, v84
	s_waitcnt vmcnt(22)
	v_lshlrev_b32_e32 v45, 16, v200
	v_add_u32_e32 v47, v60, v61
	v_sub_u32_e32 v60, v47, v84
	v_cvt_f32_i32_e32 v47, v46
	v_cvt_f32_i32_e32 v46, v60
	v_lshlrev_b32_e32 v44, 16, v201
	v_pk_fma_f32 v[142:143], v[44:45], v[46:47], v[142:143]
	v_and_b32_e32 v44, 0xf0f0f0f, v56
	v_mov_b32_e32 v46, 0
	v_dot4c_i32_i8_e32 v46, v44, v4
	v_lshrrev_b32_e32 v44, 4, v56
	v_and_b32_e32 v44, 0xf0f0f0f, v44
	v_dot4c_i32_i8_e32 v46, v44, v5
	v_and_b32_e32 v44, 0xf0f0f0f, v57
	v_mov_b32_e32 v47, 0
	v_dot4c_i32_i8_e32 v47, v44, v6
	v_lshrrev_b32_e32 v44, 4, v57
	v_and_b32_e32 v44, 0xf0f0f0f, v44
	v_dot4c_i32_i8_e32 v47, v44, v7
	v_and_b32_e32 v44, 0xf0f0f0f, v58
	v_dot4c_i32_i8_e32 v46, v44, v0
	v_lshrrev_b32_e32 v44, 4, v58
	v_and_b32_e32 v44, 0xf0f0f0f, v44
	v_dot4c_i32_i8_e32 v46, v44, v1
	v_and_b32_e32 v44, 0xf0f0f0f, v59
	v_dot4c_i32_i8_e32 v47, v44, v2
	v_lshrrev_b32_e32 v44, 4, v59
	v_and_b32_e32 v44, 0xf0f0f0f, v44
	v_dot4c_i32_i8_e32 v47, v44, v3
	v_and_b32_e32 v44, 0xf0f0f0f, v48
	v_mov_b32_e32 v56, 0
	v_dot4c_i32_i8_e32 v56, v44, v4
	v_lshrrev_b32_e32 v44, 4, v48
	v_and_b32_e32 v44, 0xf0f0f0f, v44
	v_dot4c_i32_i8_e32 v56, v44, v5
	v_and_b32_e32 v44, 0xf0f0f0f, v49
	v_mov_b32_e32 v48, 0
	v_dot4c_i32_i8_e32 v48, v44, v6
	v_lshrrev_b32_e32 v44, 4, v49
	v_and_b32_e32 v44, 0xf0f0f0f, v44
	v_dot4c_i32_i8_e32 v48, v44, v7
	v_and_b32_e32 v44, 0xf0f0f0f, v50
	v_dot4c_i32_i8_e32 v56, v44, v0
	v_lshrrev_b32_e32 v44, 4, v50
	v_and_b32_e32 v44, 0xf0f0f0f, v44
	v_dot4c_i32_i8_e32 v56, v44, v1
	v_and_b32_e32 v44, 0xf0f0f0f, v51
	v_dot4c_i32_i8_e32 v48, v44, v2
	v_lshrrev_b32_e32 v44, 4, v51
	v_and_b32_e32 v44, 0xf0f0f0f, v44
	v_dot4c_i32_i8_e32 v48, v44, v3
	v_add_u32_e32 v46, v46, v47
	v_sub_u32_e32 v46, v46, v84
	s_waitcnt vmcnt(20)
	v_lshlrev_b32_e32 v45, 16, v202
	v_add_u32_e32 v47, v56, v48
	v_sub_u32_e32 v48, v47, v84
	v_cvt_f32_i32_e32 v47, v46
	v_cvt_f32_i32_e32 v46, v48
	v_lshlrev_b32_e32 v44, 16, v203
	v_pk_fma_f32 v[140:141], v[44:45], v[46:47], v[140:141]
	v_and_b32_e32 v44, 0xf0f0f0f, v40
	v_mov_b32_e32 v45, 0
	v_lshrrev_b32_e32 v40, 4, v40
	v_dot4c_i32_i8_e32 v45, v44, v4
	v_and_b32_e32 v40, 0xf0f0f0f, v40
	v_dot4c_i32_i8_e32 v45, v40, v5
	v_and_b32_e32 v40, 0xf0f0f0f, v41
	v_mov_b32_e32 v44, 0
	v_dot4c_i32_i8_e32 v44, v40, v6
	v_lshrrev_b32_e32 v40, 4, v41
	v_and_b32_e32 v40, 0xf0f0f0f, v40
	v_dot4c_i32_i8_e32 v44, v40, v7
	v_and_b32_e32 v40, 0xf0f0f0f, v42
	v_dot4c_i32_i8_e32 v45, v40, v0
	v_lshrrev_b32_e32 v40, 4, v42
	v_and_b32_e32 v40, 0xf0f0f0f, v40
	v_dot4c_i32_i8_e32 v45, v40, v1
	v_and_b32_e32 v40, 0xf0f0f0f, v43
	v_dot4c_i32_i8_e32 v44, v40, v2
	v_lshrrev_b32_e32 v40, 4, v43
	v_and_b32_e32 v40, 0xf0f0f0f, v40
	v_dot4c_i32_i8_e32 v44, v40, v3
	v_and_b32_e32 v40, 0xf0f0f0f, v24
	v_mov_b32_e32 v41, 0
	v_lshrrev_b32_e32 v24, 4, v24
	v_dot4c_i32_i8_e32 v41, v40, v4
	v_and_b32_e32 v24, 0xf0f0f0f, v24
	v_dot4c_i32_i8_e32 v41, v24, v5
	v_and_b32_e32 v24, 0xf0f0f0f, v25
	v_mov_b32_e32 v40, 0
	v_dot4c_i32_i8_e32 v40, v24, v6
	v_lshrrev_b32_e32 v24, 4, v25
	v_and_b32_e32 v24, 0xf0f0f0f, v24
	v_dot4c_i32_i8_e32 v40, v24, v7
	v_and_b32_e32 v24, 0xf0f0f0f, v26
	v_dot4c_i32_i8_e32 v41, v24, v0
	v_lshrrev_b32_e32 v24, 4, v26
	v_and_b32_e32 v24, 0xf0f0f0f, v24
	v_dot4c_i32_i8_e32 v41, v24, v1
	v_and_b32_e32 v24, 0xf0f0f0f, v27
	v_dot4c_i32_i8_e32 v40, v24, v2
	v_lshrrev_b32_e32 v24, 4, v27
	v_and_b32_e32 v24, 0xf0f0f0f, v24
	v_dot4c_i32_i8_e32 v40, v24, v3
	v_add_u32_e32 v26, v45, v44
	v_sub_u32_e32 v26, v26, v84
	s_waitcnt vmcnt(18)
	v_lshlrev_b32_e32 v25, 16, v204
	v_add_u32_e32 v27, v41, v40
	v_sub_u32_e32 v40, v27, v84
	v_cvt_f32_i32_e32 v27, v26
	v_cvt_f32_i32_e32 v26, v40
	v_lshlrev_b32_e32 v24, 16, v205
	v_pk_fma_f32 v[138:139], v[24:25], v[26:27], v[138:139]
	v_and_b32_e32 v24, 0xf0f0f0f, v12
	v_mov_b32_e32 v25, 0
	v_lshrrev_b32_e32 v12, 4, v12
	v_dot4c_i32_i8_e32 v25, v24, v4
	v_and_b32_e32 v12, 0xf0f0f0f, v12
	v_dot4c_i32_i8_e32 v25, v12, v5
	v_and_b32_e32 v12, 0xf0f0f0f, v13
	v_mov_b32_e32 v24, 0
	v_dot4c_i32_i8_e32 v24, v12, v6
	v_lshrrev_b32_e32 v12, 4, v13
	v_and_b32_e32 v12, 0xf0f0f0f, v12
	v_dot4c_i32_i8_e32 v24, v12, v7
	v_and_b32_e32 v12, 0xf0f0f0f, v14
	v_dot4c_i32_i8_e32 v25, v12, v0
	v_lshrrev_b32_e32 v12, 4, v14
	v_and_b32_e32 v12, 0xf0f0f0f, v12
	v_dot4c_i32_i8_e32 v25, v12, v1
	v_and_b32_e32 v12, 0xf0f0f0f, v15
	v_dot4c_i32_i8_e32 v24, v12, v2
	v_lshrrev_b32_e32 v12, 4, v15
	v_and_b32_e32 v12, 0xf0f0f0f, v12
	v_dot4c_i32_i8_e32 v24, v12, v3
	v_and_b32_e32 v12, 0xf0f0f0f, v8
	v_mov_b32_e32 v13, 0
	v_lshrrev_b32_e32 v8, 4, v8
	v_dot4c_i32_i8_e32 v13, v12, v4
	v_and_b32_e32 v8, 0xf0f0f0f, v8
	v_dot4c_i32_i8_e32 v13, v8, v5
	v_and_b32_e32 v8, 0xf0f0f0f, v9
	v_mov_b32_e32 v12, 0
	v_dot4c_i32_i8_e32 v12, v8, v6
	v_lshrrev_b32_e32 v8, 4, v9
	v_and_b32_e32 v8, 0xf0f0f0f, v8
	v_dot4c_i32_i8_e32 v12, v8, v7
	v_and_b32_e32 v8, 0xf0f0f0f, v10
	v_dot4c_i32_i8_e32 v13, v8, v0
	v_lshrrev_b32_e32 v8, 4, v10
	v_and_b32_e32 v8, 0xf0f0f0f, v8
	v_dot4c_i32_i8_e32 v13, v8, v1
	v_and_b32_e32 v8, 0xf0f0f0f, v11
	v_dot4c_i32_i8_e32 v12, v8, v2
	v_lshrrev_b32_e32 v8, 4, v11
	v_and_b32_e32 v8, 0xf0f0f0f, v8
	v_dot4c_i32_i8_e32 v12, v8, v3
	v_add_u32_e32 v10, v25, v24
	v_sub_u32_e32 v10, v10, v84
	s_waitcnt vmcnt(16)
	v_lshlrev_b32_e32 v9, 16, v206
	v_add_u32_e32 v11, v13, v12
	v_sub_u32_e32 v12, v11, v84
	v_cvt_f32_i32_e32 v11, v10
	v_cvt_f32_i32_e32 v10, v12
	v_lshlrev_b32_e32 v8, 16, v207
	v_pk_fma_f32 v[136:137], v[8:9], v[10:11], v[136:137]
	ds_read_u16 v8, v93 offset:16896
	ds_read_u16 v9, v93 offset:16912
	ds_read_u16 v10, v93 offset:16928
	ds_read_u16 v11, v93 offset:16944
	s_waitcnt lgkmcnt(3)
	v_add_u32_e32 v8, s44, v8
	v_lshl_or_b32 v12, v8, 7, v165
	v_lshl_or_b32 v40, v8, 5, v248
	s_waitcnt lgkmcnt(2)
	v_add_u32_e32 v8, s44, v9
	v_lshl_or_b32 v9, v8, 7, v165
	v_lshl_or_b32 v41, v8, 5, v248
	s_waitcnt lgkmcnt(1)
	v_add_u32_e32 v8, s44, v10
	global_load_dwordx4 v[76:79], v12, s[0:1]
	global_load_dwordx4 v[72:75], v9, s[0:1]
	v_lshl_or_b32 v9, v8, 7, v165
	v_lshl_or_b32 v42, v8, 5, v248
	s_waitcnt lgkmcnt(0)
	v_add_u32_e32 v8, s44, v11
	global_load_dwordx4 v[60:63], v9, s[0:1]
	v_lshl_or_b32 v9, v8, 7, v165
	v_lshl_or_b32 v43, v8, 5, v248
	ds_read_u16 v8, v93 offset:16960
	global_load_dwordx4 v[56:59], v9, s[0:1]
	s_waitcnt lgkmcnt(0)
	v_add_u32_e32 v8, s44, v8
	v_lshl_or_b32 v9, v8, 7, v165
	v_lshl_or_b32 v48, v8, 5, v248
	ds_read_u16 v8, v93 offset:16976
	global_load_dwordx4 v[44:47], v9, s[0:1]
	s_waitcnt lgkmcnt(0)
	v_add_u32_e32 v8, s44, v8
	v_lshl_or_b32 v9, v8, 7, v165
	v_lshl_or_b32 v49, v8, 5, v248
	ds_read_u16 v8, v93 offset:16992
	global_load_dwordx4 v[24:27], v9, s[0:1]
	s_waitcnt lgkmcnt(0)
	v_add_u32_e32 v8, s44, v8
	v_lshl_or_b32 v9, v8, 7, v165
	v_lshl_or_b32 v50, v8, 5, v248
	ds_read_u16 v8, v93 offset:17008
	global_load_dwordx4 v[12:15], v9, s[0:1]
	s_waitcnt lgkmcnt(0)
	v_add_u32_e32 v51, s44, v8
	v_lshl_or_b32 v8, v51, 7, v165
	global_load_dwordx4 v[8:11], v8, s[0:1]
	v_lshl_or_b32 v51, v51, 5, v248
	global_load_dword v217, v41, s[46:47]
	global_load_dword v216, v40, s[46:47]
	global_load_dword v219, v43, s[46:47]
	global_load_dword v218, v42, s[46:47]
	global_load_dword v221, v49, s[46:47]
	global_load_dword v220, v48, s[46:47]
	global_load_dword v223, v51, s[46:47]
	global_load_dword v222, v50, s[46:47]
	s_waitcnt vmcnt(31)
	v_and_b32_e32 v40, 0xf0f0f0f, v80
	v_mov_b32_e32 v42, 0
	v_dot4c_i32_i8_e32 v42, v40, v4
	v_lshrrev_b32_e32 v40, 4, v80
	v_and_b32_e32 v40, 0xf0f0f0f, v40
	v_dot4c_i32_i8_e32 v42, v40, v5
	v_and_b32_e32 v40, 0xf0f0f0f, v81
	v_mov_b32_e32 v43, 0
	v_dot4c_i32_i8_e32 v43, v40, v6
	v_lshrrev_b32_e32 v40, 4, v81
	v_and_b32_e32 v40, 0xf0f0f0f, v40
	v_dot4c_i32_i8_e32 v43, v40, v7
	v_and_b32_e32 v40, 0xf0f0f0f, v82
	v_dot4c_i32_i8_e32 v42, v40, v0
	v_lshrrev_b32_e32 v40, 4, v82
	v_and_b32_e32 v40, 0xf0f0f0f, v40
	v_dot4c_i32_i8_e32 v42, v40, v1
	v_and_b32_e32 v40, 0xf0f0f0f, v83
	v_dot4c_i32_i8_e32 v43, v40, v2
	v_lshrrev_b32_e32 v40, 4, v83
	v_and_b32_e32 v40, 0xf0f0f0f, v40
	v_dot4c_i32_i8_e32 v43, v40, v3
	s_waitcnt vmcnt(30)
	v_and_b32_e32 v40, 0xf0f0f0f, v68
	v_mov_b32_e32 v48, 0
	v_dot4c_i32_i8_e32 v48, v40, v4
	v_lshrrev_b32_e32 v40, 4, v68
	v_and_b32_e32 v40, 0xf0f0f0f, v40
	v_dot4c_i32_i8_e32 v48, v40, v5
	v_and_b32_e32 v40, 0xf0f0f0f, v69
	v_mov_b32_e32 v49, 0
	v_dot4c_i32_i8_e32 v49, v40, v6
	v_lshrrev_b32_e32 v40, 4, v69
	v_and_b32_e32 v40, 0xf0f0f0f, v40
	v_dot4c_i32_i8_e32 v49, v40, v7
	v_and_b32_e32 v40, 0xf0f0f0f, v70
	v_dot4c_i32_i8_e32 v48, v40, v0
	v_lshrrev_b32_e32 v40, 4, v70
	v_and_b32_e32 v40, 0xf0f0f0f, v40
	v_dot4c_i32_i8_e32 v48, v40, v1
	v_and_b32_e32 v40, 0xf0f0f0f, v71
	v_dot4c_i32_i8_e32 v49, v40, v2
	v_lshrrev_b32_e32 v40, 4, v71
	v_and_b32_e32 v40, 0xf0f0f0f, v40
	v_dot4c_i32_i8_e32 v49, v40, v3
	v_add_u32_e32 v42, v42, v43
	v_sub_u32_e32 v42, v42, v84
	s_waitcnt vmcnt(22)
	v_lshlrev_b32_e32 v41, 16, v208
	v_sub_u32_e32 v43, v49, v84
	v_add_u32_e32 v48, v43, v48
	v_cvt_f32_i32_e32 v43, v42
	v_cvt_f32_i32_e32 v42, v48
	v_lshlrev_b32_e32 v40, 16, v209
	v_pk_fma_f32 v[134:135], v[40:41], v[42:43], v[134:135]
	v_and_b32_e32 v40, 0xf0f0f0f, v52
	v_mov_b32_e32 v41, 0
	v_dot4c_i32_i8_e32 v41, v40, v4
	v_lshrrev_b32_e32 v40, 4, v52
	v_and_b32_e32 v40, 0xf0f0f0f, v40
	v_dot4c_i32_i8_e32 v41, v40, v5
	v_and_b32_e32 v40, 0xf0f0f0f, v53
	v_mov_b32_e32 v42, 0
	v_dot4c_i32_i8_e32 v42, v40, v6
	v_lshrrev_b32_e32 v40, 4, v53
	v_and_b32_e32 v40, 0xf0f0f0f, v40
	v_dot4c_i32_i8_e32 v42, v40, v7
	v_and_b32_e32 v40, 0xf0f0f0f, v54
	v_dot4c_i32_i8_e32 v41, v40, v0
	v_lshrrev_b32_e32 v40, 4, v54
	v_and_b32_e32 v40, 0xf0f0f0f, v40
	v_dot4c_i32_i8_e32 v41, v40, v1
	v_and_b32_e32 v40, 0xf0f0f0f, v55
	v_dot4c_i32_i8_e32 v42, v40, v2
	v_lshrrev_b32_e32 v40, 4, v55
	v_and_b32_e32 v40, 0xf0f0f0f, v40
	v_dot4c_i32_i8_e32 v42, v40, v3
	v_and_b32_e32 v40, 0xf0f0f0f, v36
	v_mov_b32_e32 v43, 0
	v_lshrrev_b32_e32 v36, 4, v36
	v_dot4c_i32_i8_e32 v43, v40, v4
	v_and_b32_e32 v36, 0xf0f0f0f, v36
	v_dot4c_i32_i8_e32 v43, v36, v5
	v_and_b32_e32 v36, 0xf0f0f0f, v37
	v_mov_b32_e32 v40, 0
	v_dot4c_i32_i8_e32 v40, v36, v6
	v_lshrrev_b32_e32 v36, 4, v37
	v_and_b32_e32 v36, 0xf0f0f0f, v36
	v_dot4c_i32_i8_e32 v40, v36, v7
	v_and_b32_e32 v36, 0xf0f0f0f, v38
	v_dot4c_i32_i8_e32 v43, v36, v0
	v_lshrrev_b32_e32 v36, 4, v38
	v_and_b32_e32 v36, 0xf0f0f0f, v36
	v_dot4c_i32_i8_e32 v43, v36, v1
	v_and_b32_e32 v36, 0xf0f0f0f, v39
	v_dot4c_i32_i8_e32 v40, v36, v2
	v_lshrrev_b32_e32 v36, 4, v39
	v_and_b32_e32 v36, 0xf0f0f0f, v36
	v_dot4c_i32_i8_e32 v40, v36, v3
	v_sub_u32_e32 v38, v42, v84
	v_add_u32_e32 v38, v38, v41
	s_waitcnt vmcnt(20)
	v_lshlrev_b32_e32 v37, 16, v210
	v_sub_u32_e32 v39, v40, v84
	v_add_u32_e32 v40, v39, v43
	v_cvt_f32_i32_e32 v39, v38
	v_cvt_f32_i32_e32 v38, v40
	v_lshlrev_b32_e32 v36, 16, v211
	v_pk_fma_f32 v[132:133], v[36:37], v[38:39], v[132:133]
	v_and_b32_e32 v36, 0xf0f0f0f, v32
	v_mov_b32_e32 v37, 0
	v_lshrrev_b32_e32 v32, 4, v32
	v_dot4c_i32_i8_e32 v37, v36, v4
	v_and_b32_e32 v32, 0xf0f0f0f, v32
	v_dot4c_i32_i8_e32 v37, v32, v5
	v_and_b32_e32 v32, 0xf0f0f0f, v33
	v_mov_b32_e32 v36, 0
	v_dot4c_i32_i8_e32 v36, v32, v6
	v_lshrrev_b32_e32 v32, 4, v33
	v_and_b32_e32 v32, 0xf0f0f0f, v32
	v_dot4c_i32_i8_e32 v36, v32, v7
	v_and_b32_e32 v32, 0xf0f0f0f, v34
	v_dot4c_i32_i8_e32 v37, v32, v0
	v_lshrrev_b32_e32 v32, 4, v34
	v_and_b32_e32 v32, 0xf0f0f0f, v32
	v_dot4c_i32_i8_e32 v37, v32, v1
	v_and_b32_e32 v32, 0xf0f0f0f, v35
	v_dot4c_i32_i8_e32 v36, v32, v2
	v_lshrrev_b32_e32 v32, 4, v35
	v_and_b32_e32 v32, 0xf0f0f0f, v32
	v_dot4c_i32_i8_e32 v36, v32, v3
	v_and_b32_e32 v32, 0xf0f0f0f, v28
	v_mov_b32_e32 v33, 0
	v_lshrrev_b32_e32 v28, 4, v28
	v_dot4c_i32_i8_e32 v33, v32, v4
	v_and_b32_e32 v28, 0xf0f0f0f, v28
	v_dot4c_i32_i8_e32 v33, v28, v5
	v_and_b32_e32 v28, 0xf0f0f0f, v29
	v_mov_b32_e32 v32, 0
	v_dot4c_i32_i8_e32 v32, v28, v6
	v_lshrrev_b32_e32 v28, 4, v29
	v_and_b32_e32 v28, 0xf0f0f0f, v28
	v_dot4c_i32_i8_e32 v32, v28, v7
	v_and_b32_e32 v28, 0xf0f0f0f, v30
	v_dot4c_i32_i8_e32 v33, v28, v0
	v_lshrrev_b32_e32 v28, 4, v30
	v_and_b32_e32 v28, 0xf0f0f0f, v28
	v_dot4c_i32_i8_e32 v33, v28, v1
	v_and_b32_e32 v28, 0xf0f0f0f, v31
	v_dot4c_i32_i8_e32 v32, v28, v2
	v_lshrrev_b32_e32 v28, 4, v31
	v_and_b32_e32 v28, 0xf0f0f0f, v28
	v_dot4c_i32_i8_e32 v32, v28, v3
	v_sub_u32_e32 v30, v36, v84
	v_add_u32_e32 v30, v30, v37
	s_waitcnt vmcnt(18)
	v_lshlrev_b32_e32 v29, 16, v212
	v_sub_u32_e32 v31, v32, v84
	v_add_u32_e32 v32, v31, v33
	v_cvt_f32_i32_e32 v31, v30
	v_cvt_f32_i32_e32 v30, v32
	v_lshlrev_b32_e32 v28, 16, v213
	v_pk_fma_f32 v[130:131], v[28:29], v[30:31], v[130:131]
	v_and_b32_e32 v28, 0xf0f0f0f, v20
	v_mov_b32_e32 v29, 0
	v_lshrrev_b32_e32 v20, 4, v20
	v_dot4c_i32_i8_e32 v29, v28, v4
	v_and_b32_e32 v20, 0xf0f0f0f, v20
	v_dot4c_i32_i8_e32 v29, v20, v5
	v_and_b32_e32 v20, 0xf0f0f0f, v21
	v_mov_b32_e32 v28, 0
	v_dot4c_i32_i8_e32 v28, v20, v6
	v_lshrrev_b32_e32 v20, 4, v21
	v_and_b32_e32 v20, 0xf0f0f0f, v20
	v_dot4c_i32_i8_e32 v28, v20, v7
	v_and_b32_e32 v20, 0xf0f0f0f, v22
	v_dot4c_i32_i8_e32 v29, v20, v0
	v_lshrrev_b32_e32 v20, 4, v22
	v_and_b32_e32 v20, 0xf0f0f0f, v20
	v_dot4c_i32_i8_e32 v29, v20, v1
	v_and_b32_e32 v20, 0xf0f0f0f, v23
	v_dot4c_i32_i8_e32 v28, v20, v2
	v_lshrrev_b32_e32 v20, 4, v23
	v_and_b32_e32 v20, 0xf0f0f0f, v20
	v_dot4c_i32_i8_e32 v28, v20, v3
	v_and_b32_e32 v20, 0xf0f0f0f, v16
	v_mov_b32_e32 v21, 0
	v_dot4c_i32_i8_e32 v21, v20, v4
	v_lshrrev_b32_e32 v4, 4, v16
	v_and_b32_e32 v4, 0xf0f0f0f, v4
	v_dot4c_i32_i8_e32 v21, v4, v5
	v_and_b32_e32 v4, 0xf0f0f0f, v17
	v_mov_b32_e32 v5, 0
	v_dot4c_i32_i8_e32 v5, v4, v6
	v_lshrrev_b32_e32 v4, 4, v17
	v_and_b32_e32 v4, 0xf0f0f0f, v4
	v_dot4c_i32_i8_e32 v5, v4, v7
	v_and_b32_e32 v4, 0xf0f0f0f, v18
	v_dot4c_i32_i8_e32 v21, v4, v0
	v_lshrrev_b32_e32 v0, 4, v18
	v_and_b32_e32 v0, 0xf0f0f0f, v0
	v_dot4c_i32_i8_e32 v21, v0, v1
	v_and_b32_e32 v0, 0xf0f0f0f, v19
	v_dot4c_i32_i8_e32 v5, v0, v2
	v_lshrrev_b32_e32 v0, 4, v19
	v_and_b32_e32 v0, 0xf0f0f0f, v0
	v_dot4c_i32_i8_e32 v5, v0, v3
	v_sub_u32_e32 v2, v28, v84
	v_add_u32_e32 v2, v2, v29
	s_waitcnt vmcnt(16)
	v_lshlrev_b32_e32 v1, 16, v214
	v_sub_u32_e32 v3, v5, v84
	v_add_u32_e32 v4, v3, v21
	v_cvt_f32_i32_e32 v3, v2
	v_cvt_f32_i32_e32 v2, v4
	v_lshlrev_b32_e32 v0, 16, v215
	ds_read_b128 v[32:35], v166 offset:8192
	ds_read_b128 v[28:31], v166 offset:8208
	v_pk_fma_f32 v[128:129], v[0:1], v[2:3], v[128:129]
	ds_read_u16 v1, v93 offset:17024
	ds_read_u16 v2, v93 offset:17040
	ds_read_u16 v3, v93 offset:17056
	ds_read_u16 v4, v93 offset:17072
	v_mov_b32_e32 v0, 0
	s_waitcnt lgkmcnt(3)
	v_add_u32_e32 v1, s44, v1
	v_lshl_or_b32 v5, v1, 7, v165
	s_waitcnt lgkmcnt(2)
	v_add_u32_e32 v2, s44, v2
	global_load_dwordx4 v[84:87], v5, s[0:1]
	v_lshl_or_b32 v5, v2, 7, v165
	s_waitcnt lgkmcnt(1)
	v_add_u32_e32 v3, s44, v3
	global_load_dwordx4 v[80:83], v5, s[0:1]
	v_lshl_or_b32 v5, v3, 7, v165
	s_waitcnt lgkmcnt(0)
	v_add_u32_e32 v4, s44, v4
	global_load_dwordx4 v[68:71], v5, s[0:1]
	v_lshl_or_b32 v5, v4, 7, v165
	global_load_dwordx4 v[64:67], v5, s[0:1]
	ds_read_u16 v5, v93 offset:17088
	v_dot4c_i32_i8_e32 v0, 0x1010101, v32
	v_dot4c_i32_i8_e32 v0, 0x1010101, v33
	v_dot4c_i32_i8_e32 v0, 0x1010101, v34
	v_dot4c_i32_i8_e32 v0, 0x1010101, v35
	s_waitcnt lgkmcnt(0)
	v_add_u32_e32 v5, s44, v5
	v_lshl_or_b32 v6, v5, 7, v165
	global_load_dwordx4 v[52:55], v6, s[0:1]
	ds_read_u16 v6, v93 offset:17104
	v_dot4c_i32_i8_e32 v0, 0x1010101, v28
	v_dot4c_i32_i8_e32 v0, 0x1010101, v29
	v_dot4c_i32_i8_e32 v0, 0x1010101, v30
	v_dot4c_i32_i8_e32 v0, 0x1010101, v31
	s_waitcnt lgkmcnt(0)
	v_add_u32_e32 v6, s44, v6
	v_lshl_or_b32 v7, v6, 7, v165
	global_load_dwordx4 v[48:51], v7, s[0:1]
	ds_read_u16 v7, v93 offset:17120
	v_lshl_or_b32 v2, v2, 5, v248
	v_lshl_or_b32 v1, v1, 5, v248
	v_lshl_or_b32 v3, v3, 5, v248
	v_lshl_or_b32 v4, v4, 5, v248
	s_waitcnt lgkmcnt(0)
	v_add_u32_e32 v7, s44, v7
	v_lshl_or_b32 v16, v7, 7, v165
	global_load_dwordx4 v[40:43], v16, s[0:1]
	ds_read_u16 v16, v93 offset:17136
	v_lshl_or_b32 v5, v5, 5, v248
	v_lshl_or_b32 v6, v6, 5, v248
	v_lshl_or_b32 v7, v7, 5, v248
	v_lshlrev_b32_e32 v169, 3, v0
	s_waitcnt lgkmcnt(0)
	v_add_u32_e32 v16, s44, v16
	v_lshl_or_b32 v17, v16, 7, v165
	global_load_dwordx4 v[36:39], v17, s[0:1]
	v_lshl_or_b32 v16, v16, 5, v248
	global_load_dword v225, v2, s[46:47]
	global_load_dword v224, v1, s[46:47]
	global_load_dword v227, v4, s[46:47]
	global_load_dword v226, v3, s[46:47]
	global_load_dword v229, v6, s[46:47]
	global_load_dword v228, v5, s[46:47]
	global_load_dword v231, v16, s[46:47]
	global_load_dword v230, v7, s[46:47]
	s_waitcnt vmcnt(31)
	v_and_b32_e32 v0, 0xf0f0f0f, v76
	v_mov_b32_e32 v2, 0
	v_dot4c_i32_i8_e32 v2, v0, v32
	v_lshrrev_b32_e32 v0, 4, v76
	v_and_b32_e32 v0, 0xf0f0f0f, v0
	v_dot4c_i32_i8_e32 v2, v0, v33
	v_and_b32_e32 v0, 0xf0f0f0f, v77
	v_mov_b32_e32 v3, 0
	v_dot4c_i32_i8_e32 v3, v0, v34
	v_lshrrev_b32_e32 v0, 4, v77
	v_and_b32_e32 v0, 0xf0f0f0f, v0
	v_dot4c_i32_i8_e32 v3, v0, v35
	v_and_b32_e32 v0, 0xf0f0f0f, v78
	v_dot4c_i32_i8_e32 v2, v0, v28
	v_lshrrev_b32_e32 v0, 4, v78
	v_and_b32_e32 v0, 0xf0f0f0f, v0
	v_dot4c_i32_i8_e32 v2, v0, v29
	v_and_b32_e32 v0, 0xf0f0f0f, v79
	v_dot4c_i32_i8_e32 v3, v0, v30
	v_lshrrev_b32_e32 v0, 4, v79
	v_and_b32_e32 v0, 0xf0f0f0f, v0
	v_dot4c_i32_i8_e32 v3, v0, v31
	s_waitcnt vmcnt(30)
	v_and_b32_e32 v0, 0xf0f0f0f, v72
	v_mov_b32_e32 v4, 0
	v_dot4c_i32_i8_e32 v4, v0, v32
	v_lshrrev_b32_e32 v0, 4, v72
	v_and_b32_e32 v0, 0xf0f0f0f, v0
	v_dot4c_i32_i8_e32 v4, v0, v33
	v_and_b32_e32 v0, 0xf0f0f0f, v73
	v_mov_b32_e32 v5, 0
	v_dot4c_i32_i8_e32 v5, v0, v34
	v_lshrrev_b32_e32 v0, 4, v73
	v_and_b32_e32 v0, 0xf0f0f0f, v0
	v_dot4c_i32_i8_e32 v5, v0, v35
	v_and_b32_e32 v0, 0xf0f0f0f, v74
	v_dot4c_i32_i8_e32 v4, v0, v28
	v_lshrrev_b32_e32 v0, 4, v74
	v_and_b32_e32 v0, 0xf0f0f0f, v0
	v_dot4c_i32_i8_e32 v4, v0, v29
	v_and_b32_e32 v0, 0xf0f0f0f, v75
	v_dot4c_i32_i8_e32 v5, v0, v30
	v_lshrrev_b32_e32 v0, 4, v75
	v_and_b32_e32 v0, 0xf0f0f0f, v0
	v_dot4c_i32_i8_e32 v5, v0, v31
	v_add_u32_e32 v2, v2, v3
	v_sub_u32_e32 v2, v2, v169
	s_waitcnt vmcnt(22)
	v_lshlrev_b32_e32 v1, 16, v216
	v_add_u32_e32 v3, v4, v5
	v_sub_u32_e32 v4, v3, v169
	v_cvt_f32_i32_e32 v3, v2
	v_cvt_f32_i32_e32 v2, v4
	v_lshlrev_b32_e32 v0, 16, v217
	v_mov_b32_e32 v4, 0
	v_mov_b32_e32 v5, 0
	v_pk_fma_f32 v[126:127], v[0:1], v[2:3], v[126:127]
	v_and_b32_e32 v0, 0xf0f0f0f, v60
	v_mov_b32_e32 v2, 0
	v_dot4c_i32_i8_e32 v2, v0, v32
	v_lshrrev_b32_e32 v0, 4, v60
	v_and_b32_e32 v0, 0xf0f0f0f, v0
	v_dot4c_i32_i8_e32 v2, v0, v33
	v_and_b32_e32 v0, 0xf0f0f0f, v61
	v_mov_b32_e32 v3, 0
	v_dot4c_i32_i8_e32 v3, v0, v34
	v_lshrrev_b32_e32 v0, 4, v61
	v_and_b32_e32 v0, 0xf0f0f0f, v0
	v_dot4c_i32_i8_e32 v3, v0, v35
	v_and_b32_e32 v0, 0xf0f0f0f, v62
	v_dot4c_i32_i8_e32 v2, v0, v28
	v_lshrrev_b32_e32 v0, 4, v62
	v_and_b32_e32 v0, 0xf0f0f0f, v0
	v_dot4c_i32_i8_e32 v2, v0, v29
	v_and_b32_e32 v0, 0xf0f0f0f, v63
	v_dot4c_i32_i8_e32 v3, v0, v30
	v_lshrrev_b32_e32 v0, 4, v63
	v_and_b32_e32 v0, 0xf0f0f0f, v0
	v_dot4c_i32_i8_e32 v3, v0, v31
	v_and_b32_e32 v0, 0xf0f0f0f, v56
	v_dot4c_i32_i8_e32 v4, v0, v32
	v_lshrrev_b32_e32 v0, 4, v56
	v_and_b32_e32 v0, 0xf0f0f0f, v0
	v_dot4c_i32_i8_e32 v4, v0, v33
	v_and_b32_e32 v0, 0xf0f0f0f, v57
	v_dot4c_i32_i8_e32 v5, v0, v34
	v_lshrrev_b32_e32 v0, 4, v57
	v_and_b32_e32 v0, 0xf0f0f0f, v0
	v_dot4c_i32_i8_e32 v5, v0, v35
	v_and_b32_e32 v0, 0xf0f0f0f, v58
	v_dot4c_i32_i8_e32 v4, v0, v28
	v_lshrrev_b32_e32 v0, 4, v58
	v_and_b32_e32 v0, 0xf0f0f0f, v0
	v_dot4c_i32_i8_e32 v4, v0, v29
	v_and_b32_e32 v0, 0xf0f0f0f, v59
	v_dot4c_i32_i8_e32 v5, v0, v30
	v_lshrrev_b32_e32 v0, 4, v59
	v_and_b32_e32 v0, 0xf0f0f0f, v0
	v_dot4c_i32_i8_e32 v5, v0, v31
	v_add_u32_e32 v2, v2, v3
	v_sub_u32_e32 v2, v2, v169
	s_waitcnt vmcnt(20)
	v_lshlrev_b32_e32 v1, 16, v218
	v_add_u32_e32 v3, v4, v5
	v_sub_u32_e32 v4, v3, v169
	v_cvt_f32_i32_e32 v3, v2
	v_cvt_f32_i32_e32 v2, v4
	v_lshlrev_b32_e32 v0, 16, v219
	v_mov_b32_e32 v4, 0
	v_mov_b32_e32 v5, 0
	v_pk_fma_f32 v[124:125], v[0:1], v[2:3], v[124:125]
	v_and_b32_e32 v0, 0xf0f0f0f, v44
	v_mov_b32_e32 v2, 0
	v_dot4c_i32_i8_e32 v2, v0, v32
	v_lshrrev_b32_e32 v0, 4, v44
	v_and_b32_e32 v0, 0xf0f0f0f, v0
	v_dot4c_i32_i8_e32 v2, v0, v33
	v_and_b32_e32 v0, 0xf0f0f0f, v45
	v_mov_b32_e32 v3, 0
	v_dot4c_i32_i8_e32 v3, v0, v34
	v_lshrrev_b32_e32 v0, 4, v45
	v_and_b32_e32 v0, 0xf0f0f0f, v0
	v_dot4c_i32_i8_e32 v3, v0, v35
	v_and_b32_e32 v0, 0xf0f0f0f, v46
	v_dot4c_i32_i8_e32 v2, v0, v28
	v_lshrrev_b32_e32 v0, 4, v46
	v_and_b32_e32 v0, 0xf0f0f0f, v0
	v_dot4c_i32_i8_e32 v2, v0, v29
	v_and_b32_e32 v0, 0xf0f0f0f, v47
	v_dot4c_i32_i8_e32 v3, v0, v30
	v_lshrrev_b32_e32 v0, 4, v47
	v_and_b32_e32 v0, 0xf0f0f0f, v0
	v_dot4c_i32_i8_e32 v3, v0, v31
	v_and_b32_e32 v0, 0xf0f0f0f, v24
	v_dot4c_i32_i8_e32 v4, v0, v32
	v_lshrrev_b32_e32 v0, 4, v24
	v_and_b32_e32 v0, 0xf0f0f0f, v0
	v_dot4c_i32_i8_e32 v4, v0, v33
	v_and_b32_e32 v0, 0xf0f0f0f, v25
	v_dot4c_i32_i8_e32 v5, v0, v34
	v_lshrrev_b32_e32 v0, 4, v25
	v_and_b32_e32 v0, 0xf0f0f0f, v0
	v_dot4c_i32_i8_e32 v5, v0, v35
	v_and_b32_e32 v0, 0xf0f0f0f, v26
	v_dot4c_i32_i8_e32 v4, v0, v28
	v_lshrrev_b32_e32 v0, 4, v26
	v_and_b32_e32 v0, 0xf0f0f0f, v0
	v_dot4c_i32_i8_e32 v4, v0, v29
	v_and_b32_e32 v0, 0xf0f0f0f, v27
	v_dot4c_i32_i8_e32 v5, v0, v30
	v_lshrrev_b32_e32 v0, 4, v27
	v_and_b32_e32 v0, 0xf0f0f0f, v0
	v_dot4c_i32_i8_e32 v5, v0, v31
	v_add_u32_e32 v2, v2, v3
	v_sub_u32_e32 v2, v2, v169
	s_waitcnt vmcnt(18)
	v_lshlrev_b32_e32 v1, 16, v220
	v_add_u32_e32 v3, v4, v5
	v_sub_u32_e32 v4, v3, v169
	v_cvt_f32_i32_e32 v3, v2
	v_cvt_f32_i32_e32 v2, v4
	v_lshlrev_b32_e32 v0, 16, v221
	v_mov_b32_e32 v4, 0
	v_mov_b32_e32 v5, 0
	v_pk_fma_f32 v[122:123], v[0:1], v[2:3], v[122:123]
	v_and_b32_e32 v0, 0xf0f0f0f, v12
	v_mov_b32_e32 v2, 0
	v_dot4c_i32_i8_e32 v2, v0, v32
	v_lshrrev_b32_e32 v0, 4, v12
	v_and_b32_e32 v0, 0xf0f0f0f, v0
	v_dot4c_i32_i8_e32 v2, v0, v33
	v_and_b32_e32 v0, 0xf0f0f0f, v13
	v_mov_b32_e32 v3, 0
	v_dot4c_i32_i8_e32 v3, v0, v34
	v_lshrrev_b32_e32 v0, 4, v13
	v_and_b32_e32 v0, 0xf0f0f0f, v0
	v_dot4c_i32_i8_e32 v3, v0, v35
	v_and_b32_e32 v0, 0xf0f0f0f, v14
	v_dot4c_i32_i8_e32 v2, v0, v28
	v_lshrrev_b32_e32 v0, 4, v14
	v_and_b32_e32 v0, 0xf0f0f0f, v0
	v_dot4c_i32_i8_e32 v2, v0, v29
	v_and_b32_e32 v0, 0xf0f0f0f, v15
	v_dot4c_i32_i8_e32 v3, v0, v30
	v_lshrrev_b32_e32 v0, 4, v15
	v_and_b32_e32 v0, 0xf0f0f0f, v0
	v_dot4c_i32_i8_e32 v3, v0, v31
	v_and_b32_e32 v0, 0xf0f0f0f, v8
	v_dot4c_i32_i8_e32 v4, v0, v32
	v_lshrrev_b32_e32 v0, 4, v8
	v_and_b32_e32 v0, 0xf0f0f0f, v0
	v_dot4c_i32_i8_e32 v4, v0, v33
	v_and_b32_e32 v0, 0xf0f0f0f, v9
	v_dot4c_i32_i8_e32 v5, v0, v34
	v_lshrrev_b32_e32 v0, 4, v9
	v_and_b32_e32 v0, 0xf0f0f0f, v0
	v_dot4c_i32_i8_e32 v5, v0, v35
	v_and_b32_e32 v0, 0xf0f0f0f, v10
	v_dot4c_i32_i8_e32 v4, v0, v28
	v_lshrrev_b32_e32 v0, 4, v10
	v_and_b32_e32 v0, 0xf0f0f0f, v0
	v_dot4c_i32_i8_e32 v4, v0, v29
	v_and_b32_e32 v0, 0xf0f0f0f, v11
	v_dot4c_i32_i8_e32 v5, v0, v30
	v_lshrrev_b32_e32 v0, 4, v11
	v_and_b32_e32 v0, 0xf0f0f0f, v0
	v_dot4c_i32_i8_e32 v5, v0, v31
	v_add_u32_e32 v2, v2, v3
	v_sub_u32_e32 v2, v2, v169
	s_waitcnt vmcnt(16)
	v_lshlrev_b32_e32 v1, 16, v222
	v_add_u32_e32 v3, v4, v5
	v_sub_u32_e32 v4, v3, v169
	v_cvt_f32_i32_e32 v3, v2
	v_cvt_f32_i32_e32 v2, v4
	v_lshlrev_b32_e32 v0, 16, v223
	v_pk_fma_f32 v[120:121], v[0:1], v[2:3], v[120:121]
	ds_read_u16 v0, v93 offset:17152
	ds_read_u16 v1, v93 offset:17168
	ds_read_u16 v2, v93 offset:17184
	ds_read_u16 v3, v93 offset:17200
	s_waitcnt lgkmcnt(3)
	v_add_u32_e32 v0, s44, v0
	v_lshl_or_b32 v4, v0, 7, v165
	v_lshl_or_b32 v44, v0, 5, v248
	s_waitcnt lgkmcnt(2)
	v_add_u32_e32 v0, s44, v1
	v_lshl_or_b32 v1, v0, 7, v165
	v_lshl_or_b32 v45, v0, 5, v248
	s_waitcnt lgkmcnt(1)
	v_add_u32_e32 v0, s44, v2
	global_load_dwordx4 v[72:75], v4, s[0:1]
	global_load_dwordx4 v[24:27], v1, s[0:1]
	v_lshl_or_b32 v1, v0, 7, v165
	v_lshl_or_b32 v46, v0, 5, v248
	s_waitcnt lgkmcnt(0)
	v_add_u32_e32 v0, s44, v3
	global_load_dwordx4 v[20:23], v1, s[0:1]
	v_lshl_or_b32 v1, v0, 7, v165
	v_lshl_or_b32 v47, v0, 5, v248
	ds_read_u16 v0, v93 offset:17216
	global_load_dwordx4 v[16:19], v1, s[0:1]
	s_waitcnt lgkmcnt(0)
	v_add_u32_e32 v0, s44, v0
	v_lshl_or_b32 v1, v0, 7, v165
	v_lshl_or_b32 v56, v0, 5, v248
	ds_read_u16 v0, v93 offset:17232
	global_load_dwordx4 v[12:15], v1, s[0:1]
	s_waitcnt lgkmcnt(0)
	v_add_u32_e32 v0, s44, v0
	v_lshl_or_b32 v1, v0, 7, v165
	v_lshl_or_b32 v57, v0, 5, v248
	ds_read_u16 v0, v93 offset:17248
	global_load_dwordx4 v[8:11], v1, s[0:1]
	s_waitcnt lgkmcnt(0)
	v_add_u32_e32 v0, s44, v0
	v_lshl_or_b32 v1, v0, 7, v165
	v_lshl_or_b32 v58, v0, 5, v248
	ds_read_u16 v0, v93 offset:17264
	global_load_dwordx4 v[4:7], v1, s[0:1]
	s_waitcnt lgkmcnt(0)
	v_add_u32_e32 v59, s44, v0
	v_lshl_or_b32 v0, v59, 7, v165
	global_load_dwordx4 v[0:3], v0, s[0:1]
	v_lshl_or_b32 v59, v59, 5, v248
	global_load_dword v233, v45, s[46:47]
	global_load_dword v232, v44, s[46:47]
	global_load_dword v235, v47, s[46:47]
	global_load_dword v234, v46, s[46:47]
	global_load_dword v236, v56, s[46:47]
	global_load_dword v237, v57, s[46:47]
	global_load_dword v238, v58, s[46:47]
	global_load_dword v239, v59, s[46:47]
	s_waitcnt vmcnt(31)
	v_and_b32_e32 v44, 0xf0f0f0f, v84
	v_mov_b32_e32 v46, 0
	v_dot4c_i32_i8_e32 v46, v44, v32
	v_lshrrev_b32_e32 v44, 4, v84
	v_and_b32_e32 v44, 0xf0f0f0f, v44
	v_dot4c_i32_i8_e32 v46, v44, v33
	v_and_b32_e32 v44, 0xf0f0f0f, v85
	v_mov_b32_e32 v47, 0
	v_dot4c_i32_i8_e32 v47, v44, v34
	v_lshrrev_b32_e32 v44, 4, v85
	v_and_b32_e32 v44, 0xf0f0f0f, v44
	v_dot4c_i32_i8_e32 v47, v44, v35
	v_and_b32_e32 v44, 0xf0f0f0f, v86
	v_dot4c_i32_i8_e32 v46, v44, v28
	v_lshrrev_b32_e32 v44, 4, v86
	v_and_b32_e32 v44, 0xf0f0f0f, v44
	v_dot4c_i32_i8_e32 v46, v44, v29
	v_and_b32_e32 v44, 0xf0f0f0f, v87
	v_dot4c_i32_i8_e32 v47, v44, v30
	v_lshrrev_b32_e32 v44, 4, v87
	v_and_b32_e32 v44, 0xf0f0f0f, v44
	v_dot4c_i32_i8_e32 v47, v44, v31
	s_waitcnt vmcnt(30)
	v_and_b32_e32 v44, 0xf0f0f0f, v80
	v_mov_b32_e32 v56, 0
	v_dot4c_i32_i8_e32 v56, v44, v32
	v_lshrrev_b32_e32 v44, 4, v80
	v_and_b32_e32 v44, 0xf0f0f0f, v44
	v_dot4c_i32_i8_e32 v56, v44, v33
	v_and_b32_e32 v44, 0xf0f0f0f, v81
	v_mov_b32_e32 v57, 0
	v_dot4c_i32_i8_e32 v57, v44, v34
	v_lshrrev_b32_e32 v44, 4, v81
	v_and_b32_e32 v44, 0xf0f0f0f, v44
	v_dot4c_i32_i8_e32 v57, v44, v35
	v_and_b32_e32 v44, 0xf0f0f0f, v82
	v_dot4c_i32_i8_e32 v56, v44, v28
	v_lshrrev_b32_e32 v44, 4, v82
	v_and_b32_e32 v44, 0xf0f0f0f, v44
	v_dot4c_i32_i8_e32 v56, v44, v29
	v_and_b32_e32 v44, 0xf0f0f0f, v83
	v_dot4c_i32_i8_e32 v57, v44, v30
	v_lshrrev_b32_e32 v44, 4, v83
	v_and_b32_e32 v44, 0xf0f0f0f, v44
	v_dot4c_i32_i8_e32 v57, v44, v31
	v_add_u32_e32 v46, v46, v47
	v_sub_u32_e32 v46, v46, v169
	s_waitcnt vmcnt(22)
	v_lshlrev_b32_e32 v45, 16, v224
	v_sub_u32_e32 v47, v57, v169
	v_add_u32_e32 v56, v47, v56
	v_cvt_f32_i32_e32 v47, v46
	v_cvt_f32_i32_e32 v46, v56
	v_lshlrev_b32_e32 v44, 16, v225
	v_mov_b32_e32 v56, 0
	v_mov_b32_e32 v57, 0
	v_pk_fma_f32 v[118:119], v[44:45], v[46:47], v[118:119]
	v_and_b32_e32 v44, 0xf0f0f0f, v68
	v_mov_b32_e32 v46, 0
	v_dot4c_i32_i8_e32 v46, v44, v32
	v_lshrrev_b32_e32 v44, 4, v68
	v_and_b32_e32 v44, 0xf0f0f0f, v44
	v_dot4c_i32_i8_e32 v46, v44, v33
	v_and_b32_e32 v44, 0xf0f0f0f, v69
	v_mov_b32_e32 v47, 0
	v_dot4c_i32_i8_e32 v47, v44, v34
	v_lshrrev_b32_e32 v44, 4, v69
	v_and_b32_e32 v44, 0xf0f0f0f, v44
	v_dot4c_i32_i8_e32 v47, v44, v35
	v_and_b32_e32 v44, 0xf0f0f0f, v70
	v_dot4c_i32_i8_e32 v46, v44, v28
	v_lshrrev_b32_e32 v44, 4, v70
	v_and_b32_e32 v44, 0xf0f0f0f, v44
	v_dot4c_i32_i8_e32 v46, v44, v29
	v_and_b32_e32 v44, 0xf0f0f0f, v71
	v_dot4c_i32_i8_e32 v47, v44, v30
	v_lshrrev_b32_e32 v44, 4, v71
	v_and_b32_e32 v44, 0xf0f0f0f, v44
	v_dot4c_i32_i8_e32 v47, v44, v31
	v_and_b32_e32 v44, 0xf0f0f0f, v64
	v_dot4c_i32_i8_e32 v56, v44, v32
	v_lshrrev_b32_e32 v44, 4, v64
	v_and_b32_e32 v44, 0xf0f0f0f, v44
	v_dot4c_i32_i8_e32 v56, v44, v33
	v_and_b32_e32 v44, 0xf0f0f0f, v65
	v_dot4c_i32_i8_e32 v57, v44, v34
	v_lshrrev_b32_e32 v44, 4, v65
	v_and_b32_e32 v44, 0xf0f0f0f, v44
	v_dot4c_i32_i8_e32 v57, v44, v35
	v_and_b32_e32 v44, 0xf0f0f0f, v66
	v_dot4c_i32_i8_e32 v56, v44, v28
	v_lshrrev_b32_e32 v44, 4, v66
	v_and_b32_e32 v44, 0xf0f0f0f, v44
	v_dot4c_i32_i8_e32 v56, v44, v29
	v_and_b32_e32 v44, 0xf0f0f0f, v67
	v_dot4c_i32_i8_e32 v57, v44, v30
	v_lshrrev_b32_e32 v44, 4, v67
	v_and_b32_e32 v44, 0xf0f0f0f, v44
	v_dot4c_i32_i8_e32 v57, v44, v31
	v_sub_u32_e32 v47, v47, v169
	v_add_u32_e32 v46, v47, v46
	v_cvt_f32_i32_e32 v47, v46
	v_sub_u32_e32 v57, v57, v169
	v_add_u32_e32 v56, v57, v56
	v_cvt_f32_i32_e32 v46, v56
	s_waitcnt vmcnt(20)
	v_lshlrev_b32_e32 v45, 16, v226
	v_lshlrev_b32_e32 v44, 16, v227
	v_pk_fma_f32 v[116:117], v[44:45], v[46:47], v[116:117]
	v_and_b32_e32 v44, 0xf0f0f0f, v52
	v_mov_b32_e32 v46, 0
	v_dot4c_i32_i8_e32 v46, v44, v32
	v_lshrrev_b32_e32 v44, 4, v52
	v_and_b32_e32 v44, 0xf0f0f0f, v44
	v_dot4c_i32_i8_e32 v46, v44, v33
	v_and_b32_e32 v44, 0xf0f0f0f, v53
	v_mov_b32_e32 v47, 0
	v_dot4c_i32_i8_e32 v47, v44, v34
	v_lshrrev_b32_e32 v44, 4, v53
	v_and_b32_e32 v44, 0xf0f0f0f, v44
	v_dot4c_i32_i8_e32 v47, v44, v35
	v_and_b32_e32 v44, 0xf0f0f0f, v54
	v_dot4c_i32_i8_e32 v46, v44, v28
	v_lshrrev_b32_e32 v44, 4, v54
	v_and_b32_e32 v44, 0xf0f0f0f, v44
	v_dot4c_i32_i8_e32 v46, v44, v29
	v_and_b32_e32 v44, 0xf0f0f0f, v55
	v_dot4c_i32_i8_e32 v47, v44, v30
	v_lshrrev_b32_e32 v44, 4, v55
	v_and_b32_e32 v44, 0xf0f0f0f, v44
	v_dot4c_i32_i8_e32 v47, v44, v31
	v_and_b32_e32 v44, 0xf0f0f0f, v48
	v_mov_b32_e32 v52, 0
	v_dot4c_i32_i8_e32 v52, v44, v32
	v_lshrrev_b32_e32 v44, 4, v48
	v_and_b32_e32 v44, 0xf0f0f0f, v44
	v_dot4c_i32_i8_e32 v52, v44, v33
	v_and_b32_e32 v44, 0xf0f0f0f, v49
	v_mov_b32_e32 v48, 0
	v_dot4c_i32_i8_e32 v48, v44, v34
	v_lshrrev_b32_e32 v44, 4, v49
	v_and_b32_e32 v44, 0xf0f0f0f, v44
	v_dot4c_i32_i8_e32 v48, v44, v35
	v_and_b32_e32 v44, 0xf0f0f0f, v50
	v_dot4c_i32_i8_e32 v52, v44, v28
	v_lshrrev_b32_e32 v44, 4, v50
	v_and_b32_e32 v44, 0xf0f0f0f, v44
	v_dot4c_i32_i8_e32 v52, v44, v29
	v_and_b32_e32 v44, 0xf0f0f0f, v51
	v_dot4c_i32_i8_e32 v48, v44, v30
	v_lshrrev_b32_e32 v44, 4, v51
	v_and_b32_e32 v44, 0xf0f0f0f, v44
	v_dot4c_i32_i8_e32 v48, v44, v31
	v_sub_u32_e32 v47, v47, v169
	v_add_u32_e32 v46, v47, v46
	v_cvt_f32_i32_e32 v47, v46
	v_sub_u32_e32 v48, v48, v169
	v_add_u32_e32 v48, v48, v52
	v_cvt_f32_i32_e32 v46, v48
	s_waitcnt vmcnt(18)
	v_lshlrev_b32_e32 v45, 16, v228
	v_lshlrev_b32_e32 v44, 16, v229
	v_pk_fma_f32 v[114:115], v[44:45], v[46:47], v[114:115]
	v_and_b32_e32 v44, 0xf0f0f0f, v40
	v_mov_b32_e32 v45, 0
	v_lshrrev_b32_e32 v40, 4, v40
	v_dot4c_i32_i8_e32 v45, v44, v32
	v_and_b32_e32 v40, 0xf0f0f0f, v40
	v_dot4c_i32_i8_e32 v45, v40, v33
	v_and_b32_e32 v40, 0xf0f0f0f, v41
	v_mov_b32_e32 v44, 0
	v_dot4c_i32_i8_e32 v44, v40, v34
	v_lshrrev_b32_e32 v40, 4, v41
	v_and_b32_e32 v40, 0xf0f0f0f, v40
	v_dot4c_i32_i8_e32 v44, v40, v35
	v_and_b32_e32 v40, 0xf0f0f0f, v42
	v_dot4c_i32_i8_e32 v45, v40, v28
	v_lshrrev_b32_e32 v40, 4, v42
	v_and_b32_e32 v40, 0xf0f0f0f, v40
	v_dot4c_i32_i8_e32 v45, v40, v29
	v_and_b32_e32 v40, 0xf0f0f0f, v43
	v_dot4c_i32_i8_e32 v44, v40, v30
	v_lshrrev_b32_e32 v40, 4, v43
	v_and_b32_e32 v40, 0xf0f0f0f, v40
	v_dot4c_i32_i8_e32 v44, v40, v31
	v_and_b32_e32 v40, 0xf0f0f0f, v36
	v_mov_b32_e32 v41, 0
	v_dot4c_i32_i8_e32 v41, v40, v32
	v_lshrrev_b32_e32 v32, 4, v36
	v_and_b32_e32 v32, 0xf0f0f0f, v32
	v_dot4c_i32_i8_e32 v41, v32, v33
	v_and_b32_e32 v32, 0xf0f0f0f, v37
	v_mov_b32_e32 v33, 0
	v_dot4c_i32_i8_e32 v33, v32, v34
	v_lshrrev_b32_e32 v32, 4, v37
	v_and_b32_e32 v32, 0xf0f0f0f, v32
	v_dot4c_i32_i8_e32 v33, v32, v35
	v_and_b32_e32 v32, 0xf0f0f0f, v38
	v_dot4c_i32_i8_e32 v41, v32, v28
	v_lshrrev_b32_e32 v28, 4, v38
	v_and_b32_e32 v28, 0xf0f0f0f, v28
	v_dot4c_i32_i8_e32 v41, v28, v29
	v_and_b32_e32 v28, 0xf0f0f0f, v39
	v_dot4c_i32_i8_e32 v33, v28, v30
	v_lshrrev_b32_e32 v28, 4, v39
	v_and_b32_e32 v28, 0xf0f0f0f, v28
	v_dot4c_i32_i8_e32 v33, v28, v31
	v_sub_u32_e32 v30, v44, v169
	v_add_u32_e32 v30, v30, v45
	s_waitcnt vmcnt(16)
	v_lshlrev_b32_e32 v29, 16, v230
	v_sub_u32_e32 v31, v33, v169
	v_add_u32_e32 v32, v31, v41
	v_cvt_f32_i32_e32 v31, v30
	v_cvt_f32_i32_e32 v30, v32
	v_lshlrev_b32_e32 v28, 16, v231
	ds_read_b128 v[36:39], v166 offset:12288
	ds_read_b128 v[32:35], v166 offset:12304
	v_add_u32_e32 v166, 0x100, v166
	v_pk_fma_f32 v[112:113], v[28:29], v[30:31], v[112:113]
	ds_read_u16 v29, v93 offset:17280
	ds_read_u16 v30, v93 offset:17296
	ds_read_u16 v31, v93 offset:17312
	ds_read_u16 v40, v93 offset:17328
	v_mov_b32_e32 v28, 0
	s_waitcnt lgkmcnt(3)
	v_add_u32_e32 v29, s44, v29
	v_lshl_or_b32 v41, v29, 7, v165
	s_waitcnt lgkmcnt(2)
	v_add_u32_e32 v30, s44, v30
	global_load_dwordx4 v[68:71], v41, s[0:1]
	v_lshl_or_b32 v41, v30, 7, v165
	s_waitcnt lgkmcnt(1)
	v_add_u32_e32 v31, s44, v31
	global_load_dwordx4 v[64:67], v41, s[0:1]
	v_lshl_or_b32 v41, v31, 7, v165
	s_waitcnt lgkmcnt(0)
	v_add_u32_e32 v40, s44, v40
	global_load_dwordx4 v[60:63], v41, s[0:1]
	v_lshl_or_b32 v41, v40, 7, v165
	v_lshl_or_b32 v79, v40, 5, v248
	ds_read_u16 v40, v93 offset:17344
	global_load_dwordx4 v[56:59], v41, s[0:1]
	v_dot4c_i32_i8_e32 v28, 0x1010101, v36
	v_dot4c_i32_i8_e32 v28, 0x1010101, v37
	v_dot4c_i32_i8_e32 v28, 0x1010101, v38
	s_waitcnt lgkmcnt(0)
	v_add_u32_e32 v40, s44, v40
	v_lshl_or_b32 v41, v40, 7, v165
	v_lshl_or_b32 v80, v40, 5, v248
	ds_read_u16 v40, v93 offset:17360
	global_load_dwordx4 v[52:55], v41, s[0:1]
	v_dot4c_i32_i8_e32 v28, 0x1010101, v39
	v_dot4c_i32_i8_e32 v28, 0x1010101, v32
	v_dot4c_i32_i8_e32 v28, 0x1010101, v33
	s_waitcnt lgkmcnt(0)
	v_add_u32_e32 v40, s44, v40
	v_lshl_or_b32 v41, v40, 7, v165
	v_lshl_or_b32 v82, v40, 5, v248
	ds_read_u16 v40, v93 offset:17376
	global_load_dwordx4 v[48:51], v41, s[0:1]
	v_dot4c_i32_i8_e32 v28, 0x1010101, v34
	v_dot4c_i32_i8_e32 v28, 0x1010101, v35
	v_lshl_or_b32 v29, v29, 5, v248
	s_waitcnt lgkmcnt(0)
	v_add_u32_e32 v40, s44, v40
	v_lshl_or_b32 v41, v40, 7, v165
	v_lshl_or_b32 v87, v40, 5, v248
	ds_read_u16 v40, v93 offset:17392
	v_lshl_or_b32 v30, v30, 5, v248
	v_lshl_or_b32 v31, v31, 5, v248
	global_load_dwordx4 v[44:47], v41, s[0:1]
	s_waitcnt lgkmcnt(0)
	v_add_u32_e32 v78, s44, v40
	v_lshl_or_b32 v40, v78, 7, v165
	global_load_dwordx4 v[40:43], v40, s[0:1]
	v_lshl_or_b32 v169, v78, 5, v248
	v_lshlrev_b32_e32 v78, 3, v28
	global_load_dword v240, v29, s[46:47]
	global_load_dword v241, v30, s[46:47]
	global_load_dword v242, v31, s[46:47]
	global_load_dword v243, v79, s[46:47]
	global_load_dword v244, v80, s[46:47]
	s_nop 0
	global_load_dword v245, v82, s[46:47]
	s_nop 0
	global_load_dword v246, v87, s[46:47]
	global_load_dword v247, v169, s[46:47]
	s_waitcnt vmcnt(31)
	v_and_b32_e32 v29, 0xf0f0f0f, v72
	v_mov_b32_e32 v28, 0
	v_dot4c_i32_i8_e32 v28, v29, v36
	v_lshrrev_b32_e32 v29, 4, v72
	v_and_b32_e32 v29, 0xf0f0f0f, v29
	v_dot4c_i32_i8_e32 v28, v29, v37
	v_and_b32_e32 v30, 0xf0f0f0f, v73
	v_mov_b32_e32 v29, 0
	v_dot4c_i32_i8_e32 v29, v30, v38
	v_lshrrev_b32_e32 v30, 4, v73
	v_and_b32_e32 v30, 0xf0f0f0f, v30
	v_dot4c_i32_i8_e32 v29, v30, v39
	v_and_b32_e32 v30, 0xf0f0f0f, v74
	v_dot4c_i32_i8_e32 v28, v30, v32
	v_lshrrev_b32_e32 v30, 4, v74
	v_and_b32_e32 v30, 0xf0f0f0f, v30
	v_dot4c_i32_i8_e32 v28, v30, v33
	v_and_b32_e32 v30, 0xf0f0f0f, v75
	v_dot4c_i32_i8_e32 v29, v30, v34
	v_lshrrev_b32_e32 v30, 4, v75
	v_and_b32_e32 v30, 0xf0f0f0f, v30
	v_dot4c_i32_i8_e32 v29, v30, v35
	s_waitcnt vmcnt(30)
	v_and_b32_e32 v31, 0xf0f0f0f, v24
	v_mov_b32_e32 v30, 0
	v_lshrrev_b32_e32 v24, 4, v24
	v_dot4c_i32_i8_e32 v30, v31, v36
	v_and_b32_e32 v24, 0xf0f0f0f, v24
	v_dot4c_i32_i8_e32 v30, v24, v37
	v_and_b32_e32 v24, 0xf0f0f0f, v25
	v_mov_b32_e32 v31, 0
	v_dot4c_i32_i8_e32 v31, v24, v38
	v_lshrrev_b32_e32 v24, 4, v25
	v_and_b32_e32 v24, 0xf0f0f0f, v24
	v_dot4c_i32_i8_e32 v31, v24, v39
	v_and_b32_e32 v24, 0xf0f0f0f, v26
	v_dot4c_i32_i8_e32 v30, v24, v32
	v_lshrrev_b32_e32 v24, 4, v26
	v_and_b32_e32 v24, 0xf0f0f0f, v24
	v_dot4c_i32_i8_e32 v30, v24, v33
	v_and_b32_e32 v24, 0xf0f0f0f, v27
	v_dot4c_i32_i8_e32 v31, v24, v34
	v_lshrrev_b32_e32 v24, 4, v27
	v_and_b32_e32 v24, 0xf0f0f0f, v24
	v_dot4c_i32_i8_e32 v31, v24, v35
	v_add_u32_e32 v26, v28, v29
	v_sub_u32_e32 v26, v26, v78
	s_waitcnt vmcnt(22)
	v_lshlrev_b32_e32 v25, 16, v232
	v_add_u32_e32 v27, v30, v31
	v_sub_u32_e32 v28, v27, v78
	v_cvt_f32_i32_e32 v27, v26
	v_cvt_f32_i32_e32 v26, v28
	v_lshlrev_b32_e32 v24, 16, v233
	s_cselect_b32 s44, s44, s45
	v_pk_fma_f32 v[110:111], v[24:25], v[26:27], v[110:111]
	v_and_b32_e32 v24, 0xf0f0f0f, v20
	v_mov_b32_e32 v25, 0
	v_lshrrev_b32_e32 v20, 4, v20
	v_dot4c_i32_i8_e32 v25, v24, v36
	v_and_b32_e32 v20, 0xf0f0f0f, v20
	v_dot4c_i32_i8_e32 v25, v20, v37
	v_and_b32_e32 v20, 0xf0f0f0f, v21
	v_mov_b32_e32 v24, 0
	v_dot4c_i32_i8_e32 v24, v20, v38
	v_lshrrev_b32_e32 v20, 4, v21
	v_and_b32_e32 v20, 0xf0f0f0f, v20
	v_dot4c_i32_i8_e32 v24, v20, v39
	v_and_b32_e32 v20, 0xf0f0f0f, v22
	v_dot4c_i32_i8_e32 v25, v20, v32
	v_lshrrev_b32_e32 v20, 4, v22
	v_and_b32_e32 v20, 0xf0f0f0f, v20
	v_dot4c_i32_i8_e32 v25, v20, v33
	v_and_b32_e32 v20, 0xf0f0f0f, v23
	v_dot4c_i32_i8_e32 v24, v20, v34
	v_lshrrev_b32_e32 v20, 4, v23
	v_and_b32_e32 v20, 0xf0f0f0f, v20
	v_dot4c_i32_i8_e32 v24, v20, v35
	v_and_b32_e32 v20, 0xf0f0f0f, v16
	v_mov_b32_e32 v21, 0
	v_lshrrev_b32_e32 v16, 4, v16
	v_dot4c_i32_i8_e32 v21, v20, v36
	v_and_b32_e32 v16, 0xf0f0f0f, v16
	v_dot4c_i32_i8_e32 v21, v16, v37
	v_and_b32_e32 v16, 0xf0f0f0f, v17
	v_mov_b32_e32 v20, 0
	v_dot4c_i32_i8_e32 v20, v16, v38
	v_lshrrev_b32_e32 v16, 4, v17
	v_and_b32_e32 v16, 0xf0f0f0f, v16
	v_dot4c_i32_i8_e32 v20, v16, v39
	v_and_b32_e32 v16, 0xf0f0f0f, v18
	v_dot4c_i32_i8_e32 v21, v16, v32
	v_lshrrev_b32_e32 v16, 4, v18
	v_and_b32_e32 v16, 0xf0f0f0f, v16
	v_dot4c_i32_i8_e32 v21, v16, v33
	v_and_b32_e32 v16, 0xf0f0f0f, v19
	v_dot4c_i32_i8_e32 v20, v16, v34
	v_lshrrev_b32_e32 v16, 4, v19
	v_and_b32_e32 v16, 0xf0f0f0f, v16
	v_dot4c_i32_i8_e32 v20, v16, v35
	v_add_u32_e32 v18, v25, v24
	v_sub_u32_e32 v18, v18, v78
	s_waitcnt vmcnt(20)
; #define P12_ISSUE(c_, i_, h_, CW_, SC_) do { _Pragma("unroll") for (int bb = 0; bb < 8; ++bb) { const unsigned ro = (unsigned)(c_) * 16384u + (unsigned)EL[(i_) * 128 + ((h_) * 8 + bb) * 8 + g8]; \
;         CW_[bb] = *(const v4u*)(U4 + (size_t)(ro * 128u + 16u * (unsigned)k8)); SC_[bb] = USS[(size_t)(ro * 8u + (unsigned)k8)]; } } while (0)
; #define P12_COMP(i_, h_, CW_, SC_) do { _Pragma("unroll") for (int bb = 0; bb < 8; ++bb) { int a0 = 0, a1 = 0; P12_U4(CW_[bb].x, xa.x, xa.y, a0); P12_U4(CW_[bb].y, xa.z, xa.w, a1); P12_U4(CW_[bb].z, xb.x, xb.y, a0); P12_U4(CW_[bb].w, xb.z, xb.w, a1); \
;         psum[(i_)][(h_) * 8 + bb] += __uint_as_float(SC_[bb] << 16) * (float)((a0 + a1) - xo); } } while (0)
; #define P12_BAR() asm volatile("" ::: "memory")
; __device__ __forceinline__ void p12_peer(Frame& F) {
;     ...
;           P12_XQ(c, 0); P12_ISSUE(c, 0, 1, cwB, scB); P12_BAR(); P12_COMP(0, 0, cwA, scA); P12_ISSUE(c, 1, 0, cwA, scA); P12_BAR(); P12_COMP(0, 1, cwB, scB);
;           P12_XQ(c, 1); P12_ISSUE(c, 1, 1, cwB, scB); P12_BAR(); P12_COMP(1, 0, cwA, scA); P12_ISSUE(c, 2, 0, cwA, scA); P12_BAR(); P12_COMP(1, 1, cwB, scB);
;           P12_XQ(c, 2); P12_ISSUE(c, 2, 1, cwB, scB); P12_BAR(); P12_COMP(2, 0, cwA, scA); P12_ISSUE(c, 3, 0, cwA, scA); P12_BAR(); P12_COMP(2, 1, cwB, scB);
;           P12_XQ(c, 3); P12_ISSUE(c, 3, 1, cwB, scB); P12_BAR(); P12_COMP(3, 0, cwA, scA); P12_ISSUE(cn, 0, 0, cwA, scA); P12_BAR(); P12_COMP(3, 1, cwB, scB);
	v_lshlrev_b32_e32 v17, 16, v234
	v_add_u32_e32 v19, v21, v20
	v_sub_u32_e32 v20, v19, v78
	v_cvt_f32_i32_e32 v19, v18
	v_cvt_f32_i32_e32 v18, v20
	v_lshlrev_b32_e32 v16, 16, v235
	v_mov_b32_e32 v90, 0
	s_cmp_eq_u32 s45, 0x40000
	v_pk_fma_f32 v[108:109], v[16:17], v[18:19], v[108:109]
	v_and_b32_e32 v16, 0xf0f0f0f, v12
	v_mov_b32_e32 v17, 0
	v_lshrrev_b32_e32 v12, 4, v12
	v_dot4c_i32_i8_e32 v17, v16, v36
	v_and_b32_e32 v12, 0xf0f0f0f, v12
	v_dot4c_i32_i8_e32 v17, v12, v37
	v_and_b32_e32 v12, 0xf0f0f0f, v13
	v_mov_b32_e32 v16, 0
	v_dot4c_i32_i8_e32 v16, v12, v38
	v_lshrrev_b32_e32 v12, 4, v13
	v_and_b32_e32 v12, 0xf0f0f0f, v12
	v_dot4c_i32_i8_e32 v16, v12, v39
	v_and_b32_e32 v12, 0xf0f0f0f, v14
	v_dot4c_i32_i8_e32 v17, v12, v32
	v_lshrrev_b32_e32 v12, 4, v14
	v_and_b32_e32 v12, 0xf0f0f0f, v12
	v_dot4c_i32_i8_e32 v17, v12, v33
	v_and_b32_e32 v12, 0xf0f0f0f, v15
	v_dot4c_i32_i8_e32 v16, v12, v34
	v_lshrrev_b32_e32 v12, 4, v15
	v_and_b32_e32 v12, 0xf0f0f0f, v12
	v_dot4c_i32_i8_e32 v16, v12, v35
	v_and_b32_e32 v12, 0xf0f0f0f, v8
	v_mov_b32_e32 v13, 0
	v_lshrrev_b32_e32 v8, 4, v8
	v_dot4c_i32_i8_e32 v13, v12, v36
	v_and_b32_e32 v8, 0xf0f0f0f, v8
	v_dot4c_i32_i8_e32 v13, v8, v37
	v_and_b32_e32 v8, 0xf0f0f0f, v9
	v_mov_b32_e32 v12, 0
	v_dot4c_i32_i8_e32 v12, v8, v38
	v_lshrrev_b32_e32 v8, 4, v9
	v_and_b32_e32 v8, 0xf0f0f0f, v8
	v_dot4c_i32_i8_e32 v12, v8, v39
	v_and_b32_e32 v8, 0xf0f0f0f, v10
	v_dot4c_i32_i8_e32 v13, v8, v32
	v_lshrrev_b32_e32 v8, 4, v10
	v_and_b32_e32 v8, 0xf0f0f0f, v8
	v_dot4c_i32_i8_e32 v13, v8, v33
	v_and_b32_e32 v8, 0xf0f0f0f, v11
	v_dot4c_i32_i8_e32 v12, v8, v34
	v_lshrrev_b32_e32 v8, 4, v11
	v_and_b32_e32 v8, 0xf0f0f0f, v8
	v_dot4c_i32_i8_e32 v12, v8, v35
	v_add_u32_e32 v11, v17, v16
	s_waitcnt vmcnt(18)
	v_lshlrev_b32_e32 v9, 16, v237
	v_lshlrev_b32_e32 v8, 16, v236
	v_add_u32_e32 v10, v13, v12
	v_sub_u32_e32 v12, v11, v78
	v_sub_u32_e32 v10, v10, v78
	v_cvt_f32_i32_e32 v11, v10
	v_cvt_f32_i32_e32 v10, v12
	s_waitcnt vmcnt(15)
	v_and_b32_e32 v89, 0xf0f0f0f, v68
	v_lshrrev_b32_e32 v68, 4, v68
	v_dot4c_i32_i8_e32 v90, v89, v36
	v_pk_fma_f32 v[106:107], v[8:9], v[10:11], v[106:107]
	v_and_b32_e32 v8, 0xf0f0f0f, v4
	v_mov_b32_e32 v9, 0
	v_lshrrev_b32_e32 v4, 4, v4
	v_dot4c_i32_i8_e32 v9, v8, v36
	v_and_b32_e32 v4, 0xf0f0f0f, v4
	v_dot4c_i32_i8_e32 v9, v4, v37
	v_and_b32_e32 v4, 0xf0f0f0f, v5
	v_mov_b32_e32 v8, 0
	v_dot4c_i32_i8_e32 v8, v4, v38
	v_lshrrev_b32_e32 v4, 4, v5
	v_and_b32_e32 v4, 0xf0f0f0f, v4
	v_dot4c_i32_i8_e32 v8, v4, v39
	v_and_b32_e32 v4, 0xf0f0f0f, v6
	v_dot4c_i32_i8_e32 v9, v4, v32
	v_lshrrev_b32_e32 v4, 4, v6
	v_and_b32_e32 v4, 0xf0f0f0f, v4
	v_dot4c_i32_i8_e32 v9, v4, v33
	v_and_b32_e32 v4, 0xf0f0f0f, v7
	v_dot4c_i32_i8_e32 v8, v4, v34
	v_lshrrev_b32_e32 v4, 4, v7
	v_and_b32_e32 v4, 0xf0f0f0f, v4
	v_dot4c_i32_i8_e32 v8, v4, v35
	v_and_b32_e32 v4, 0xf0f0f0f, v0
	v_mov_b32_e32 v5, 0
	v_lshrrev_b32_e32 v0, 4, v0
	v_dot4c_i32_i8_e32 v5, v4, v36
	v_and_b32_e32 v0, 0xf0f0f0f, v0
	v_dot4c_i32_i8_e32 v5, v0, v37
	v_and_b32_e32 v0, 0xf0f0f0f, v1
	v_mov_b32_e32 v4, 0
	v_dot4c_i32_i8_e32 v4, v0, v38
	v_lshrrev_b32_e32 v0, 4, v1
	v_and_b32_e32 v0, 0xf0f0f0f, v0
	v_dot4c_i32_i8_e32 v4, v0, v39
	v_and_b32_e32 v0, 0xf0f0f0f, v2
	v_dot4c_i32_i8_e32 v5, v0, v32
	v_lshrrev_b32_e32 v0, 4, v2
	v_and_b32_e32 v0, 0xf0f0f0f, v0
	v_dot4c_i32_i8_e32 v5, v0, v33
	v_and_b32_e32 v0, 0xf0f0f0f, v3
	v_dot4c_i32_i8_e32 v4, v0, v34
	v_lshrrev_b32_e32 v0, 4, v3
	v_and_b32_e32 v0, 0xf0f0f0f, v0
	v_dot4c_i32_i8_e32 v4, v0, v35
	v_add_u32_e32 v3, v9, v8
	v_lshlrev_b32_e32 v1, 16, v239
	v_lshlrev_b32_e32 v0, 16, v238
	v_add_u32_e32 v2, v5, v4
	v_sub_u32_e32 v4, v3, v78
	v_sub_u32_e32 v2, v2, v78
	v_cvt_f32_i32_e32 v3, v2
	v_cvt_f32_i32_e32 v2, v4
	v_and_b32_e32 v68, 0xf0f0f0f, v68
	v_dot4c_i32_i8_e32 v90, v68, v37
	v_and_b32_e32 v68, 0xf0f0f0f, v69
	v_pk_fma_f32 v[104:105], v[0:1], v[2:3], v[104:105]
	ds_read_u16 v0, v93 offset:16384
	ds_read_u16 v1, v93 offset:16400
	ds_read_u16 v2, v93 offset:16416
	ds_read_u16 v3, v93 offset:16432
	v_mov_b32_e32 v89, 0
	s_waitcnt lgkmcnt(3)
	v_add_u32_e32 v0, s44, v0
	v_lshl_or_b32 v4, v0, 7, v165
	v_lshl_or_b32 v0, v0, 4, v95
	global_load_dwordx4 v[28:31], v4, s[0:1]
	global_load_ushort v72, v95, s[18:19]
	s_waitcnt lgkmcnt(2)
	v_add_u32_e32 v0, s44, v1
	v_dot4c_i32_i8_e32 v89, v68, v38
	v_lshrrev_b32_e32 v68, 4, v69
	v_lshl_or_b32 v1, v0, 7, v165
	v_lshl_or_b32 v0, v0, 4, v95
	v_and_b32_e32 v68, 0xf0f0f0f, v68
	global_load_dwordx4 v[24:27], v1, s[0:1]
	global_load_ushort v73, v95, s[18:19]
	s_waitcnt lgkmcnt(1)
	v_add_u32_e32 v0, s44, v2
	v_dot4c_i32_i8_e32 v89, v68, v39
	v_and_b32_e32 v68, 0xf0f0f0f, v70
	v_lshl_or_b32 v1, v0, 7, v165
	v_lshl_or_b32 v0, v0, 4, v95
	v_dot4c_i32_i8_e32 v90, v68, v32
	v_lshrrev_b32_e32 v68, 4, v70
	global_load_dwordx4 v[20:23], v1, s[0:1]
	global_load_ushort v74, v95, s[18:19]
	s_waitcnt lgkmcnt(0)
	v_add_u32_e32 v0, s44, v3
	v_and_b32_e32 v68, 0xf0f0f0f, v68
	v_lshl_or_b32 v1, v0, 7, v165
	v_lshl_or_b32 v0, v0, 4, v95
	v_dot4c_i32_i8_e32 v90, v68, v33
	v_and_b32_e32 v68, 0xf0f0f0f, v71
	global_load_dwordx4 v[16:19], v1, s[0:1]
	global_load_ushort v75, v95, s[18:19]
	ds_read_u16 v0, v93 offset:16448
	v_dot4c_i32_i8_e32 v89, v68, v34
	v_lshrrev_b32_e32 v68, 4, v71
	v_and_b32_e32 v68, 0xf0f0f0f, v68
	v_dot4c_i32_i8_e32 v89, v68, v35
	s_waitcnt vmcnt(22)
	v_and_b32_e32 v68, 0xf0f0f0f, v64
	v_mov_b32_e32 v69, 0
	v_lshrrev_b32_e32 v64, 4, v64
	v_dot4c_i32_i8_e32 v69, v68, v36
	v_and_b32_e32 v64, 0xf0f0f0f, v64
	v_dot4c_i32_i8_e32 v69, v64, v37
	v_and_b32_e32 v64, 0xf0f0f0f, v65
	v_mov_b32_e32 v68, 0
	s_waitcnt lgkmcnt(0)
	v_add_u32_e32 v0, s44, v0
	v_dot4c_i32_i8_e32 v68, v64, v38
	v_lshrrev_b32_e32 v64, 4, v65
	v_lshl_or_b32 v1, v0, 7, v165
	v_lshl_or_b32 v0, v0, 4, v95
	v_and_b32_e32 v64, 0xf0f0f0f, v64
	global_load_dwordx4 v[12:15], v1, s[0:1]
	global_load_ushort v76, v95, s[18:19]
	ds_read_u16 v0, v93 offset:16464
	v_dot4c_i32_i8_e32 v68, v64, v39
	v_and_b32_e32 v64, 0xf0f0f0f, v66
	v_dot4c_i32_i8_e32 v69, v64, v32
	v_lshrrev_b32_e32 v64, 4, v66
	v_and_b32_e32 v64, 0xf0f0f0f, v64
	v_dot4c_i32_i8_e32 v69, v64, v33
	v_and_b32_e32 v64, 0xf0f0f0f, v67
	v_dot4c_i32_i8_e32 v68, v64, v34
	v_lshrrev_b32_e32 v64, 4, v67
	s_waitcnt lgkmcnt(0)
	v_add_u32_e32 v0, s44, v0
	v_and_b32_e32 v64, 0xf0f0f0f, v64
	v_lshl_or_b32 v1, v0, 7, v165
	v_lshl_or_b32 v0, v0, 4, v95
	v_dot4c_i32_i8_e32 v68, v64, v35
	global_load_dwordx4 v[8:11], v1, s[0:1]
	global_load_ushort v77, v95, s[18:19]
	ds_read_u16 v0, v93 offset:16480
	v_add_u32_e32 v66, v90, v89
	v_sub_u32_e32 v67, v68, v78
	v_add_u32_e32 v67, v67, v69
	v_sub_u32_e32 v66, v66, v78
	v_cvt_f32_i32_e32 v66, v66
	v_cvt_f32_i32_e32 v67, v67
	s_waitcnt lgkmcnt(0)
	v_add_u32_e32 v0, s44, v0
	s_waitcnt vmcnt(18)
	v_lshlrev_b32_e32 v65, 16, v241
	v_lshlrev_b32_e32 v64, 16, v240
	v_lshl_or_b32 v1, v0, 7, v165
	v_lshl_or_b32 v0, v0, 4, v95
	v_pk_fma_f32 v[102:103], v[64:65], v[66:67], v[102:103]
	v_and_b32_e32 v64, 0xf0f0f0f, v60
	v_mov_b32_e32 v65, 0
	v_lshrrev_b32_e32 v60, 4, v60
	global_load_dwordx4 v[4:7], v1, s[0:1]
	global_load_ushort v87, v95, s[18:19]
	ds_read_u16 v0, v93 offset:16496
	v_dot4c_i32_i8_e32 v65, v64, v36
	v_and_b32_e32 v60, 0xf0f0f0f, v60
	v_dot4c_i32_i8_e32 v65, v60, v37
	v_and_b32_e32 v60, 0xf0f0f0f, v61
	v_mov_b32_e32 v64, 0
	v_dot4c_i32_i8_e32 v64, v60, v38
	v_lshrrev_b32_e32 v60, 4, v61
	v_and_b32_e32 v60, 0xf0f0f0f, v60
	v_dot4c_i32_i8_e32 v64, v60, v39
	v_and_b32_e32 v60, 0xf0f0f0f, v62
	s_waitcnt lgkmcnt(0)
	v_add_u32_e32 v88, s44, v0
	v_dot4c_i32_i8_e32 v65, v60, v32
	v_lshrrev_b32_e32 v60, 4, v62
	v_lshl_or_b32 v0, v88, 7, v165
	v_lshl_or_b32 v88, v88, 4, v95
	v_and_b32_e32 v60, 0xf0f0f0f, v60
	global_load_dwordx4 v[0:3], v0, s[0:1]
	v_dot4c_i32_i8_e32 v65, v60, v33
	global_load_ushort v88, v95, s[18:19]
	v_and_b32_e32 v60, 0xf0f0f0f, v63
	v_dot4c_i32_i8_e32 v64, v60, v34
	v_lshrrev_b32_e32 v60, 4, v63
	v_and_b32_e32 v60, 0xf0f0f0f, v60
	v_dot4c_i32_i8_e32 v64, v60, v35
	v_and_b32_e32 v60, 0xf0f0f0f, v56
	v_mov_b32_e32 v61, 0
	v_lshrrev_b32_e32 v56, 4, v56
	v_dot4c_i32_i8_e32 v61, v60, v36
	v_and_b32_e32 v56, 0xf0f0f0f, v56
	v_dot4c_i32_i8_e32 v61, v56, v37
	v_and_b32_e32 v56, 0xf0f0f0f, v57
	v_mov_b32_e32 v60, 0
	v_dot4c_i32_i8_e32 v60, v56, v38
	v_lshrrev_b32_e32 v56, 4, v57
	v_and_b32_e32 v56, 0xf0f0f0f, v56
	v_dot4c_i32_i8_e32 v60, v56, v39
	v_and_b32_e32 v56, 0xf0f0f0f, v58
	v_dot4c_i32_i8_e32 v61, v56, v32
	v_lshrrev_b32_e32 v56, 4, v58
	v_and_b32_e32 v56, 0xf0f0f0f, v56
	v_dot4c_i32_i8_e32 v61, v56, v33
	v_and_b32_e32 v56, 0xf0f0f0f, v59
	v_dot4c_i32_i8_e32 v60, v56, v34
	v_lshrrev_b32_e32 v56, 4, v59
	v_and_b32_e32 v56, 0xf0f0f0f, v56
	v_dot4c_i32_i8_e32 v60, v56, v35
	v_sub_u32_e32 v59, v64, v78
	s_waitcnt vmcnt(20)
	v_lshlrev_b32_e32 v57, 16, v243
	v_lshlrev_b32_e32 v56, 16, v242
	v_sub_u32_e32 v58, v60, v78
	v_add_u32_e32 v60, v59, v65
	v_add_u32_e32 v58, v58, v61
	v_cvt_f32_i32_e32 v59, v58
	v_cvt_f32_i32_e32 v58, v60
	s_mov_b32 s44, s45
	v_pk_fma_f32 v[100:101], v[56:57], v[58:59], v[100:101]
	v_and_b32_e32 v56, 0xf0f0f0f, v52
	v_mov_b32_e32 v57, 0
	v_lshrrev_b32_e32 v52, 4, v52
	v_dot4c_i32_i8_e32 v57, v56, v36
	v_and_b32_e32 v52, 0xf0f0f0f, v52
	v_dot4c_i32_i8_e32 v57, v52, v37
	v_and_b32_e32 v52, 0xf0f0f0f, v53
	v_mov_b32_e32 v56, 0
	v_dot4c_i32_i8_e32 v56, v52, v38
	v_lshrrev_b32_e32 v52, 4, v53
	v_and_b32_e32 v52, 0xf0f0f0f, v52
	v_dot4c_i32_i8_e32 v56, v52, v39
	v_and_b32_e32 v52, 0xf0f0f0f, v54
	v_dot4c_i32_i8_e32 v57, v52, v32
	v_lshrrev_b32_e32 v52, 4, v54
	v_and_b32_e32 v52, 0xf0f0f0f, v52
	v_dot4c_i32_i8_e32 v57, v52, v33
	v_and_b32_e32 v52, 0xf0f0f0f, v55
	v_dot4c_i32_i8_e32 v56, v52, v34
	v_lshrrev_b32_e32 v52, 4, v55
	v_and_b32_e32 v52, 0xf0f0f0f, v52
	v_dot4c_i32_i8_e32 v56, v52, v35
	v_and_b32_e32 v52, 0xf0f0f0f, v48
	v_mov_b32_e32 v53, 0
	v_lshrrev_b32_e32 v48, 4, v48
	v_dot4c_i32_i8_e32 v53, v52, v36
	v_and_b32_e32 v48, 0xf0f0f0f, v48
	v_dot4c_i32_i8_e32 v53, v48, v37
	v_and_b32_e32 v48, 0xf0f0f0f, v49
	v_mov_b32_e32 v52, 0
	v_dot4c_i32_i8_e32 v52, v48, v38
	v_lshrrev_b32_e32 v48, 4, v49
	v_and_b32_e32 v48, 0xf0f0f0f, v48
	v_dot4c_i32_i8_e32 v52, v48, v39
	v_and_b32_e32 v48, 0xf0f0f0f, v50
	v_dot4c_i32_i8_e32 v53, v48, v32
	v_lshrrev_b32_e32 v48, 4, v50
	v_and_b32_e32 v48, 0xf0f0f0f, v48
	v_dot4c_i32_i8_e32 v53, v48, v33
	v_and_b32_e32 v48, 0xf0f0f0f, v51
	v_dot4c_i32_i8_e32 v52, v48, v34
	v_lshrrev_b32_e32 v48, 4, v51
	v_and_b32_e32 v48, 0xf0f0f0f, v48
	v_dot4c_i32_i8_e32 v52, v48, v35
	v_sub_u32_e32 v51, v56, v78
	s_waitcnt vmcnt(18)
; #define P12_ISSUE(c_, i_, h_, CW_, SC_) do { _Pragma("unroll") for (int bb = 0; bb < 8; ++bb) { const unsigned ro = (unsigned)(c_) * 16384u + (unsigned)EL[(i_) * 128 + ((h_) * 8 + bb) * 8 + g8]; \
;         CW_[bb] = *(const v4u*)(U4 + (size_t)(ro * 128u + 16u * (unsigned)k8)); SC_[bb] = USS[(size_t)(ro * 8u + (unsigned)k8)]; } } while (0)
; #define P12_COMP(i_, h_, CW_, SC_) do { _Pragma("unroll") for (int bb = 0; bb < 8; ++bb) { int a0 = 0, a1 = 0; P12_U4(CW_[bb].x, xa.x, xa.y, a0); P12_U4(CW_[bb].y, xa.z, xa.w, a1); P12_U4(CW_[bb].z, xb.x, xb.y, a0); P12_U4(CW_[bb].w, xb.z, xb.w, a1); \
;         psum[(i_)][(h_) * 8 + bb] += __uint_as_float(SC_[bb] << 16) * (float)((a0 + a1) - xo); } } while (0)
; #define P12_BAR() asm volatile("" ::: "memory")
; __device__ __forceinline__ void p12_peer(Frame& F) {
;     ...
;           P12_XQ(c, 0); P12_ISSUE(c, 0, 1, cwB, scB); P12_BAR(); P12_COMP(0, 0, cwA, scA); P12_ISSUE(c, 1, 0, cwA, scA); P12_BAR(); P12_COMP(0, 1, cwB, scB);
	v_lshlrev_b32_e32 v49, 16, v245
	v_lshlrev_b32_e32 v48, 16, v244
	v_sub_u32_e32 v50, v52, v78
	v_add_u32_e32 v52, v51, v57
	v_add_u32_e32 v50, v50, v53
	v_cvt_f32_i32_e32 v51, v50
	v_cvt_f32_i32_e32 v50, v52
	v_pk_fma_f32 v[98:99], v[48:49], v[50:51], v[98:99]
	v_and_b32_e32 v48, 0xf0f0f0f, v44
	v_mov_b32_e32 v49, 0
	v_lshrrev_b32_e32 v44, 4, v44
	v_dot4c_i32_i8_e32 v49, v48, v36
	v_and_b32_e32 v44, 0xf0f0f0f, v44
	v_dot4c_i32_i8_e32 v49, v44, v37
	v_and_b32_e32 v44, 0xf0f0f0f, v45
	v_mov_b32_e32 v48, 0
	v_dot4c_i32_i8_e32 v48, v44, v38
	v_lshrrev_b32_e32 v44, 4, v45
	v_and_b32_e32 v44, 0xf0f0f0f, v44
	v_dot4c_i32_i8_e32 v48, v44, v39
	v_and_b32_e32 v44, 0xf0f0f0f, v46
	v_dot4c_i32_i8_e32 v49, v44, v32
	v_lshrrev_b32_e32 v44, 4, v46
	v_and_b32_e32 v44, 0xf0f0f0f, v44
	v_dot4c_i32_i8_e32 v49, v44, v33
	v_and_b32_e32 v44, 0xf0f0f0f, v47
	v_dot4c_i32_i8_e32 v48, v44, v34
	v_lshrrev_b32_e32 v44, 4, v47
	v_and_b32_e32 v44, 0xf0f0f0f, v44
	v_dot4c_i32_i8_e32 v48, v44, v35
	v_and_b32_e32 v44, 0xf0f0f0f, v40
	v_mov_b32_e32 v45, 0
	v_dot4c_i32_i8_e32 v45, v44, v36
	v_lshrrev_b32_e32 v36, 4, v40
	v_and_b32_e32 v36, 0xf0f0f0f, v36
	v_dot4c_i32_i8_e32 v45, v36, v37
	v_and_b32_e32 v36, 0xf0f0f0f, v41
	v_mov_b32_e32 v37, 0
	v_dot4c_i32_i8_e32 v37, v36, v38
	v_lshrrev_b32_e32 v36, 4, v41
	v_and_b32_e32 v36, 0xf0f0f0f, v36
	v_dot4c_i32_i8_e32 v37, v36, v39
	v_and_b32_e32 v36, 0xf0f0f0f, v42
	v_dot4c_i32_i8_e32 v45, v36, v32
	v_lshrrev_b32_e32 v32, 4, v42
	v_and_b32_e32 v32, 0xf0f0f0f, v32
	v_dot4c_i32_i8_e32 v45, v32, v33
	v_and_b32_e32 v32, 0xf0f0f0f, v43
	v_dot4c_i32_i8_e32 v37, v32, v34
	v_lshrrev_b32_e32 v32, 4, v43
	v_and_b32_e32 v32, 0xf0f0f0f, v32
	v_dot4c_i32_i8_e32 v37, v32, v35
	v_sub_u32_e32 v35, v48, v78
	v_add_u32_e32 v36, v35, v49
	s_waitcnt vmcnt(16)
	v_lshlrev_b32_e32 v33, 16, v247
	v_sub_u32_e32 v34, v37, v78
	v_add_u32_e32 v34, v34, v45
	v_cvt_f32_i32_e32 v35, v34
	v_cvt_f32_i32_e32 v34, v36
	v_lshlrev_b32_e32 v32, 16, v246
	s_waitcnt vmcnt(0)
	v_perm_b32 v40, v190, v191, s48
	v_perm_b32 v41, v188, v189, s48
	v_pk_fma_f32 v[96:97], v[32:33], v[34:35], v[96:97]
	v_perm_b32 v42, v186, v187, s48
	v_perm_b32 v43, v184, v185, s48
	ds_read_b128 v[36:39], v166
	ds_read_b128 v[32:35], v166 offset:16
	ds_read_u16 v44, v93 offset:16512
	ds_read_u16 v45, v93 offset:16528
	ds_read_u16 v46, v93 offset:16544
	ds_read_u16 v47, v93 offset:16560
	v_mov_b32_e32 v48, 0
	s_waitcnt lgkmcnt(3)
	v_add_u32_e32 v44, s44, v44
	v_lshl_or_b32 v49, v44, 7, v165
	global_load_dwordx4 v[88:91], v49, s[0:1]
	v_lshl_or_b32 v49, v44, 4, v95
	s_waitcnt lgkmcnt(2)
	v_add_u32_e32 v44, s44, v45
	v_lshl_or_b32 v45, v44, 7, v165
	v_lshl_or_b32 v50, v44, 4, v95
	s_waitcnt lgkmcnt(1)
	v_add_u32_e32 v44, s44, v46
	global_load_dwordx4 v[84:87], v45, s[0:1]
	v_lshl_or_b32 v45, v44, 7, v165
	v_lshl_or_b32 v51, v44, 4, v95
	s_waitcnt lgkmcnt(0)
	v_add_u32_e32 v44, s44, v47
	global_load_dwordx4 v[80:83], v45, s[0:1]
	v_lshl_or_b32 v45, v44, 7, v165
	v_lshl_or_b32 v56, v44, 4, v95
	ds_read_u16 v44, v93 offset:16576
	global_load_dwordx4 v[76:79], v45, s[0:1]
	v_dot4c_i32_i8_e32 v48, 0x1010101, v36
	v_dot4c_i32_i8_e32 v48, 0x1010101, v37
	v_dot4c_i32_i8_e32 v48, 0x1010101, v38
	s_waitcnt lgkmcnt(0)
	v_add_u32_e32 v44, s44, v44
	v_lshl_or_b32 v45, v44, 7, v165
	v_lshl_or_b32 v57, v44, 4, v95
	ds_read_u16 v44, v93 offset:16592
	global_load_dwordx4 v[68:71], v45, s[0:1]
	v_dot4c_i32_i8_e32 v48, 0x1010101, v39
	v_dot4c_i32_i8_e32 v48, 0x1010101, v32
	v_dot4c_i32_i8_e32 v48, 0x1010101, v33
	s_waitcnt lgkmcnt(0)
	v_add_u32_e32 v44, s44, v44
	v_lshl_or_b32 v45, v44, 7, v165
	v_lshl_or_b32 v58, v44, 4, v95
	ds_read_u16 v44, v93 offset:16608
	global_load_dwordx4 v[60:63], v45, s[0:1]
	v_dot4c_i32_i8_e32 v48, 0x1010101, v34
	v_dot4c_i32_i8_e32 v48, 0x1010101, v35
	s_add_i32 s45, s44, 0x4000
	s_waitcnt lgkmcnt(0)
	v_add_u32_e32 v44, s44, v44
	v_lshl_or_b32 v45, v44, 7, v165
	v_lshl_or_b32 v59, v44, 4, v95
	ds_read_u16 v44, v93 offset:16624
	global_load_dwordx4 v[52:55], v45, s[0:1]
	v_lshlrev_b32_e32 v171, 3, v48
	s_waitcnt vmcnt(14)
	v_and_b32_e32 v48, 0xf0f0f0f, v28
	v_lshrrev_b32_e32 v28, 4, v28
	s_waitcnt lgkmcnt(0)
	v_add_u32_e32 v64, s44, v44
	v_lshl_or_b32 v44, v64, 7, v165
	global_load_dwordx4 v[44:47], v44, s[0:1]
	v_lshl_or_b32 v64, v64, 4, v95
	global_load_ushort v182, v95, s[18:19]
	global_load_ushort v183, v95, s[18:19]
	global_load_ushort v180, v95, s[18:19]
	global_load_ushort v181, v95, s[18:19]
	global_load_ushort v176, v95, s[18:19]
	global_load_ushort v177, v95, s[18:19]
	global_load_ushort v172, v95, s[18:19]
	global_load_ushort v173, v95, s[18:19]
	v_mov_b32_e32 v49, 0
	v_dot4c_i32_i8_e32 v49, v48, v36
	v_and_b32_e32 v28, 0xf0f0f0f, v28
	v_dot4c_i32_i8_e32 v49, v28, v37
	v_and_b32_e32 v28, 0xf0f0f0f, v29
	v_mov_b32_e32 v48, 0
	v_dot4c_i32_i8_e32 v48, v28, v38
	v_lshrrev_b32_e32 v28, 4, v29
	v_and_b32_e32 v28, 0xf0f0f0f, v28
	v_dot4c_i32_i8_e32 v48, v28, v39
	v_and_b32_e32 v28, 0xf0f0f0f, v30
	v_dot4c_i32_i8_e32 v49, v28, v32
	v_lshrrev_b32_e32 v28, 4, v30
	v_and_b32_e32 v28, 0xf0f0f0f, v28
	v_dot4c_i32_i8_e32 v49, v28, v33
	v_and_b32_e32 v28, 0xf0f0f0f, v31
	v_dot4c_i32_i8_e32 v48, v28, v34
	v_lshrrev_b32_e32 v28, 4, v31
	v_and_b32_e32 v28, 0xf0f0f0f, v28
	v_dot4c_i32_i8_e32 v48, v28, v35
	s_waitcnt vmcnt(22)
	v_and_b32_e32 v28, 0xf0f0f0f, v24
	v_mov_b32_e32 v29, 0
	v_lshrrev_b32_e32 v24, 4, v24
	v_dot4c_i32_i8_e32 v29, v28, v36
	v_and_b32_e32 v24, 0xf0f0f0f, v24
	v_dot4c_i32_i8_e32 v29, v24, v37
	v_and_b32_e32 v24, 0xf0f0f0f, v25
	v_mov_b32_e32 v28, 0
	v_dot4c_i32_i8_e32 v28, v24, v38
	v_lshrrev_b32_e32 v24, 4, v25
	v_and_b32_e32 v24, 0xf0f0f0f, v24
	v_dot4c_i32_i8_e32 v28, v24, v39
	v_and_b32_e32 v24, 0xf0f0f0f, v26
	v_dot4c_i32_i8_e32 v29, v24, v32
	v_lshrrev_b32_e32 v24, 4, v26
	v_and_b32_e32 v24, 0xf0f0f0f, v24
	v_dot4c_i32_i8_e32 v29, v24, v33
	v_and_b32_e32 v24, 0xf0f0f0f, v27
	v_dot4c_i32_i8_e32 v28, v24, v34
	v_lshrrev_b32_e32 v24, 4, v27
	v_and_b32_e32 v24, 0xf0f0f0f, v24
	v_dot4c_i32_i8_e32 v28, v24, v35
	v_add_u32_e32 v26, v49, v48
	v_sub_u32_e32 v26, v26, v171
	v_and_b32_e32 v25, 0xffff0000, v43
	v_add_u32_e32 v27, v29, v28
	v_sub_u32_e32 v28, v27, v171
	v_cvt_f32_i32_e32 v27, v26
	v_cvt_f32_i32_e32 v26, v28
	v_lshlrev_b32_e32 v24, 16, v43
	s_cmp_eq_u32 s44, 0x3c000
	v_pk_fma_f32 v[158:159], v[24:25], v[26:27], v[158:159]
	s_waitcnt vmcnt(21)
	v_and_b32_e32 v24, 0xf0f0f0f, v20
	v_mov_b32_e32 v25, 0
	v_lshrrev_b32_e32 v20, 4, v20
	v_dot4c_i32_i8_e32 v25, v24, v36
	v_and_b32_e32 v20, 0xf0f0f0f, v20
	v_dot4c_i32_i8_e32 v25, v20, v37
	v_and_b32_e32 v20, 0xf0f0f0f, v21
	v_mov_b32_e32 v24, 0
	v_dot4c_i32_i8_e32 v24, v20, v38
	v_lshrrev_b32_e32 v20, 4, v21
	v_and_b32_e32 v20, 0xf0f0f0f, v20
	v_dot4c_i32_i8_e32 v24, v20, v39
	v_and_b32_e32 v20, 0xf0f0f0f, v22
	v_dot4c_i32_i8_e32 v25, v20, v32
	v_lshrrev_b32_e32 v20, 4, v22
	v_and_b32_e32 v20, 0xf0f0f0f, v20
	v_dot4c_i32_i8_e32 v25, v20, v33
	v_and_b32_e32 v20, 0xf0f0f0f, v23
	v_dot4c_i32_i8_e32 v24, v20, v34
	v_lshrrev_b32_e32 v20, 4, v23
	v_and_b32_e32 v20, 0xf0f0f0f, v20
	v_dot4c_i32_i8_e32 v24, v20, v35
	s_waitcnt vmcnt(20)
	v_and_b32_e32 v20, 0xf0f0f0f, v16
	v_mov_b32_e32 v21, 0
	v_lshrrev_b32_e32 v16, 4, v16
	v_dot4c_i32_i8_e32 v21, v20, v36
	v_and_b32_e32 v16, 0xf0f0f0f, v16
	v_dot4c_i32_i8_e32 v21, v16, v37
	v_and_b32_e32 v16, 0xf0f0f0f, v17
	v_mov_b32_e32 v20, 0
	v_dot4c_i32_i8_e32 v20, v16, v38
	v_lshrrev_b32_e32 v16, 4, v17
	v_and_b32_e32 v16, 0xf0f0f0f, v16
	v_dot4c_i32_i8_e32 v20, v16, v39
	v_and_b32_e32 v16, 0xf0f0f0f, v18
	v_dot4c_i32_i8_e32 v21, v16, v32
	v_lshrrev_b32_e32 v16, 4, v18
	v_and_b32_e32 v16, 0xf0f0f0f, v16
	v_dot4c_i32_i8_e32 v21, v16, v33
	v_and_b32_e32 v16, 0xf0f0f0f, v19
	v_dot4c_i32_i8_e32 v20, v16, v34
	v_lshrrev_b32_e32 v16, 4, v19
	v_and_b32_e32 v16, 0xf0f0f0f, v16
	v_dot4c_i32_i8_e32 v20, v16, v35
	v_add_u32_e32 v18, v25, v24
	v_sub_u32_e32 v18, v18, v171
	v_and_b32_e32 v17, 0xffff0000, v42
	v_add_u32_e32 v19, v21, v20
	v_sub_u32_e32 v20, v19, v171
	v_cvt_f32_i32_e32 v19, v18
	v_cvt_f32_i32_e32 v18, v20
	v_lshlrev_b32_e32 v16, 16, v42
	v_pk_fma_f32 v[156:157], v[16:17], v[18:19], v[156:157]
	s_waitcnt vmcnt(19)
	v_and_b32_e32 v16, 0xf0f0f0f, v12
	v_mov_b32_e32 v17, 0
	v_lshrrev_b32_e32 v12, 4, v12
	v_dot4c_i32_i8_e32 v17, v16, v36
	v_and_b32_e32 v12, 0xf0f0f0f, v12
	v_dot4c_i32_i8_e32 v17, v12, v37
	v_and_b32_e32 v12, 0xf0f0f0f, v13
	v_mov_b32_e32 v16, 0
	v_dot4c_i32_i8_e32 v16, v12, v38
	v_lshrrev_b32_e32 v12, 4, v13
	v_and_b32_e32 v12, 0xf0f0f0f, v12
	v_dot4c_i32_i8_e32 v16, v12, v39
	v_and_b32_e32 v12, 0xf0f0f0f, v14
	v_dot4c_i32_i8_e32 v17, v12, v32
	v_lshrrev_b32_e32 v12, 4, v14
	v_and_b32_e32 v12, 0xf0f0f0f, v12
	v_dot4c_i32_i8_e32 v17, v12, v33
	v_and_b32_e32 v12, 0xf0f0f0f, v15
	v_dot4c_i32_i8_e32 v16, v12, v34
	v_lshrrev_b32_e32 v12, 4, v15
	v_and_b32_e32 v12, 0xf0f0f0f, v12
	v_dot4c_i32_i8_e32 v16, v12, v35
	s_waitcnt vmcnt(18)
	v_and_b32_e32 v12, 0xf0f0f0f, v8
	v_mov_b32_e32 v13, 0
	v_lshrrev_b32_e32 v8, 4, v8
	v_dot4c_i32_i8_e32 v13, v12, v36
	v_and_b32_e32 v8, 0xf0f0f0f, v8
	v_dot4c_i32_i8_e32 v13, v8, v37
	v_and_b32_e32 v8, 0xf0f0f0f, v9
	v_mov_b32_e32 v12, 0
	v_dot4c_i32_i8_e32 v12, v8, v38
	v_lshrrev_b32_e32 v8, 4, v9
	v_and_b32_e32 v8, 0xf0f0f0f, v8
	v_dot4c_i32_i8_e32 v12, v8, v39
	v_and_b32_e32 v8, 0xf0f0f0f, v10
	v_dot4c_i32_i8_e32 v13, v8, v32
	v_lshrrev_b32_e32 v8, 4, v10
	v_and_b32_e32 v8, 0xf0f0f0f, v8
	v_dot4c_i32_i8_e32 v13, v8, v33
	v_and_b32_e32 v8, 0xf0f0f0f, v11
	v_dot4c_i32_i8_e32 v12, v8, v34
	v_lshrrev_b32_e32 v8, 4, v11
	v_and_b32_e32 v8, 0xf0f0f0f, v8
	v_dot4c_i32_i8_e32 v12, v8, v35
	v_add_u32_e32 v10, v17, v16
	v_sub_u32_e32 v10, v10, v171
	v_and_b32_e32 v9, 0xffff0000, v41
	v_add_u32_e32 v11, v13, v12
	v_sub_u32_e32 v12, v11, v171
	v_cvt_f32_i32_e32 v11, v10
	v_cvt_f32_i32_e32 v10, v12
	v_lshlrev_b32_e32 v8, 16, v41
	v_pk_fma_f32 v[154:155], v[8:9], v[10:11], v[154:155]
	s_waitcnt vmcnt(17)
	v_and_b32_e32 v8, 0xf0f0f0f, v4
	v_mov_b32_e32 v9, 0
	v_lshrrev_b32_e32 v4, 4, v4
	v_dot4c_i32_i8_e32 v9, v8, v36
	v_and_b32_e32 v4, 0xf0f0f0f, v4
	v_dot4c_i32_i8_e32 v9, v4, v37
	v_and_b32_e32 v4, 0xf0f0f0f, v5
	v_mov_b32_e32 v8, 0
	v_dot4c_i32_i8_e32 v8, v4, v38
	v_lshrrev_b32_e32 v4, 4, v5
	v_and_b32_e32 v4, 0xf0f0f0f, v4
	v_dot4c_i32_i8_e32 v8, v4, v39
	v_and_b32_e32 v4, 0xf0f0f0f, v6
	v_dot4c_i32_i8_e32 v9, v4, v32
	v_lshrrev_b32_e32 v4, 4, v6
	v_and_b32_e32 v4, 0xf0f0f0f, v4
	v_dot4c_i32_i8_e32 v9, v4, v33
	v_and_b32_e32 v4, 0xf0f0f0f, v7
	v_dot4c_i32_i8_e32 v8, v4, v34
	v_lshrrev_b32_e32 v4, 4, v7
	v_and_b32_e32 v4, 0xf0f0f0f, v4
	v_dot4c_i32_i8_e32 v8, v4, v35
	s_waitcnt vmcnt(16)
	v_and_b32_e32 v4, 0xf0f0f0f, v0
	v_mov_b32_e32 v5, 0
	v_lshrrev_b32_e32 v0, 4, v0
	v_dot4c_i32_i8_e32 v5, v4, v36
	v_and_b32_e32 v0, 0xf0f0f0f, v0
	v_dot4c_i32_i8_e32 v5, v0, v37
	v_and_b32_e32 v0, 0xf0f0f0f, v1
	v_mov_b32_e32 v4, 0
	v_dot4c_i32_i8_e32 v4, v0, v38
	v_lshrrev_b32_e32 v0, 4, v1
	v_and_b32_e32 v0, 0xf0f0f0f, v0
	v_dot4c_i32_i8_e32 v4, v0, v39
	v_and_b32_e32 v0, 0xf0f0f0f, v2
	v_dot4c_i32_i8_e32 v5, v0, v32
	v_lshrrev_b32_e32 v0, 4, v2
	v_and_b32_e32 v0, 0xf0f0f0f, v0
	v_dot4c_i32_i8_e32 v5, v0, v33
	v_and_b32_e32 v0, 0xf0f0f0f, v3
	v_dot4c_i32_i8_e32 v4, v0, v34
	v_lshrrev_b32_e32 v0, 4, v3
	v_and_b32_e32 v0, 0xf0f0f0f, v0
	v_dot4c_i32_i8_e32 v4, v0, v35
	v_add_u32_e32 v2, v9, v8
	v_sub_u32_e32 v2, v2, v171
	v_and_b32_e32 v1, 0xffff0000, v40
	v_add_u32_e32 v3, v5, v4
	v_sub_u32_e32 v4, v3, v171
	v_cvt_f32_i32_e32 v3, v2
	v_cvt_f32_i32_e32 v2, v4
	v_lshlrev_b32_e32 v0, 16, v40
	v_pk_fma_f32 v[152:153], v[0:1], v[2:3], v[152:153]
	ds_read_u16 v0, v93 offset:16640
	ds_read_u16 v1, v93 offset:16656
	ds_read_u16 v2, v93 offset:16672
	ds_read_u16 v3, v93 offset:16688
	s_waitcnt lgkmcnt(3)
	v_add_u32_e32 v0, s44, v0
	v_lshl_or_b32 v4, v0, 7, v165
	s_waitcnt lgkmcnt(2)
	v_add_u32_e32 v1, s44, v1
	global_load_dwordx4 v[72:75], v4, s[0:1]
	v_lshl_or_b32 v4, v1, 7, v165
	s_waitcnt lgkmcnt(1)
	v_add_u32_e32 v2, s44, v2
	global_load_dwordx4 v[64:67], v4, s[0:1]
	v_lshl_or_b32 v4, v2, 7, v165
	s_waitcnt lgkmcnt(0)
	v_add_u32_e32 v3, s44, v3
	global_load_dwordx4 v[56:59], v4, s[0:1]
	v_lshl_or_b32 v4, v3, 7, v165
	global_load_dwordx4 v[48:51], v4, s[0:1]
	ds_read_u16 v4, v93 offset:16704
	v_lshl_or_b32 v0, v0, 4, v95
	v_lshl_or_b32 v1, v1, 4, v95
	v_lshl_or_b32 v2, v2, 4, v95
	v_lshl_or_b32 v3, v3, 4, v95
	s_waitcnt lgkmcnt(0)
	v_add_u32_e32 v4, s44, v4
	v_lshl_or_b32 v5, v4, 7, v165
	global_load_dwordx4 v[40:43], v5, s[0:1]
	ds_read_u16 v5, v93 offset:16720
	v_lshl_or_b32 v4, v4, 4, v95
	s_waitcnt lgkmcnt(0)
	v_add_u32_e32 v5, s44, v5
	v_lshl_or_b32 v6, v5, 7, v165
	global_load_dwordx4 v[24:27], v6, s[0:1]
	ds_read_u16 v6, v93 offset:16736
	v_lshl_or_b32 v5, v5, 4, v95
	s_waitcnt lgkmcnt(0)
	v_add_u32_e32 v6, s44, v6
	v_lshl_or_b32 v7, v6, 7, v165
	global_load_dwordx4 v[12:15], v7, s[0:1]
	ds_read_u16 v7, v93 offset:16752
	v_lshl_or_b32 v6, v6, 4, v95
	s_waitcnt lgkmcnt(0)
	v_add_u32_e32 v7, s44, v7
	v_lshl_or_b32 v8, v7, 7, v165
	global_load_dwordx4 v[8:11], v8, s[0:1]
	v_lshl_or_b32 v7, v7, 4, v95
	global_load_ushort v178, v95, s[18:19]
	global_load_ushort v179, v95, s[18:19]
	global_load_ushort v174, v95, s[18:19]
	global_load_ushort v175, v95, s[18:19]
	global_load_ushort v169, v95, s[18:19]
	global_load_ushort v170, v95, s[18:19]
	global_load_ushort v167, v95, s[18:19]
	global_load_ushort v168, v95, s[18:19]
	s_waitcnt vmcnt(31)
	v_and_b32_e32 v0, 0xf0f0f0f, v88
	v_mov_b32_e32 v2, 0
	v_dot4c_i32_i8_e32 v2, v0, v36
	v_lshrrev_b32_e32 v0, 4, v88
	v_and_b32_e32 v0, 0xf0f0f0f, v0
	v_dot4c_i32_i8_e32 v2, v0, v37
	v_and_b32_e32 v0, 0xf0f0f0f, v89
	v_mov_b32_e32 v3, 0
	v_dot4c_i32_i8_e32 v3, v0, v38
	v_lshrrev_b32_e32 v0, 4, v89
	v_and_b32_e32 v0, 0xf0f0f0f, v0
	v_dot4c_i32_i8_e32 v3, v0, v39
	v_and_b32_e32 v0, 0xf0f0f0f, v90
	v_dot4c_i32_i8_e32 v2, v0, v32
	v_lshrrev_b32_e32 v0, 4, v90
	v_and_b32_e32 v0, 0xf0f0f0f, v0
	v_dot4c_i32_i8_e32 v2, v0, v33
	v_and_b32_e32 v0, 0xf0f0f0f, v91
	v_dot4c_i32_i8_e32 v3, v0, v34
	v_lshrrev_b32_e32 v0, 4, v91
	v_and_b32_e32 v0, 0xf0f0f0f, v0
	v_dot4c_i32_i8_e32 v3, v0, v35
	s_waitcnt vmcnt(30)
	v_and_b32_e32 v0, 0xf0f0f0f, v84
	v_mov_b32_e32 v4, 0
	v_dot4c_i32_i8_e32 v4, v0, v36
	v_lshrrev_b32_e32 v0, 4, v84
	v_and_b32_e32 v0, 0xf0f0f0f, v0
	v_dot4c_i32_i8_e32 v4, v0, v37
	v_and_b32_e32 v0, 0xf0f0f0f, v85
	v_mov_b32_e32 v5, 0
	v_dot4c_i32_i8_e32 v5, v0, v38
	v_lshrrev_b32_e32 v0, 4, v85
	v_and_b32_e32 v0, 0xf0f0f0f, v0
	v_dot4c_i32_i8_e32 v5, v0, v39
	v_and_b32_e32 v0, 0xf0f0f0f, v86
	v_dot4c_i32_i8_e32 v4, v0, v32
	v_lshrrev_b32_e32 v0, 4, v86
	v_and_b32_e32 v0, 0xf0f0f0f, v0
	v_dot4c_i32_i8_e32 v4, v0, v33
	v_and_b32_e32 v0, 0xf0f0f0f, v87
	v_dot4c_i32_i8_e32 v5, v0, v34
	v_lshrrev_b32_e32 v0, 4, v87
	v_and_b32_e32 v0, 0xf0f0f0f, v0
	v_dot4c_i32_i8_e32 v5, v0, v35
	v_add_u32_e32 v2, v2, v3
	v_sub_u32_e32 v2, v2, v171
	s_waitcnt vmcnt(22)
	v_and_b32_e32 v1, 0xffff0000, v192
	v_sub_u32_e32 v3, v5, v171
	v_add_u32_e32 v4, v3, v4
	v_cvt_f32_i32_e32 v3, v2
	v_cvt_f32_i32_e32 v2, v4
	v_and_b32_e32 v0, 0xffff0000, v193
	v_mov_b32_e32 v4, 0
	v_mov_b32_e32 v5, 0
	v_pk_fma_f32 v[150:151], v[0:1], v[2:3], v[150:151]
	v_and_b32_e32 v0, 0xf0f0f0f, v80
	v_mov_b32_e32 v2, 0
	v_dot4c_i32_i8_e32 v2, v0, v36
	v_lshrrev_b32_e32 v0, 4, v80
	v_and_b32_e32 v0, 0xf0f0f0f, v0
	v_dot4c_i32_i8_e32 v2, v0, v37
	v_and_b32_e32 v0, 0xf0f0f0f, v81
	v_mov_b32_e32 v3, 0
	v_dot4c_i32_i8_e32 v3, v0, v38
	v_lshrrev_b32_e32 v0, 4, v81
	v_and_b32_e32 v0, 0xf0f0f0f, v0
	v_dot4c_i32_i8_e32 v3, v0, v39
	v_and_b32_e32 v0, 0xf0f0f0f, v82
	v_dot4c_i32_i8_e32 v2, v0, v32
	v_lshrrev_b32_e32 v0, 4, v82
	v_and_b32_e32 v0, 0xf0f0f0f, v0
	v_dot4c_i32_i8_e32 v2, v0, v33
	v_and_b32_e32 v0, 0xf0f0f0f, v83
	v_dot4c_i32_i8_e32 v3, v0, v34
	v_lshrrev_b32_e32 v0, 4, v83
	v_and_b32_e32 v0, 0xf0f0f0f, v0
	v_dot4c_i32_i8_e32 v3, v0, v35
	v_and_b32_e32 v0, 0xf0f0f0f, v76
	v_dot4c_i32_i8_e32 v4, v0, v36
	v_lshrrev_b32_e32 v0, 4, v76
	v_and_b32_e32 v0, 0xf0f0f0f, v0
	v_dot4c_i32_i8_e32 v4, v0, v37
	v_and_b32_e32 v0, 0xf0f0f0f, v77
	v_dot4c_i32_i8_e32 v5, v0, v38
	v_lshrrev_b32_e32 v0, 4, v77
	v_and_b32_e32 v0, 0xf0f0f0f, v0
	v_dot4c_i32_i8_e32 v5, v0, v39
	v_and_b32_e32 v0, 0xf0f0f0f, v78
	v_dot4c_i32_i8_e32 v4, v0, v32
	v_lshrrev_b32_e32 v0, 4, v78
	v_and_b32_e32 v0, 0xf0f0f0f, v0
	v_dot4c_i32_i8_e32 v4, v0, v33
	v_and_b32_e32 v0, 0xf0f0f0f, v79
	v_dot4c_i32_i8_e32 v5, v0, v34
	v_lshrrev_b32_e32 v0, 4, v79
	v_and_b32_e32 v0, 0xf0f0f0f, v0
	v_dot4c_i32_i8_e32 v5, v0, v35
	v_sub_u32_e32 v3, v3, v171
	v_add_u32_e32 v2, v3, v2
	v_cvt_f32_i32_e32 v3, v2
	v_sub_u32_e32 v5, v5, v171
	v_add_u32_e32 v4, v5, v4
	v_cvt_f32_i32_e32 v2, v4
	s_waitcnt vmcnt(20)
; #define P12_ISSUE(c_, i_, h_, CW_, SC_) do { _Pragma("unroll") for (int bb = 0; bb < 8; ++bb) { const unsigned ro = (unsigned)(c_) * 16384u + (unsigned)EL[(i_) * 128 + ((h_) * 8 + bb) * 8 + g8]; \
;         CW_[bb] = *(const v4u*)(U4 + (size_t)(ro * 128u + 16u * (unsigned)k8)); SC_[bb] = USS[(size_t)(ro * 8u + (unsigned)k8)]; } } while (0)
; #define P12_COMP(i_, h_, CW_, SC_) do { _Pragma("unroll") for (int bb = 0; bb < 8; ++bb) { int a0 = 0, a1 = 0; P12_U4(CW_[bb].x, xa.x, xa.y, a0); P12_U4(CW_[bb].y, xa.z, xa.w, a1); P12_U4(CW_[bb].z, xb.x, xb.y, a0); P12_U4(CW_[bb].w, xb.z, xb.w, a1); \
;         psum[(i_)][(h_) * 8 + bb] += __uint_as_float(SC_[bb] << 16) * (float)((a0 + a1) - xo); } } while (0)
; #define P12_BAR() asm volatile("" ::: "memory")
; __device__ __forceinline__ void p12_peer(Frame& F) {
;     ...
;     { v4u cwA[8], cwB[8]; unsigned scA[8], scB[8]; v4u xa, xb; int xo;
;       P12_ISSUE(0, 0, 0, cwA, scA);
; _Pragma("nounroll")
;       for (int c = 0; c < 16; ++c) { const int cn = c + 1 < 16 ? c + 1 : 15;
;           P12_XQ(c, 0); P12_ISSUE(c, 0, 1, cwB, scB); P12_BAR(); P12_COMP(0, 0, cwA, scA); P12_ISSUE(c, 1, 0, cwA, scA); P12_BAR(); P12_COMP(0, 1, cwB, scB);
;           P12_XQ(c, 1); P12_ISSUE(c, 1, 1, cwB, scB); P12_BAR(); P12_COMP(1, 0, cwA, scA); P12_ISSUE(c, 2, 0, cwA, scA); P12_BAR(); P12_COMP(1, 1, cwB, scB);
;           P12_XQ(c, 2); P12_ISSUE(c, 2, 1, cwB, scB); P12_BAR(); P12_COMP(2, 0, cwA, scA); P12_ISSUE(c, 3, 0, cwA, scA); P12_BAR(); P12_COMP(2, 1, cwB, scB);
;           P12_XQ(c, 3); P12_ISSUE(c, 3, 1, cwB, scB); P12_BAR(); P12_COMP(3, 0, cwA, scA); P12_ISSUE(cn, 0, 0, cwA, scA); P12_BAR(); P12_COMP(3, 1, cwB, scB);
	v_and_b32_e32 v1, 0xffff0000, v194
	v_and_b32_e32 v0, 0xffff0000, v195
	v_mov_b32_e32 v4, 0
	v_pk_fma_f32 v[148:149], v[0:1], v[2:3], v[148:149]
	v_and_b32_e32 v0, 0xf0f0f0f, v68
	v_mov_b32_e32 v2, 0
	v_dot4c_i32_i8_e32 v2, v0, v36
	v_lshrrev_b32_e32 v0, 4, v68
	v_and_b32_e32 v0, 0xf0f0f0f, v0
	v_dot4c_i32_i8_e32 v2, v0, v37
	v_and_b32_e32 v0, 0xf0f0f0f, v69
	v_mov_b32_e32 v3, 0
	v_dot4c_i32_i8_e32 v3, v0, v38
	v_lshrrev_b32_e32 v0, 4, v69
	v_and_b32_e32 v0, 0xf0f0f0f, v0
	v_dot4c_i32_i8_e32 v3, v0, v39
	v_and_b32_e32 v0, 0xf0f0f0f, v70
	v_dot4c_i32_i8_e32 v2, v0, v32
	v_lshrrev_b32_e32 v0, 4, v70
	v_and_b32_e32 v0, 0xf0f0f0f, v0
	v_dot4c_i32_i8_e32 v2, v0, v33
	v_and_b32_e32 v0, 0xf0f0f0f, v71
	v_dot4c_i32_i8_e32 v3, v0, v34
	v_lshrrev_b32_e32 v0, 4, v71
	v_and_b32_e32 v0, 0xf0f0f0f, v0
	v_dot4c_i32_i8_e32 v3, v0, v35
	v_and_b32_e32 v0, 0xf0f0f0f, v60
	v_dot4c_i32_i8_e32 v4, v0, v36
	v_lshrrev_b32_e32 v0, 4, v60
	v_and_b32_e32 v0, 0xf0f0f0f, v0
	v_dot4c_i32_i8_e32 v4, v0, v37
	v_and_b32_e32 v0, 0xf0f0f0f, v61
	v_mov_b32_e32 v5, 0
	v_dot4c_i32_i8_e32 v5, v0, v38
	v_lshrrev_b32_e32 v0, 4, v61
	v_and_b32_e32 v0, 0xf0f0f0f, v0
	v_dot4c_i32_i8_e32 v5, v0, v39
	v_and_b32_e32 v0, 0xf0f0f0f, v62
	v_dot4c_i32_i8_e32 v4, v0, v32
	v_lshrrev_b32_e32 v0, 4, v62
	v_and_b32_e32 v0, 0xf0f0f0f, v0
	v_dot4c_i32_i8_e32 v4, v0, v33
	v_and_b32_e32 v0, 0xf0f0f0f, v63
	v_dot4c_i32_i8_e32 v5, v0, v34
	v_lshrrev_b32_e32 v0, 4, v63
	v_and_b32_e32 v0, 0xf0f0f0f, v0
	v_dot4c_i32_i8_e32 v5, v0, v35
	v_sub_u32_e32 v3, v3, v171
	v_add_u32_e32 v2, v3, v2
	v_cvt_f32_i32_e32 v3, v2
	v_sub_u32_e32 v5, v5, v171
	v_add_u32_e32 v4, v5, v4
	v_cvt_f32_i32_e32 v2, v4
	s_waitcnt vmcnt(18)
	v_and_b32_e32 v1, 0xffff0000, v196
	v_and_b32_e32 v0, 0xffff0000, v197
	v_mov_b32_e32 v4, 0
	v_pk_fma_f32 v[146:147], v[0:1], v[2:3], v[146:147]
	v_and_b32_e32 v0, 0xf0f0f0f, v52
	v_mov_b32_e32 v2, 0
	v_dot4c_i32_i8_e32 v2, v0, v36
	v_lshrrev_b32_e32 v0, 4, v52
	v_and_b32_e32 v0, 0xf0f0f0f, v0
	v_dot4c_i32_i8_e32 v2, v0, v37
	v_and_b32_e32 v0, 0xf0f0f0f, v53
	v_mov_b32_e32 v3, 0
	v_dot4c_i32_i8_e32 v3, v0, v38
	v_lshrrev_b32_e32 v0, 4, v53
	v_and_b32_e32 v0, 0xf0f0f0f, v0
	v_dot4c_i32_i8_e32 v3, v0, v39
	v_and_b32_e32 v0, 0xf0f0f0f, v54
	v_dot4c_i32_i8_e32 v2, v0, v32
	v_lshrrev_b32_e32 v0, 4, v54
	v_and_b32_e32 v0, 0xf0f0f0f, v0
	v_dot4c_i32_i8_e32 v2, v0, v33
	v_and_b32_e32 v0, 0xf0f0f0f, v55
	v_dot4c_i32_i8_e32 v3, v0, v34
	v_lshrrev_b32_e32 v0, 4, v55
	v_and_b32_e32 v0, 0xf0f0f0f, v0
	v_dot4c_i32_i8_e32 v3, v0, v35
	v_and_b32_e32 v0, 0xf0f0f0f, v44
	v_dot4c_i32_i8_e32 v4, v0, v36
	v_lshrrev_b32_e32 v0, 4, v44
	v_and_b32_e32 v0, 0xf0f0f0f, v0
	v_dot4c_i32_i8_e32 v4, v0, v37
	v_and_b32_e32 v0, 0xf0f0f0f, v45
	v_mov_b32_e32 v5, 0
	v_dot4c_i32_i8_e32 v5, v0, v38
	v_lshrrev_b32_e32 v0, 4, v45
	v_and_b32_e32 v0, 0xf0f0f0f, v0
	v_dot4c_i32_i8_e32 v5, v0, v39
	v_and_b32_e32 v0, 0xf0f0f0f, v46
	v_dot4c_i32_i8_e32 v4, v0, v32
	v_lshrrev_b32_e32 v0, 4, v46
	v_and_b32_e32 v0, 0xf0f0f0f, v0
	v_dot4c_i32_i8_e32 v4, v0, v33
	v_and_b32_e32 v0, 0xf0f0f0f, v47
	v_dot4c_i32_i8_e32 v5, v0, v34
	v_lshrrev_b32_e32 v0, 4, v47
	v_and_b32_e32 v0, 0xf0f0f0f, v0
	v_dot4c_i32_i8_e32 v5, v0, v35
	v_sub_u32_e32 v3, v3, v171
	v_add_u32_e32 v2, v3, v2
	v_cvt_f32_i32_e32 v3, v2
	v_sub_u32_e32 v5, v5, v171
	v_add_u32_e32 v4, v5, v4
	v_cvt_f32_i32_e32 v2, v4
	s_waitcnt vmcnt(16)
	v_and_b32_e32 v1, 0xffff0000, v198
	v_and_b32_e32 v0, 0xffff0000, v199
	v_pk_fma_f32 v[144:145], v[0:1], v[2:3], v[144:145]
	ds_read_b128 v[4:7], v166 offset:4096
	ds_read_b128 v[0:3], v166 offset:4112
	ds_read_u16 v16, v93 offset:16768
	ds_read_u16 v17, v93 offset:16784
	ds_read_u16 v18, v93 offset:16800
	ds_read_u16 v19, v93 offset:16816
	v_mov_b32_e32 v44, 0
	s_waitcnt lgkmcnt(3)
	v_add_u32_e32 v16, s44, v16
	v_lshl_or_b32 v20, v16, 7, v165
	v_lshl_or_b32 v45, v16, 4, v95
	s_waitcnt lgkmcnt(2)
	v_add_u32_e32 v16, s44, v17
	v_lshl_or_b32 v17, v16, 7, v165
	v_lshl_or_b32 v46, v16, 4, v95
	s_waitcnt lgkmcnt(1)
	v_add_u32_e32 v16, s44, v18
	global_load_dwordx4 v[80:83], v20, s[0:1]
	global_load_dwordx4 v[68:71], v17, s[0:1]
	v_lshl_or_b32 v17, v16, 7, v165
	v_lshl_or_b32 v47, v16, 4, v95
	s_waitcnt lgkmcnt(0)
	v_add_u32_e32 v16, s44, v19
	global_load_dwordx4 v[52:55], v17, s[0:1]
	v_lshl_or_b32 v17, v16, 7, v165
	v_lshl_or_b32 v60, v16, 4, v95
	ds_read_u16 v16, v93 offset:16832
	global_load_dwordx4 v[36:39], v17, s[0:1]
	v_dot4c_i32_i8_e32 v44, 0x1010101, v4
	v_dot4c_i32_i8_e32 v44, 0x1010101, v5
	v_dot4c_i32_i8_e32 v44, 0x1010101, v6
	s_waitcnt lgkmcnt(0)
	v_add_u32_e32 v16, s44, v16
	v_lshl_or_b32 v17, v16, 7, v165
	v_lshl_or_b32 v61, v16, 4, v95
	ds_read_u16 v16, v93 offset:16848
	global_load_dwordx4 v[32:35], v17, s[0:1]
	v_dot4c_i32_i8_e32 v44, 0x1010101, v7
	v_dot4c_i32_i8_e32 v44, 0x1010101, v0
	v_dot4c_i32_i8_e32 v44, 0x1010101, v1
	s_waitcnt lgkmcnt(0)
	v_add_u32_e32 v16, s44, v16
	v_lshl_or_b32 v17, v16, 7, v165
	v_lshl_or_b32 v62, v16, 4, v95
	ds_read_u16 v16, v93 offset:16864
	global_load_dwordx4 v[28:31], v17, s[0:1]
	v_dot4c_i32_i8_e32 v44, 0x1010101, v2
	v_dot4c_i32_i8_e32 v44, 0x1010101, v3
	s_waitcnt lgkmcnt(0)
	v_add_u32_e32 v16, s44, v16
	v_lshl_or_b32 v17, v16, 7, v165
	v_lshl_or_b32 v63, v16, 4, v95
	ds_read_u16 v16, v93 offset:16880
	global_load_dwordx4 v[20:23], v17, s[0:1]
	v_lshlrev_b32_e32 v84, 3, v44
	s_waitcnt vmcnt(22)
	v_and_b32_e32 v44, 0xf0f0f0f, v72
	s_waitcnt lgkmcnt(0)
; #define P12_ISSUE(c_, i_, h_, CW_, SC_) do { _Pragma("unroll") for (int bb = 0; bb < 8; ++bb) { const unsigned ro = (unsigned)(c_) * 16384u + (unsigned)EL[(i_) * 128 + ((h_) * 8 + bb) * 8 + g8]; \
;         CW_[bb] = *(const v4u*)(U4 + (size_t)(ro * 128u + 16u * (unsigned)k8)); SC_[bb] = USS[(size_t)(ro * 8u + (unsigned)k8)]; } } while (0)
; #define P12_COMP(i_, h_, CW_, SC_) do { _Pragma("unroll") for (int bb = 0; bb < 8; ++bb) { int a0 = 0, a1 = 0; P12_U4(CW_[bb].x, xa.x, xa.y, a0); P12_U4(CW_[bb].y, xa.z, xa.w, a1); P12_U4(CW_[bb].z, xb.x, xb.y, a0); P12_U4(CW_[bb].w, xb.z, xb.w, a1); \
;         psum[(i_)][(h_) * 8 + bb] += __uint_as_float(SC_[bb] << 16) * (float)((a0 + a1) - xo); } } while (0)
; #define P12_BAR() asm volatile("" ::: "memory")
; __device__ __forceinline__ void p12_peer(Frame& F) {
;     ...
;     { v4u cwA[8], cwB[8]; unsigned scA[8], scB[8]; v4u xa, xb; int xo;
;       P12_ISSUE(0, 0, 0, cwA, scA);
; _Pragma("nounroll")
;       for (int c = 0; c < 16; ++c) { const int cn = c + 1 < 16 ? c + 1 : 15;
;           P12_XQ(c, 0); P12_ISSUE(c, 0, 1, cwB, scB); P12_BAR(); P12_COMP(0, 0, cwA, scA); P12_ISSUE(c, 1, 0, cwA, scA); P12_BAR(); P12_COMP(0, 1, cwB, scB);
;           P12_XQ(c, 1); P12_ISSUE(c, 1, 1, cwB, scB); P12_BAR(); P12_COMP(1, 0, cwA, scA); P12_ISSUE(c, 2, 0, cwA, scA); P12_BAR(); P12_COMP(1, 1, cwB, scB);
;           P12_XQ(c, 2); P12_ISSUE(c, 2, 1, cwB, scB); P12_BAR(); P12_COMP(2, 0, cwA, scA); P12_ISSUE(c, 3, 0, cwA, scA); P12_BAR(); P12_COMP(2, 1, cwB, scB);
;           P12_XQ(c, 3); P12_ISSUE(c, 3, 1, cwB, scB); P12_BAR(); P12_COMP(3, 0, cwA, scA); P12_ISSUE(cn, 0, 0, cwA, scA); P12_BAR(); P12_COMP(3, 1, cwB, scB);
	v_add_u32_e32 v76, s44, v16
	v_lshl_or_b32 v16, v76, 7, v165
	global_load_dwordx4 v[16:19], v16, s[0:1]
	v_lshl_or_b32 v76, v76, 4, v95
	global_load_ushort v180, v95, s[18:19]
	global_load_ushort v181, v95, s[18:19]
	global_load_ushort v172, v95, s[18:19]
	global_load_ushort v173, v95, s[18:19]
	global_load_ushort v87, v95, s[18:19]
	global_load_ushort v171, v95, s[18:19]
	global_load_ushort v85, v95, s[18:19]
	global_load_ushort v86, v95, s[18:19]
	v_mov_b32_e32 v46, 0
	v_dot4c_i32_i8_e32 v46, v44, v4
	v_lshrrev_b32_e32 v44, 4, v72
	v_and_b32_e32 v44, 0xf0f0f0f, v44
	v_dot4c_i32_i8_e32 v46, v44, v5
	v_and_b32_e32 v44, 0xf0f0f0f, v73
	v_mov_b32_e32 v47, 0
	v_dot4c_i32_i8_e32 v47, v44, v6
	v_lshrrev_b32_e32 v44, 4, v73
	v_and_b32_e32 v44, 0xf0f0f0f, v44
	v_dot4c_i32_i8_e32 v47, v44, v7
	v_and_b32_e32 v44, 0xf0f0f0f, v74
	v_dot4c_i32_i8_e32 v46, v44, v0
	v_lshrrev_b32_e32 v44, 4, v74
	v_and_b32_e32 v44, 0xf0f0f0f, v44
	v_dot4c_i32_i8_e32 v46, v44, v1
	v_and_b32_e32 v44, 0xf0f0f0f, v75
	v_dot4c_i32_i8_e32 v47, v44, v2
	v_lshrrev_b32_e32 v44, 4, v75
	v_and_b32_e32 v44, 0xf0f0f0f, v44
	v_dot4c_i32_i8_e32 v47, v44, v3
	s_waitcnt vmcnt(30)
	v_and_b32_e32 v44, 0xf0f0f0f, v64
	v_mov_b32_e32 v60, 0
	v_dot4c_i32_i8_e32 v60, v44, v4
	v_lshrrev_b32_e32 v44, 4, v64
	v_and_b32_e32 v44, 0xf0f0f0f, v44
	v_dot4c_i32_i8_e32 v60, v44, v5
	v_and_b32_e32 v44, 0xf0f0f0f, v65
	v_mov_b32_e32 v61, 0
	v_dot4c_i32_i8_e32 v61, v44, v6
	v_lshrrev_b32_e32 v44, 4, v65
	v_and_b32_e32 v44, 0xf0f0f0f, v44
	v_dot4c_i32_i8_e32 v61, v44, v7
	v_and_b32_e32 v44, 0xf0f0f0f, v66
	v_dot4c_i32_i8_e32 v60, v44, v0
	v_lshrrev_b32_e32 v44, 4, v66
	v_and_b32_e32 v44, 0xf0f0f0f, v44
	v_dot4c_i32_i8_e32 v60, v44, v1
	v_and_b32_e32 v44, 0xf0f0f0f, v67
	v_dot4c_i32_i8_e32 v61, v44, v2
	v_lshrrev_b32_e32 v44, 4, v67
	v_and_b32_e32 v44, 0xf0f0f0f, v44
	v_dot4c_i32_i8_e32 v61, v44, v3
	v_add_u32_e32 v46, v46, v47
	v_sub_u32_e32 v46, v46, v84
	s_waitcnt vmcnt(22)
	v_and_b32_e32 v45, 0xffff0000, v200
	v_add_u32_e32 v47, v60, v61
	v_sub_u32_e32 v60, v47, v84
	v_cvt_f32_i32_e32 v47, v46
	v_cvt_f32_i32_e32 v46, v60
	v_and_b32_e32 v44, 0xffff0000, v201
	v_pk_fma_f32 v[142:143], v[44:45], v[46:47], v[142:143]
	v_and_b32_e32 v44, 0xf0f0f0f, v56
	v_mov_b32_e32 v46, 0
	v_dot4c_i32_i8_e32 v46, v44, v4
	v_lshrrev_b32_e32 v44, 4, v56
	v_and_b32_e32 v44, 0xf0f0f0f, v44
	v_dot4c_i32_i8_e32 v46, v44, v5
	v_and_b32_e32 v44, 0xf0f0f0f, v57
	v_mov_b32_e32 v47, 0
	v_dot4c_i32_i8_e32 v47, v44, v6
	v_lshrrev_b32_e32 v44, 4, v57
	v_and_b32_e32 v44, 0xf0f0f0f, v44
	v_dot4c_i32_i8_e32 v47, v44, v7
	v_and_b32_e32 v44, 0xf0f0f0f, v58
	v_dot4c_i32_i8_e32 v46, v44, v0
	v_lshrrev_b32_e32 v44, 4, v58
	v_and_b32_e32 v44, 0xf0f0f0f, v44
	v_dot4c_i32_i8_e32 v46, v44, v1
	v_and_b32_e32 v44, 0xf0f0f0f, v59
	v_dot4c_i32_i8_e32 v47, v44, v2
	v_lshrrev_b32_e32 v44, 4, v59
	v_and_b32_e32 v44, 0xf0f0f0f, v44
	v_dot4c_i32_i8_e32 v47, v44, v3
	v_and_b32_e32 v44, 0xf0f0f0f, v48
	v_mov_b32_e32 v56, 0
	v_dot4c_i32_i8_e32 v56, v44, v4
	v_lshrrev_b32_e32 v44, 4, v48
	v_and_b32_e32 v44, 0xf0f0f0f, v44
	v_dot4c_i32_i8_e32 v56, v44, v5
	v_and_b32_e32 v44, 0xf0f0f0f, v49
	v_mov_b32_e32 v48, 0
	v_dot4c_i32_i8_e32 v48, v44, v6
	v_lshrrev_b32_e32 v44, 4, v49
	v_and_b32_e32 v44, 0xf0f0f0f, v44
	v_dot4c_i32_i8_e32 v48, v44, v7
	v_and_b32_e32 v44, 0xf0f0f0f, v50
	v_dot4c_i32_i8_e32 v56, v44, v0
	v_lshrrev_b32_e32 v44, 4, v50
	v_and_b32_e32 v44, 0xf0f0f0f, v44
	v_dot4c_i32_i8_e32 v56, v44, v1
	v_and_b32_e32 v44, 0xf0f0f0f, v51
	v_dot4c_i32_i8_e32 v48, v44, v2
	v_lshrrev_b32_e32 v44, 4, v51
	v_and_b32_e32 v44, 0xf0f0f0f, v44
	v_dot4c_i32_i8_e32 v48, v44, v3
	v_add_u32_e32 v46, v46, v47
	v_sub_u32_e32 v46, v46, v84
	s_waitcnt vmcnt(20)
	v_and_b32_e32 v45, 0xffff0000, v202
	v_add_u32_e32 v47, v56, v48
	v_sub_u32_e32 v48, v47, v84
	v_cvt_f32_i32_e32 v47, v46
	v_cvt_f32_i32_e32 v46, v48
	v_and_b32_e32 v44, 0xffff0000, v203
	v_pk_fma_f32 v[140:141], v[44:45], v[46:47], v[140:141]
	v_and_b32_e32 v44, 0xf0f0f0f, v40
	v_mov_b32_e32 v45, 0
	v_lshrrev_b32_e32 v40, 4, v40
	v_dot4c_i32_i8_e32 v45, v44, v4
	v_and_b32_e32 v40, 0xf0f0f0f, v40
	v_dot4c_i32_i8_e32 v45, v40, v5
	v_and_b32_e32 v40, 0xf0f0f0f, v41
	v_mov_b32_e32 v44, 0
	v_dot4c_i32_i8_e32 v44, v40, v6
	v_lshrrev_b32_e32 v40, 4, v41
	v_and_b32_e32 v40, 0xf0f0f0f, v40
	v_dot4c_i32_i8_e32 v44, v40, v7
	v_and_b32_e32 v40, 0xf0f0f0f, v42
	v_dot4c_i32_i8_e32 v45, v40, v0
	v_lshrrev_b32_e32 v40, 4, v42
	v_and_b32_e32 v40, 0xf0f0f0f, v40
	v_dot4c_i32_i8_e32 v45, v40, v1
	v_and_b32_e32 v40, 0xf0f0f0f, v43
	v_dot4c_i32_i8_e32 v44, v40, v2
	v_lshrrev_b32_e32 v40, 4, v43
	v_and_b32_e32 v40, 0xf0f0f0f, v40
	v_dot4c_i32_i8_e32 v44, v40, v3
	v_and_b32_e32 v40, 0xf0f0f0f, v24
	v_mov_b32_e32 v41, 0
	v_lshrrev_b32_e32 v24, 4, v24
	v_dot4c_i32_i8_e32 v41, v40, v4
	v_and_b32_e32 v24, 0xf0f0f0f, v24
	v_dot4c_i32_i8_e32 v41, v24, v5
	v_and_b32_e32 v24, 0xf0f0f0f, v25
	v_mov_b32_e32 v40, 0
	v_dot4c_i32_i8_e32 v40, v24, v6
	v_lshrrev_b32_e32 v24, 4, v25
	v_and_b32_e32 v24, 0xf0f0f0f, v24
	v_dot4c_i32_i8_e32 v40, v24, v7
	v_and_b32_e32 v24, 0xf0f0f0f, v26
	v_dot4c_i32_i8_e32 v41, v24, v0
	v_lshrrev_b32_e32 v24, 4, v26
	v_and_b32_e32 v24, 0xf0f0f0f, v24
	v_dot4c_i32_i8_e32 v41, v24, v1
	v_and_b32_e32 v24, 0xf0f0f0f, v27
	v_dot4c_i32_i8_e32 v40, v24, v2
	v_lshrrev_b32_e32 v24, 4, v27
	v_and_b32_e32 v24, 0xf0f0f0f, v24
	v_dot4c_i32_i8_e32 v40, v24, v3
	v_add_u32_e32 v26, v45, v44
	v_sub_u32_e32 v26, v26, v84
	s_waitcnt vmcnt(18)
; #define P12_ISSUE(c_, i_, h_, CW_, SC_) do { _Pragma("unroll") for (int bb = 0; bb < 8; ++bb) { const unsigned ro = (unsigned)(c_) * 16384u + (unsigned)EL[(i_) * 128 + ((h_) * 8 + bb) * 8 + g8]; \
;         CW_[bb] = *(const v4u*)(U4 + (size_t)(ro * 128u + 16u * (unsigned)k8)); SC_[bb] = USS[(size_t)(ro * 8u + (unsigned)k8)]; } } while (0)
; #define P12_COMP(i_, h_, CW_, SC_) do { _Pragma("unroll") for (int bb = 0; bb < 8; ++bb) { int a0 = 0, a1 = 0; P12_U4(CW_[bb].x, xa.x, xa.y, a0); P12_U4(CW_[bb].y, xa.z, xa.w, a1); P12_U4(CW_[bb].z, xb.x, xb.y, a0); P12_U4(CW_[bb].w, xb.z, xb.w, a1); \
;         psum[(i_)][(h_) * 8 + bb] += __uint_as_float(SC_[bb] << 16) * (float)((a0 + a1) - xo); } } while (0)
; #define P12_BAR() asm volatile("" ::: "memory")
; __device__ __forceinline__ void p12_peer(Frame& F) {
;     ...
;     { v4u cwA[8], cwB[8]; unsigned scA[8], scB[8]; v4u xa, xb; int xo;
;       P12_ISSUE(0, 0, 0, cwA, scA);
; _Pragma("nounroll")
;       for (int c = 0; c < 16; ++c) { const int cn = c + 1 < 16 ? c + 1 : 15;
;           P12_XQ(c, 0); P12_ISSUE(c, 0, 1, cwB, scB); P12_BAR(); P12_COMP(0, 0, cwA, scA); P12_ISSUE(c, 1, 0, cwA, scA); P12_BAR(); P12_COMP(0, 1, cwB, scB);
;           P12_XQ(c, 1); P12_ISSUE(c, 1, 1, cwB, scB); P12_BAR(); P12_COMP(1, 0, cwA, scA); P12_ISSUE(c, 2, 0, cwA, scA); P12_BAR(); P12_COMP(1, 1, cwB, scB);
;           P12_XQ(c, 2); P12_ISSUE(c, 2, 1, cwB, scB); P12_BAR(); P12_COMP(2, 0, cwA, scA); P12_ISSUE(c, 3, 0, cwA, scA); P12_BAR(); P12_COMP(2, 1, cwB, scB);
;           P12_XQ(c, 3); P12_ISSUE(c, 3, 1, cwB, scB); P12_BAR(); P12_COMP(3, 0, cwA, scA); P12_ISSUE(cn, 0, 0, cwA, scA); P12_BAR(); P12_COMP(3, 1, cwB, scB);
	v_and_b32_e32 v25, 0xffff0000, v204
	v_add_u32_e32 v27, v41, v40
	v_sub_u32_e32 v40, v27, v84
	v_cvt_f32_i32_e32 v27, v26
	v_cvt_f32_i32_e32 v26, v40
	v_and_b32_e32 v24, 0xffff0000, v205
	v_pk_fma_f32 v[138:139], v[24:25], v[26:27], v[138:139]
	v_and_b32_e32 v24, 0xf0f0f0f, v12
	v_mov_b32_e32 v25, 0
	v_lshrrev_b32_e32 v12, 4, v12
	v_dot4c_i32_i8_e32 v25, v24, v4
	v_and_b32_e32 v12, 0xf0f0f0f, v12
	v_dot4c_i32_i8_e32 v25, v12, v5
	v_and_b32_e32 v12, 0xf0f0f0f, v13
	v_mov_b32_e32 v24, 0
	v_dot4c_i32_i8_e32 v24, v12, v6
	v_lshrrev_b32_e32 v12, 4, v13
	v_and_b32_e32 v12, 0xf0f0f0f, v12
	v_dot4c_i32_i8_e32 v24, v12, v7
	v_and_b32_e32 v12, 0xf0f0f0f, v14
	v_dot4c_i32_i8_e32 v25, v12, v0
	v_lshrrev_b32_e32 v12, 4, v14
	v_and_b32_e32 v12, 0xf0f0f0f, v12
	v_dot4c_i32_i8_e32 v25, v12, v1
	v_and_b32_e32 v12, 0xf0f0f0f, v15
	v_dot4c_i32_i8_e32 v24, v12, v2
	v_lshrrev_b32_e32 v12, 4, v15
	v_and_b32_e32 v12, 0xf0f0f0f, v12
	v_dot4c_i32_i8_e32 v24, v12, v3
	v_and_b32_e32 v12, 0xf0f0f0f, v8
	v_mov_b32_e32 v13, 0
	v_lshrrev_b32_e32 v8, 4, v8
	v_dot4c_i32_i8_e32 v13, v12, v4
	v_and_b32_e32 v8, 0xf0f0f0f, v8
	v_dot4c_i32_i8_e32 v13, v8, v5
	v_and_b32_e32 v8, 0xf0f0f0f, v9
	v_mov_b32_e32 v12, 0
	v_dot4c_i32_i8_e32 v12, v8, v6
	v_lshrrev_b32_e32 v8, 4, v9
	v_and_b32_e32 v8, 0xf0f0f0f, v8
	v_dot4c_i32_i8_e32 v12, v8, v7
	v_and_b32_e32 v8, 0xf0f0f0f, v10
	v_dot4c_i32_i8_e32 v13, v8, v0
	v_lshrrev_b32_e32 v8, 4, v10
	v_and_b32_e32 v8, 0xf0f0f0f, v8
	v_dot4c_i32_i8_e32 v13, v8, v1
	v_and_b32_e32 v8, 0xf0f0f0f, v11
	v_dot4c_i32_i8_e32 v12, v8, v2
	v_lshrrev_b32_e32 v8, 4, v11
	v_and_b32_e32 v8, 0xf0f0f0f, v8
	v_dot4c_i32_i8_e32 v12, v8, v3
	v_add_u32_e32 v10, v25, v24
	v_sub_u32_e32 v10, v10, v84
	s_waitcnt vmcnt(16)
	v_and_b32_e32 v9, 0xffff0000, v206
	v_add_u32_e32 v11, v13, v12
	v_sub_u32_e32 v12, v11, v84
	v_cvt_f32_i32_e32 v11, v10
	v_cvt_f32_i32_e32 v10, v12
	v_and_b32_e32 v8, 0xffff0000, v207
	v_pk_fma_f32 v[136:137], v[8:9], v[10:11], v[136:137]
	ds_read_u16 v8, v93 offset:16896
	ds_read_u16 v9, v93 offset:16912
	ds_read_u16 v10, v93 offset:16928
	ds_read_u16 v11, v93 offset:16944
	s_waitcnt lgkmcnt(3)
	v_add_u32_e32 v8, s44, v8
	v_lshl_or_b32 v12, v8, 7, v165
	v_lshl_or_b32 v40, v8, 4, v95
	s_waitcnt lgkmcnt(2)
	v_add_u32_e32 v8, s44, v9
	v_lshl_or_b32 v9, v8, 7, v165
	v_lshl_or_b32 v41, v8, 4, v95
	s_waitcnt lgkmcnt(1)
	v_add_u32_e32 v8, s44, v10
	global_load_dwordx4 v[76:79], v12, s[0:1]
	global_load_dwordx4 v[72:75], v9, s[0:1]
	v_lshl_or_b32 v9, v8, 7, v165
	v_lshl_or_b32 v42, v8, 4, v95
	s_waitcnt lgkmcnt(0)
	v_add_u32_e32 v8, s44, v11
	global_load_dwordx4 v[60:63], v9, s[0:1]
	v_lshl_or_b32 v9, v8, 7, v165
	v_lshl_or_b32 v43, v8, 4, v95
	ds_read_u16 v8, v93 offset:16960
	global_load_dwordx4 v[56:59], v9, s[0:1]
	s_waitcnt lgkmcnt(0)
	v_add_u32_e32 v8, s44, v8
	v_lshl_or_b32 v9, v8, 7, v165
	v_lshl_or_b32 v48, v8, 4, v95
	ds_read_u16 v8, v93 offset:16976
	global_load_dwordx4 v[44:47], v9, s[0:1]
	s_waitcnt lgkmcnt(0)
	v_add_u32_e32 v8, s44, v8
	v_lshl_or_b32 v9, v8, 7, v165
	v_lshl_or_b32 v49, v8, 4, v95
	ds_read_u16 v8, v93 offset:16992
	global_load_dwordx4 v[24:27], v9, s[0:1]
	s_waitcnt lgkmcnt(0)
	v_add_u32_e32 v8, s44, v8
	v_lshl_or_b32 v9, v8, 7, v165
	v_lshl_or_b32 v50, v8, 4, v95
	ds_read_u16 v8, v93 offset:17008
	global_load_dwordx4 v[12:15], v9, s[0:1]
	s_waitcnt lgkmcnt(0)
	v_add_u32_e32 v51, s44, v8
	v_lshl_or_b32 v8, v51, 7, v165
	global_load_dwordx4 v[8:11], v8, s[0:1]
	v_lshl_or_b32 v51, v51, 4, v95
	global_load_ushort v176, v95, s[18:19]
	global_load_ushort v177, v95, s[18:19]
	global_load_ushort v167, v95, s[18:19]
	global_load_ushort v168, v95, s[18:19]
	global_load_ushort v90, v95, s[18:19]
	global_load_ushort v91, v95, s[18:19]
	global_load_ushort v88, v95, s[18:19]
	global_load_ushort v89, v95, s[18:19]
	s_waitcnt vmcnt(31)
	v_and_b32_e32 v40, 0xf0f0f0f, v80
	v_mov_b32_e32 v42, 0
	v_dot4c_i32_i8_e32 v42, v40, v4
	v_lshrrev_b32_e32 v40, 4, v80
	v_and_b32_e32 v40, 0xf0f0f0f, v40
	v_dot4c_i32_i8_e32 v42, v40, v5
	v_and_b32_e32 v40, 0xf0f0f0f, v81
	v_mov_b32_e32 v43, 0
	v_dot4c_i32_i8_e32 v43, v40, v6
	v_lshrrev_b32_e32 v40, 4, v81
	v_and_b32_e32 v40, 0xf0f0f0f, v40
	v_dot4c_i32_i8_e32 v43, v40, v7
	v_and_b32_e32 v40, 0xf0f0f0f, v82
	v_dot4c_i32_i8_e32 v42, v40, v0
	v_lshrrev_b32_e32 v40, 4, v82
	v_and_b32_e32 v40, 0xf0f0f0f, v40
	v_dot4c_i32_i8_e32 v42, v40, v1
	v_and_b32_e32 v40, 0xf0f0f0f, v83
	v_dot4c_i32_i8_e32 v43, v40, v2
	v_lshrrev_b32_e32 v40, 4, v83
	v_and_b32_e32 v40, 0xf0f0f0f, v40
	v_dot4c_i32_i8_e32 v43, v40, v3
	s_waitcnt vmcnt(30)
	v_and_b32_e32 v40, 0xf0f0f0f, v68
	v_mov_b32_e32 v48, 0
	v_dot4c_i32_i8_e32 v48, v40, v4
	v_lshrrev_b32_e32 v40, 4, v68
	v_and_b32_e32 v40, 0xf0f0f0f, v40
	v_dot4c_i32_i8_e32 v48, v40, v5
	v_and_b32_e32 v40, 0xf0f0f0f, v69
	v_mov_b32_e32 v49, 0
	v_dot4c_i32_i8_e32 v49, v40, v6
	v_lshrrev_b32_e32 v40, 4, v69
	v_and_b32_e32 v40, 0xf0f0f0f, v40
	v_dot4c_i32_i8_e32 v49, v40, v7
	v_and_b32_e32 v40, 0xf0f0f0f, v70
	v_dot4c_i32_i8_e32 v48, v40, v0
	v_lshrrev_b32_e32 v40, 4, v70
	v_and_b32_e32 v40, 0xf0f0f0f, v40
	v_dot4c_i32_i8_e32 v48, v40, v1
	v_and_b32_e32 v40, 0xf0f0f0f, v71
	v_dot4c_i32_i8_e32 v49, v40, v2
	v_lshrrev_b32_e32 v40, 4, v71
	v_and_b32_e32 v40, 0xf0f0f0f, v40
	v_dot4c_i32_i8_e32 v49, v40, v3
	v_add_u32_e32 v42, v42, v43
	v_sub_u32_e32 v42, v42, v84
	s_waitcnt vmcnt(22)
; #define P12_ISSUE(c_, i_, h_, CW_, SC_) do { _Pragma("unroll") for (int bb = 0; bb < 8; ++bb) { const unsigned ro = (unsigned)(c_) * 16384u + (unsigned)EL[(i_) * 128 + ((h_) * 8 + bb) * 8 + g8]; \
;         CW_[bb] = *(const v4u*)(U4 + (size_t)(ro * 128u + 16u * (unsigned)k8)); SC_[bb] = USS[(size_t)(ro * 8u + (unsigned)k8)]; } } while (0)
; #define P12_COMP(i_, h_, CW_, SC_) do { _Pragma("unroll") for (int bb = 0; bb < 8; ++bb) { int a0 = 0, a1 = 0; P12_U4(CW_[bb].x, xa.x, xa.y, a0); P12_U4(CW_[bb].y, xa.z, xa.w, a1); P12_U4(CW_[bb].z, xb.x, xb.y, a0); P12_U4(CW_[bb].w, xb.z, xb.w, a1); \
;         psum[(i_)][(h_) * 8 + bb] += __uint_as_float(SC_[bb] << 16) * (float)((a0 + a1) - xo); } } while (0)
; #define P12_BAR() asm volatile("" ::: "memory")
; __device__ __forceinline__ void p12_peer(Frame& F) {
;     ...
;     { v4u cwA[8], cwB[8]; unsigned scA[8], scB[8]; v4u xa, xb; int xo;
;       P12_ISSUE(0, 0, 0, cwA, scA);
; _Pragma("nounroll")
;       for (int c = 0; c < 16; ++c) { const int cn = c + 1 < 16 ? c + 1 : 15;
;           P12_XQ(c, 0); P12_ISSUE(c, 0, 1, cwB, scB); P12_BAR(); P12_COMP(0, 0, cwA, scA); P12_ISSUE(c, 1, 0, cwA, scA); P12_BAR(); P12_COMP(0, 1, cwB, scB);
;           P12_XQ(c, 1); P12_ISSUE(c, 1, 1, cwB, scB); P12_BAR(); P12_COMP(1, 0, cwA, scA); P12_ISSUE(c, 2, 0, cwA, scA); P12_BAR(); P12_COMP(1, 1, cwB, scB);
;           P12_XQ(c, 2); P12_ISSUE(c, 2, 1, cwB, scB); P12_BAR(); P12_COMP(2, 0, cwA, scA); P12_ISSUE(c, 3, 0, cwA, scA); P12_BAR(); P12_COMP(2, 1, cwB, scB);
;           P12_XQ(c, 3); P12_ISSUE(c, 3, 1, cwB, scB); P12_BAR(); P12_COMP(3, 0, cwA, scA); P12_ISSUE(cn, 0, 0, cwA, scA); P12_BAR(); P12_COMP(3, 1, cwB, scB);
	v_and_b32_e32 v41, 0xffff0000, v208
	v_sub_u32_e32 v43, v49, v84
	v_add_u32_e32 v48, v43, v48
	v_cvt_f32_i32_e32 v43, v42
	v_cvt_f32_i32_e32 v42, v48
	v_and_b32_e32 v40, 0xffff0000, v209
	v_pk_fma_f32 v[134:135], v[40:41], v[42:43], v[134:135]
	v_and_b32_e32 v40, 0xf0f0f0f, v52
	v_mov_b32_e32 v41, 0
	v_dot4c_i32_i8_e32 v41, v40, v4
	v_lshrrev_b32_e32 v40, 4, v52
	v_and_b32_e32 v40, 0xf0f0f0f, v40
	v_dot4c_i32_i8_e32 v41, v40, v5
	v_and_b32_e32 v40, 0xf0f0f0f, v53
	v_mov_b32_e32 v42, 0
	v_dot4c_i32_i8_e32 v42, v40, v6
	v_lshrrev_b32_e32 v40, 4, v53
	v_and_b32_e32 v40, 0xf0f0f0f, v40
	v_dot4c_i32_i8_e32 v42, v40, v7
	v_and_b32_e32 v40, 0xf0f0f0f, v54
	v_dot4c_i32_i8_e32 v41, v40, v0
	v_lshrrev_b32_e32 v40, 4, v54
	v_and_b32_e32 v40, 0xf0f0f0f, v40
	v_dot4c_i32_i8_e32 v41, v40, v1
	v_and_b32_e32 v40, 0xf0f0f0f, v55
	v_dot4c_i32_i8_e32 v42, v40, v2
	v_lshrrev_b32_e32 v40, 4, v55
	v_and_b32_e32 v40, 0xf0f0f0f, v40
	v_dot4c_i32_i8_e32 v42, v40, v3
	v_and_b32_e32 v40, 0xf0f0f0f, v36
	v_mov_b32_e32 v43, 0
	v_lshrrev_b32_e32 v36, 4, v36
	v_dot4c_i32_i8_e32 v43, v40, v4
	v_and_b32_e32 v36, 0xf0f0f0f, v36
	v_dot4c_i32_i8_e32 v43, v36, v5
	v_and_b32_e32 v36, 0xf0f0f0f, v37
	v_mov_b32_e32 v40, 0
	v_dot4c_i32_i8_e32 v40, v36, v6
	v_lshrrev_b32_e32 v36, 4, v37
	v_and_b32_e32 v36, 0xf0f0f0f, v36
	v_dot4c_i32_i8_e32 v40, v36, v7
	v_and_b32_e32 v36, 0xf0f0f0f, v38
	v_dot4c_i32_i8_e32 v43, v36, v0
	v_lshrrev_b32_e32 v36, 4, v38
	v_and_b32_e32 v36, 0xf0f0f0f, v36
	v_dot4c_i32_i8_e32 v43, v36, v1
	v_and_b32_e32 v36, 0xf0f0f0f, v39
	v_dot4c_i32_i8_e32 v40, v36, v2
	v_lshrrev_b32_e32 v36, 4, v39
	v_and_b32_e32 v36, 0xf0f0f0f, v36
	v_dot4c_i32_i8_e32 v40, v36, v3
	v_sub_u32_e32 v38, v42, v84
	v_add_u32_e32 v38, v38, v41
	s_waitcnt vmcnt(20)
	v_and_b32_e32 v37, 0xffff0000, v210
	v_sub_u32_e32 v39, v40, v84
	v_add_u32_e32 v40, v39, v43
	v_cvt_f32_i32_e32 v39, v38
	v_cvt_f32_i32_e32 v38, v40
	v_and_b32_e32 v36, 0xffff0000, v211
	v_pk_fma_f32 v[132:133], v[36:37], v[38:39], v[132:133]
	v_and_b32_e32 v36, 0xf0f0f0f, v32
	v_mov_b32_e32 v37, 0
	v_lshrrev_b32_e32 v32, 4, v32
	v_dot4c_i32_i8_e32 v37, v36, v4
	v_and_b32_e32 v32, 0xf0f0f0f, v32
	v_dot4c_i32_i8_e32 v37, v32, v5
	v_and_b32_e32 v32, 0xf0f0f0f, v33
	v_mov_b32_e32 v36, 0
	v_dot4c_i32_i8_e32 v36, v32, v6
	v_lshrrev_b32_e32 v32, 4, v33
	v_and_b32_e32 v32, 0xf0f0f0f, v32
	v_dot4c_i32_i8_e32 v36, v32, v7
	v_and_b32_e32 v32, 0xf0f0f0f, v34
	v_dot4c_i32_i8_e32 v37, v32, v0
	v_lshrrev_b32_e32 v32, 4, v34
	v_and_b32_e32 v32, 0xf0f0f0f, v32
	v_dot4c_i32_i8_e32 v37, v32, v1
	v_and_b32_e32 v32, 0xf0f0f0f, v35
	v_dot4c_i32_i8_e32 v36, v32, v2
	v_lshrrev_b32_e32 v32, 4, v35
	v_and_b32_e32 v32, 0xf0f0f0f, v32
	v_dot4c_i32_i8_e32 v36, v32, v3
	v_and_b32_e32 v32, 0xf0f0f0f, v28
	v_mov_b32_e32 v33, 0
	v_lshrrev_b32_e32 v28, 4, v28
	v_dot4c_i32_i8_e32 v33, v32, v4
	v_and_b32_e32 v28, 0xf0f0f0f, v28
	v_dot4c_i32_i8_e32 v33, v28, v5
	v_and_b32_e32 v28, 0xf0f0f0f, v29
	v_mov_b32_e32 v32, 0
	v_dot4c_i32_i8_e32 v32, v28, v6
	v_lshrrev_b32_e32 v28, 4, v29
	v_and_b32_e32 v28, 0xf0f0f0f, v28
	v_dot4c_i32_i8_e32 v32, v28, v7
	v_and_b32_e32 v28, 0xf0f0f0f, v30
	v_dot4c_i32_i8_e32 v33, v28, v0
	v_lshrrev_b32_e32 v28, 4, v30
	v_and_b32_e32 v28, 0xf0f0f0f, v28
	v_dot4c_i32_i8_e32 v33, v28, v1
	v_and_b32_e32 v28, 0xf0f0f0f, v31
	v_dot4c_i32_i8_e32 v32, v28, v2
	v_lshrrev_b32_e32 v28, 4, v31
	v_and_b32_e32 v28, 0xf0f0f0f, v28
	v_dot4c_i32_i8_e32 v32, v28, v3
	v_sub_u32_e32 v30, v36, v84
	v_add_u32_e32 v30, v30, v37
	s_waitcnt vmcnt(18)
	v_and_b32_e32 v29, 0xffff0000, v212
	v_sub_u32_e32 v31, v32, v84
	v_add_u32_e32 v32, v31, v33
	v_cvt_f32_i32_e32 v31, v30
	v_cvt_f32_i32_e32 v30, v32
	v_and_b32_e32 v28, 0xffff0000, v213
	v_pk_fma_f32 v[130:131], v[28:29], v[30:31], v[130:131]
	v_and_b32_e32 v28, 0xf0f0f0f, v20
	v_mov_b32_e32 v29, 0
	v_lshrrev_b32_e32 v20, 4, v20
	v_dot4c_i32_i8_e32 v29, v28, v4
	v_and_b32_e32 v20, 0xf0f0f0f, v20
	v_dot4c_i32_i8_e32 v29, v20, v5
	v_and_b32_e32 v20, 0xf0f0f0f, v21
	v_mov_b32_e32 v28, 0
	v_dot4c_i32_i8_e32 v28, v20, v6
	v_lshrrev_b32_e32 v20, 4, v21
	v_and_b32_e32 v20, 0xf0f0f0f, v20
	v_dot4c_i32_i8_e32 v28, v20, v7
	v_and_b32_e32 v20, 0xf0f0f0f, v22
	v_dot4c_i32_i8_e32 v29, v20, v0
	v_lshrrev_b32_e32 v20, 4, v22
	v_and_b32_e32 v20, 0xf0f0f0f, v20
	v_dot4c_i32_i8_e32 v29, v20, v1
	v_and_b32_e32 v20, 0xf0f0f0f, v23
	v_dot4c_i32_i8_e32 v28, v20, v2
	v_lshrrev_b32_e32 v20, 4, v23
	v_and_b32_e32 v20, 0xf0f0f0f, v20
	v_dot4c_i32_i8_e32 v28, v20, v3
	v_and_b32_e32 v20, 0xf0f0f0f, v16
	v_mov_b32_e32 v21, 0
	v_dot4c_i32_i8_e32 v21, v20, v4
	v_lshrrev_b32_e32 v4, 4, v16
	v_and_b32_e32 v4, 0xf0f0f0f, v4
	v_dot4c_i32_i8_e32 v21, v4, v5
	v_and_b32_e32 v4, 0xf0f0f0f, v17
	v_mov_b32_e32 v5, 0
	v_dot4c_i32_i8_e32 v5, v4, v6
	v_lshrrev_b32_e32 v4, 4, v17
	v_and_b32_e32 v4, 0xf0f0f0f, v4
	v_dot4c_i32_i8_e32 v5, v4, v7
	v_and_b32_e32 v4, 0xf0f0f0f, v18
	v_dot4c_i32_i8_e32 v21, v4, v0
	v_lshrrev_b32_e32 v0, 4, v18
	v_and_b32_e32 v0, 0xf0f0f0f, v0
	v_dot4c_i32_i8_e32 v21, v0, v1
	v_and_b32_e32 v0, 0xf0f0f0f, v19
	v_dot4c_i32_i8_e32 v5, v0, v2
	v_lshrrev_b32_e32 v0, 4, v19
	v_and_b32_e32 v0, 0xf0f0f0f, v0
	v_dot4c_i32_i8_e32 v5, v0, v3
	v_sub_u32_e32 v2, v28, v84
	v_add_u32_e32 v2, v2, v29
	s_waitcnt vmcnt(16)
	v_and_b32_e32 v1, 0xffff0000, v214
	v_sub_u32_e32 v3, v5, v84
	v_add_u32_e32 v4, v3, v21
	v_cvt_f32_i32_e32 v3, v2
	v_cvt_f32_i32_e32 v2, v4
	v_and_b32_e32 v0, 0xffff0000, v215
	ds_read_b128 v[32:35], v166 offset:8192
	ds_read_b128 v[28:31], v166 offset:8208
	v_pk_fma_f32 v[128:129], v[0:1], v[2:3], v[128:129]
	ds_read_u16 v1, v93 offset:17024
	ds_read_u16 v2, v93 offset:17040
	ds_read_u16 v3, v93 offset:17056
	ds_read_u16 v4, v93 offset:17072
	v_mov_b32_e32 v0, 0
	s_waitcnt lgkmcnt(3)
; #define P12_ISSUE(c_, i_, h_, CW_, SC_) do { _Pragma("unroll") for (int bb = 0; bb < 8; ++bb) { const unsigned ro = (unsigned)(c_) * 16384u + (unsigned)EL[(i_) * 128 + ((h_) * 8 + bb) * 8 + g8]; \
;         CW_[bb] = *(const v4u*)(U4 + (size_t)(ro * 128u + 16u * (unsigned)k8)); SC_[bb] = USS[(size_t)(ro * 8u + (unsigned)k8)]; } } while (0)
; #define P12_COMP(i_, h_, CW_, SC_) do { _Pragma("unroll") for (int bb = 0; bb < 8; ++bb) { int a0 = 0, a1 = 0; P12_U4(CW_[bb].x, xa.x, xa.y, a0); P12_U4(CW_[bb].y, xa.z, xa.w, a1); P12_U4(CW_[bb].z, xb.x, xb.y, a0); P12_U4(CW_[bb].w, xb.z, xb.w, a1); \
;         psum[(i_)][(h_) * 8 + bb] += __uint_as_float(SC_[bb] << 16) * (float)((a0 + a1) - xo); } } while (0)
; #define P12_BAR() asm volatile("" ::: "memory")
; __device__ __forceinline__ void p12_peer(Frame& F) {
;     ...
;     { v4u cwA[8], cwB[8]; unsigned scA[8], scB[8]; v4u xa, xb; int xo;
;       P12_ISSUE(0, 0, 0, cwA, scA);
; _Pragma("nounroll")
;       for (int c = 0; c < 16; ++c) { const int cn = c + 1 < 16 ? c + 1 : 15;
;           P12_XQ(c, 0); P12_ISSUE(c, 0, 1, cwB, scB); P12_BAR(); P12_COMP(0, 0, cwA, scA); P12_ISSUE(c, 1, 0, cwA, scA); P12_BAR(); P12_COMP(0, 1, cwB, scB);
;           P12_XQ(c, 1); P12_ISSUE(c, 1, 1, cwB, scB); P12_BAR(); P12_COMP(1, 0, cwA, scA); P12_ISSUE(c, 2, 0, cwA, scA); P12_BAR(); P12_COMP(1, 1, cwB, scB);
;           P12_XQ(c, 2); P12_ISSUE(c, 2, 1, cwB, scB); P12_BAR(); P12_COMP(2, 0, cwA, scA); P12_ISSUE(c, 3, 0, cwA, scA); P12_BAR(); P12_COMP(2, 1, cwB, scB);
;           P12_XQ(c, 3); P12_ISSUE(c, 3, 1, cwB, scB); P12_BAR(); P12_COMP(3, 0, cwA, scA); P12_ISSUE(cn, 0, 0, cwA, scA); P12_BAR(); P12_COMP(3, 1, cwB, scB);
	v_add_u32_e32 v1, s44, v1
	v_lshl_or_b32 v5, v1, 7, v165
	s_waitcnt lgkmcnt(2)
	v_add_u32_e32 v2, s44, v2
	global_load_dwordx4 v[84:87], v5, s[0:1]
	v_lshl_or_b32 v5, v2, 7, v165
	s_waitcnt lgkmcnt(1)
	v_add_u32_e32 v3, s44, v3
	global_load_dwordx4 v[80:83], v5, s[0:1]
	v_lshl_or_b32 v5, v3, 7, v165
	s_waitcnt lgkmcnt(0)
	v_add_u32_e32 v4, s44, v4
	global_load_dwordx4 v[68:71], v5, s[0:1]
	v_lshl_or_b32 v5, v4, 7, v165
	global_load_dwordx4 v[64:67], v5, s[0:1]
	ds_read_u16 v5, v93 offset:17088
	v_dot4c_i32_i8_e32 v0, 0x1010101, v32
	v_dot4c_i32_i8_e32 v0, 0x1010101, v33
	v_dot4c_i32_i8_e32 v0, 0x1010101, v34
	v_dot4c_i32_i8_e32 v0, 0x1010101, v35
	s_waitcnt lgkmcnt(0)
	v_add_u32_e32 v5, s44, v5
	v_lshl_or_b32 v6, v5, 7, v165
	global_load_dwordx4 v[52:55], v6, s[0:1]
	ds_read_u16 v6, v93 offset:17104
	v_dot4c_i32_i8_e32 v0, 0x1010101, v28
	v_dot4c_i32_i8_e32 v0, 0x1010101, v29
	v_dot4c_i32_i8_e32 v0, 0x1010101, v30
	v_dot4c_i32_i8_e32 v0, 0x1010101, v31
	s_waitcnt lgkmcnt(0)
	v_add_u32_e32 v6, s44, v6
	v_lshl_or_b32 v7, v6, 7, v165
	global_load_dwordx4 v[48:51], v7, s[0:1]
	ds_read_u16 v7, v93 offset:17120
	v_lshl_or_b32 v2, v2, 4, v95
	v_lshl_or_b32 v1, v1, 4, v95
	v_lshl_or_b32 v3, v3, 4, v95
	v_lshl_or_b32 v4, v4, 4, v95
	s_waitcnt lgkmcnt(0)
	v_add_u32_e32 v7, s44, v7
	v_lshl_or_b32 v16, v7, 7, v165
	global_load_dwordx4 v[40:43], v16, s[0:1]
	ds_read_u16 v16, v93 offset:17136
	v_lshl_or_b32 v5, v5, 4, v95
	v_lshl_or_b32 v6, v6, 4, v95
	v_lshl_or_b32 v7, v7, 4, v95
	v_lshlrev_b32_e32 v169, 3, v0
	s_waitcnt lgkmcnt(0)
	v_add_u32_e32 v16, s44, v16
	v_lshl_or_b32 v17, v16, 7, v165
	global_load_dwordx4 v[36:39], v17, s[0:1]
	v_lshl_or_b32 v16, v16, 4, v95
	global_load_ushort v178, v95, s[18:19]
	global_load_ushort v179, v95, s[18:19]
	global_load_ushort v174, v95, s[18:19]
	global_load_ushort v175, v95, s[18:19]
	global_load_ushort v172, v95, s[18:19]
	global_load_ushort v173, v95, s[18:19]
	global_load_ushort v170, v95, s[18:19]
	global_load_ushort v171, v95, s[18:19]
	s_waitcnt vmcnt(31)
	v_and_b32_e32 v0, 0xf0f0f0f, v76
	v_mov_b32_e32 v2, 0
	v_dot4c_i32_i8_e32 v2, v0, v32
	v_lshrrev_b32_e32 v0, 4, v76
	v_and_b32_e32 v0, 0xf0f0f0f, v0
	v_dot4c_i32_i8_e32 v2, v0, v33
	v_and_b32_e32 v0, 0xf0f0f0f, v77
	v_mov_b32_e32 v3, 0
	v_dot4c_i32_i8_e32 v3, v0, v34
	v_lshrrev_b32_e32 v0, 4, v77
	v_and_b32_e32 v0, 0xf0f0f0f, v0
	v_dot4c_i32_i8_e32 v3, v0, v35
	v_and_b32_e32 v0, 0xf0f0f0f, v78
	v_dot4c_i32_i8_e32 v2, v0, v28
	v_lshrrev_b32_e32 v0, 4, v78
	v_and_b32_e32 v0, 0xf0f0f0f, v0
	v_dot4c_i32_i8_e32 v2, v0, v29
	v_and_b32_e32 v0, 0xf0f0f0f, v79
	v_dot4c_i32_i8_e32 v3, v0, v30
	v_lshrrev_b32_e32 v0, 4, v79
	v_and_b32_e32 v0, 0xf0f0f0f, v0
	v_dot4c_i32_i8_e32 v3, v0, v31
	s_waitcnt vmcnt(30)
	v_and_b32_e32 v0, 0xf0f0f0f, v72
	v_mov_b32_e32 v4, 0
	v_dot4c_i32_i8_e32 v4, v0, v32
	v_lshrrev_b32_e32 v0, 4, v72
	v_and_b32_e32 v0, 0xf0f0f0f, v0
	v_dot4c_i32_i8_e32 v4, v0, v33
	v_and_b32_e32 v0, 0xf0f0f0f, v73
	v_mov_b32_e32 v5, 0
	v_dot4c_i32_i8_e32 v5, v0, v34
	v_lshrrev_b32_e32 v0, 4, v73
	v_and_b32_e32 v0, 0xf0f0f0f, v0
	v_dot4c_i32_i8_e32 v5, v0, v35
	v_and_b32_e32 v0, 0xf0f0f0f, v74
	v_dot4c_i32_i8_e32 v4, v0, v28
	v_lshrrev_b32_e32 v0, 4, v74
	v_and_b32_e32 v0, 0xf0f0f0f, v0
	v_dot4c_i32_i8_e32 v4, v0, v29
	v_and_b32_e32 v0, 0xf0f0f0f, v75
	v_dot4c_i32_i8_e32 v5, v0, v30
	v_lshrrev_b32_e32 v0, 4, v75
	v_and_b32_e32 v0, 0xf0f0f0f, v0
	v_dot4c_i32_i8_e32 v5, v0, v31
	v_add_u32_e32 v2, v2, v3
	v_sub_u32_e32 v2, v2, v169
	s_waitcnt vmcnt(22)
	v_and_b32_e32 v1, 0xffff0000, v216
	v_add_u32_e32 v3, v4, v5
	v_sub_u32_e32 v4, v3, v169
	v_cvt_f32_i32_e32 v3, v2
	v_cvt_f32_i32_e32 v2, v4
	v_and_b32_e32 v0, 0xffff0000, v217
	v_mov_b32_e32 v4, 0
	v_mov_b32_e32 v5, 0
	v_pk_fma_f32 v[126:127], v[0:1], v[2:3], v[126:127]
	v_and_b32_e32 v0, 0xf0f0f0f, v60
	v_mov_b32_e32 v2, 0
	v_dot4c_i32_i8_e32 v2, v0, v32
	v_lshrrev_b32_e32 v0, 4, v60
	v_and_b32_e32 v0, 0xf0f0f0f, v0
	v_dot4c_i32_i8_e32 v2, v0, v33
	v_and_b32_e32 v0, 0xf0f0f0f, v61
	v_mov_b32_e32 v3, 0
	v_dot4c_i32_i8_e32 v3, v0, v34
	v_lshrrev_b32_e32 v0, 4, v61
	v_and_b32_e32 v0, 0xf0f0f0f, v0
	v_dot4c_i32_i8_e32 v3, v0, v35
	v_and_b32_e32 v0, 0xf0f0f0f, v62
	v_dot4c_i32_i8_e32 v2, v0, v28
	v_lshrrev_b32_e32 v0, 4, v62
	v_and_b32_e32 v0, 0xf0f0f0f, v0
	v_dot4c_i32_i8_e32 v2, v0, v29
	v_and_b32_e32 v0, 0xf0f0f0f, v63
	v_dot4c_i32_i8_e32 v3, v0, v30
	v_lshrrev_b32_e32 v0, 4, v63
	v_and_b32_e32 v0, 0xf0f0f0f, v0
	v_dot4c_i32_i8_e32 v3, v0, v31
	v_and_b32_e32 v0, 0xf0f0f0f, v56
	v_dot4c_i32_i8_e32 v4, v0, v32
	v_lshrrev_b32_e32 v0, 4, v56
	v_and_b32_e32 v0, 0xf0f0f0f, v0
	v_dot4c_i32_i8_e32 v4, v0, v33
	v_and_b32_e32 v0, 0xf0f0f0f, v57
	v_dot4c_i32_i8_e32 v5, v0, v34
	v_lshrrev_b32_e32 v0, 4, v57
	v_and_b32_e32 v0, 0xf0f0f0f, v0
	v_dot4c_i32_i8_e32 v5, v0, v35
	v_and_b32_e32 v0, 0xf0f0f0f, v58
	v_dot4c_i32_i8_e32 v4, v0, v28
	v_lshrrev_b32_e32 v0, 4, v58
	v_and_b32_e32 v0, 0xf0f0f0f, v0
	v_dot4c_i32_i8_e32 v4, v0, v29
	v_and_b32_e32 v0, 0xf0f0f0f, v59
	v_dot4c_i32_i8_e32 v5, v0, v30
	v_lshrrev_b32_e32 v0, 4, v59
	v_and_b32_e32 v0, 0xf0f0f0f, v0
	v_dot4c_i32_i8_e32 v5, v0, v31
	v_add_u32_e32 v2, v2, v3
	v_sub_u32_e32 v2, v2, v169
	s_waitcnt vmcnt(20)
; #define P12_ISSUE(c_, i_, h_, CW_, SC_) do { _Pragma("unroll") for (int bb = 0; bb < 8; ++bb) { const unsigned ro = (unsigned)(c_) * 16384u + (unsigned)EL[(i_) * 128 + ((h_) * 8 + bb) * 8 + g8]; \
;         CW_[bb] = *(const v4u*)(U4 + (size_t)(ro * 128u + 16u * (unsigned)k8)); SC_[bb] = USS[(size_t)(ro * 8u + (unsigned)k8)]; } } while (0)
; #define P12_COMP(i_, h_, CW_, SC_) do { _Pragma("unroll") for (int bb = 0; bb < 8; ++bb) { int a0 = 0, a1 = 0; P12_U4(CW_[bb].x, xa.x, xa.y, a0); P12_U4(CW_[bb].y, xa.z, xa.w, a1); P12_U4(CW_[bb].z, xb.x, xb.y, a0); P12_U4(CW_[bb].w, xb.z, xb.w, a1); \
;         psum[(i_)][(h_) * 8 + bb] += __uint_as_float(SC_[bb] << 16) * (float)((a0 + a1) - xo); } } while (0)
; #define P12_BAR() asm volatile("" ::: "memory")
; __device__ __forceinline__ void p12_peer(Frame& F) {
;     ...
;     { v4u cwA[8], cwB[8]; unsigned scA[8], scB[8]; v4u xa, xb; int xo;
;       P12_ISSUE(0, 0, 0, cwA, scA);
; _Pragma("nounroll")
;       for (int c = 0; c < 16; ++c) { const int cn = c + 1 < 16 ? c + 1 : 15;
;           P12_XQ(c, 0); P12_ISSUE(c, 0, 1, cwB, scB); P12_BAR(); P12_COMP(0, 0, cwA, scA); P12_ISSUE(c, 1, 0, cwA, scA); P12_BAR(); P12_COMP(0, 1, cwB, scB);
;           P12_XQ(c, 1); P12_ISSUE(c, 1, 1, cwB, scB); P12_BAR(); P12_COMP(1, 0, cwA, scA); P12_ISSUE(c, 2, 0, cwA, scA); P12_BAR(); P12_COMP(1, 1, cwB, scB);
;           P12_XQ(c, 2); P12_ISSUE(c, 2, 1, cwB, scB); P12_BAR(); P12_COMP(2, 0, cwA, scA); P12_ISSUE(c, 3, 0, cwA, scA); P12_BAR(); P12_COMP(2, 1, cwB, scB);
;           P12_XQ(c, 3); P12_ISSUE(c, 3, 1, cwB, scB); P12_BAR(); P12_COMP(3, 0, cwA, scA); P12_ISSUE(cn, 0, 0, cwA, scA); P12_BAR(); P12_COMP(3, 1, cwB, scB);
	v_and_b32_e32 v1, 0xffff0000, v218
	v_add_u32_e32 v3, v4, v5
	v_sub_u32_e32 v4, v3, v169
	v_cvt_f32_i32_e32 v3, v2
	v_cvt_f32_i32_e32 v2, v4
	v_and_b32_e32 v0, 0xffff0000, v219
	v_mov_b32_e32 v4, 0
	v_mov_b32_e32 v5, 0
	v_pk_fma_f32 v[124:125], v[0:1], v[2:3], v[124:125]
	v_and_b32_e32 v0, 0xf0f0f0f, v44
	v_mov_b32_e32 v2, 0
	v_dot4c_i32_i8_e32 v2, v0, v32
	v_lshrrev_b32_e32 v0, 4, v44
	v_and_b32_e32 v0, 0xf0f0f0f, v0
	v_dot4c_i32_i8_e32 v2, v0, v33
	v_and_b32_e32 v0, 0xf0f0f0f, v45
	v_mov_b32_e32 v3, 0
	v_dot4c_i32_i8_e32 v3, v0, v34
	v_lshrrev_b32_e32 v0, 4, v45
	v_and_b32_e32 v0, 0xf0f0f0f, v0
	v_dot4c_i32_i8_e32 v3, v0, v35
	v_and_b32_e32 v0, 0xf0f0f0f, v46
	v_dot4c_i32_i8_e32 v2, v0, v28
	v_lshrrev_b32_e32 v0, 4, v46
	v_and_b32_e32 v0, 0xf0f0f0f, v0
	v_dot4c_i32_i8_e32 v2, v0, v29
	v_and_b32_e32 v0, 0xf0f0f0f, v47
	v_dot4c_i32_i8_e32 v3, v0, v30
	v_lshrrev_b32_e32 v0, 4, v47
	v_and_b32_e32 v0, 0xf0f0f0f, v0
	v_dot4c_i32_i8_e32 v3, v0, v31
	v_and_b32_e32 v0, 0xf0f0f0f, v24
	v_dot4c_i32_i8_e32 v4, v0, v32
	v_lshrrev_b32_e32 v0, 4, v24
	v_and_b32_e32 v0, 0xf0f0f0f, v0
	v_dot4c_i32_i8_e32 v4, v0, v33
	v_and_b32_e32 v0, 0xf0f0f0f, v25
	v_dot4c_i32_i8_e32 v5, v0, v34
	v_lshrrev_b32_e32 v0, 4, v25
	v_and_b32_e32 v0, 0xf0f0f0f, v0
	v_dot4c_i32_i8_e32 v5, v0, v35
	v_and_b32_e32 v0, 0xf0f0f0f, v26
	v_dot4c_i32_i8_e32 v4, v0, v28
	v_lshrrev_b32_e32 v0, 4, v26
	v_and_b32_e32 v0, 0xf0f0f0f, v0
	v_dot4c_i32_i8_e32 v4, v0, v29
	v_and_b32_e32 v0, 0xf0f0f0f, v27
	v_dot4c_i32_i8_e32 v5, v0, v30
	v_lshrrev_b32_e32 v0, 4, v27
	v_and_b32_e32 v0, 0xf0f0f0f, v0
	v_dot4c_i32_i8_e32 v5, v0, v31
	v_add_u32_e32 v2, v2, v3
	v_sub_u32_e32 v2, v2, v169
	s_waitcnt vmcnt(18)
	v_and_b32_e32 v1, 0xffff0000, v220
	v_add_u32_e32 v3, v4, v5
	v_sub_u32_e32 v4, v3, v169
	v_cvt_f32_i32_e32 v3, v2
	v_cvt_f32_i32_e32 v2, v4
	v_and_b32_e32 v0, 0xffff0000, v221
	v_mov_b32_e32 v4, 0
	v_mov_b32_e32 v5, 0
	v_pk_fma_f32 v[122:123], v[0:1], v[2:3], v[122:123]
	v_and_b32_e32 v0, 0xf0f0f0f, v12
	v_mov_b32_e32 v2, 0
	v_dot4c_i32_i8_e32 v2, v0, v32
	v_lshrrev_b32_e32 v0, 4, v12
	v_and_b32_e32 v0, 0xf0f0f0f, v0
	v_dot4c_i32_i8_e32 v2, v0, v33
	v_and_b32_e32 v0, 0xf0f0f0f, v13
	v_mov_b32_e32 v3, 0
	v_dot4c_i32_i8_e32 v3, v0, v34
	v_lshrrev_b32_e32 v0, 4, v13
	v_and_b32_e32 v0, 0xf0f0f0f, v0
	v_dot4c_i32_i8_e32 v3, v0, v35
	v_and_b32_e32 v0, 0xf0f0f0f, v14
	v_dot4c_i32_i8_e32 v2, v0, v28
	v_lshrrev_b32_e32 v0, 4, v14
	v_and_b32_e32 v0, 0xf0f0f0f, v0
	v_dot4c_i32_i8_e32 v2, v0, v29
	v_and_b32_e32 v0, 0xf0f0f0f, v15
	v_dot4c_i32_i8_e32 v3, v0, v30
	v_lshrrev_b32_e32 v0, 4, v15
	v_and_b32_e32 v0, 0xf0f0f0f, v0
	v_dot4c_i32_i8_e32 v3, v0, v31
	v_and_b32_e32 v0, 0xf0f0f0f, v8
	v_dot4c_i32_i8_e32 v4, v0, v32
	v_lshrrev_b32_e32 v0, 4, v8
	v_and_b32_e32 v0, 0xf0f0f0f, v0
	v_dot4c_i32_i8_e32 v4, v0, v33
	v_and_b32_e32 v0, 0xf0f0f0f, v9
	v_dot4c_i32_i8_e32 v5, v0, v34
	v_lshrrev_b32_e32 v0, 4, v9
	v_and_b32_e32 v0, 0xf0f0f0f, v0
	v_dot4c_i32_i8_e32 v5, v0, v35
	v_and_b32_e32 v0, 0xf0f0f0f, v10
	v_dot4c_i32_i8_e32 v4, v0, v28
	v_lshrrev_b32_e32 v0, 4, v10
	v_and_b32_e32 v0, 0xf0f0f0f, v0
	v_dot4c_i32_i8_e32 v4, v0, v29
	v_and_b32_e32 v0, 0xf0f0f0f, v11
	v_dot4c_i32_i8_e32 v5, v0, v30
	v_lshrrev_b32_e32 v0, 4, v11
	v_and_b32_e32 v0, 0xf0f0f0f, v0
	v_dot4c_i32_i8_e32 v5, v0, v31
	v_add_u32_e32 v2, v2, v3
	v_sub_u32_e32 v2, v2, v169
	s_waitcnt vmcnt(16)
	v_and_b32_e32 v1, 0xffff0000, v222
	v_add_u32_e32 v3, v4, v5
	v_sub_u32_e32 v4, v3, v169
	v_cvt_f32_i32_e32 v3, v2
	v_cvt_f32_i32_e32 v2, v4
	v_and_b32_e32 v0, 0xffff0000, v223
	v_pk_fma_f32 v[120:121], v[0:1], v[2:3], v[120:121]
	ds_read_u16 v0, v93 offset:17152
	ds_read_u16 v1, v93 offset:17168
	ds_read_u16 v2, v93 offset:17184
	ds_read_u16 v3, v93 offset:17200
	s_waitcnt lgkmcnt(3)
	v_add_u32_e32 v0, s44, v0
	v_lshl_or_b32 v4, v0, 7, v165
	v_lshl_or_b32 v44, v0, 4, v95
	s_waitcnt lgkmcnt(2)
	v_add_u32_e32 v0, s44, v1
	v_lshl_or_b32 v1, v0, 7, v165
	v_lshl_or_b32 v45, v0, 4, v95
	s_waitcnt lgkmcnt(1)
	v_add_u32_e32 v0, s44, v2
	global_load_dwordx4 v[72:75], v4, s[0:1]
	global_load_dwordx4 v[24:27], v1, s[0:1]
	v_lshl_or_b32 v1, v0, 7, v165
	v_lshl_or_b32 v46, v0, 4, v95
	s_waitcnt lgkmcnt(0)
	v_add_u32_e32 v0, s44, v3
	global_load_dwordx4 v[20:23], v1, s[0:1]
	v_lshl_or_b32 v1, v0, 7, v165
	v_lshl_or_b32 v47, v0, 4, v95
	ds_read_u16 v0, v93 offset:17216
	global_load_dwordx4 v[16:19], v1, s[0:1]
	s_waitcnt lgkmcnt(0)
	v_add_u32_e32 v0, s44, v0
	v_lshl_or_b32 v1, v0, 7, v165
	v_lshl_or_b32 v56, v0, 4, v95
	ds_read_u16 v0, v93 offset:17232
	global_load_dwordx4 v[12:15], v1, s[0:1]
	s_waitcnt lgkmcnt(0)
	v_add_u32_e32 v0, s44, v0
	v_lshl_or_b32 v1, v0, 7, v165
	v_lshl_or_b32 v57, v0, 4, v95
	ds_read_u16 v0, v93 offset:17248
	global_load_dwordx4 v[8:11], v1, s[0:1]
	s_waitcnt lgkmcnt(0)
	v_add_u32_e32 v0, s44, v0
	v_lshl_or_b32 v1, v0, 7, v165
	v_lshl_or_b32 v58, v0, 4, v95
	ds_read_u16 v0, v93 offset:17264
	global_load_dwordx4 v[4:7], v1, s[0:1]
	s_waitcnt lgkmcnt(0)
	v_add_u32_e32 v59, s44, v0
	v_lshl_or_b32 v0, v59, 7, v165
	global_load_dwordx4 v[0:3], v0, s[0:1]
	v_lshl_or_b32 v59, v59, 4, v95
	global_load_ushort v167, v95, s[18:19]
	global_load_ushort v168, v95, s[18:19]
	global_load_ushort v90, v95, s[18:19]
	global_load_ushort v91, v95, s[18:19]
	global_load_ushort v88, v95, s[18:19]
	global_load_ushort v89, v95, s[18:19]
	global_load_ushort v76, v95, s[18:19]
	global_load_ushort v77, v95, s[18:19]
	s_waitcnt vmcnt(31)
; #define P12_ISSUE(c_, i_, h_, CW_, SC_) do { _Pragma("unroll") for (int bb = 0; bb < 8; ++bb) { const unsigned ro = (unsigned)(c_) * 16384u + (unsigned)EL[(i_) * 128 + ((h_) * 8 + bb) * 8 + g8]; \
;         CW_[bb] = *(const v4u*)(U4 + (size_t)(ro * 128u + 16u * (unsigned)k8)); SC_[bb] = USS[(size_t)(ro * 8u + (unsigned)k8)]; } } while (0)
; #define P12_COMP(i_, h_, CW_, SC_) do { _Pragma("unroll") for (int bb = 0; bb < 8; ++bb) { int a0 = 0, a1 = 0; P12_U4(CW_[bb].x, xa.x, xa.y, a0); P12_U4(CW_[bb].y, xa.z, xa.w, a1); P12_U4(CW_[bb].z, xb.x, xb.y, a0); P12_U4(CW_[bb].w, xb.z, xb.w, a1); \
;         psum[(i_)][(h_) * 8 + bb] += __uint_as_float(SC_[bb] << 16) * (float)((a0 + a1) - xo); } } while (0)
; #define P12_BAR() asm volatile("" ::: "memory")
; __device__ __forceinline__ void p12_peer(Frame& F) {
;     ...
;     { v4u cwA[8], cwB[8]; unsigned scA[8], scB[8]; v4u xa, xb; int xo;
;       P12_ISSUE(0, 0, 0, cwA, scA);
; _Pragma("nounroll")
;       for (int c = 0; c < 16; ++c) { const int cn = c + 1 < 16 ? c + 1 : 15;
;           P12_XQ(c, 0); P12_ISSUE(c, 0, 1, cwB, scB); P12_BAR(); P12_COMP(0, 0, cwA, scA); P12_ISSUE(c, 1, 0, cwA, scA); P12_BAR(); P12_COMP(0, 1, cwB, scB);
;           P12_XQ(c, 1); P12_ISSUE(c, 1, 1, cwB, scB); P12_BAR(); P12_COMP(1, 0, cwA, scA); P12_ISSUE(c, 2, 0, cwA, scA); P12_BAR(); P12_COMP(1, 1, cwB, scB);
;           P12_XQ(c, 2); P12_ISSUE(c, 2, 1, cwB, scB); P12_BAR(); P12_COMP(2, 0, cwA, scA); P12_ISSUE(c, 3, 0, cwA, scA); P12_BAR(); P12_COMP(2, 1, cwB, scB);
;           P12_XQ(c, 3); P12_ISSUE(c, 3, 1, cwB, scB); P12_BAR(); P12_COMP(3, 0, cwA, scA); P12_ISSUE(cn, 0, 0, cwA, scA); P12_BAR(); P12_COMP(3, 1, cwB, scB);
	v_and_b32_e32 v44, 0xf0f0f0f, v84
	v_mov_b32_e32 v46, 0
	v_dot4c_i32_i8_e32 v46, v44, v32
	v_lshrrev_b32_e32 v44, 4, v84
	v_and_b32_e32 v44, 0xf0f0f0f, v44
	v_dot4c_i32_i8_e32 v46, v44, v33
	v_and_b32_e32 v44, 0xf0f0f0f, v85
	v_mov_b32_e32 v47, 0
	v_dot4c_i32_i8_e32 v47, v44, v34
	v_lshrrev_b32_e32 v44, 4, v85
	v_and_b32_e32 v44, 0xf0f0f0f, v44
	v_dot4c_i32_i8_e32 v47, v44, v35
	v_and_b32_e32 v44, 0xf0f0f0f, v86
	v_dot4c_i32_i8_e32 v46, v44, v28
	v_lshrrev_b32_e32 v44, 4, v86
	v_and_b32_e32 v44, 0xf0f0f0f, v44
	v_dot4c_i32_i8_e32 v46, v44, v29
	v_and_b32_e32 v44, 0xf0f0f0f, v87
	v_dot4c_i32_i8_e32 v47, v44, v30
	v_lshrrev_b32_e32 v44, 4, v87
	v_and_b32_e32 v44, 0xf0f0f0f, v44
	v_dot4c_i32_i8_e32 v47, v44, v31
	s_waitcnt vmcnt(30)
	v_and_b32_e32 v44, 0xf0f0f0f, v80
	v_mov_b32_e32 v56, 0
	v_dot4c_i32_i8_e32 v56, v44, v32
	v_lshrrev_b32_e32 v44, 4, v80
	v_and_b32_e32 v44, 0xf0f0f0f, v44
	v_dot4c_i32_i8_e32 v56, v44, v33
	v_and_b32_e32 v44, 0xf0f0f0f, v81
	v_mov_b32_e32 v57, 0
	v_dot4c_i32_i8_e32 v57, v44, v34
	v_lshrrev_b32_e32 v44, 4, v81
	v_and_b32_e32 v44, 0xf0f0f0f, v44
	v_dot4c_i32_i8_e32 v57, v44, v35
	v_and_b32_e32 v44, 0xf0f0f0f, v82
	v_dot4c_i32_i8_e32 v56, v44, v28
	v_lshrrev_b32_e32 v44, 4, v82
	v_and_b32_e32 v44, 0xf0f0f0f, v44
	v_dot4c_i32_i8_e32 v56, v44, v29
	v_and_b32_e32 v44, 0xf0f0f0f, v83
	v_dot4c_i32_i8_e32 v57, v44, v30
	v_lshrrev_b32_e32 v44, 4, v83
	v_and_b32_e32 v44, 0xf0f0f0f, v44
	v_dot4c_i32_i8_e32 v57, v44, v31
	v_add_u32_e32 v46, v46, v47
	v_sub_u32_e32 v46, v46, v169
	s_waitcnt vmcnt(22)
	v_and_b32_e32 v45, 0xffff0000, v224
	v_sub_u32_e32 v47, v57, v169
	v_add_u32_e32 v56, v47, v56
	v_cvt_f32_i32_e32 v47, v46
	v_cvt_f32_i32_e32 v46, v56
	v_and_b32_e32 v44, 0xffff0000, v225
	v_mov_b32_e32 v56, 0
	v_mov_b32_e32 v57, 0
	v_pk_fma_f32 v[118:119], v[44:45], v[46:47], v[118:119]
	v_and_b32_e32 v44, 0xf0f0f0f, v68
	v_mov_b32_e32 v46, 0
	v_dot4c_i32_i8_e32 v46, v44, v32
	v_lshrrev_b32_e32 v44, 4, v68
	v_and_b32_e32 v44, 0xf0f0f0f, v44
	v_dot4c_i32_i8_e32 v46, v44, v33
	v_and_b32_e32 v44, 0xf0f0f0f, v69
	v_mov_b32_e32 v47, 0
	v_dot4c_i32_i8_e32 v47, v44, v34
	v_lshrrev_b32_e32 v44, 4, v69
	v_and_b32_e32 v44, 0xf0f0f0f, v44
	v_dot4c_i32_i8_e32 v47, v44, v35
	v_and_b32_e32 v44, 0xf0f0f0f, v70
	v_dot4c_i32_i8_e32 v46, v44, v28
	v_lshrrev_b32_e32 v44, 4, v70
	v_and_b32_e32 v44, 0xf0f0f0f, v44
	v_dot4c_i32_i8_e32 v46, v44, v29
	v_and_b32_e32 v44, 0xf0f0f0f, v71
	v_dot4c_i32_i8_e32 v47, v44, v30
	v_lshrrev_b32_e32 v44, 4, v71
	v_and_b32_e32 v44, 0xf0f0f0f, v44
	v_dot4c_i32_i8_e32 v47, v44, v31
	v_and_b32_e32 v44, 0xf0f0f0f, v64
	v_dot4c_i32_i8_e32 v56, v44, v32
	v_lshrrev_b32_e32 v44, 4, v64
	v_and_b32_e32 v44, 0xf0f0f0f, v44
	v_dot4c_i32_i8_e32 v56, v44, v33
	v_and_b32_e32 v44, 0xf0f0f0f, v65
	v_dot4c_i32_i8_e32 v57, v44, v34
	v_lshrrev_b32_e32 v44, 4, v65
	v_and_b32_e32 v44, 0xf0f0f0f, v44
	v_dot4c_i32_i8_e32 v57, v44, v35
	v_and_b32_e32 v44, 0xf0f0f0f, v66
	v_dot4c_i32_i8_e32 v56, v44, v28
	v_lshrrev_b32_e32 v44, 4, v66
	v_and_b32_e32 v44, 0xf0f0f0f, v44
	v_dot4c_i32_i8_e32 v56, v44, v29
	v_and_b32_e32 v44, 0xf0f0f0f, v67
	v_dot4c_i32_i8_e32 v57, v44, v30
	v_lshrrev_b32_e32 v44, 4, v67
	v_and_b32_e32 v44, 0xf0f0f0f, v44
	v_dot4c_i32_i8_e32 v57, v44, v31
	v_sub_u32_e32 v47, v47, v169
	v_add_u32_e32 v46, v47, v46
	v_cvt_f32_i32_e32 v47, v46
	v_sub_u32_e32 v57, v57, v169
	v_add_u32_e32 v56, v57, v56
	v_cvt_f32_i32_e32 v46, v56
	s_waitcnt vmcnt(20)
	v_and_b32_e32 v45, 0xffff0000, v226
	v_and_b32_e32 v44, 0xffff0000, v227
	v_pk_fma_f32 v[116:117], v[44:45], v[46:47], v[116:117]
	v_and_b32_e32 v44, 0xf0f0f0f, v52
	v_mov_b32_e32 v46, 0
	v_dot4c_i32_i8_e32 v46, v44, v32
	v_lshrrev_b32_e32 v44, 4, v52
	v_and_b32_e32 v44, 0xf0f0f0f, v44
	v_dot4c_i32_i8_e32 v46, v44, v33
	v_and_b32_e32 v44, 0xf0f0f0f, v53
	v_mov_b32_e32 v47, 0
	v_dot4c_i32_i8_e32 v47, v44, v34
	v_lshrrev_b32_e32 v44, 4, v53
	v_and_b32_e32 v44, 0xf0f0f0f, v44
	v_dot4c_i32_i8_e32 v47, v44, v35
	v_and_b32_e32 v44, 0xf0f0f0f, v54
	v_dot4c_i32_i8_e32 v46, v44, v28
	v_lshrrev_b32_e32 v44, 4, v54
	v_and_b32_e32 v44, 0xf0f0f0f, v44
	v_dot4c_i32_i8_e32 v46, v44, v29
	v_and_b32_e32 v44, 0xf0f0f0f, v55
	v_dot4c_i32_i8_e32 v47, v44, v30
	v_lshrrev_b32_e32 v44, 4, v55
	v_and_b32_e32 v44, 0xf0f0f0f, v44
	v_dot4c_i32_i8_e32 v47, v44, v31
	v_and_b32_e32 v44, 0xf0f0f0f, v48
	v_mov_b32_e32 v52, 0
	v_dot4c_i32_i8_e32 v52, v44, v32
	v_lshrrev_b32_e32 v44, 4, v48
	v_and_b32_e32 v44, 0xf0f0f0f, v44
	v_dot4c_i32_i8_e32 v52, v44, v33
	v_and_b32_e32 v44, 0xf0f0f0f, v49
	v_mov_b32_e32 v48, 0
	v_dot4c_i32_i8_e32 v48, v44, v34
	v_lshrrev_b32_e32 v44, 4, v49
	v_and_b32_e32 v44, 0xf0f0f0f, v44
	v_dot4c_i32_i8_e32 v48, v44, v35
	v_and_b32_e32 v44, 0xf0f0f0f, v50
	v_dot4c_i32_i8_e32 v52, v44, v28
	v_lshrrev_b32_e32 v44, 4, v50
	v_and_b32_e32 v44, 0xf0f0f0f, v44
	v_dot4c_i32_i8_e32 v52, v44, v29
	v_and_b32_e32 v44, 0xf0f0f0f, v51
	v_dot4c_i32_i8_e32 v48, v44, v30
	v_lshrrev_b32_e32 v44, 4, v51
	v_and_b32_e32 v44, 0xf0f0f0f, v44
	v_dot4c_i32_i8_e32 v48, v44, v31
	v_sub_u32_e32 v47, v47, v169
	v_add_u32_e32 v46, v47, v46
	v_cvt_f32_i32_e32 v47, v46
	v_sub_u32_e32 v48, v48, v169
	v_add_u32_e32 v48, v48, v52
	v_cvt_f32_i32_e32 v46, v48
	s_waitcnt vmcnt(18)
; #define P12_ISSUE(c_, i_, h_, CW_, SC_) do { _Pragma("unroll") for (int bb = 0; bb < 8; ++bb) { const unsigned ro = (unsigned)(c_) * 16384u + (unsigned)EL[(i_) * 128 + ((h_) * 8 + bb) * 8 + g8]; \
;         CW_[bb] = *(const v4u*)(U4 + (size_t)(ro * 128u + 16u * (unsigned)k8)); SC_[bb] = USS[(size_t)(ro * 8u + (unsigned)k8)]; } } while (0)
; #define P12_COMP(i_, h_, CW_, SC_) do { _Pragma("unroll") for (int bb = 0; bb < 8; ++bb) { int a0 = 0, a1 = 0; P12_U4(CW_[bb].x, xa.x, xa.y, a0); P12_U4(CW_[bb].y, xa.z, xa.w, a1); P12_U4(CW_[bb].z, xb.x, xb.y, a0); P12_U4(CW_[bb].w, xb.z, xb.w, a1); \
;         psum[(i_)][(h_) * 8 + bb] += __uint_as_float(SC_[bb] << 16) * (float)((a0 + a1) - xo); } } while (0)
; #define P12_BAR() asm volatile("" ::: "memory")
; __device__ __forceinline__ void p12_peer(Frame& F) {
;     ...
;     { v4u cwA[8], cwB[8]; unsigned scA[8], scB[8]; v4u xa, xb; int xo;
;       P12_ISSUE(0, 0, 0, cwA, scA);
; _Pragma("nounroll")
;       for (int c = 0; c < 16; ++c) { const int cn = c + 1 < 16 ? c + 1 : 15;
;           P12_XQ(c, 0); P12_ISSUE(c, 0, 1, cwB, scB); P12_BAR(); P12_COMP(0, 0, cwA, scA); P12_ISSUE(c, 1, 0, cwA, scA); P12_BAR(); P12_COMP(0, 1, cwB, scB);
;           P12_XQ(c, 1); P12_ISSUE(c, 1, 1, cwB, scB); P12_BAR(); P12_COMP(1, 0, cwA, scA); P12_ISSUE(c, 2, 0, cwA, scA); P12_BAR(); P12_COMP(1, 1, cwB, scB);
;           P12_XQ(c, 2); P12_ISSUE(c, 2, 1, cwB, scB); P12_BAR(); P12_COMP(2, 0, cwA, scA); P12_ISSUE(c, 3, 0, cwA, scA); P12_BAR(); P12_COMP(2, 1, cwB, scB);
;           P12_XQ(c, 3); P12_ISSUE(c, 3, 1, cwB, scB); P12_BAR(); P12_COMP(3, 0, cwA, scA); P12_ISSUE(cn, 0, 0, cwA, scA); P12_BAR(); P12_COMP(3, 1, cwB, scB);
	v_and_b32_e32 v45, 0xffff0000, v228
	v_and_b32_e32 v44, 0xffff0000, v229
	v_pk_fma_f32 v[114:115], v[44:45], v[46:47], v[114:115]
	v_and_b32_e32 v44, 0xf0f0f0f, v40
	v_mov_b32_e32 v45, 0
	v_lshrrev_b32_e32 v40, 4, v40
	v_dot4c_i32_i8_e32 v45, v44, v32
	v_and_b32_e32 v40, 0xf0f0f0f, v40
	v_dot4c_i32_i8_e32 v45, v40, v33
	v_and_b32_e32 v40, 0xf0f0f0f, v41
	v_mov_b32_e32 v44, 0
	v_dot4c_i32_i8_e32 v44, v40, v34
	v_lshrrev_b32_e32 v40, 4, v41
	v_and_b32_e32 v40, 0xf0f0f0f, v40
	v_dot4c_i32_i8_e32 v44, v40, v35
	v_and_b32_e32 v40, 0xf0f0f0f, v42
	v_dot4c_i32_i8_e32 v45, v40, v28
	v_lshrrev_b32_e32 v40, 4, v42
	v_and_b32_e32 v40, 0xf0f0f0f, v40
	v_dot4c_i32_i8_e32 v45, v40, v29
	v_and_b32_e32 v40, 0xf0f0f0f, v43
	v_dot4c_i32_i8_e32 v44, v40, v30
	v_lshrrev_b32_e32 v40, 4, v43
	v_and_b32_e32 v40, 0xf0f0f0f, v40
	v_dot4c_i32_i8_e32 v44, v40, v31
	v_and_b32_e32 v40, 0xf0f0f0f, v36
	v_mov_b32_e32 v41, 0
	v_dot4c_i32_i8_e32 v41, v40, v32
	v_lshrrev_b32_e32 v32, 4, v36
	v_and_b32_e32 v32, 0xf0f0f0f, v32
	v_dot4c_i32_i8_e32 v41, v32, v33
	v_and_b32_e32 v32, 0xf0f0f0f, v37
	v_mov_b32_e32 v33, 0
	v_dot4c_i32_i8_e32 v33, v32, v34
	v_lshrrev_b32_e32 v32, 4, v37
	v_and_b32_e32 v32, 0xf0f0f0f, v32
	v_dot4c_i32_i8_e32 v33, v32, v35
	v_and_b32_e32 v32, 0xf0f0f0f, v38
	v_dot4c_i32_i8_e32 v41, v32, v28
	v_lshrrev_b32_e32 v28, 4, v38
	v_and_b32_e32 v28, 0xf0f0f0f, v28
	v_dot4c_i32_i8_e32 v41, v28, v29
	v_and_b32_e32 v28, 0xf0f0f0f, v39
	v_dot4c_i32_i8_e32 v33, v28, v30
	v_lshrrev_b32_e32 v28, 4, v39
	v_and_b32_e32 v28, 0xf0f0f0f, v28
	v_dot4c_i32_i8_e32 v33, v28, v31
	v_sub_u32_e32 v30, v44, v169
	v_add_u32_e32 v30, v30, v45
	s_waitcnt vmcnt(16)
	v_and_b32_e32 v29, 0xffff0000, v230
	v_sub_u32_e32 v31, v33, v169
	v_add_u32_e32 v32, v31, v41
	v_cvt_f32_i32_e32 v31, v30
	v_cvt_f32_i32_e32 v30, v32
	v_and_b32_e32 v28, 0xffff0000, v231
	ds_read_b128 v[36:39], v166 offset:12288
	ds_read_b128 v[32:35], v166 offset:12304
	v_add_u32_e32 v166, 0x100, v166
	v_pk_fma_f32 v[112:113], v[28:29], v[30:31], v[112:113]
	ds_read_u16 v29, v93 offset:17280
	ds_read_u16 v30, v93 offset:17296
	ds_read_u16 v31, v93 offset:17312
	ds_read_u16 v40, v93 offset:17328
	v_mov_b32_e32 v28, 0
	s_waitcnt lgkmcnt(3)
	v_add_u32_e32 v29, s44, v29
	v_lshl_or_b32 v41, v29, 7, v165
	s_waitcnt lgkmcnt(2)
	v_add_u32_e32 v30, s44, v30
	global_load_dwordx4 v[68:71], v41, s[0:1]
	v_lshl_or_b32 v41, v30, 7, v165
	s_waitcnt lgkmcnt(1)
	v_add_u32_e32 v31, s44, v31
	global_load_dwordx4 v[64:67], v41, s[0:1]
	v_lshl_or_b32 v41, v31, 7, v165
	s_waitcnt lgkmcnt(0)
	v_add_u32_e32 v40, s44, v40
	global_load_dwordx4 v[60:63], v41, s[0:1]
	v_lshl_or_b32 v41, v40, 7, v165
	v_lshl_or_b32 v79, v40, 4, v95
	ds_read_u16 v40, v93 offset:17344
	global_load_dwordx4 v[56:59], v41, s[0:1]
	v_dot4c_i32_i8_e32 v28, 0x1010101, v36
	v_dot4c_i32_i8_e32 v28, 0x1010101, v37
	v_dot4c_i32_i8_e32 v28, 0x1010101, v38
	s_waitcnt lgkmcnt(0)
	v_add_u32_e32 v40, s44, v40
	v_lshl_or_b32 v41, v40, 7, v165
	v_lshl_or_b32 v80, v40, 4, v95
	ds_read_u16 v40, v93 offset:17360
	global_load_dwordx4 v[52:55], v41, s[0:1]
	v_dot4c_i32_i8_e32 v28, 0x1010101, v39
	v_dot4c_i32_i8_e32 v28, 0x1010101, v32
	v_dot4c_i32_i8_e32 v28, 0x1010101, v33
	s_waitcnt lgkmcnt(0)
	v_add_u32_e32 v40, s44, v40
	v_lshl_or_b32 v41, v40, 7, v165
	v_lshl_or_b32 v82, v40, 4, v95
	ds_read_u16 v40, v93 offset:17376
	global_load_dwordx4 v[48:51], v41, s[0:1]
	v_dot4c_i32_i8_e32 v28, 0x1010101, v34
	v_dot4c_i32_i8_e32 v28, 0x1010101, v35
	v_lshl_or_b32 v29, v29, 4, v95
	s_waitcnt lgkmcnt(0)
	v_add_u32_e32 v40, s44, v40
	v_lshl_or_b32 v41, v40, 7, v165
	v_lshl_or_b32 v87, v40, 4, v95
	ds_read_u16 v40, v93 offset:17392
	v_lshl_or_b32 v30, v30, 4, v95
	v_lshl_or_b32 v31, v31, 4, v95
	global_load_dwordx4 v[44:47], v41, s[0:1]
	s_waitcnt lgkmcnt(0)
	v_add_u32_e32 v78, s44, v40
	v_lshl_or_b32 v40, v78, 7, v165
	global_load_dwordx4 v[40:43], v40, s[0:1]
	v_lshl_or_b32 v169, v78, 4, v95
	v_lshlrev_b32_e32 v78, 3, v28
	global_load_ushort v85, v95, s[18:19]
	global_load_ushort v86, v95, s[18:19]
	global_load_ushort v83, v95, s[18:19]
	global_load_ushort v84, v95, s[18:19]
	global_load_ushort v81, v95, s[18:19]
	s_nop 0
	global_load_ushort v82, v95, s[18:19]
	s_nop 0
	global_load_ushort v79, v95, s[18:19]
	global_load_ushort v80, v95, s[18:19]
	s_waitcnt vmcnt(31)
	v_and_b32_e32 v29, 0xf0f0f0f, v72
	v_mov_b32_e32 v28, 0
	v_dot4c_i32_i8_e32 v28, v29, v36
	v_lshrrev_b32_e32 v29, 4, v72
	v_and_b32_e32 v29, 0xf0f0f0f, v29
	v_dot4c_i32_i8_e32 v28, v29, v37
	v_and_b32_e32 v30, 0xf0f0f0f, v73
	v_mov_b32_e32 v29, 0
	v_dot4c_i32_i8_e32 v29, v30, v38
	v_lshrrev_b32_e32 v30, 4, v73
	v_and_b32_e32 v30, 0xf0f0f0f, v30
	v_dot4c_i32_i8_e32 v29, v30, v39
	v_and_b32_e32 v30, 0xf0f0f0f, v74
	v_dot4c_i32_i8_e32 v28, v30, v32
	v_lshrrev_b32_e32 v30, 4, v74
	v_and_b32_e32 v30, 0xf0f0f0f, v30
	v_dot4c_i32_i8_e32 v28, v30, v33
	v_and_b32_e32 v30, 0xf0f0f0f, v75
	v_dot4c_i32_i8_e32 v29, v30, v34
	v_lshrrev_b32_e32 v30, 4, v75
	v_and_b32_e32 v30, 0xf0f0f0f, v30
	v_dot4c_i32_i8_e32 v29, v30, v35
	s_waitcnt vmcnt(30)
	v_and_b32_e32 v31, 0xf0f0f0f, v24
	v_mov_b32_e32 v30, 0
	v_lshrrev_b32_e32 v24, 4, v24
	v_dot4c_i32_i8_e32 v30, v31, v36
	v_and_b32_e32 v24, 0xf0f0f0f, v24
	v_dot4c_i32_i8_e32 v30, v24, v37
	v_and_b32_e32 v24, 0xf0f0f0f, v25
	v_mov_b32_e32 v31, 0
	v_dot4c_i32_i8_e32 v31, v24, v38
	v_lshrrev_b32_e32 v24, 4, v25
	v_and_b32_e32 v24, 0xf0f0f0f, v24
	v_dot4c_i32_i8_e32 v31, v24, v39
	v_and_b32_e32 v24, 0xf0f0f0f, v26
	v_dot4c_i32_i8_e32 v30, v24, v32
	v_lshrrev_b32_e32 v24, 4, v26
	v_and_b32_e32 v24, 0xf0f0f0f, v24
	v_dot4c_i32_i8_e32 v30, v24, v33
	v_and_b32_e32 v24, 0xf0f0f0f, v27
	v_dot4c_i32_i8_e32 v31, v24, v34
	v_lshrrev_b32_e32 v24, 4, v27
	v_and_b32_e32 v24, 0xf0f0f0f, v24
	v_dot4c_i32_i8_e32 v31, v24, v35
	v_add_u32_e32 v26, v28, v29
	v_sub_u32_e32 v26, v26, v78
	s_waitcnt vmcnt(22)
; #define P12_ISSUE(c_, i_, h_, CW_, SC_) do { _Pragma("unroll") for (int bb = 0; bb < 8; ++bb) { const unsigned ro = (unsigned)(c_) * 16384u + (unsigned)EL[(i_) * 128 + ((h_) * 8 + bb) * 8 + g8]; \
;         CW_[bb] = *(const v4u*)(U4 + (size_t)(ro * 128u + 16u * (unsigned)k8)); SC_[bb] = USS[(size_t)(ro * 8u + (unsigned)k8)]; } } while (0)
; #define P12_COMP(i_, h_, CW_, SC_) do { _Pragma("unroll") for (int bb = 0; bb < 8; ++bb) { int a0 = 0, a1 = 0; P12_U4(CW_[bb].x, xa.x, xa.y, a0); P12_U4(CW_[bb].y, xa.z, xa.w, a1); P12_U4(CW_[bb].z, xb.x, xb.y, a0); P12_U4(CW_[bb].w, xb.z, xb.w, a1); \
;         psum[(i_)][(h_) * 8 + bb] += __uint_as_float(SC_[bb] << 16) * (float)((a0 + a1) - xo); } } while (0)
; #define P12_BAR() asm volatile("" ::: "memory")
; __device__ __forceinline__ void p12_peer(Frame& F) {
;     ...
;     { v4u cwA[8], cwB[8]; unsigned scA[8], scB[8]; v4u xa, xb; int xo;
;       P12_ISSUE(0, 0, 0, cwA, scA);
; _Pragma("nounroll")
;       for (int c = 0; c < 16; ++c) { const int cn = c + 1 < 16 ? c + 1 : 15;
;           P12_XQ(c, 0); P12_ISSUE(c, 0, 1, cwB, scB); P12_BAR(); P12_COMP(0, 0, cwA, scA); P12_ISSUE(c, 1, 0, cwA, scA); P12_BAR(); P12_COMP(0, 1, cwB, scB);
;           P12_XQ(c, 1); P12_ISSUE(c, 1, 1, cwB, scB); P12_BAR(); P12_COMP(1, 0, cwA, scA); P12_ISSUE(c, 2, 0, cwA, scA); P12_BAR(); P12_COMP(1, 1, cwB, scB);
;           P12_XQ(c, 2); P12_ISSUE(c, 2, 1, cwB, scB); P12_BAR(); P12_COMP(2, 0, cwA, scA); P12_ISSUE(c, 3, 0, cwA, scA); P12_BAR(); P12_COMP(2, 1, cwB, scB);
;           P12_XQ(c, 3); P12_ISSUE(c, 3, 1, cwB, scB); P12_BAR(); P12_COMP(3, 0, cwA, scA); P12_ISSUE(cn, 0, 0, cwA, scA); P12_BAR(); P12_COMP(3, 1, cwB, scB);
	v_and_b32_e32 v25, 0xffff0000, v232
	v_add_u32_e32 v27, v30, v31
	v_sub_u32_e32 v28, v27, v78
	v_cvt_f32_i32_e32 v27, v26
	v_cvt_f32_i32_e32 v26, v28
	v_and_b32_e32 v24, 0xffff0000, v233
	s_cselect_b32 s44, s44, s45
	s_lshl_b32 s49, s44, 4
	s_sub_u32 s46, s18, s49
	s_subb_u32 s47, s19, 0
	s_cmp_eq_u32 s45, 0x40000
	v_pk_fma_f32 v[110:111], v[24:25], v[26:27], v[110:111]
	v_and_b32_e32 v24, 0xf0f0f0f, v20
	v_mov_b32_e32 v25, 0
	v_lshrrev_b32_e32 v20, 4, v20
	v_dot4c_i32_i8_e32 v25, v24, v36
	v_and_b32_e32 v20, 0xf0f0f0f, v20
	v_dot4c_i32_i8_e32 v25, v20, v37
	v_and_b32_e32 v20, 0xf0f0f0f, v21
	v_mov_b32_e32 v24, 0
	v_dot4c_i32_i8_e32 v24, v20, v38
	v_lshrrev_b32_e32 v20, 4, v21
	v_and_b32_e32 v20, 0xf0f0f0f, v20
	v_dot4c_i32_i8_e32 v24, v20, v39
	v_and_b32_e32 v20, 0xf0f0f0f, v22
	v_dot4c_i32_i8_e32 v25, v20, v32
	v_lshrrev_b32_e32 v20, 4, v22
	v_and_b32_e32 v20, 0xf0f0f0f, v20
	v_dot4c_i32_i8_e32 v25, v20, v33
	v_and_b32_e32 v20, 0xf0f0f0f, v23
	v_dot4c_i32_i8_e32 v24, v20, v34
	v_lshrrev_b32_e32 v20, 4, v23
	v_and_b32_e32 v20, 0xf0f0f0f, v20
	v_dot4c_i32_i8_e32 v24, v20, v35
	v_and_b32_e32 v20, 0xf0f0f0f, v16
	v_mov_b32_e32 v21, 0
	v_lshrrev_b32_e32 v16, 4, v16
	v_dot4c_i32_i8_e32 v21, v20, v36
	v_and_b32_e32 v16, 0xf0f0f0f, v16
	v_dot4c_i32_i8_e32 v21, v16, v37
	v_and_b32_e32 v16, 0xf0f0f0f, v17
	v_mov_b32_e32 v20, 0
	v_dot4c_i32_i8_e32 v20, v16, v38
	v_lshrrev_b32_e32 v16, 4, v17
	v_and_b32_e32 v16, 0xf0f0f0f, v16
	v_dot4c_i32_i8_e32 v20, v16, v39
	v_and_b32_e32 v16, 0xf0f0f0f, v18
	v_dot4c_i32_i8_e32 v21, v16, v32
	v_lshrrev_b32_e32 v16, 4, v18
	v_and_b32_e32 v16, 0xf0f0f0f, v16
	v_dot4c_i32_i8_e32 v21, v16, v33
	v_and_b32_e32 v16, 0xf0f0f0f, v19
	v_dot4c_i32_i8_e32 v20, v16, v34
	v_lshrrev_b32_e32 v16, 4, v19
	v_and_b32_e32 v16, 0xf0f0f0f, v16
	v_dot4c_i32_i8_e32 v20, v16, v35
	v_add_u32_e32 v18, v25, v24
	v_sub_u32_e32 v18, v18, v78
	s_waitcnt vmcnt(20)
	v_and_b32_e32 v17, 0xffff0000, v234
	v_add_u32_e32 v19, v21, v20
	v_sub_u32_e32 v20, v19, v78
	v_cvt_f32_i32_e32 v19, v18
	v_cvt_f32_i32_e32 v18, v20
	v_and_b32_e32 v16, 0xffff0000, v235
	v_mov_b32_e32 v90, 0
	s_cmp_eq_u32 s45, 0x40000
	v_pk_fma_f32 v[108:109], v[16:17], v[18:19], v[108:109]
	v_and_b32_e32 v16, 0xf0f0f0f, v12
	v_mov_b32_e32 v17, 0
	v_lshrrev_b32_e32 v12, 4, v12
	v_dot4c_i32_i8_e32 v17, v16, v36
	v_and_b32_e32 v12, 0xf0f0f0f, v12
	v_dot4c_i32_i8_e32 v17, v12, v37
	v_and_b32_e32 v12, 0xf0f0f0f, v13
	v_mov_b32_e32 v16, 0
	v_dot4c_i32_i8_e32 v16, v12, v38
	v_lshrrev_b32_e32 v12, 4, v13
	v_and_b32_e32 v12, 0xf0f0f0f, v12
	v_dot4c_i32_i8_e32 v16, v12, v39
	v_and_b32_e32 v12, 0xf0f0f0f, v14
	v_dot4c_i32_i8_e32 v17, v12, v32
	v_lshrrev_b32_e32 v12, 4, v14
	v_and_b32_e32 v12, 0xf0f0f0f, v12
	v_dot4c_i32_i8_e32 v17, v12, v33
	v_and_b32_e32 v12, 0xf0f0f0f, v15
	v_dot4c_i32_i8_e32 v16, v12, v34
	v_lshrrev_b32_e32 v12, 4, v15
	v_and_b32_e32 v12, 0xf0f0f0f, v12
	v_dot4c_i32_i8_e32 v16, v12, v35
	v_and_b32_e32 v12, 0xf0f0f0f, v8
	v_mov_b32_e32 v13, 0
	v_lshrrev_b32_e32 v8, 4, v8
	v_dot4c_i32_i8_e32 v13, v12, v36
	v_and_b32_e32 v8, 0xf0f0f0f, v8
	v_dot4c_i32_i8_e32 v13, v8, v37
	v_and_b32_e32 v8, 0xf0f0f0f, v9
	v_mov_b32_e32 v12, 0
	v_dot4c_i32_i8_e32 v12, v8, v38
	v_lshrrev_b32_e32 v8, 4, v9
	v_and_b32_e32 v8, 0xf0f0f0f, v8
	v_dot4c_i32_i8_e32 v12, v8, v39
	v_and_b32_e32 v8, 0xf0f0f0f, v10
	v_dot4c_i32_i8_e32 v13, v8, v32
	v_lshrrev_b32_e32 v8, 4, v10
	v_and_b32_e32 v8, 0xf0f0f0f, v8
	v_dot4c_i32_i8_e32 v13, v8, v33
	v_and_b32_e32 v8, 0xf0f0f0f, v11
	v_dot4c_i32_i8_e32 v12, v8, v34
	v_lshrrev_b32_e32 v8, 4, v11
	v_and_b32_e32 v8, 0xf0f0f0f, v8
	v_dot4c_i32_i8_e32 v12, v8, v35
	v_add_u32_e32 v11, v17, v16
	s_waitcnt vmcnt(18)
	v_and_b32_e32 v9, 0xffff0000, v237
	v_and_b32_e32 v8, 0xffff0000, v236
	v_add_u32_e32 v10, v13, v12
	v_sub_u32_e32 v12, v11, v78
	v_sub_u32_e32 v10, v10, v78
	v_cvt_f32_i32_e32 v11, v10
	v_cvt_f32_i32_e32 v10, v12
	s_waitcnt vmcnt(15)
	v_and_b32_e32 v89, 0xf0f0f0f, v68
	v_lshrrev_b32_e32 v68, 4, v68
	v_dot4c_i32_i8_e32 v90, v89, v36
	v_pk_fma_f32 v[106:107], v[8:9], v[10:11], v[106:107]
	v_and_b32_e32 v8, 0xf0f0f0f, v4
	v_mov_b32_e32 v9, 0
	v_lshrrev_b32_e32 v4, 4, v4
	v_dot4c_i32_i8_e32 v9, v8, v36
	v_and_b32_e32 v4, 0xf0f0f0f, v4
	v_dot4c_i32_i8_e32 v9, v4, v37
	v_and_b32_e32 v4, 0xf0f0f0f, v5
	v_mov_b32_e32 v8, 0
	v_dot4c_i32_i8_e32 v8, v4, v38
	v_lshrrev_b32_e32 v4, 4, v5
	v_and_b32_e32 v4, 0xf0f0f0f, v4
	v_dot4c_i32_i8_e32 v8, v4, v39
	v_and_b32_e32 v4, 0xf0f0f0f, v6
	v_dot4c_i32_i8_e32 v9, v4, v32
	v_lshrrev_b32_e32 v4, 4, v6
	v_and_b32_e32 v4, 0xf0f0f0f, v4
	v_dot4c_i32_i8_e32 v9, v4, v33
	v_and_b32_e32 v4, 0xf0f0f0f, v7
	v_dot4c_i32_i8_e32 v8, v4, v34
	v_lshrrev_b32_e32 v4, 4, v7
	v_and_b32_e32 v4, 0xf0f0f0f, v4
	v_dot4c_i32_i8_e32 v8, v4, v35
	v_and_b32_e32 v4, 0xf0f0f0f, v0
	v_mov_b32_e32 v5, 0
	v_lshrrev_b32_e32 v0, 4, v0
	v_dot4c_i32_i8_e32 v5, v4, v36
	v_and_b32_e32 v0, 0xf0f0f0f, v0
	v_dot4c_i32_i8_e32 v5, v0, v37
	v_and_b32_e32 v0, 0xf0f0f0f, v1
	v_mov_b32_e32 v4, 0
	v_dot4c_i32_i8_e32 v4, v0, v38
	v_lshrrev_b32_e32 v0, 4, v1
	v_and_b32_e32 v0, 0xf0f0f0f, v0
	v_dot4c_i32_i8_e32 v4, v0, v39
	v_and_b32_e32 v0, 0xf0f0f0f, v2
	v_dot4c_i32_i8_e32 v5, v0, v32
	v_lshrrev_b32_e32 v0, 4, v2
	v_and_b32_e32 v0, 0xf0f0f0f, v0
	v_dot4c_i32_i8_e32 v5, v0, v33
	v_and_b32_e32 v0, 0xf0f0f0f, v3
	v_dot4c_i32_i8_e32 v4, v0, v34
	v_lshrrev_b32_e32 v0, 4, v3
	v_and_b32_e32 v0, 0xf0f0f0f, v0
	v_dot4c_i32_i8_e32 v4, v0, v35
	v_add_u32_e32 v3, v9, v8
	v_and_b32_e32 v1, 0xffff0000, v239
	v_and_b32_e32 v0, 0xffff0000, v238
	v_add_u32_e32 v2, v5, v4
	v_sub_u32_e32 v4, v3, v78
	v_sub_u32_e32 v2, v2, v78
	v_cvt_f32_i32_e32 v3, v2
	v_cvt_f32_i32_e32 v2, v4
	v_and_b32_e32 v68, 0xf0f0f0f, v68
	v_dot4c_i32_i8_e32 v90, v68, v37
	v_and_b32_e32 v68, 0xf0f0f0f, v69
	v_pk_fma_f32 v[104:105], v[0:1], v[2:3], v[104:105]
	ds_read_u16 v0, v93 offset:16384
	ds_read_u16 v1, v93 offset:16400
	ds_read_u16 v2, v93 offset:16416
	ds_read_u16 v3, v93 offset:16432
	v_mov_b32_e32 v89, 0
	s_waitcnt lgkmcnt(3)
; #define P12_ISSUE(c_, i_, h_, CW_, SC_) do { _Pragma("unroll") for (int bb = 0; bb < 8; ++bb) { const unsigned ro = (unsigned)(c_) * 16384u + (unsigned)EL[(i_) * 128 + ((h_) * 8 + bb) * 8 + g8]; \
;         CW_[bb] = *(const v4u*)(U4 + (size_t)(ro * 128u + 16u * (unsigned)k8)); SC_[bb] = USS[(size_t)(ro * 8u + (unsigned)k8)]; } } while (0)
; #define P12_COMP(i_, h_, CW_, SC_) do { _Pragma("unroll") for (int bb = 0; bb < 8; ++bb) { int a0 = 0, a1 = 0; P12_U4(CW_[bb].x, xa.x, xa.y, a0); P12_U4(CW_[bb].y, xa.z, xa.w, a1); P12_U4(CW_[bb].z, xb.x, xb.y, a0); P12_U4(CW_[bb].w, xb.z, xb.w, a1); \
;         psum[(i_)][(h_) * 8 + bb] += __uint_as_float(SC_[bb] << 16) * (float)((a0 + a1) - xo); } } while (0)
; #define P12_BAR() asm volatile("" ::: "memory")
; __device__ __forceinline__ void p12_peer(Frame& F) {
;     ...
;     { v4u cwA[8], cwB[8]; unsigned scA[8], scB[8]; v4u xa, xb; int xo;
;       P12_ISSUE(0, 0, 0, cwA, scA);
; _Pragma("nounroll")
;       for (int c = 0; c < 16; ++c) { const int cn = c + 1 < 16 ? c + 1 : 15;
;           P12_XQ(c, 0); P12_ISSUE(c, 0, 1, cwB, scB); P12_BAR(); P12_COMP(0, 0, cwA, scA); P12_ISSUE(c, 1, 0, cwA, scA); P12_BAR(); P12_COMP(0, 1, cwB, scB);
;           P12_XQ(c, 1); P12_ISSUE(c, 1, 1, cwB, scB); P12_BAR(); P12_COMP(1, 0, cwA, scA); P12_ISSUE(c, 2, 0, cwA, scA); P12_BAR(); P12_COMP(1, 1, cwB, scB);
;           P12_XQ(c, 2); P12_ISSUE(c, 2, 1, cwB, scB); P12_BAR(); P12_COMP(2, 0, cwA, scA); P12_ISSUE(c, 3, 0, cwA, scA); P12_BAR(); P12_COMP(2, 1, cwB, scB);
;           P12_XQ(c, 3); P12_ISSUE(c, 3, 1, cwB, scB); P12_BAR(); P12_COMP(3, 0, cwA, scA); P12_ISSUE(cn, 0, 0, cwA, scA); P12_BAR(); P12_COMP(3, 1, cwB, scB);
	v_add_u32_e32 v0, s44, v0
	v_lshl_or_b32 v4, v0, 7, v165
	v_lshl_or_b32 v0, v0, 5, v248
	global_load_dwordx4 v[28:31], v4, s[0:1]
	global_load_dword v184, v0, s[46:47]
	s_waitcnt lgkmcnt(2)
	v_add_u32_e32 v0, s44, v1
	v_dot4c_i32_i8_e32 v89, v68, v38
	v_lshrrev_b32_e32 v68, 4, v69
	v_lshl_or_b32 v1, v0, 7, v165
	v_lshl_or_b32 v0, v0, 5, v248
	v_and_b32_e32 v68, 0xf0f0f0f, v68
	global_load_dwordx4 v[24:27], v1, s[0:1]
	global_load_dword v185, v0, s[46:47]
	s_waitcnt lgkmcnt(1)
	v_add_u32_e32 v0, s44, v2
	v_dot4c_i32_i8_e32 v89, v68, v39
	v_and_b32_e32 v68, 0xf0f0f0f, v70
	v_lshl_or_b32 v1, v0, 7, v165
	v_lshl_or_b32 v0, v0, 5, v248
	v_dot4c_i32_i8_e32 v90, v68, v32
	v_lshrrev_b32_e32 v68, 4, v70
	global_load_dwordx4 v[20:23], v1, s[0:1]
	global_load_dword v186, v0, s[46:47]
	s_waitcnt lgkmcnt(0)
	v_add_u32_e32 v0, s44, v3
	v_and_b32_e32 v68, 0xf0f0f0f, v68
	v_lshl_or_b32 v1, v0, 7, v165
	v_lshl_or_b32 v0, v0, 5, v248
	v_dot4c_i32_i8_e32 v90, v68, v33
	v_and_b32_e32 v68, 0xf0f0f0f, v71
	global_load_dwordx4 v[16:19], v1, s[0:1]
	global_load_dword v187, v0, s[46:47]
	ds_read_u16 v0, v93 offset:16448
	v_dot4c_i32_i8_e32 v89, v68, v34
	v_lshrrev_b32_e32 v68, 4, v71
	v_and_b32_e32 v68, 0xf0f0f0f, v68
	v_dot4c_i32_i8_e32 v89, v68, v35
	s_waitcnt vmcnt(22)
	v_and_b32_e32 v68, 0xf0f0f0f, v64
	v_mov_b32_e32 v69, 0
	v_lshrrev_b32_e32 v64, 4, v64
	v_dot4c_i32_i8_e32 v69, v68, v36
	v_and_b32_e32 v64, 0xf0f0f0f, v64
	v_dot4c_i32_i8_e32 v69, v64, v37
	v_and_b32_e32 v64, 0xf0f0f0f, v65
	v_mov_b32_e32 v68, 0
	s_waitcnt lgkmcnt(0)
	v_add_u32_e32 v0, s44, v0
	v_dot4c_i32_i8_e32 v68, v64, v38
	v_lshrrev_b32_e32 v64, 4, v65
	v_lshl_or_b32 v1, v0, 7, v165
	v_lshl_or_b32 v0, v0, 5, v248
	v_and_b32_e32 v64, 0xf0f0f0f, v64
	global_load_dwordx4 v[12:15], v1, s[0:1]
	global_load_dword v188, v0, s[46:47]
	ds_read_u16 v0, v93 offset:16464
	v_dot4c_i32_i8_e32 v68, v64, v39
	v_and_b32_e32 v64, 0xf0f0f0f, v66
	v_dot4c_i32_i8_e32 v69, v64, v32
	v_lshrrev_b32_e32 v64, 4, v66
	v_and_b32_e32 v64, 0xf0f0f0f, v64
	v_dot4c_i32_i8_e32 v69, v64, v33
	v_and_b32_e32 v64, 0xf0f0f0f, v67
	v_dot4c_i32_i8_e32 v68, v64, v34
	v_lshrrev_b32_e32 v64, 4, v67
	s_waitcnt lgkmcnt(0)
	v_add_u32_e32 v0, s44, v0
	v_and_b32_e32 v64, 0xf0f0f0f, v64
	v_lshl_or_b32 v1, v0, 7, v165
	v_lshl_or_b32 v0, v0, 5, v248
	v_dot4c_i32_i8_e32 v68, v64, v35
	global_load_dwordx4 v[8:11], v1, s[0:1]
	global_load_dword v189, v0, s[46:47]
	ds_read_u16 v0, v93 offset:16480
	v_add_u32_e32 v66, v90, v89
	v_sub_u32_e32 v67, v68, v78
	v_add_u32_e32 v67, v67, v69
	v_sub_u32_e32 v66, v66, v78
	v_cvt_f32_i32_e32 v66, v66
	v_cvt_f32_i32_e32 v67, v67
	s_waitcnt lgkmcnt(0)
	v_add_u32_e32 v0, s44, v0
	s_waitcnt vmcnt(18)
	v_and_b32_e32 v65, 0xffff0000, v241
	v_and_b32_e32 v64, 0xffff0000, v240
	v_lshl_or_b32 v1, v0, 7, v165
	v_lshl_or_b32 v0, v0, 5, v248
	v_pk_fma_f32 v[102:103], v[64:65], v[66:67], v[102:103]
	v_and_b32_e32 v64, 0xf0f0f0f, v60
	v_mov_b32_e32 v65, 0
	v_lshrrev_b32_e32 v60, 4, v60
	global_load_dwordx4 v[4:7], v1, s[0:1]
	global_load_dword v190, v0, s[46:47]
	ds_read_u16 v0, v93 offset:16496
	v_dot4c_i32_i8_e32 v65, v64, v36
	v_and_b32_e32 v60, 0xf0f0f0f, v60
	v_dot4c_i32_i8_e32 v65, v60, v37
	v_and_b32_e32 v60, 0xf0f0f0f, v61
	v_mov_b32_e32 v64, 0
	v_dot4c_i32_i8_e32 v64, v60, v38
	v_lshrrev_b32_e32 v60, 4, v61
	v_and_b32_e32 v60, 0xf0f0f0f, v60
	v_dot4c_i32_i8_e32 v64, v60, v39
	v_and_b32_e32 v60, 0xf0f0f0f, v62
	s_waitcnt lgkmcnt(0)
	v_add_u32_e32 v88, s44, v0
	v_dot4c_i32_i8_e32 v65, v60, v32
	v_lshrrev_b32_e32 v60, 4, v62
	v_lshl_or_b32 v0, v88, 7, v165
	v_lshl_or_b32 v88, v88, 5, v248
	v_and_b32_e32 v60, 0xf0f0f0f, v60
	global_load_dwordx4 v[0:3], v0, s[0:1]
	v_dot4c_i32_i8_e32 v65, v60, v33
	global_load_dword v191, v88, s[46:47]
	v_and_b32_e32 v60, 0xf0f0f0f, v63
	v_dot4c_i32_i8_e32 v64, v60, v34
	v_lshrrev_b32_e32 v60, 4, v63
	v_and_b32_e32 v60, 0xf0f0f0f, v60
	v_dot4c_i32_i8_e32 v64, v60, v35
	v_and_b32_e32 v60, 0xf0f0f0f, v56
	v_mov_b32_e32 v61, 0
	v_lshrrev_b32_e32 v56, 4, v56
	v_dot4c_i32_i8_e32 v61, v60, v36
	v_and_b32_e32 v56, 0xf0f0f0f, v56
	v_dot4c_i32_i8_e32 v61, v56, v37
	v_and_b32_e32 v56, 0xf0f0f0f, v57
	v_mov_b32_e32 v60, 0
	v_dot4c_i32_i8_e32 v60, v56, v38
	v_lshrrev_b32_e32 v56, 4, v57
	v_and_b32_e32 v56, 0xf0f0f0f, v56
	v_dot4c_i32_i8_e32 v60, v56, v39
	v_and_b32_e32 v56, 0xf0f0f0f, v58
	v_dot4c_i32_i8_e32 v61, v56, v32
	v_lshrrev_b32_e32 v56, 4, v58
	v_and_b32_e32 v56, 0xf0f0f0f, v56
	v_dot4c_i32_i8_e32 v61, v56, v33
	v_and_b32_e32 v56, 0xf0f0f0f, v59
	v_dot4c_i32_i8_e32 v60, v56, v34
	v_lshrrev_b32_e32 v56, 4, v59
	v_and_b32_e32 v56, 0xf0f0f0f, v56
	v_dot4c_i32_i8_e32 v60, v56, v35
	v_sub_u32_e32 v59, v64, v78
	s_waitcnt vmcnt(20)
	v_and_b32_e32 v57, 0xffff0000, v243
	v_and_b32_e32 v56, 0xffff0000, v242
	v_sub_u32_e32 v58, v60, v78
	v_add_u32_e32 v60, v59, v65
	v_add_u32_e32 v58, v58, v61
	v_cvt_f32_i32_e32 v59, v58
	v_cvt_f32_i32_e32 v58, v60
	s_mov_b32 s44, s45
	v_pk_fma_f32 v[100:101], v[56:57], v[58:59], v[100:101]
	v_and_b32_e32 v56, 0xf0f0f0f, v52
	v_mov_b32_e32 v57, 0
	v_lshrrev_b32_e32 v52, 4, v52
	v_dot4c_i32_i8_e32 v57, v56, v36
	v_and_b32_e32 v52, 0xf0f0f0f, v52
	v_dot4c_i32_i8_e32 v57, v52, v37
	v_and_b32_e32 v52, 0xf0f0f0f, v53
	v_mov_b32_e32 v56, 0
	v_dot4c_i32_i8_e32 v56, v52, v38
	v_lshrrev_b32_e32 v52, 4, v53
	v_and_b32_e32 v52, 0xf0f0f0f, v52
	v_dot4c_i32_i8_e32 v56, v52, v39
	v_and_b32_e32 v52, 0xf0f0f0f, v54
	v_dot4c_i32_i8_e32 v57, v52, v32
	v_lshrrev_b32_e32 v52, 4, v54
	v_and_b32_e32 v52, 0xf0f0f0f, v52
	v_dot4c_i32_i8_e32 v57, v52, v33
	v_and_b32_e32 v52, 0xf0f0f0f, v55
	v_dot4c_i32_i8_e32 v56, v52, v34
	v_lshrrev_b32_e32 v52, 4, v55
	v_and_b32_e32 v52, 0xf0f0f0f, v52
	v_dot4c_i32_i8_e32 v56, v52, v35
	v_and_b32_e32 v52, 0xf0f0f0f, v48
	v_mov_b32_e32 v53, 0
	v_lshrrev_b32_e32 v48, 4, v48
	v_dot4c_i32_i8_e32 v53, v52, v36
	v_and_b32_e32 v48, 0xf0f0f0f, v48
	v_dot4c_i32_i8_e32 v53, v48, v37
	v_and_b32_e32 v48, 0xf0f0f0f, v49
	v_mov_b32_e32 v52, 0
	v_dot4c_i32_i8_e32 v52, v48, v38
	v_lshrrev_b32_e32 v48, 4, v49
	v_and_b32_e32 v48, 0xf0f0f0f, v48
	v_dot4c_i32_i8_e32 v52, v48, v39
	v_and_b32_e32 v48, 0xf0f0f0f, v50
	v_dot4c_i32_i8_e32 v53, v48, v32
	v_lshrrev_b32_e32 v48, 4, v50
	v_and_b32_e32 v48, 0xf0f0f0f, v48
	v_dot4c_i32_i8_e32 v53, v48, v33
	v_and_b32_e32 v48, 0xf0f0f0f, v51
	v_dot4c_i32_i8_e32 v52, v48, v34
	v_lshrrev_b32_e32 v48, 4, v51
	v_and_b32_e32 v48, 0xf0f0f0f, v48
	v_dot4c_i32_i8_e32 v52, v48, v35
	v_sub_u32_e32 v51, v56, v78
	s_waitcnt vmcnt(18)
; #define P12_ISSUE(c_, i_, h_, CW_, SC_) do { _Pragma("unroll") for (int bb = 0; bb < 8; ++bb) { const unsigned ro = (unsigned)(c_) * 16384u + (unsigned)EL[(i_) * 128 + ((h_) * 8 + bb) * 8 + g8]; \
;         CW_[bb] = *(const v4u*)(U4 + (size_t)(ro * 128u + 16u * (unsigned)k8)); SC_[bb] = USS[(size_t)(ro * 8u + (unsigned)k8)]; } } while (0)
; #define P12_COMP(i_, h_, CW_, SC_) do { _Pragma("unroll") for (int bb = 0; bb < 8; ++bb) { int a0 = 0, a1 = 0; P12_U4(CW_[bb].x, xa.x, xa.y, a0); P12_U4(CW_[bb].y, xa.z, xa.w, a1); P12_U4(CW_[bb].z, xb.x, xb.y, a0); P12_U4(CW_[bb].w, xb.z, xb.w, a1); \
;         psum[(i_)][(h_) * 8 + bb] += __uint_as_float(SC_[bb] << 16) * (float)((a0 + a1) - xo); } } while (0)
; #define P12_BAR() asm volatile("" ::: "memory")
; __device__ __forceinline__ void p12_peer(Frame& F) {
;     ...
;     { v4u cwA[8], cwB[8]; unsigned scA[8], scB[8]; v4u xa, xb; int xo;
;       P12_ISSUE(0, 0, 0, cwA, scA);
; _Pragma("nounroll")
;       for (int c = 0; c < 16; ++c) { const int cn = c + 1 < 16 ? c + 1 : 15;
;           P12_XQ(c, 0); P12_ISSUE(c, 0, 1, cwB, scB); P12_BAR(); P12_COMP(0, 0, cwA, scA); P12_ISSUE(c, 1, 0, cwA, scA); P12_BAR(); P12_COMP(0, 1, cwB, scB);
;           P12_XQ(c, 1); P12_ISSUE(c, 1, 1, cwB, scB); P12_BAR(); P12_COMP(1, 0, cwA, scA); P12_ISSUE(c, 2, 0, cwA, scA); P12_BAR(); P12_COMP(1, 1, cwB, scB);
;           P12_XQ(c, 2); P12_ISSUE(c, 2, 1, cwB, scB); P12_BAR(); P12_COMP(2, 0, cwA, scA); P12_ISSUE(c, 3, 0, cwA, scA); P12_BAR(); P12_COMP(2, 1, cwB, scB);
;           P12_XQ(c, 3); P12_ISSUE(c, 3, 1, cwB, scB); P12_BAR(); P12_COMP(3, 0, cwA, scA); P12_ISSUE(cn, 0, 0, cwA, scA); P12_BAR(); P12_COMP(3, 1, cwB, scB);
	v_and_b32_e32 v49, 0xffff0000, v245
	v_and_b32_e32 v48, 0xffff0000, v244
	v_sub_u32_e32 v50, v52, v78
	v_add_u32_e32 v52, v51, v57
	v_add_u32_e32 v50, v50, v53
	v_cvt_f32_i32_e32 v51, v50
	v_cvt_f32_i32_e32 v50, v52
	v_pk_fma_f32 v[98:99], v[48:49], v[50:51], v[98:99]
	v_and_b32_e32 v48, 0xf0f0f0f, v44
	v_mov_b32_e32 v49, 0
	v_lshrrev_b32_e32 v44, 4, v44
	v_dot4c_i32_i8_e32 v49, v48, v36
	v_and_b32_e32 v44, 0xf0f0f0f, v44
	v_dot4c_i32_i8_e32 v49, v44, v37
	v_and_b32_e32 v44, 0xf0f0f0f, v45
	v_mov_b32_e32 v48, 0
	v_dot4c_i32_i8_e32 v48, v44, v38
	v_lshrrev_b32_e32 v44, 4, v45
	v_and_b32_e32 v44, 0xf0f0f0f, v44
	v_dot4c_i32_i8_e32 v48, v44, v39
	v_and_b32_e32 v44, 0xf0f0f0f, v46
	v_dot4c_i32_i8_e32 v49, v44, v32
	v_lshrrev_b32_e32 v44, 4, v46
	v_and_b32_e32 v44, 0xf0f0f0f, v44
	v_dot4c_i32_i8_e32 v49, v44, v33
	v_and_b32_e32 v44, 0xf0f0f0f, v47
	v_dot4c_i32_i8_e32 v48, v44, v34
	v_lshrrev_b32_e32 v44, 4, v47
	v_and_b32_e32 v44, 0xf0f0f0f, v44
	v_dot4c_i32_i8_e32 v48, v44, v35
	v_and_b32_e32 v44, 0xf0f0f0f, v40
	v_mov_b32_e32 v45, 0
	v_dot4c_i32_i8_e32 v45, v44, v36
	v_lshrrev_b32_e32 v36, 4, v40
	v_and_b32_e32 v36, 0xf0f0f0f, v36
	v_dot4c_i32_i8_e32 v45, v36, v37
	v_and_b32_e32 v36, 0xf0f0f0f, v41
	v_mov_b32_e32 v37, 0
	v_dot4c_i32_i8_e32 v37, v36, v38
	v_lshrrev_b32_e32 v36, 4, v41
	v_and_b32_e32 v36, 0xf0f0f0f, v36
	v_dot4c_i32_i8_e32 v37, v36, v39
	v_and_b32_e32 v36, 0xf0f0f0f, v42
	v_dot4c_i32_i8_e32 v45, v36, v32
	v_lshrrev_b32_e32 v32, 4, v42
	v_and_b32_e32 v32, 0xf0f0f0f, v32
	v_dot4c_i32_i8_e32 v45, v32, v33
	v_and_b32_e32 v32, 0xf0f0f0f, v43
	v_dot4c_i32_i8_e32 v37, v32, v34
	v_lshrrev_b32_e32 v32, 4, v43
	v_and_b32_e32 v32, 0xf0f0f0f, v32
	v_dot4c_i32_i8_e32 v37, v32, v35
	v_sub_u32_e32 v35, v48, v78
	v_add_u32_e32 v36, v35, v49
	s_waitcnt vmcnt(16)
	v_and_b32_e32 v33, 0xffff0000, v247
	v_sub_u32_e32 v34, v37, v78
	v_add_u32_e32 v34, v34, v45
	v_cvt_f32_i32_e32 v35, v34
	v_cvt_f32_i32_e32 v34, v36
	v_and_b32_e32 v32, 0xffff0000, v246
	s_waitcnt vmcnt(0)
	v_perm_b32 v40, v190, v191, s43
	v_perm_b32 v41, v188, v189, s43
	v_pk_fma_f32 v[96:97], v[32:33], v[34:35], v[96:97]
	v_perm_b32 v42, v186, v187, s43
	v_perm_b32 v43, v184, v185, s43
	s_cbranch_scc0 .LBB0_3272
; #define LDS_WAIT() asm volatile("s_waitcnt lgkmcnt(0)" ::: "memory")
; __device__ __forceinline__ float wave_sum(float v) { v = dpp_add16(v); return (rdlane(v, 0) + rdlane(v, 16)) + (rdlane(v, 32) + rdlane(v, 48)); }
; __device__ __forceinline__ float wave_max(float v) { v = dpp_max16(v); return fmaxf(fmaxf(rdlane(v, 0), rdlane(v, 16)), fmaxf(rdlane(v, 32), rdlane(v, 48))); }
; __device__ __forceinline__ void p12_peer(Frame& F) {
;     ...
;         mxa = wave_max(mxa); const float inv = mxa > 0.f ? 127.0f / mxa : 0.f;
;         const float rsn = 1.0f / sqrtf(wave_sum(PSQ[(size_t)t * 64 + F.lane]) * (1.f / D_) + 1e-6f);
;         sx[i] = mxa * rsn * (1.0f / 127.0f);
;     ...
;     asm volatile("" ::: "memory"); LDS_WAIT();
; #pragma unroll
;     for (int i = 0; i < 4; ++i) { const int t = F.gw + i * F.NGW;
; #pragma unroll
;         for (int b = 0; b < 16; ++b) { float d = psum[i][b];
;             d += __builtin_bit_cast(float, __builtin_amdgcn_update_dpp(0, __builtin_bit_cast(int, d), 0xB1, 0xF, 0xF, false));
;             d += __builtin_bit_cast(float, __builtin_amdgcn_update_dpp(0, __builtin_bit_cast(int, d), 0x4E, 0xF, 0xF, false));
;             d += __builtin_bit_cast(float, __builtin_amdgcn_update_dpp(0, __builtin_bit_cast(int, d), 0x141, 0xF, 0xF, false));
;             const int idx = b * 8 + g8; const float w = PGT[(size_t)t * 128 + idx] * gelu_erf(sx[i] * d) * VSC[EL[i * 128 + idx]];
;             if (k8 == 0) WL[i * 128 + idx] = w; } }
	v_mov_b32_e32 v0, s41
	v_mov_b32_e32 v1, s42
	v_add_f32_e32 v0, s39, v0
	v_add_f32_e32 v1, s40, v1
	v_add_f32_e32 v0, v0, v1
	v_mov_b32_e32 v1, 0x358637bd
	v_fmac_f32_e32 v1, 0x39800000, v0
	s_mov_b32 s0, 0xf800000
	v_mul_f32_e32 v0, 0x4f800000, v1
	v_cmp_gt_f32_e32 vcc, s0, v1
	s_add_u32 s43, s68, 0x1200000
	s_addc_u32 s44, s69, 0
	v_cndmask_b32_e32 v0, v1, v0, vcc
	v_sqrt_f32_e32 v1, v0
	s_add_u32 s18, s68, 0xf000000
	s_addc_u32 s19, s69, 0
	v_add_u32_e32 v2, -1, v1
	v_fma_f32 v3, -v2, v1, v0
	v_cmp_ge_f32_e64 s[0:1], 0, v3
	v_add_u32_e32 v3, 1, v1
	s_add_u32 s2, s43, s2
	v_cndmask_b32_e64 v2, v1, v2, s[0:1]
	v_fma_f32 v1, -v3, v1, v0
	v_cmp_lt_f32_e64 s[0:1], 0, v1
	s_waitcnt lgkmcnt(0)
	s_addc_u32 s3, s44, s3
	v_ashrrev_i32_e32 v95, 31, v94
	v_cndmask_b32_e64 v1, v2, v3, s[0:1]
	v_mul_f32_e32 v2, 0x37800000, v1
	v_cndmask_b32_e32 v1, v1, v2, vcc
	v_mov_b32_e32 v2, 0x260
	v_cmp_class_f32_e32 vcc, v0, v2
	s_nop 1
	v_cndmask_b32_e32 v2, v1, v0, vcc
	v_div_scale_f32 v3, s[0:1], v2, v2, 1.0
	v_rcp_f32_e32 v4, v3
	v_lshl_add_u64 v[0:1], v[94:95], 2, s[2:3]
	ds_read_u16 v20, v93 offset:16384
	ds_read_u16 v21, v93 offset:16400
	ds_read_u16 v22, v93 offset:16416
	ds_read_u16 v23, v93 offset:16432
	ds_read_u16 v24, v93 offset:16448
	ds_read_u16 v25, v93 offset:16464
	ds_read_u16 v26, v93 offset:16480
	ds_read_u16 v27, v93 offset:16496
	s_waitcnt lgkmcnt(0)
	ds_read_u16 v28, v93 offset:16512
	ds_read_u16 v29, v93 offset:16528
	ds_read_u16 v30, v93 offset:16544
	ds_read_u16 v31, v93 offset:16560
	ds_read_u16 v32, v93 offset:16576
	ds_read_u16 v33, v93 offset:16592
	ds_read_u16 v34, v93 offset:16608
	ds_read_u16 v35, v93 offset:16624
	s_waitcnt lgkmcnt(0)
	v_lshlrev_b32_e32 v20, 2, v20
	v_lshlrev_b32_e32 v21, 2, v21
	v_lshlrev_b32_e32 v22, 2, v22
	v_lshlrev_b32_e32 v23, 2, v23
	v_lshlrev_b32_e32 v24, 2, v24
	v_lshlrev_b32_e32 v25, 2, v25
	v_lshlrev_b32_e32 v26, 2, v26
	v_lshlrev_b32_e32 v27, 2, v27
	v_lshlrev_b32_e32 v28, 2, v28
	v_lshlrev_b32_e32 v29, 2, v29
	v_lshlrev_b32_e32 v30, 2, v30
	v_lshlrev_b32_e32 v31, 2, v31
	v_lshlrev_b32_e32 v32, 2, v32
	v_lshlrev_b32_e32 v33, 2, v33
	v_lshlrev_b32_e32 v34, 2, v34
	v_lshlrev_b32_e32 v35, 2, v35
	global_load_dword v40, v[0:1], off offset:0
	global_load_dword v60, v20, s[18:19]
	global_load_dword v41, v[0:1], off offset:32
	global_load_dword v61, v21, s[18:19]
	global_load_dword v42, v[0:1], off offset:64
	global_load_dword v62, v22, s[18:19]
	global_load_dword v43, v[0:1], off offset:96
	global_load_dword v63, v23, s[18:19]
	global_load_dword v44, v[0:1], off offset:128
	global_load_dword v64, v24, s[18:19]
	global_load_dword v45, v[0:1], off offset:160
	global_load_dword v65, v25, s[18:19]
	global_load_dword v46, v[0:1], off offset:192
	global_load_dword v66, v26, s[18:19]
	global_load_dword v47, v[0:1], off offset:224
	global_load_dword v67, v27, s[18:19]
	global_load_dword v48, v[0:1], off offset:256
	global_load_dword v68, v28, s[18:19]
	global_load_dword v49, v[0:1], off offset:288
	global_load_dword v69, v29, s[18:19]
	global_load_dword v50, v[0:1], off offset:320
	global_load_dword v70, v30, s[18:19]
	global_load_dword v51, v[0:1], off offset:352
	global_load_dword v71, v31, s[18:19]
	global_load_dword v52, v[0:1], off offset:384
	global_load_dword v72, v32, s[18:19]
	global_load_dword v53, v[0:1], off offset:416
	global_load_dword v73, v33, s[18:19]
	global_load_dword v54, v[0:1], off offset:448
	global_load_dword v74, v34, s[18:19]
	global_load_dword v55, v[0:1], off offset:480
	global_load_dword v75, v35, s[18:19]
	s_waitcnt vmcnt(0)
	v_cmp_eq_u32_e64 s[0:1], 0, v164
	v_fma_f32 v5, -v3, v4, 1.0
	v_fmac_f32_e32 v4, v5, v4
	v_div_scale_f32 v5, vcc, 1.0, v2, 1.0
	v_mul_f32_e32 v6, v5, v4
	v_fma_f32 v7, -v3, v6, v5
	v_fmac_f32_e32 v6, v7, v4
	v_fma_f32 v3, -v3, v6, v5
	v_div_fmas_f32 v3, v3, v4, v6
	v_div_fixup_f32 v2, v3, v2, 1.0
	v_add_f32_dpp v5, v159, v159 quad_perm:[1,0,3,2] row_mask:0xf bank_mask:0xf bound_ctrl:1
	v_mul_f32_e32 v3, v163, v2
	v_mov_b32_e32 v6, 0
	v_add_f32_dpp v5, v5, v5 quad_perm:[2,3,0,1] row_mask:0xf bank_mask:0xf bound_ctrl:1
	v_mov_b32_e32 v4, 0
	v_lshl_add_u32 v2, v94, 2, s20
	v_mul_f32_e32 v3, 0x3c010204, v3
	v_mov_b32_dpp v6, v5 row_half_mirror row_mask:0xf bank_mask:0xf
	s_and_saveexec_b64 s[2:3], s[0:1]
	s_cbranch_execz .LBB0_3275
	v_add_f32_e32 v5, v5, v6
	v_mul_f32_e32 v5, v3, v5
	s_mov_b32 s39, 0x3e6d3388
	v_mul_f32_e32 v6, v5, v5
	s_waitcnt lgkmcnt(0)
	v_fma_f32 v7, |v5|, s39, 1.0
	v_rcp_f32_e32 v7, v7
	v_mov_b32_e32 v10, 0xbf3a00e3
	v_mul_f32_e32 v6, 0xbf38aa3b, v6
	v_exp_f32_e32 v6, v6
	v_fmac_f32_e32 v10, 0x3f07dc22, v7
	v_fmaak_f32 v10, v7, v10, 0x3f35f0e3
	v_fmaak_f32 v10, v7, v10, 0xbe11a98e
	v_fmaak_f32 v10, v7, v10, 0x3e027906
	v_mul_f32_e32 v7, v7, v10
	v_mul_f32_e32 v6, v6, v7
	v_mul_f32_e32 v7, v5, v6
	v_fma_f32 v6, -v5, v6, v5
	v_cmp_gt_f32_e32 vcc, 0, v5
	s_nop 1
	v_cndmask_b32_e32 v5, v6, v7, vcc
	s_waitcnt vmcnt(1)
	v_mul_f32_e32 v5, v5, v40
	s_waitcnt vmcnt(0)
	v_mul_f32_e32 v5, v5, v60
	ds_write_b32 v2, v5
